# baseline (speedup 1.0000x reference)
.Lpf_vQ:
	s_lshl_b32 s25, s25, 6
	s_add_u32 s29, s10, s25
	s_lshr_b32 s29, s29, 4
	v_add_u32_e32 v5, s25, v3
	v_lshlrev_b32_e32 v5, 7, v5
	v_add_u32_e32 v15, v5, v6
	v_add_u32_e32 v16, v5, v7
	v_add_u32_e32 v5, 0x8000, v9
	v_add_u32_e32 v17, v5, v6
	v_add_u32_e32 v18, v5, v7
	v_add_u32_e32 v19, 0x18000, v15
	v_add_u32_e32 v20, 0x18000, v16
	v_add_u32_e32 v21, 0x18000, v17
	v_add_u32_e32 v22, 0x18000, v18
	v_lshlrev_b32_e32 v5, 4, v4
	global_load_dwordx4 v[24:27], v5, s[14:15] offset:0
	global_load_dwordx4 v[28:31], v5, s[14:15] offset:64
	global_load_dwordx4 v[32:35], v5, s[14:15] offset:128
	global_load_dwordx4 v[36:39], v5, s[14:15] offset:192
	global_load_dwordx4 v[40:43], v5, s[16:17] offset:0
	global_load_dwordx4 v[44:47], v5, s[16:17] offset:64
	global_load_dwordx4 v[48:51], v5, s[16:17] offset:128
	global_load_dwordx4 v[52:55], v5, s[16:17] offset:192
	s_add_u32 m0, s28, 0x0
	s_nop 0
	global_load_lds_dwordx4 v10, s[4:5]
	s_add_u32 m0, s28, 0x2000
	s_nop 0
	global_load_lds_dwordx4 v11, s[4:5]
	s_add_u32 m0, s28, 0x4000
	s_nop 0
	global_load_lds_dwordx4 v12, s[4:5]
	s_add_u32 m0, s28, 0x6000
	s_nop 0
	global_load_lds_dwordx4 v13, s[4:5]
	s_add_u32 s4, s4, s20
	s_addc_u32 s5, s5, 0
	s_add_u32 m0, s28, 0x8000
	s_nop 0
	global_load_lds_dwordx4 v10, s[6:7]
	s_add_u32 m0, s28, 0xa000
	s_nop 0
	global_load_lds_dwordx4 v11, s[6:7]
	s_add_u32 s6, s6, s20
	s_addc_u32 s7, s7, 0
	s_add_u32 m0, s28, 0xc000
	s_nop 0
	global_load_lds_dwordx4 v10, s[4:5]
	s_add_u32 m0, s28, 0xe000
	s_nop 0
	global_load_lds_dwordx4 v11, s[4:5]
	s_add_u32 m0, s28, 0x10000
	s_nop 0
	global_load_lds_dwordx4 v12, s[4:5]
	s_add_u32 m0, s28, 0x12000
	s_nop 0
	global_load_lds_dwordx4 v13, s[4:5]
	s_add_u32 s4, s4, s20
	s_addc_u32 s5, s5, 0
	s_add_u32 m0, s28, 0x14000
	s_nop 0
	global_load_lds_dwordx4 v10, s[6:7]
	s_add_u32 m0, s28, 0x16000
	s_nop 0
	global_load_lds_dwordx4 v11, s[6:7]
	s_add_u32 s6, s6, s20
	s_addc_u32 s7, s7, 0
	s_add_u32 m0, s28, 0x18000
	s_nop 0
	global_load_lds_dwordx4 v10, s[4:5]
	s_add_u32 m0, s28, 0x1a000
	s_nop 0
	global_load_lds_dwordx4 v11, s[4:5]
	s_add_u32 m0, s28, 0x1c000
	s_nop 0
	global_load_lds_dwordx4 v12, s[4:5]
	s_add_u32 m0, s28, 0x1e000
	s_nop 0
	global_load_lds_dwordx4 v13, s[4:5]
	s_add_u32 s4, s4, s20
	s_addc_u32 s5, s5, 0
	s_add_u32 m0, s28, 0x20000
	s_nop 0
	global_load_lds_dwordx4 v10, s[6:7]
	s_add_u32 m0, s28, 0x22000
	s_nop 0
	global_load_lds_dwordx4 v11, s[6:7]
	s_add_u32 s6, s6, s20
	s_addc_u32 s7, s7, 0
	s_waitcnt vmcnt(12) lgkmcnt(0)
	s_barrier
	s_waitcnt lgkmcnt(7)
	ds_read_b128 v[136:139], v15
	ds_read_b128 v[156:159], v17
	ds_read_b128 v[160:163], v17 offset:2048
	ds_read_b128 v[164:167], v17 offset:4096
	ds_read_b128 v[168:171], v17 offset:6144
	ds_read_b128 v[140:143], v15 offset:2048
	ds_read_b128 v[144:147], v15 offset:4096
	ds_read_b128 v[148:151], v15 offset:6144
	s_waitcnt lgkmcnt(7)
	ds_read_b128 v[172:175], v16
	ds_read_b128 v[192:195], v18
	ds_read_b128 v[196:199], v18 offset:2048
	ds_read_b128 v[200:203], v18 offset:4096
	ds_read_b128 v[204:207], v18 offset:6144
	ds_read_b128 v[176:179], v16 offset:2048
	ds_read_b128 v[180:183], v16 offset:4096
	ds_read_b128 v[184:187], v16 offset:6144
	s_waitcnt lgkmcnt(8)
	v_mfma_f32_16x16x32_f16 v[56:59], v[156:159], v[136:139], 0
	v_mfma_f32_16x16x32_f16 v[60:63], v[160:163], v[136:139], 0
	v_mfma_f32_16x16x32_f16 v[64:67], v[164:167], v[136:139], 0
	v_mfma_f32_16x16x32_f16 v[68:71], v[168:171], v[136:139], 0
	v_mfma_f32_16x16x32_f16 v[72:75], v[156:159], v[140:143], 0
	v_mfma_f32_16x16x32_f16 v[76:79], v[160:163], v[140:143], 0
	v_mfma_f32_16x16x32_f16 v[80:83], v[164:167], v[140:143], 0
	v_mfma_f32_16x16x32_f16 v[84:87], v[168:171], v[140:143], 0
	v_mfma_f32_16x16x32_f16 v[88:91], v[156:159], v[144:147], 0
	v_mfma_f32_16x16x32_f16 v[92:95], v[160:163], v[144:147], 0
	v_mfma_f32_16x16x32_f16 v[96:99], v[164:167], v[144:147], 0
	v_mfma_f32_16x16x32_f16 v[100:103], v[168:171], v[144:147], 0
	v_mfma_f32_16x16x32_f16 v[104:107], v[156:159], v[148:151], 0
	v_mfma_f32_16x16x32_f16 v[108:111], v[160:163], v[148:151], 0
	v_mfma_f32_16x16x32_f16 v[112:115], v[164:167], v[148:151], 0
	v_mfma_f32_16x16x32_f16 v[116:119], v[168:171], v[148:151], 0
	s_waitcnt vmcnt(6) lgkmcnt(0)
	s_barrier
	s_waitcnt lgkmcnt(7)
	ds_read_b128 v[136:139], v15 offset:49152
	ds_read_b128 v[156:159], v17 offset:49152
	ds_read_b128 v[160:163], v17 offset:51200
	ds_read_b128 v[164:167], v17 offset:53248
	ds_read_b128 v[168:171], v17 offset:55296
	ds_read_b128 v[140:143], v15 offset:51200
	ds_read_b128 v[144:147], v15 offset:53248
	ds_read_b128 v[148:151], v15 offset:55296
	s_waitcnt lgkmcnt(8)
	v_mfma_f32_16x16x32_f16 v[56:59], v[192:195], v[172:175], v[56:59]
	s_add_u32 m0, s28, 0x0
	v_mfma_f32_16x16x32_f16 v[60:63], v[196:199], v[172:175], v[60:63]
	global_load_lds_dwordx4 v10, s[4:5]
	v_mfma_f32_16x16x32_f16 v[64:67], v[200:203], v[172:175], v[64:67]
	v_mfma_f32_16x16x32_f16 v[68:71], v[204:207], v[172:175], v[68:71]
	v_mfma_f32_16x16x32_f16 v[72:75], v[192:195], v[176:179], v[72:75]
	v_mfma_f32_16x16x32_f16 v[76:79], v[196:199], v[176:179], v[76:79]
	s_add_u32 m0, s28, 0x2000
	v_mfma_f32_16x16x32_f16 v[80:83], v[200:203], v[176:179], v[80:83]
	global_load_lds_dwordx4 v11, s[4:5]
	v_mfma_f32_16x16x32_f16 v[84:87], v[204:207], v[176:179], v[84:87]
	v_mfma_f32_16x16x32_f16 v[88:91], v[192:195], v[180:183], v[88:91]
	v_mfma_f32_16x16x32_f16 v[92:95], v[196:199], v[180:183], v[92:95]
	v_mfma_f32_16x16x32_f16 v[96:99], v[200:203], v[180:183], v[96:99]
	s_add_u32 m0, s28, 0x4000
	v_mfma_f32_16x16x32_f16 v[100:103], v[204:207], v[180:183], v[100:103]
	global_load_lds_dwordx4 v12, s[4:5]
	v_mfma_f32_16x16x32_f16 v[104:107], v[192:195], v[184:187], v[104:107]
	v_mfma_f32_16x16x32_f16 v[108:111], v[196:199], v[184:187], v[108:111]
	v_mfma_f32_16x16x32_f16 v[112:115], v[200:203], v[184:187], v[112:115]
	v_mfma_f32_16x16x32_f16 v[116:119], v[204:207], v[184:187], v[116:119]
	s_waitcnt lgkmcnt(7)
	ds_read_b128 v[172:175], v16 offset:49152
	ds_read_b128 v[192:195], v18 offset:49152
	ds_read_b128 v[196:199], v18 offset:51200
	ds_read_b128 v[200:203], v18 offset:53248
	ds_read_b128 v[204:207], v18 offset:55296
	ds_read_b128 v[176:179], v16 offset:51200
	ds_read_b128 v[180:183], v16 offset:53248
	ds_read_b128 v[184:187], v16 offset:55296
	s_waitcnt lgkmcnt(8)
	v_mfma_f32_16x16x32_f16 v[56:59], v[156:159], v[136:139], v[56:59]
	s_add_u32 m0, s28, 0x6000
	v_mfma_f32_16x16x32_f16 v[60:63], v[160:163], v[136:139], v[60:63]
	global_load_lds_dwordx4 v13, s[4:5]
	s_add_u32 s4, s4, s20
	s_addc_u32 s5, s5, 0
	v_mfma_f32_16x16x32_f16 v[64:67], v[164:167], v[136:139], v[64:67]
	v_mfma_f32_16x16x32_f16 v[68:71], v[168:171], v[136:139], v[68:71]
	v_mfma_f32_16x16x32_f16 v[72:75], v[156:159], v[140:143], v[72:75]
	v_mfma_f32_16x16x32_f16 v[76:79], v[160:163], v[140:143], v[76:79]
	s_add_u32 m0, s28, 0x8000
	v_mfma_f32_16x16x32_f16 v[80:83], v[164:167], v[140:143], v[80:83]
	global_load_lds_dwordx4 v10, s[6:7]
	v_mfma_f32_16x16x32_f16 v[84:87], v[168:171], v[140:143], v[84:87]
	v_mfma_f32_16x16x32_f16 v[88:91], v[156:159], v[144:147], v[88:91]
	v_mfma_f32_16x16x32_f16 v[92:95], v[160:163], v[144:147], v[92:95]
	v_mfma_f32_16x16x32_f16 v[96:99], v[164:167], v[144:147], v[96:99]
	s_add_u32 m0, s28, 0xa000
	v_mfma_f32_16x16x32_f16 v[100:103], v[168:171], v[144:147], v[100:103]
	global_load_lds_dwordx4 v11, s[6:7]
	s_add_u32 s6, s6, s20
	s_addc_u32 s7, s7, 0
	v_mfma_f32_16x16x32_f16 v[104:107], v[156:159], v[148:151], v[104:107]
	v_mfma_f32_16x16x32_f16 v[108:111], v[160:163], v[148:151], v[108:111]
	v_mfma_f32_16x16x32_f16 v[112:115], v[164:167], v[148:151], v[112:115]
	v_mfma_f32_16x16x32_f16 v[116:119], v[168:171], v[148:151], v[116:119]
	s_waitcnt vmcnt(6) lgkmcnt(0)
	s_barrier
	s_waitcnt lgkmcnt(7)
	ds_read_b128 v[136:139], v19
	ds_read_b128 v[156:159], v21
	ds_read_b128 v[160:163], v21 offset:2048
	ds_read_b128 v[164:167], v21 offset:4096
	ds_read_b128 v[168:171], v21 offset:6144
	ds_read_b128 v[140:143], v19 offset:2048
	ds_read_b128 v[144:147], v19 offset:4096
	ds_read_b128 v[148:151], v19 offset:6144
	s_waitcnt lgkmcnt(8)
	v_mfma_f32_16x16x32_f16 v[56:59], v[192:195], v[172:175], v[56:59]
	s_add_u32 m0, s28, 0xc000
	v_mfma_f32_16x16x32_f16 v[60:63], v[196:199], v[172:175], v[60:63]
	global_load_lds_dwordx4 v10, s[4:5]
	v_mfma_f32_16x16x32_f16 v[64:67], v[200:203], v[172:175], v[64:67]
	v_mfma_f32_16x16x32_f16 v[68:71], v[204:207], v[172:175], v[68:71]
	v_mfma_f32_16x16x32_f16 v[72:75], v[192:195], v[176:179], v[72:75]
	v_mfma_f32_16x16x32_f16 v[76:79], v[196:199], v[176:179], v[76:79]
	s_add_u32 m0, s28, 0xe000
	v_mfma_f32_16x16x32_f16 v[80:83], v[200:203], v[176:179], v[80:83]
	global_load_lds_dwordx4 v11, s[4:5]
	v_mfma_f32_16x16x32_f16 v[84:87], v[204:207], v[176:179], v[84:87]
	v_mfma_f32_16x16x32_f16 v[88:91], v[192:195], v[180:183], v[88:91]
	v_mfma_f32_16x16x32_f16 v[92:95], v[196:199], v[180:183], v[92:95]
	v_mfma_f32_16x16x32_f16 v[96:99], v[200:203], v[180:183], v[96:99]
	s_add_u32 m0, s28, 0x10000
	v_mfma_f32_16x16x32_f16 v[100:103], v[204:207], v[180:183], v[100:103]
	global_load_lds_dwordx4 v12, s[4:5]
	v_mfma_f32_16x16x32_f16 v[104:107], v[192:195], v[184:187], v[104:107]
	v_mfma_f32_16x16x32_f16 v[108:111], v[196:199], v[184:187], v[108:111]
	v_mfma_f32_16x16x32_f16 v[112:115], v[200:203], v[184:187], v[112:115]
	v_mfma_f32_16x16x32_f16 v[116:119], v[204:207], v[184:187], v[116:119]
	s_waitcnt lgkmcnt(7)
	ds_read_b128 v[172:175], v20
	ds_read_b128 v[192:195], v22
	ds_read_b128 v[196:199], v22 offset:2048
	ds_read_b128 v[200:203], v22 offset:4096
	ds_read_b128 v[204:207], v22 offset:6144
	ds_read_b128 v[176:179], v20 offset:2048
	ds_read_b128 v[180:183], v20 offset:4096
	ds_read_b128 v[184:187], v20 offset:6144
	s_waitcnt lgkmcnt(8)
	v_mfma_f32_16x16x32_f16 v[56:59], v[156:159], v[136:139], v[56:59]
	s_add_u32 m0, s28, 0x12000
	v_mfma_f32_16x16x32_f16 v[60:63], v[160:163], v[136:139], v[60:63]
	global_load_lds_dwordx4 v13, s[4:5]
	s_add_u32 s4, s4, s20
	s_addc_u32 s5, s5, 0
	v_mfma_f32_16x16x32_f16 v[64:67], v[164:167], v[136:139], v[64:67]
	v_mfma_f32_16x16x32_f16 v[68:71], v[168:171], v[136:139], v[68:71]
	v_mfma_f32_16x16x32_f16 v[72:75], v[156:159], v[140:143], v[72:75]
	v_mfma_f32_16x16x32_f16 v[76:79], v[160:163], v[140:143], v[76:79]
	s_add_u32 m0, s28, 0x14000
	v_mfma_f32_16x16x32_f16 v[80:83], v[164:167], v[140:143], v[80:83]
	global_load_lds_dwordx4 v10, s[6:7]
	v_mfma_f32_16x16x32_f16 v[84:87], v[168:171], v[140:143], v[84:87]
	v_mfma_f32_16x16x32_f16 v[88:91], v[156:159], v[144:147], v[88:91]
	v_mfma_f32_16x16x32_f16 v[92:95], v[160:163], v[144:147], v[92:95]
	v_mfma_f32_16x16x32_f16 v[96:99], v[164:167], v[144:147], v[96:99]
	s_add_u32 m0, s28, 0x16000
	v_mfma_f32_16x16x32_f16 v[100:103], v[168:171], v[144:147], v[100:103]
	global_load_lds_dwordx4 v11, s[6:7]
	s_add_u32 s6, s6, s20
	s_addc_u32 s7, s7, 0
	v_mfma_f32_16x16x32_f16 v[104:107], v[156:159], v[148:151], v[104:107]
	v_mfma_f32_16x16x32_f16 v[108:111], v[160:163], v[148:151], v[108:111]
	v_mfma_f32_16x16x32_f16 v[112:115], v[164:167], v[148:151], v[112:115]
	v_mfma_f32_16x16x32_f16 v[116:119], v[168:171], v[148:151], v[116:119]
	s_waitcnt vmcnt(6) lgkmcnt(0)
	s_barrier
	s_waitcnt lgkmcnt(7)
	ds_read_b128 v[136:139], v15
	ds_read_b128 v[156:159], v17
	ds_read_b128 v[160:163], v17 offset:2048
	ds_read_b128 v[164:167], v17 offset:4096
	ds_read_b128 v[168:171], v17 offset:6144
	ds_read_b128 v[140:143], v15 offset:2048
	ds_read_b128 v[144:147], v15 offset:4096
	ds_read_b128 v[148:151], v15 offset:6144
	s_waitcnt lgkmcnt(8)
	v_mfma_f32_16x16x32_f16 v[56:59], v[192:195], v[172:175], v[56:59]
	s_add_u32 m0, s28, 0x18000
	v_mfma_f32_16x16x32_f16 v[60:63], v[196:199], v[172:175], v[60:63]
	global_load_lds_dwordx4 v10, s[4:5]
	v_mfma_f32_16x16x32_f16 v[64:67], v[200:203], v[172:175], v[64:67]
	v_mfma_f32_16x16x32_f16 v[68:71], v[204:207], v[172:175], v[68:71]
	v_mfma_f32_16x16x32_f16 v[72:75], v[192:195], v[176:179], v[72:75]
	v_mfma_f32_16x16x32_f16 v[76:79], v[196:199], v[176:179], v[76:79]
	s_add_u32 m0, s28, 0x1a000
	v_mfma_f32_16x16x32_f16 v[80:83], v[200:203], v[176:179], v[80:83]
	global_load_lds_dwordx4 v11, s[4:5]
	v_mfma_f32_16x16x32_f16 v[84:87], v[204:207], v[176:179], v[84:87]
	v_mfma_f32_16x16x32_f16 v[88:91], v[192:195], v[180:183], v[88:91]
	v_mfma_f32_16x16x32_f16 v[92:95], v[196:199], v[180:183], v[92:95]
	v_mfma_f32_16x16x32_f16 v[96:99], v[200:203], v[180:183], v[96:99]
	s_add_u32 m0, s28, 0x1c000
	v_mfma_f32_16x16x32_f16 v[100:103], v[204:207], v[180:183], v[100:103]
	global_load_lds_dwordx4 v12, s[4:5]
	v_mfma_f32_16x16x32_f16 v[104:107], v[192:195], v[184:187], v[104:107]
	v_mfma_f32_16x16x32_f16 v[108:111], v[196:199], v[184:187], v[108:111]
	v_mfma_f32_16x16x32_f16 v[112:115], v[200:203], v[184:187], v[112:115]
	v_mfma_f32_16x16x32_f16 v[116:119], v[204:207], v[184:187], v[116:119]
	s_waitcnt lgkmcnt(7)
	ds_read_b128 v[172:175], v16
	ds_read_b128 v[192:195], v18
	ds_read_b128 v[196:199], v18 offset:2048
	ds_read_b128 v[200:203], v18 offset:4096
	ds_read_b128 v[204:207], v18 offset:6144
	ds_read_b128 v[176:179], v16 offset:2048
	ds_read_b128 v[180:183], v16 offset:4096
	ds_read_b128 v[184:187], v16 offset:6144
	s_waitcnt lgkmcnt(8)
	v_mfma_f32_16x16x32_f16 v[56:59], v[156:159], v[136:139], v[56:59]
	s_add_u32 m0, s28, 0x1e000
	v_mfma_f32_16x16x32_f16 v[60:63], v[160:163], v[136:139], v[60:63]
	global_load_lds_dwordx4 v13, s[4:5]
	s_add_u32 s4, s4, s20
	s_addc_u32 s5, s5, 0
	v_mfma_f32_16x16x32_f16 v[64:67], v[164:167], v[136:139], v[64:67]
	v_mfma_f32_16x16x32_f16 v[68:71], v[168:171], v[136:139], v[68:71]
	v_mfma_f32_16x16x32_f16 v[72:75], v[156:159], v[140:143], v[72:75]
	v_mfma_f32_16x16x32_f16 v[76:79], v[160:163], v[140:143], v[76:79]
	s_add_u32 m0, s28, 0x20000
	v_mfma_f32_16x16x32_f16 v[80:83], v[164:167], v[140:143], v[80:83]
	global_load_lds_dwordx4 v10, s[6:7]
	v_mfma_f32_16x16x32_f16 v[84:87], v[168:171], v[140:143], v[84:87]
	v_mfma_f32_16x16x32_f16 v[88:91], v[156:159], v[144:147], v[88:91]
	v_mfma_f32_16x16x32_f16 v[92:95], v[160:163], v[144:147], v[92:95]
	v_mfma_f32_16x16x32_f16 v[96:99], v[164:167], v[144:147], v[96:99]
	s_add_u32 m0, s28, 0x22000
	v_mfma_f32_16x16x32_f16 v[100:103], v[168:171], v[144:147], v[100:103]
	global_load_lds_dwordx4 v11, s[6:7]
	s_add_u32 s6, s6, s20
	s_addc_u32 s7, s7, 0
	v_mfma_f32_16x16x32_f16 v[104:107], v[156:159], v[148:151], v[104:107]
	v_mfma_f32_16x16x32_f16 v[108:111], v[160:163], v[148:151], v[108:111]
	v_mfma_f32_16x16x32_f16 v[112:115], v[164:167], v[148:151], v[112:115]
	v_mfma_f32_16x16x32_f16 v[116:119], v[168:171], v[148:151], v[116:119]
	s_waitcnt vmcnt(6) lgkmcnt(0)
	s_barrier
	s_waitcnt lgkmcnt(7)
	ds_read_b128 v[136:139], v15 offset:49152
	ds_read_b128 v[156:159], v17 offset:49152
	ds_read_b128 v[160:163], v17 offset:51200
	ds_read_b128 v[164:167], v17 offset:53248
	ds_read_b128 v[168:171], v17 offset:55296
	ds_read_b128 v[140:143], v15 offset:51200
	ds_read_b128 v[144:147], v15 offset:53248
	ds_read_b128 v[148:151], v15 offset:55296
	s_waitcnt lgkmcnt(8)
	v_mfma_f32_16x16x32_f16 v[56:59], v[192:195], v[172:175], v[56:59]
	s_add_u32 m0, s28, 0x0
	v_mfma_f32_16x16x32_f16 v[60:63], v[196:199], v[172:175], v[60:63]
	global_load_lds_dwordx4 v10, s[4:5]
	v_mfma_f32_16x16x32_f16 v[64:67], v[200:203], v[172:175], v[64:67]
	v_mfma_f32_16x16x32_f16 v[68:71], v[204:207], v[172:175], v[68:71]
	v_mfma_f32_16x16x32_f16 v[72:75], v[192:195], v[176:179], v[72:75]
	v_mfma_f32_16x16x32_f16 v[76:79], v[196:199], v[176:179], v[76:79]
	s_add_u32 m0, s28, 0x2000
	v_mfma_f32_16x16x32_f16 v[80:83], v[200:203], v[176:179], v[80:83]
	global_load_lds_dwordx4 v11, s[4:5]
	v_mfma_f32_16x16x32_f16 v[84:87], v[204:207], v[176:179], v[84:87]
	v_mfma_f32_16x16x32_f16 v[88:91], v[192:195], v[180:183], v[88:91]
	v_mfma_f32_16x16x32_f16 v[92:95], v[196:199], v[180:183], v[92:95]
	v_mfma_f32_16x16x32_f16 v[96:99], v[200:203], v[180:183], v[96:99]
	s_add_u32 m0, s28, 0x4000
	v_mfma_f32_16x16x32_f16 v[100:103], v[204:207], v[180:183], v[100:103]
	global_load_lds_dwordx4 v12, s[4:5]
	v_mfma_f32_16x16x32_f16 v[104:107], v[192:195], v[184:187], v[104:107]
	v_mfma_f32_16x16x32_f16 v[108:111], v[196:199], v[184:187], v[108:111]
	v_mfma_f32_16x16x32_f16 v[112:115], v[200:203], v[184:187], v[112:115]
	v_mfma_f32_16x16x32_f16 v[116:119], v[204:207], v[184:187], v[116:119]
	s_waitcnt lgkmcnt(7)
	ds_read_b128 v[172:175], v16 offset:49152
	ds_read_b128 v[192:195], v18 offset:49152
	ds_read_b128 v[196:199], v18 offset:51200
	ds_read_b128 v[200:203], v18 offset:53248
	ds_read_b128 v[204:207], v18 offset:55296
	ds_read_b128 v[176:179], v16 offset:51200
	ds_read_b128 v[180:183], v16 offset:53248
	ds_read_b128 v[184:187], v16 offset:55296
	s_waitcnt lgkmcnt(8)
	v_mfma_f32_16x16x32_f16 v[56:59], v[156:159], v[136:139], v[56:59]
	s_add_u32 m0, s28, 0x6000
	v_mfma_f32_16x16x32_f16 v[60:63], v[160:163], v[136:139], v[60:63]
	global_load_lds_dwordx4 v13, s[4:5]
	s_add_u32 s4, s4, s20
	s_addc_u32 s5, s5, 0
	v_mfma_f32_16x16x32_f16 v[64:67], v[164:167], v[136:139], v[64:67]
	v_mfma_f32_16x16x32_f16 v[68:71], v[168:171], v[136:139], v[68:71]
	v_mfma_f32_16x16x32_f16 v[72:75], v[156:159], v[140:143], v[72:75]
	v_mfma_f32_16x16x32_f16 v[76:79], v[160:163], v[140:143], v[76:79]
	s_add_u32 m0, s28, 0x8000
	v_mfma_f32_16x16x32_f16 v[80:83], v[164:167], v[140:143], v[80:83]
	global_load_lds_dwordx4 v10, s[6:7]
	v_mfma_f32_16x16x32_f16 v[84:87], v[168:171], v[140:143], v[84:87]
	v_mfma_f32_16x16x32_f16 v[88:91], v[156:159], v[144:147], v[88:91]
	v_mfma_f32_16x16x32_f16 v[92:95], v[160:163], v[144:147], v[92:95]
	v_mfma_f32_16x16x32_f16 v[96:99], v[164:167], v[144:147], v[96:99]
	s_add_u32 m0, s28, 0xa000
	v_mfma_f32_16x16x32_f16 v[100:103], v[168:171], v[144:147], v[100:103]
	global_load_lds_dwordx4 v11, s[6:7]
	s_add_u32 s6, s6, s20
	s_addc_u32 s7, s7, 0
	v_mfma_f32_16x16x32_f16 v[104:107], v[156:159], v[148:151], v[104:107]
	v_mfma_f32_16x16x32_f16 v[108:111], v[160:163], v[148:151], v[108:111]
	v_mfma_f32_16x16x32_f16 v[112:115], v[164:167], v[148:151], v[112:115]
	v_mfma_f32_16x16x32_f16 v[116:119], v[168:171], v[148:151], v[116:119]
	s_waitcnt vmcnt(6) lgkmcnt(0)
	s_barrier
	s_waitcnt lgkmcnt(7)
	ds_read_b128 v[136:139], v19
	ds_read_b128 v[156:159], v21
	ds_read_b128 v[160:163], v21 offset:2048
	ds_read_b128 v[164:167], v21 offset:4096
	ds_read_b128 v[168:171], v21 offset:6144
	ds_read_b128 v[140:143], v19 offset:2048
	ds_read_b128 v[144:147], v19 offset:4096
	ds_read_b128 v[148:151], v19 offset:6144
	s_waitcnt lgkmcnt(8)
	v_mfma_f32_16x16x32_f16 v[56:59], v[192:195], v[172:175], v[56:59]
	s_add_u32 m0, s28, 0xc000
	v_mfma_f32_16x16x32_f16 v[60:63], v[196:199], v[172:175], v[60:63]
	global_load_lds_dwordx4 v10, s[4:5]
	v_mfma_f32_16x16x32_f16 v[64:67], v[200:203], v[172:175], v[64:67]
	v_mfma_f32_16x16x32_f16 v[68:71], v[204:207], v[172:175], v[68:71]
	v_mfma_f32_16x16x32_f16 v[72:75], v[192:195], v[176:179], v[72:75]
	v_mfma_f32_16x16x32_f16 v[76:79], v[196:199], v[176:179], v[76:79]
	s_add_u32 m0, s28, 0xe000
	v_mfma_f32_16x16x32_f16 v[80:83], v[200:203], v[176:179], v[80:83]
	global_load_lds_dwordx4 v11, s[4:5]
	v_mfma_f32_16x16x32_f16 v[84:87], v[204:207], v[176:179], v[84:87]
	v_mfma_f32_16x16x32_f16 v[88:91], v[192:195], v[180:183], v[88:91]
	v_mfma_f32_16x16x32_f16 v[92:95], v[196:199], v[180:183], v[92:95]
	v_mfma_f32_16x16x32_f16 v[96:99], v[200:203], v[180:183], v[96:99]
	s_add_u32 m0, s28, 0x10000
	v_mfma_f32_16x16x32_f16 v[100:103], v[204:207], v[180:183], v[100:103]
	global_load_lds_dwordx4 v12, s[4:5]
	v_mfma_f32_16x16x32_f16 v[104:107], v[192:195], v[184:187], v[104:107]
	v_mfma_f32_16x16x32_f16 v[108:111], v[196:199], v[184:187], v[108:111]
	v_mfma_f32_16x16x32_f16 v[112:115], v[200:203], v[184:187], v[112:115]
	v_mfma_f32_16x16x32_f16 v[116:119], v[204:207], v[184:187], v[116:119]
	s_waitcnt lgkmcnt(7)
	ds_read_b128 v[172:175], v20
	ds_read_b128 v[192:195], v22
	ds_read_b128 v[196:199], v22 offset:2048
	ds_read_b128 v[200:203], v22 offset:4096
	ds_read_b128 v[204:207], v22 offset:6144
	ds_read_b128 v[176:179], v20 offset:2048
	ds_read_b128 v[180:183], v20 offset:4096
	ds_read_b128 v[184:187], v20 offset:6144
	s_waitcnt lgkmcnt(8)
	v_mfma_f32_16x16x32_f16 v[56:59], v[156:159], v[136:139], v[56:59]
	s_add_u32 m0, s28, 0x12000
	v_mfma_f32_16x16x32_f16 v[60:63], v[160:163], v[136:139], v[60:63]
	global_load_lds_dwordx4 v13, s[4:5]
	s_add_u32 s4, s4, s20
	s_addc_u32 s5, s5, 0
	v_mfma_f32_16x16x32_f16 v[64:67], v[164:167], v[136:139], v[64:67]
	v_mfma_f32_16x16x32_f16 v[68:71], v[168:171], v[136:139], v[68:71]
	v_mfma_f32_16x16x32_f16 v[72:75], v[156:159], v[140:143], v[72:75]
	v_mfma_f32_16x16x32_f16 v[76:79], v[160:163], v[140:143], v[76:79]
	s_add_u32 m0, s28, 0x14000
	v_mfma_f32_16x16x32_f16 v[80:83], v[164:167], v[140:143], v[80:83]
	global_load_lds_dwordx4 v10, s[6:7]
	v_mfma_f32_16x16x32_f16 v[84:87], v[168:171], v[140:143], v[84:87]
	v_mfma_f32_16x16x32_f16 v[88:91], v[156:159], v[144:147], v[88:91]
	v_mfma_f32_16x16x32_f16 v[92:95], v[160:163], v[144:147], v[92:95]
	v_mfma_f32_16x16x32_f16 v[96:99], v[164:167], v[144:147], v[96:99]
	s_add_u32 m0, s28, 0x16000
	v_mfma_f32_16x16x32_f16 v[100:103], v[168:171], v[144:147], v[100:103]
	global_load_lds_dwordx4 v11, s[6:7]
	s_add_u32 s6, s6, s20
	s_addc_u32 s7, s7, 0
	v_mfma_f32_16x16x32_f16 v[104:107], v[156:159], v[148:151], v[104:107]
	v_mfma_f32_16x16x32_f16 v[108:111], v[160:163], v[148:151], v[108:111]
	v_mfma_f32_16x16x32_f16 v[112:115], v[164:167], v[148:151], v[112:115]
	v_mfma_f32_16x16x32_f16 v[116:119], v[168:171], v[148:151], v[116:119]
	s_waitcnt vmcnt(6) lgkmcnt(0)
	s_barrier
	s_waitcnt lgkmcnt(7)
	ds_read_b128 v[136:139], v15
	ds_read_b128 v[156:159], v17
	ds_read_b128 v[160:163], v17 offset:2048
	ds_read_b128 v[164:167], v17 offset:4096
	ds_read_b128 v[168:171], v17 offset:6144
	ds_read_b128 v[140:143], v15 offset:2048
	ds_read_b128 v[144:147], v15 offset:4096
	ds_read_b128 v[148:151], v15 offset:6144
	s_waitcnt lgkmcnt(8)
	v_mfma_f32_16x16x32_f16 v[56:59], v[192:195], v[172:175], v[56:59]
	s_add_u32 m0, s28, 0x18000
	v_mfma_f32_16x16x32_f16 v[60:63], v[196:199], v[172:175], v[60:63]
	global_load_lds_dwordx4 v10, s[4:5]
	v_mfma_f32_16x16x32_f16 v[64:67], v[200:203], v[172:175], v[64:67]
	v_mfma_f32_16x16x32_f16 v[68:71], v[204:207], v[172:175], v[68:71]
	v_mfma_f32_16x16x32_f16 v[72:75], v[192:195], v[176:179], v[72:75]
	v_mfma_f32_16x16x32_f16 v[76:79], v[196:199], v[176:179], v[76:79]
	s_add_u32 m0, s28, 0x1a000
	v_mfma_f32_16x16x32_f16 v[80:83], v[200:203], v[176:179], v[80:83]
	global_load_lds_dwordx4 v11, s[4:5]
	v_mfma_f32_16x16x32_f16 v[84:87], v[204:207], v[176:179], v[84:87]
	v_mfma_f32_16x16x32_f16 v[88:91], v[192:195], v[180:183], v[88:91]
	v_mfma_f32_16x16x32_f16 v[92:95], v[196:199], v[180:183], v[92:95]
	v_mfma_f32_16x16x32_f16 v[96:99], v[200:203], v[180:183], v[96:99]
	s_add_u32 m0, s28, 0x1c000
	v_mfma_f32_16x16x32_f16 v[100:103], v[204:207], v[180:183], v[100:103]
	global_load_lds_dwordx4 v12, s[4:5]
	v_mfma_f32_16x16x32_f16 v[104:107], v[192:195], v[184:187], v[104:107]
	v_mfma_f32_16x16x32_f16 v[108:111], v[196:199], v[184:187], v[108:111]
	v_mfma_f32_16x16x32_f16 v[112:115], v[200:203], v[184:187], v[112:115]
	v_mfma_f32_16x16x32_f16 v[116:119], v[204:207], v[184:187], v[116:119]
	s_waitcnt lgkmcnt(7)
	ds_read_b128 v[172:175], v16
	ds_read_b128 v[192:195], v18
	ds_read_b128 v[196:199], v18 offset:2048
	ds_read_b128 v[200:203], v18 offset:4096
	ds_read_b128 v[204:207], v18 offset:6144
	ds_read_b128 v[176:179], v16 offset:2048
	ds_read_b128 v[180:183], v16 offset:4096
	ds_read_b128 v[184:187], v16 offset:6144
	s_waitcnt lgkmcnt(8)
	v_mfma_f32_16x16x32_f16 v[56:59], v[156:159], v[136:139], v[56:59]
	s_add_u32 m0, s28, 0x1e000
	v_mfma_f32_16x16x32_f16 v[60:63], v[160:163], v[136:139], v[60:63]
	global_load_lds_dwordx4 v13, s[4:5]
	s_add_u32 s4, s4, s20
	s_addc_u32 s5, s5, 0
	v_mfma_f32_16x16x32_f16 v[64:67], v[164:167], v[136:139], v[64:67]
	v_mfma_f32_16x16x32_f16 v[68:71], v[168:171], v[136:139], v[68:71]
	v_mfma_f32_16x16x32_f16 v[72:75], v[156:159], v[140:143], v[72:75]
	v_mfma_f32_16x16x32_f16 v[76:79], v[160:163], v[140:143], v[76:79]
	s_add_u32 m0, s28, 0x20000
	v_mfma_f32_16x16x32_f16 v[80:83], v[164:167], v[140:143], v[80:83]
	global_load_lds_dwordx4 v10, s[6:7]
	v_mfma_f32_16x16x32_f16 v[84:87], v[168:171], v[140:143], v[84:87]
	v_mfma_f32_16x16x32_f16 v[88:91], v[156:159], v[144:147], v[88:91]
	v_mfma_f32_16x16x32_f16 v[92:95], v[160:163], v[144:147], v[92:95]
	v_mfma_f32_16x16x32_f16 v[96:99], v[164:167], v[144:147], v[96:99]
	s_add_u32 m0, s28, 0x22000
	v_mfma_f32_16x16x32_f16 v[100:103], v[168:171], v[144:147], v[100:103]
	global_load_lds_dwordx4 v11, s[6:7]
	s_add_u32 s6, s6, s20
	s_addc_u32 s7, s7, 0
	v_mfma_f32_16x16x32_f16 v[104:107], v[156:159], v[148:151], v[104:107]
	v_mfma_f32_16x16x32_f16 v[108:111], v[160:163], v[148:151], v[108:111]
	v_mfma_f32_16x16x32_f16 v[112:115], v[164:167], v[148:151], v[112:115]
	v_mfma_f32_16x16x32_f16 v[116:119], v[168:171], v[148:151], v[116:119]
	s_waitcnt vmcnt(6) lgkmcnt(0)
	s_barrier
	s_waitcnt lgkmcnt(7)
	ds_read_b128 v[136:139], v15 offset:49152
	ds_read_b128 v[156:159], v17 offset:49152
	ds_read_b128 v[160:163], v17 offset:51200
	ds_read_b128 v[164:167], v17 offset:53248
	ds_read_b128 v[168:171], v17 offset:55296
	ds_read_b128 v[140:143], v15 offset:51200
	ds_read_b128 v[144:147], v15 offset:53248
	ds_read_b128 v[148:151], v15 offset:55296
	s_waitcnt lgkmcnt(8)
	v_mfma_f32_16x16x32_f16 v[56:59], v[192:195], v[172:175], v[56:59]
	s_add_u32 m0, s28, 0x0
	v_mfma_f32_16x16x32_f16 v[60:63], v[196:199], v[172:175], v[60:63]
	global_load_lds_dwordx4 v10, s[4:5]
	v_mfma_f32_16x16x32_f16 v[64:67], v[200:203], v[172:175], v[64:67]
	v_mfma_f32_16x16x32_f16 v[68:71], v[204:207], v[172:175], v[68:71]
	v_mfma_f32_16x16x32_f16 v[72:75], v[192:195], v[176:179], v[72:75]
	v_mfma_f32_16x16x32_f16 v[76:79], v[196:199], v[176:179], v[76:79]
	s_add_u32 m0, s28, 0x2000
	v_mfma_f32_16x16x32_f16 v[80:83], v[200:203], v[176:179], v[80:83]
	global_load_lds_dwordx4 v11, s[4:5]
	v_mfma_f32_16x16x32_f16 v[84:87], v[204:207], v[176:179], v[84:87]
	v_mfma_f32_16x16x32_f16 v[88:91], v[192:195], v[180:183], v[88:91]
	v_mfma_f32_16x16x32_f16 v[92:95], v[196:199], v[180:183], v[92:95]
	v_mfma_f32_16x16x32_f16 v[96:99], v[200:203], v[180:183], v[96:99]
	s_add_u32 m0, s28, 0x4000
	v_mfma_f32_16x16x32_f16 v[100:103], v[204:207], v[180:183], v[100:103]
	global_load_lds_dwordx4 v12, s[4:5]
	v_mfma_f32_16x16x32_f16 v[104:107], v[192:195], v[184:187], v[104:107]
	v_mfma_f32_16x16x32_f16 v[108:111], v[196:199], v[184:187], v[108:111]
	v_mfma_f32_16x16x32_f16 v[112:115], v[200:203], v[184:187], v[112:115]
	v_mfma_f32_16x16x32_f16 v[116:119], v[204:207], v[184:187], v[116:119]
	s_waitcnt lgkmcnt(7)
	ds_read_b128 v[172:175], v16 offset:49152
	ds_read_b128 v[192:195], v18 offset:49152
	ds_read_b128 v[196:199], v18 offset:51200
	ds_read_b128 v[200:203], v18 offset:53248
	ds_read_b128 v[204:207], v18 offset:55296
	ds_read_b128 v[176:179], v16 offset:51200
	ds_read_b128 v[180:183], v16 offset:53248
	ds_read_b128 v[184:187], v16 offset:55296
	s_waitcnt lgkmcnt(8)
	v_mfma_f32_16x16x32_f16 v[56:59], v[156:159], v[136:139], v[56:59]
	s_add_u32 m0, s28, 0x6000
	v_mfma_f32_16x16x32_f16 v[60:63], v[160:163], v[136:139], v[60:63]
	global_load_lds_dwordx4 v13, s[4:5]
	s_add_u32 s4, s4, s20
	s_addc_u32 s5, s5, 0
	v_mfma_f32_16x16x32_f16 v[64:67], v[164:167], v[136:139], v[64:67]
	v_mfma_f32_16x16x32_f16 v[68:71], v[168:171], v[136:139], v[68:71]
	v_mfma_f32_16x16x32_f16 v[72:75], v[156:159], v[140:143], v[72:75]
	v_mfma_f32_16x16x32_f16 v[76:79], v[160:163], v[140:143], v[76:79]
	s_add_u32 m0, s28, 0x8000
	v_mfma_f32_16x16x32_f16 v[80:83], v[164:167], v[140:143], v[80:83]
	global_load_lds_dwordx4 v10, s[6:7]
	v_mfma_f32_16x16x32_f16 v[84:87], v[168:171], v[140:143], v[84:87]
	v_mfma_f32_16x16x32_f16 v[88:91], v[156:159], v[144:147], v[88:91]
	v_mfma_f32_16x16x32_f16 v[92:95], v[160:163], v[144:147], v[92:95]
	v_mfma_f32_16x16x32_f16 v[96:99], v[164:167], v[144:147], v[96:99]
	s_add_u32 m0, s28, 0xa000
	v_mfma_f32_16x16x32_f16 v[100:103], v[168:171], v[144:147], v[100:103]
	global_load_lds_dwordx4 v11, s[6:7]
	s_add_u32 s6, s6, s20
	s_addc_u32 s7, s7, 0
	v_mfma_f32_16x16x32_f16 v[104:107], v[156:159], v[148:151], v[104:107]
	v_mfma_f32_16x16x32_f16 v[108:111], v[160:163], v[148:151], v[108:111]
	v_mfma_f32_16x16x32_f16 v[112:115], v[164:167], v[148:151], v[112:115]
	v_mfma_f32_16x16x32_f16 v[116:119], v[168:171], v[148:151], v[116:119]
	s_waitcnt vmcnt(6) lgkmcnt(0)
	s_barrier
	s_waitcnt lgkmcnt(7)
	ds_read_b128 v[136:139], v19
	ds_read_b128 v[156:159], v21
	ds_read_b128 v[160:163], v21 offset:2048
	ds_read_b128 v[164:167], v21 offset:4096
	ds_read_b128 v[168:171], v21 offset:6144
	ds_read_b128 v[140:143], v19 offset:2048
	ds_read_b128 v[144:147], v19 offset:4096
	ds_read_b128 v[148:151], v19 offset:6144
	s_waitcnt lgkmcnt(8)
	v_mfma_f32_16x16x32_f16 v[56:59], v[192:195], v[172:175], v[56:59]
	s_add_u32 m0, s28, 0xc000
	v_mfma_f32_16x16x32_f16 v[60:63], v[196:199], v[172:175], v[60:63]
	global_load_lds_dwordx4 v10, s[4:5]
	v_mfma_f32_16x16x32_f16 v[64:67], v[200:203], v[172:175], v[64:67]
	v_mfma_f32_16x16x32_f16 v[68:71], v[204:207], v[172:175], v[68:71]
	v_mfma_f32_16x16x32_f16 v[72:75], v[192:195], v[176:179], v[72:75]
	v_mfma_f32_16x16x32_f16 v[76:79], v[196:199], v[176:179], v[76:79]
	s_add_u32 m0, s28, 0xe000
	v_mfma_f32_16x16x32_f16 v[80:83], v[200:203], v[176:179], v[80:83]
	global_load_lds_dwordx4 v11, s[4:5]
	v_mfma_f32_16x16x32_f16 v[84:87], v[204:207], v[176:179], v[84:87]
	v_mfma_f32_16x16x32_f16 v[88:91], v[192:195], v[180:183], v[88:91]
	v_mfma_f32_16x16x32_f16 v[92:95], v[196:199], v[180:183], v[92:95]
	v_mfma_f32_16x16x32_f16 v[96:99], v[200:203], v[180:183], v[96:99]
	s_add_u32 m0, s28, 0x10000
	v_mfma_f32_16x16x32_f16 v[100:103], v[204:207], v[180:183], v[100:103]
	global_load_lds_dwordx4 v12, s[4:5]
	v_mfma_f32_16x16x32_f16 v[104:107], v[192:195], v[184:187], v[104:107]
	v_mfma_f32_16x16x32_f16 v[108:111], v[196:199], v[184:187], v[108:111]
	v_mfma_f32_16x16x32_f16 v[112:115], v[200:203], v[184:187], v[112:115]
	v_mfma_f32_16x16x32_f16 v[116:119], v[204:207], v[184:187], v[116:119]
	s_waitcnt lgkmcnt(7)
	ds_read_b128 v[172:175], v20
	ds_read_b128 v[192:195], v22
	ds_read_b128 v[196:199], v22 offset:2048
	ds_read_b128 v[200:203], v22 offset:4096
	ds_read_b128 v[204:207], v22 offset:6144
	ds_read_b128 v[176:179], v20 offset:2048
	ds_read_b128 v[180:183], v20 offset:4096
	ds_read_b128 v[184:187], v20 offset:6144
	s_waitcnt lgkmcnt(8)
	v_mfma_f32_16x16x32_f16 v[56:59], v[156:159], v[136:139], v[56:59]
	s_add_u32 m0, s28, 0x12000
	v_mfma_f32_16x16x32_f16 v[60:63], v[160:163], v[136:139], v[60:63]
	global_load_lds_dwordx4 v13, s[4:5]
	s_add_u32 s4, s4, s20
	s_addc_u32 s5, s5, 0
	v_mfma_f32_16x16x32_f16 v[64:67], v[164:167], v[136:139], v[64:67]
	v_mfma_f32_16x16x32_f16 v[68:71], v[168:171], v[136:139], v[68:71]
	v_mfma_f32_16x16x32_f16 v[72:75], v[156:159], v[140:143], v[72:75]
	v_mfma_f32_16x16x32_f16 v[76:79], v[160:163], v[140:143], v[76:79]
	s_add_u32 m0, s28, 0x14000
	v_mfma_f32_16x16x32_f16 v[80:83], v[164:167], v[140:143], v[80:83]
	global_load_lds_dwordx4 v10, s[6:7]
	v_mfma_f32_16x16x32_f16 v[84:87], v[168:171], v[140:143], v[84:87]
	v_mfma_f32_16x16x32_f16 v[88:91], v[156:159], v[144:147], v[88:91]
	v_mfma_f32_16x16x32_f16 v[92:95], v[160:163], v[144:147], v[92:95]
	v_mfma_f32_16x16x32_f16 v[96:99], v[164:167], v[144:147], v[96:99]
	s_add_u32 m0, s28, 0x16000
	v_mfma_f32_16x16x32_f16 v[100:103], v[168:171], v[144:147], v[100:103]
	global_load_lds_dwordx4 v11, s[6:7]
	s_add_u32 s6, s6, s20
	s_addc_u32 s7, s7, 0
	v_mfma_f32_16x16x32_f16 v[104:107], v[156:159], v[148:151], v[104:107]
	v_mfma_f32_16x16x32_f16 v[108:111], v[160:163], v[148:151], v[108:111]
	v_mfma_f32_16x16x32_f16 v[112:115], v[164:167], v[148:151], v[112:115]
	v_mfma_f32_16x16x32_f16 v[116:119], v[168:171], v[148:151], v[116:119]
	s_waitcnt vmcnt(6) lgkmcnt(0)
	s_barrier
	s_waitcnt lgkmcnt(7)
	ds_read_b128 v[136:139], v15
	ds_read_b128 v[156:159], v17
	ds_read_b128 v[160:163], v17 offset:2048
	ds_read_b128 v[164:167], v17 offset:4096
	ds_read_b128 v[168:171], v17 offset:6144
	ds_read_b128 v[140:143], v15 offset:2048
	ds_read_b128 v[144:147], v15 offset:4096
	ds_read_b128 v[148:151], v15 offset:6144
	s_waitcnt lgkmcnt(8)
	v_mfma_f32_16x16x32_f16 v[56:59], v[192:195], v[172:175], v[56:59]
	s_add_u32 m0, s28, 0x18000
	v_mfma_f32_16x16x32_f16 v[60:63], v[196:199], v[172:175], v[60:63]
	global_load_lds_dwordx4 v10, s[4:5]
	v_mfma_f32_16x16x32_f16 v[64:67], v[200:203], v[172:175], v[64:67]
	v_mfma_f32_16x16x32_f16 v[68:71], v[204:207], v[172:175], v[68:71]
	v_mfma_f32_16x16x32_f16 v[72:75], v[192:195], v[176:179], v[72:75]
	v_mfma_f32_16x16x32_f16 v[76:79], v[196:199], v[176:179], v[76:79]
	s_add_u32 m0, s28, 0x1a000
	v_mfma_f32_16x16x32_f16 v[80:83], v[200:203], v[176:179], v[80:83]
	global_load_lds_dwordx4 v11, s[4:5]
	v_mfma_f32_16x16x32_f16 v[84:87], v[204:207], v[176:179], v[84:87]
	v_mfma_f32_16x16x32_f16 v[88:91], v[192:195], v[180:183], v[88:91]
	v_mfma_f32_16x16x32_f16 v[92:95], v[196:199], v[180:183], v[92:95]
	v_mfma_f32_16x16x32_f16 v[96:99], v[200:203], v[180:183], v[96:99]
	s_add_u32 m0, s28, 0x1c000
	v_mfma_f32_16x16x32_f16 v[100:103], v[204:207], v[180:183], v[100:103]
	global_load_lds_dwordx4 v12, s[4:5]
	v_mfma_f32_16x16x32_f16 v[104:107], v[192:195], v[184:187], v[104:107]
	v_mfma_f32_16x16x32_f16 v[108:111], v[196:199], v[184:187], v[108:111]
	v_mfma_f32_16x16x32_f16 v[112:115], v[200:203], v[184:187], v[112:115]
	v_mfma_f32_16x16x32_f16 v[116:119], v[204:207], v[184:187], v[116:119]
	s_waitcnt lgkmcnt(7)
	ds_read_b128 v[172:175], v16
	ds_read_b128 v[192:195], v18
	ds_read_b128 v[196:199], v18 offset:2048
	ds_read_b128 v[200:203], v18 offset:4096
	ds_read_b128 v[204:207], v18 offset:6144
	ds_read_b128 v[176:179], v16 offset:2048
	ds_read_b128 v[180:183], v16 offset:4096
	ds_read_b128 v[184:187], v16 offset:6144
	s_waitcnt lgkmcnt(8)
	v_mfma_f32_16x16x32_f16 v[56:59], v[156:159], v[136:139], v[56:59]
	s_add_u32 m0, s28, 0x1e000
	v_mfma_f32_16x16x32_f16 v[60:63], v[160:163], v[136:139], v[60:63]
	global_load_lds_dwordx4 v13, s[4:5]
	s_add_u32 s4, s4, s20
	s_addc_u32 s5, s5, 0
	v_mfma_f32_16x16x32_f16 v[64:67], v[164:167], v[136:139], v[64:67]
	v_mfma_f32_16x16x32_f16 v[68:71], v[168:171], v[136:139], v[68:71]
	v_mfma_f32_16x16x32_f16 v[72:75], v[156:159], v[140:143], v[72:75]
	v_mfma_f32_16x16x32_f16 v[76:79], v[160:163], v[140:143], v[76:79]
	s_add_u32 m0, s28, 0x20000
	v_mfma_f32_16x16x32_f16 v[80:83], v[164:167], v[140:143], v[80:83]
	global_load_lds_dwordx4 v10, s[6:7]
	v_mfma_f32_16x16x32_f16 v[84:87], v[168:171], v[140:143], v[84:87]
	v_mfma_f32_16x16x32_f16 v[88:91], v[156:159], v[144:147], v[88:91]
	v_mfma_f32_16x16x32_f16 v[92:95], v[160:163], v[144:147], v[92:95]
	v_mfma_f32_16x16x32_f16 v[96:99], v[164:167], v[144:147], v[96:99]
	s_add_u32 m0, s28, 0x22000
	v_mfma_f32_16x16x32_f16 v[100:103], v[168:171], v[144:147], v[100:103]
	global_load_lds_dwordx4 v11, s[6:7]
	s_add_u32 s6, s6, s20
	s_addc_u32 s7, s7, 0
	v_mfma_f32_16x16x32_f16 v[104:107], v[156:159], v[148:151], v[104:107]
	v_mfma_f32_16x16x32_f16 v[108:111], v[160:163], v[148:151], v[108:111]
	v_mfma_f32_16x16x32_f16 v[112:115], v[164:167], v[148:151], v[112:115]
	v_mfma_f32_16x16x32_f16 v[116:119], v[168:171], v[148:151], v[116:119]
	s_waitcnt vmcnt(6) lgkmcnt(0)
	s_barrier
	s_waitcnt lgkmcnt(7)
	ds_read_b128 v[136:139], v15 offset:49152
	ds_read_b128 v[156:159], v17 offset:49152
	ds_read_b128 v[160:163], v17 offset:51200
	ds_read_b128 v[164:167], v17 offset:53248
	ds_read_b128 v[168:171], v17 offset:55296
	ds_read_b128 v[140:143], v15 offset:51200
	ds_read_b128 v[144:147], v15 offset:53248
	ds_read_b128 v[148:151], v15 offset:55296
	s_waitcnt lgkmcnt(8)
	v_mfma_f32_16x16x32_f16 v[56:59], v[192:195], v[172:175], v[56:59]
	s_add_u32 m0, s28, 0x0
	v_mfma_f32_16x16x32_f16 v[60:63], v[196:199], v[172:175], v[60:63]
	global_load_lds_dwordx4 v10, s[4:5]
	v_mfma_f32_16x16x32_f16 v[64:67], v[200:203], v[172:175], v[64:67]
	v_mfma_f32_16x16x32_f16 v[68:71], v[204:207], v[172:175], v[68:71]
	v_mfma_f32_16x16x32_f16 v[72:75], v[192:195], v[176:179], v[72:75]
	v_mfma_f32_16x16x32_f16 v[76:79], v[196:199], v[176:179], v[76:79]
	s_add_u32 m0, s28, 0x2000
	v_mfma_f32_16x16x32_f16 v[80:83], v[200:203], v[176:179], v[80:83]
	global_load_lds_dwordx4 v11, s[4:5]
	v_mfma_f32_16x16x32_f16 v[84:87], v[204:207], v[176:179], v[84:87]
	v_mfma_f32_16x16x32_f16 v[88:91], v[192:195], v[180:183], v[88:91]
	v_mfma_f32_16x16x32_f16 v[92:95], v[196:199], v[180:183], v[92:95]
	v_mfma_f32_16x16x32_f16 v[96:99], v[200:203], v[180:183], v[96:99]
	s_add_u32 m0, s28, 0x4000
	v_mfma_f32_16x16x32_f16 v[100:103], v[204:207], v[180:183], v[100:103]
	global_load_lds_dwordx4 v12, s[4:5]
	v_mfma_f32_16x16x32_f16 v[104:107], v[192:195], v[184:187], v[104:107]
	v_mfma_f32_16x16x32_f16 v[108:111], v[196:199], v[184:187], v[108:111]
	v_mfma_f32_16x16x32_f16 v[112:115], v[200:203], v[184:187], v[112:115]
	v_mfma_f32_16x16x32_f16 v[116:119], v[204:207], v[184:187], v[116:119]
	s_waitcnt lgkmcnt(7)
	ds_read_b128 v[172:175], v16 offset:49152
	ds_read_b128 v[192:195], v18 offset:49152
	ds_read_b128 v[196:199], v18 offset:51200
	ds_read_b128 v[200:203], v18 offset:53248
	ds_read_b128 v[204:207], v18 offset:55296
	ds_read_b128 v[176:179], v16 offset:51200
	ds_read_b128 v[180:183], v16 offset:53248
	ds_read_b128 v[184:187], v16 offset:55296
	s_waitcnt lgkmcnt(8)
	v_mfma_f32_16x16x32_f16 v[56:59], v[156:159], v[136:139], v[56:59]
	s_add_u32 m0, s28, 0x6000
	v_mfma_f32_16x16x32_f16 v[60:63], v[160:163], v[136:139], v[60:63]
	global_load_lds_dwordx4 v13, s[4:5]
	s_add_u32 s4, s4, s20
	s_addc_u32 s5, s5, 0
	v_mfma_f32_16x16x32_f16 v[64:67], v[164:167], v[136:139], v[64:67]
	v_mfma_f32_16x16x32_f16 v[68:71], v[168:171], v[136:139], v[68:71]
	v_mfma_f32_16x16x32_f16 v[72:75], v[156:159], v[140:143], v[72:75]
	v_mfma_f32_16x16x32_f16 v[76:79], v[160:163], v[140:143], v[76:79]
	s_add_u32 m0, s28, 0x8000
	v_mfma_f32_16x16x32_f16 v[80:83], v[164:167], v[140:143], v[80:83]
	global_load_lds_dwordx4 v10, s[6:7]
	v_mfma_f32_16x16x32_f16 v[84:87], v[168:171], v[140:143], v[84:87]
	v_mfma_f32_16x16x32_f16 v[88:91], v[156:159], v[144:147], v[88:91]
	v_mfma_f32_16x16x32_f16 v[92:95], v[160:163], v[144:147], v[92:95]
	v_mfma_f32_16x16x32_f16 v[96:99], v[164:167], v[144:147], v[96:99]
	s_add_u32 m0, s28, 0xa000
	v_mfma_f32_16x16x32_f16 v[100:103], v[168:171], v[144:147], v[100:103]
	global_load_lds_dwordx4 v11, s[6:7]
	s_add_u32 s6, s6, s20
	s_addc_u32 s7, s7, 0
	v_mfma_f32_16x16x32_f16 v[104:107], v[156:159], v[148:151], v[104:107]
	v_mfma_f32_16x16x32_f16 v[108:111], v[160:163], v[148:151], v[108:111]
	v_mfma_f32_16x16x32_f16 v[112:115], v[164:167], v[148:151], v[112:115]
	v_mfma_f32_16x16x32_f16 v[116:119], v[168:171], v[148:151], v[116:119]
	s_waitcnt vmcnt(6) lgkmcnt(0)
	s_barrier
	s_waitcnt lgkmcnt(7)
	ds_read_b128 v[136:139], v19
	ds_read_b128 v[156:159], v21
	ds_read_b128 v[160:163], v21 offset:2048
	ds_read_b128 v[164:167], v21 offset:4096
	ds_read_b128 v[168:171], v21 offset:6144
	ds_read_b128 v[140:143], v19 offset:2048
	ds_read_b128 v[144:147], v19 offset:4096
	ds_read_b128 v[148:151], v19 offset:6144
	s_waitcnt lgkmcnt(8)
	v_mfma_f32_16x16x32_f16 v[56:59], v[192:195], v[172:175], v[56:59]
	s_add_u32 m0, s28, 0xc000
	v_mfma_f32_16x16x32_f16 v[60:63], v[196:199], v[172:175], v[60:63]
	global_load_lds_dwordx4 v10, s[4:5]
	v_mfma_f32_16x16x32_f16 v[64:67], v[200:203], v[172:175], v[64:67]
	v_mfma_f32_16x16x32_f16 v[68:71], v[204:207], v[172:175], v[68:71]
	v_mfma_f32_16x16x32_f16 v[72:75], v[192:195], v[176:179], v[72:75]
	v_mfma_f32_16x16x32_f16 v[76:79], v[196:199], v[176:179], v[76:79]
	s_add_u32 m0, s28, 0xe000
	v_mfma_f32_16x16x32_f16 v[80:83], v[200:203], v[176:179], v[80:83]
	global_load_lds_dwordx4 v11, s[4:5]
	v_mfma_f32_16x16x32_f16 v[84:87], v[204:207], v[176:179], v[84:87]
	v_mfma_f32_16x16x32_f16 v[88:91], v[192:195], v[180:183], v[88:91]
	v_mfma_f32_16x16x32_f16 v[92:95], v[196:199], v[180:183], v[92:95]
	v_mfma_f32_16x16x32_f16 v[96:99], v[200:203], v[180:183], v[96:99]
	s_add_u32 m0, s28, 0x10000
	v_mfma_f32_16x16x32_f16 v[100:103], v[204:207], v[180:183], v[100:103]
	global_load_lds_dwordx4 v12, s[4:5]
	v_mfma_f32_16x16x32_f16 v[104:107], v[192:195], v[184:187], v[104:107]
	v_mfma_f32_16x16x32_f16 v[108:111], v[196:199], v[184:187], v[108:111]
	v_mfma_f32_16x16x32_f16 v[112:115], v[200:203], v[184:187], v[112:115]
	v_mfma_f32_16x16x32_f16 v[116:119], v[204:207], v[184:187], v[116:119]
	s_waitcnt lgkmcnt(7)
	ds_read_b128 v[172:175], v20
	ds_read_b128 v[192:195], v22
	ds_read_b128 v[196:199], v22 offset:2048
	ds_read_b128 v[200:203], v22 offset:4096
	ds_read_b128 v[204:207], v22 offset:6144
	ds_read_b128 v[176:179], v20 offset:2048
	ds_read_b128 v[180:183], v20 offset:4096
	ds_read_b128 v[184:187], v20 offset:6144
	s_waitcnt lgkmcnt(8)
	v_mfma_f32_16x16x32_f16 v[56:59], v[156:159], v[136:139], v[56:59]
	s_add_u32 m0, s28, 0x12000
	v_mfma_f32_16x16x32_f16 v[60:63], v[160:163], v[136:139], v[60:63]
	global_load_lds_dwordx4 v13, s[4:5]
	s_add_u32 s4, s4, s20
	s_addc_u32 s5, s5, 0
	v_mfma_f32_16x16x32_f16 v[64:67], v[164:167], v[136:139], v[64:67]
	v_mfma_f32_16x16x32_f16 v[68:71], v[168:171], v[136:139], v[68:71]
	v_mfma_f32_16x16x32_f16 v[72:75], v[156:159], v[140:143], v[72:75]
	v_mfma_f32_16x16x32_f16 v[76:79], v[160:163], v[140:143], v[76:79]
	s_add_u32 m0, s28, 0x14000
	v_mfma_f32_16x16x32_f16 v[80:83], v[164:167], v[140:143], v[80:83]
	global_load_lds_dwordx4 v10, s[6:7]
	v_mfma_f32_16x16x32_f16 v[84:87], v[168:171], v[140:143], v[84:87]
	v_mfma_f32_16x16x32_f16 v[88:91], v[156:159], v[144:147], v[88:91]
	v_mfma_f32_16x16x32_f16 v[92:95], v[160:163], v[144:147], v[92:95]
	v_mfma_f32_16x16x32_f16 v[96:99], v[164:167], v[144:147], v[96:99]
	s_add_u32 m0, s28, 0x16000
	v_mfma_f32_16x16x32_f16 v[100:103], v[168:171], v[144:147], v[100:103]
	global_load_lds_dwordx4 v11, s[6:7]
	s_add_u32 s6, s6, s20
	s_addc_u32 s7, s7, 0
	v_mfma_f32_16x16x32_f16 v[104:107], v[156:159], v[148:151], v[104:107]
	v_mfma_f32_16x16x32_f16 v[108:111], v[160:163], v[148:151], v[108:111]
	v_mfma_f32_16x16x32_f16 v[112:115], v[164:167], v[148:151], v[112:115]
	v_mfma_f32_16x16x32_f16 v[116:119], v[168:171], v[148:151], v[116:119]
	s_waitcnt vmcnt(6) lgkmcnt(0)
	s_barrier
	s_waitcnt lgkmcnt(7)
	ds_read_b128 v[136:139], v15
	ds_read_b128 v[156:159], v17
	ds_read_b128 v[160:163], v17 offset:2048
	ds_read_b128 v[164:167], v17 offset:4096
	ds_read_b128 v[168:171], v17 offset:6144
	ds_read_b128 v[140:143], v15 offset:2048
	ds_read_b128 v[144:147], v15 offset:4096
	ds_read_b128 v[148:151], v15 offset:6144
	s_waitcnt lgkmcnt(8)
	v_mfma_f32_16x16x32_f16 v[56:59], v[192:195], v[172:175], v[56:59]
	s_add_u32 m0, s28, 0x18000
	v_mfma_f32_16x16x32_f16 v[60:63], v[196:199], v[172:175], v[60:63]
	global_load_lds_dwordx4 v10, s[4:5]
	v_mfma_f32_16x16x32_f16 v[64:67], v[200:203], v[172:175], v[64:67]
	v_mfma_f32_16x16x32_f16 v[68:71], v[204:207], v[172:175], v[68:71]
	v_mfma_f32_16x16x32_f16 v[72:75], v[192:195], v[176:179], v[72:75]
	v_mfma_f32_16x16x32_f16 v[76:79], v[196:199], v[176:179], v[76:79]
	s_add_u32 m0, s28, 0x1a000
	v_mfma_f32_16x16x32_f16 v[80:83], v[200:203], v[176:179], v[80:83]
	global_load_lds_dwordx4 v11, s[4:5]
	v_mfma_f32_16x16x32_f16 v[84:87], v[204:207], v[176:179], v[84:87]
	v_mfma_f32_16x16x32_f16 v[88:91], v[192:195], v[180:183], v[88:91]
	v_mfma_f32_16x16x32_f16 v[92:95], v[196:199], v[180:183], v[92:95]
	v_mfma_f32_16x16x32_f16 v[96:99], v[200:203], v[180:183], v[96:99]
	s_add_u32 m0, s28, 0x1c000
	v_mfma_f32_16x16x32_f16 v[100:103], v[204:207], v[180:183], v[100:103]
	global_load_lds_dwordx4 v12, s[4:5]
	v_mfma_f32_16x16x32_f16 v[104:107], v[192:195], v[184:187], v[104:107]
	v_mfma_f32_16x16x32_f16 v[108:111], v[196:199], v[184:187], v[108:111]
	v_mfma_f32_16x16x32_f16 v[112:115], v[200:203], v[184:187], v[112:115]
	v_mfma_f32_16x16x32_f16 v[116:119], v[204:207], v[184:187], v[116:119]
	s_waitcnt lgkmcnt(7)
	ds_read_b128 v[172:175], v16
	ds_read_b128 v[192:195], v18
	ds_read_b128 v[196:199], v18 offset:2048
	ds_read_b128 v[200:203], v18 offset:4096
	ds_read_b128 v[204:207], v18 offset:6144
	ds_read_b128 v[176:179], v16 offset:2048
	ds_read_b128 v[180:183], v16 offset:4096
	ds_read_b128 v[184:187], v16 offset:6144
	s_waitcnt lgkmcnt(8)
	v_mfma_f32_16x16x32_f16 v[56:59], v[156:159], v[136:139], v[56:59]
	s_add_u32 m0, s28, 0x1e000
	v_mfma_f32_16x16x32_f16 v[60:63], v[160:163], v[136:139], v[60:63]
	global_load_lds_dwordx4 v13, s[4:5]
	s_add_u32 s4, s4, s20
	s_addc_u32 s5, s5, 0
	v_mfma_f32_16x16x32_f16 v[64:67], v[164:167], v[136:139], v[64:67]
	v_mfma_f32_16x16x32_f16 v[68:71], v[168:171], v[136:139], v[68:71]
	v_mfma_f32_16x16x32_f16 v[72:75], v[156:159], v[140:143], v[72:75]
	v_mfma_f32_16x16x32_f16 v[76:79], v[160:163], v[140:143], v[76:79]
	s_add_u32 m0, s28, 0x20000
	v_mfma_f32_16x16x32_f16 v[80:83], v[164:167], v[140:143], v[80:83]
	global_load_lds_dwordx4 v10, s[6:7]
	v_mfma_f32_16x16x32_f16 v[84:87], v[168:171], v[140:143], v[84:87]
	v_mfma_f32_16x16x32_f16 v[88:91], v[156:159], v[144:147], v[88:91]
	v_mfma_f32_16x16x32_f16 v[92:95], v[160:163], v[144:147], v[92:95]
	v_mfma_f32_16x16x32_f16 v[96:99], v[164:167], v[144:147], v[96:99]
	s_add_u32 m0, s28, 0x22000
	v_mfma_f32_16x16x32_f16 v[100:103], v[168:171], v[144:147], v[100:103]
	global_load_lds_dwordx4 v11, s[6:7]
	s_add_u32 s6, s6, s20
	s_addc_u32 s7, s7, 0
	v_mfma_f32_16x16x32_f16 v[104:107], v[156:159], v[148:151], v[104:107]
	v_mfma_f32_16x16x32_f16 v[108:111], v[160:163], v[148:151], v[108:111]
	v_mfma_f32_16x16x32_f16 v[112:115], v[164:167], v[148:151], v[112:115]
	v_mfma_f32_16x16x32_f16 v[116:119], v[168:171], v[148:151], v[116:119]
	s_waitcnt vmcnt(6) lgkmcnt(0)
	s_barrier
	s_waitcnt lgkmcnt(7)
	ds_read_b128 v[136:139], v15 offset:49152
	ds_read_b128 v[156:159], v17 offset:49152
	ds_read_b128 v[160:163], v17 offset:51200
	ds_read_b128 v[164:167], v17 offset:53248
	ds_read_b128 v[168:171], v17 offset:55296
	ds_read_b128 v[140:143], v15 offset:51200
	ds_read_b128 v[144:147], v15 offset:53248
	ds_read_b128 v[148:151], v15 offset:55296
	s_waitcnt lgkmcnt(8)
	v_mfma_f32_16x16x32_f16 v[56:59], v[192:195], v[172:175], v[56:59]
	s_add_u32 m0, s28, 0x0
	v_mfma_f32_16x16x32_f16 v[60:63], v[196:199], v[172:175], v[60:63]
	global_load_lds_dwordx4 v10, s[4:5]
	v_mfma_f32_16x16x32_f16 v[64:67], v[200:203], v[172:175], v[64:67]
	v_mfma_f32_16x16x32_f16 v[68:71], v[204:207], v[172:175], v[68:71]
	v_mfma_f32_16x16x32_f16 v[72:75], v[192:195], v[176:179], v[72:75]
	v_mfma_f32_16x16x32_f16 v[76:79], v[196:199], v[176:179], v[76:79]
	s_add_u32 m0, s28, 0x2000
	v_mfma_f32_16x16x32_f16 v[80:83], v[200:203], v[176:179], v[80:83]
	global_load_lds_dwordx4 v11, s[4:5]
	v_mfma_f32_16x16x32_f16 v[84:87], v[204:207], v[176:179], v[84:87]
	v_mfma_f32_16x16x32_f16 v[88:91], v[192:195], v[180:183], v[88:91]
	v_mfma_f32_16x16x32_f16 v[92:95], v[196:199], v[180:183], v[92:95]
	v_mfma_f32_16x16x32_f16 v[96:99], v[200:203], v[180:183], v[96:99]
	s_add_u32 m0, s28, 0x4000
	v_mfma_f32_16x16x32_f16 v[100:103], v[204:207], v[180:183], v[100:103]
	global_load_lds_dwordx4 v12, s[4:5]
	v_mfma_f32_16x16x32_f16 v[104:107], v[192:195], v[184:187], v[104:107]
	v_mfma_f32_16x16x32_f16 v[108:111], v[196:199], v[184:187], v[108:111]
	v_mfma_f32_16x16x32_f16 v[112:115], v[200:203], v[184:187], v[112:115]
	v_mfma_f32_16x16x32_f16 v[116:119], v[204:207], v[184:187], v[116:119]
	s_waitcnt lgkmcnt(7)
	ds_read_b128 v[172:175], v16 offset:49152
	ds_read_b128 v[192:195], v18 offset:49152
	ds_read_b128 v[196:199], v18 offset:51200
	ds_read_b128 v[200:203], v18 offset:53248
	ds_read_b128 v[204:207], v18 offset:55296
	ds_read_b128 v[176:179], v16 offset:51200
	ds_read_b128 v[180:183], v16 offset:53248
	ds_read_b128 v[184:187], v16 offset:55296
	s_waitcnt lgkmcnt(8)
	v_mfma_f32_16x16x32_f16 v[56:59], v[156:159], v[136:139], v[56:59]
	s_add_u32 m0, s28, 0x6000
	v_mfma_f32_16x16x32_f16 v[60:63], v[160:163], v[136:139], v[60:63]
	global_load_lds_dwordx4 v13, s[4:5]
	s_add_u32 s4, s4, s20
	s_addc_u32 s5, s5, 0
	v_mfma_f32_16x16x32_f16 v[64:67], v[164:167], v[136:139], v[64:67]
	v_mfma_f32_16x16x32_f16 v[68:71], v[168:171], v[136:139], v[68:71]
	v_mfma_f32_16x16x32_f16 v[72:75], v[156:159], v[140:143], v[72:75]
	v_mfma_f32_16x16x32_f16 v[76:79], v[160:163], v[140:143], v[76:79]
	s_add_u32 m0, s28, 0x8000
	v_mfma_f32_16x16x32_f16 v[80:83], v[164:167], v[140:143], v[80:83]
	global_load_lds_dwordx4 v10, s[6:7]
	v_mfma_f32_16x16x32_f16 v[84:87], v[168:171], v[140:143], v[84:87]
	v_mfma_f32_16x16x32_f16 v[88:91], v[156:159], v[144:147], v[88:91]
	v_mfma_f32_16x16x32_f16 v[92:95], v[160:163], v[144:147], v[92:95]
	v_mfma_f32_16x16x32_f16 v[96:99], v[164:167], v[144:147], v[96:99]
	s_add_u32 m0, s28, 0xa000
	v_mfma_f32_16x16x32_f16 v[100:103], v[168:171], v[144:147], v[100:103]
	global_load_lds_dwordx4 v11, s[6:7]
	s_add_u32 s6, s6, s20
	s_addc_u32 s7, s7, 0
	v_mfma_f32_16x16x32_f16 v[104:107], v[156:159], v[148:151], v[104:107]
	v_mfma_f32_16x16x32_f16 v[108:111], v[160:163], v[148:151], v[108:111]
	v_mfma_f32_16x16x32_f16 v[112:115], v[164:167], v[148:151], v[112:115]
	v_mfma_f32_16x16x32_f16 v[116:119], v[168:171], v[148:151], v[116:119]
	s_waitcnt vmcnt(6) lgkmcnt(0)
	s_barrier
	s_waitcnt lgkmcnt(7)
	ds_read_b128 v[136:139], v19
	ds_read_b128 v[156:159], v21
	ds_read_b128 v[160:163], v21 offset:2048
	ds_read_b128 v[164:167], v21 offset:4096
	ds_read_b128 v[168:171], v21 offset:6144
	ds_read_b128 v[140:143], v19 offset:2048
	ds_read_b128 v[144:147], v19 offset:4096
	ds_read_b128 v[148:151], v19 offset:6144
	s_waitcnt lgkmcnt(8)
	v_mfma_f32_16x16x32_f16 v[56:59], v[192:195], v[172:175], v[56:59]
	v_mfma_f32_16x16x32_f16 v[60:63], v[196:199], v[172:175], v[60:63]
	v_mfma_f32_16x16x32_f16 v[64:67], v[200:203], v[172:175], v[64:67]
	v_mfma_f32_16x16x32_f16 v[68:71], v[204:207], v[172:175], v[68:71]
	v_mfma_f32_16x16x32_f16 v[72:75], v[192:195], v[176:179], v[72:75]
	v_mfma_f32_16x16x32_f16 v[76:79], v[196:199], v[176:179], v[76:79]
	v_mfma_f32_16x16x32_f16 v[80:83], v[200:203], v[176:179], v[80:83]
	v_mfma_f32_16x16x32_f16 v[84:87], v[204:207], v[176:179], v[84:87]
	v_mfma_f32_16x16x32_f16 v[88:91], v[192:195], v[180:183], v[88:91]
	v_mfma_f32_16x16x32_f16 v[92:95], v[196:199], v[180:183], v[92:95]
	v_mfma_f32_16x16x32_f16 v[96:99], v[200:203], v[180:183], v[96:99]
	v_mfma_f32_16x16x32_f16 v[100:103], v[204:207], v[180:183], v[100:103]
	v_mfma_f32_16x16x32_f16 v[104:107], v[192:195], v[184:187], v[104:107]
	v_mfma_f32_16x16x32_f16 v[108:111], v[196:199], v[184:187], v[108:111]
	v_mfma_f32_16x16x32_f16 v[112:115], v[200:203], v[184:187], v[112:115]
	v_mfma_f32_16x16x32_f16 v[116:119], v[204:207], v[184:187], v[116:119]
	s_waitcnt lgkmcnt(7)
	ds_read_b128 v[172:175], v20
	ds_read_b128 v[192:195], v22
	ds_read_b128 v[196:199], v22 offset:2048
	ds_read_b128 v[200:203], v22 offset:4096
	ds_read_b128 v[204:207], v22 offset:6144
	ds_read_b128 v[176:179], v20 offset:2048
	ds_read_b128 v[180:183], v20 offset:4096
	ds_read_b128 v[184:187], v20 offset:6144
	s_waitcnt lgkmcnt(8)
	v_mfma_f32_16x16x32_f16 v[56:59], v[156:159], v[136:139], v[56:59]
	v_mfma_f32_16x16x32_f16 v[60:63], v[160:163], v[136:139], v[60:63]
	v_mfma_f32_16x16x32_f16 v[64:67], v[164:167], v[136:139], v[64:67]
	v_mfma_f32_16x16x32_f16 v[68:71], v[168:171], v[136:139], v[68:71]
	v_mfma_f32_16x16x32_f16 v[72:75], v[156:159], v[140:143], v[72:75]
	v_mfma_f32_16x16x32_f16 v[76:79], v[160:163], v[140:143], v[76:79]
	v_mfma_f32_16x16x32_f16 v[80:83], v[164:167], v[140:143], v[80:83]
	v_mfma_f32_16x16x32_f16 v[84:87], v[168:171], v[140:143], v[84:87]
	v_mfma_f32_16x16x32_f16 v[88:91], v[156:159], v[144:147], v[88:91]
	v_mfma_f32_16x16x32_f16 v[92:95], v[160:163], v[144:147], v[92:95]
	v_mfma_f32_16x16x32_f16 v[96:99], v[164:167], v[144:147], v[96:99]
	v_mfma_f32_16x16x32_f16 v[100:103], v[168:171], v[144:147], v[100:103]
	v_mfma_f32_16x16x32_f16 v[104:107], v[156:159], v[148:151], v[104:107]
	v_mfma_f32_16x16x32_f16 v[108:111], v[160:163], v[148:151], v[108:111]
	v_mfma_f32_16x16x32_f16 v[112:115], v[164:167], v[148:151], v[112:115]
	v_mfma_f32_16x16x32_f16 v[116:119], v[168:171], v[148:151], v[116:119]
	s_waitcnt vmcnt(0) lgkmcnt(0)
	s_barrier
	s_waitcnt lgkmcnt(7)
	ds_read_b128 v[136:139], v15
	ds_read_b128 v[156:159], v17
	ds_read_b128 v[160:163], v17 offset:2048
	ds_read_b128 v[164:167], v17 offset:4096
	ds_read_b128 v[168:171], v17 offset:6144
	ds_read_b128 v[140:143], v15 offset:2048
	ds_read_b128 v[144:147], v15 offset:4096
	ds_read_b128 v[148:151], v15 offset:6144
	s_waitcnt lgkmcnt(8)
	v_mfma_f32_16x16x32_f16 v[56:59], v[192:195], v[172:175], v[56:59]
	v_mfma_f32_16x16x32_f16 v[60:63], v[196:199], v[172:175], v[60:63]
	v_mfma_f32_16x16x32_f16 v[64:67], v[200:203], v[172:175], v[64:67]
	v_mfma_f32_16x16x32_f16 v[68:71], v[204:207], v[172:175], v[68:71]
	v_mfma_f32_16x16x32_f16 v[72:75], v[192:195], v[176:179], v[72:75]
	v_mfma_f32_16x16x32_f16 v[76:79], v[196:199], v[176:179], v[76:79]
	v_mfma_f32_16x16x32_f16 v[80:83], v[200:203], v[176:179], v[80:83]
	v_mfma_f32_16x16x32_f16 v[84:87], v[204:207], v[176:179], v[84:87]
	v_mfma_f32_16x16x32_f16 v[88:91], v[192:195], v[180:183], v[88:91]
	v_mfma_f32_16x16x32_f16 v[92:95], v[196:199], v[180:183], v[92:95]
	v_mfma_f32_16x16x32_f16 v[96:99], v[200:203], v[180:183], v[96:99]
	v_mfma_f32_16x16x32_f16 v[100:103], v[204:207], v[180:183], v[100:103]
	v_mfma_f32_16x16x32_f16 v[104:107], v[192:195], v[184:187], v[104:107]
	v_mfma_f32_16x16x32_f16 v[108:111], v[196:199], v[184:187], v[108:111]
	v_mfma_f32_16x16x32_f16 v[112:115], v[200:203], v[184:187], v[112:115]
	v_mfma_f32_16x16x32_f16 v[116:119], v[204:207], v[184:187], v[116:119]
	s_waitcnt lgkmcnt(7)
	ds_read_b128 v[172:175], v16
	ds_read_b128 v[192:195], v18
	ds_read_b128 v[196:199], v18 offset:2048
	ds_read_b128 v[200:203], v18 offset:4096
	ds_read_b128 v[204:207], v18 offset:6144
	ds_read_b128 v[176:179], v16 offset:2048
	ds_read_b128 v[180:183], v16 offset:4096
	ds_read_b128 v[184:187], v16 offset:6144
	s_waitcnt lgkmcnt(8)
	v_mfma_f32_16x16x32_f16 v[56:59], v[156:159], v[136:139], v[56:59]
	v_mfma_f32_16x16x32_f16 v[60:63], v[160:163], v[136:139], v[60:63]
	v_mfma_f32_16x16x32_f16 v[64:67], v[164:167], v[136:139], v[64:67]
	v_mfma_f32_16x16x32_f16 v[68:71], v[168:171], v[136:139], v[68:71]
	v_mfma_f32_16x16x32_f16 v[72:75], v[156:159], v[140:143], v[72:75]
	v_mfma_f32_16x16x32_f16 v[76:79], v[160:163], v[140:143], v[76:79]
	v_mfma_f32_16x16x32_f16 v[80:83], v[164:167], v[140:143], v[80:83]
	v_mfma_f32_16x16x32_f16 v[84:87], v[168:171], v[140:143], v[84:87]
	v_mfma_f32_16x16x32_f16 v[88:91], v[156:159], v[144:147], v[88:91]
	v_mfma_f32_16x16x32_f16 v[92:95], v[160:163], v[144:147], v[92:95]
	v_mfma_f32_16x16x32_f16 v[96:99], v[164:167], v[144:147], v[96:99]
	v_mfma_f32_16x16x32_f16 v[100:103], v[168:171], v[144:147], v[100:103]
	v_mfma_f32_16x16x32_f16 v[104:107], v[156:159], v[148:151], v[104:107]
	v_mfma_f32_16x16x32_f16 v[108:111], v[160:163], v[148:151], v[108:111]
	v_mfma_f32_16x16x32_f16 v[112:115], v[164:167], v[148:151], v[112:115]
	v_mfma_f32_16x16x32_f16 v[116:119], v[168:171], v[148:151], v[116:119]
	s_waitcnt lgkmcnt(0)
	v_mfma_f32_16x16x32_f16 v[56:59], v[192:195], v[172:175], v[56:59]
	v_mfma_f32_16x16x32_f16 v[60:63], v[196:199], v[172:175], v[60:63]
	v_mfma_f32_16x16x32_f16 v[64:67], v[200:203], v[172:175], v[64:67]
	v_mfma_f32_16x16x32_f16 v[68:71], v[204:207], v[172:175], v[68:71]
	v_mfma_f32_16x16x32_f16 v[72:75], v[192:195], v[176:179], v[72:75]
	v_mfma_f32_16x16x32_f16 v[76:79], v[196:199], v[176:179], v[76:79]
	v_mfma_f32_16x16x32_f16 v[80:83], v[200:203], v[176:179], v[80:83]
	v_mfma_f32_16x16x32_f16 v[84:87], v[204:207], v[176:179], v[84:87]
	v_mfma_f32_16x16x32_f16 v[88:91], v[192:195], v[180:183], v[88:91]
	v_mfma_f32_16x16x32_f16 v[92:95], v[196:199], v[180:183], v[92:95]
	v_mfma_f32_16x16x32_f16 v[96:99], v[200:203], v[180:183], v[96:99]
	v_mfma_f32_16x16x32_f16 v[100:103], v[204:207], v[180:183], v[100:103]
	v_mfma_f32_16x16x32_f16 v[104:107], v[192:195], v[184:187], v[104:107]
	v_mfma_f32_16x16x32_f16 v[108:111], v[196:199], v[184:187], v[108:111]
	v_mfma_f32_16x16x32_f16 v[112:115], v[200:203], v[184:187], v[112:115]
	v_mfma_f32_16x16x32_f16 v[116:119], v[204:207], v[184:187], v[116:119]
	s_nop 7
	s_nop 1
	v_mov_b32_e32 v213, s19
	v_pk_add_f32 v[56:57], v[56:57], v[24:25]
	v_pk_add_f32 v[58:59], v[58:59], v[26:27]
	v_pk_add_f32 v[60:61], v[60:61], v[28:29]
	v_pk_add_f32 v[62:63], v[62:63], v[30:31]
	v_pk_add_f32 v[64:65], v[64:65], v[32:33]
	v_pk_add_f32 v[66:67], v[66:67], v[34:35]
	v_pk_add_f32 v[68:69], v[68:69], v[36:37]
	v_pk_add_f32 v[70:71], v[70:71], v[38:39]
	v_pk_mul_f32 v[208:209], v[56:57], v[56:57]
	v_pk_fma_f32 v[208:209], v[58:59], v[58:59], v[208:209]
	v_pk_fma_f32 v[208:209], v[60:61], v[60:61], v[208:209]
	v_pk_fma_f32 v[208:209], v[62:63], v[62:63], v[208:209]
	v_pk_fma_f32 v[208:209], v[64:65], v[64:65], v[208:209]
	v_pk_fma_f32 v[208:209], v[66:67], v[66:67], v[208:209]
	v_pk_fma_f32 v[208:209], v[68:69], v[68:69], v[208:209]
	v_pk_fma_f32 v[208:209], v[70:71], v[70:71], v[208:209]
	v_add_f32_e32 v208, v208, v209
	v_mov_b32_e32 v209, v208
	s_nop 1
	v_permlane16_swap_b32_e32 v208, v209
	v_add_f32_e32 v208, v208, v209
	v_mov_b32_e32 v209, v208
	s_nop 1
	v_permlane32_swap_b32_e32 v208, v209
	v_add_f32_e32 v208, v208, v209
	v_mov_b32_e32 v210, 0x358637bd
	v_fmac_f32_e32 v210, 0x3c800000, v208
	v_rsq_f32_e32 v210, v210
	s_add_u32 s24, s29, 0
	s_lshr_b32 s8, s24, 1
	s_lshl_b32 s8, s8, 12
	s_and_b32 s24, s24, 1
	s_lshl_b32 s24, s24, 8
	s_add_u32 s8, s8, s24
	v_mul_f32_e32 v210, v213, v210
	v_add_u32_e32 v212, s8, v23
	v_pk_mul_f32 v[56:57], v[56:57], v[210:211] op_sel_hi:[1,0]
	v_pk_mul_f32 v[58:59], v[58:59], v[210:211] op_sel_hi:[1,0]
	v_pk_mul_f32 v[56:57], v[56:57], v[40:41]
	v_pk_mul_f32 v[58:59], v[58:59], v[42:43]
	v_cvt_pk_f16_f32 v56, v56, v57
	v_cvt_pk_f16_f32 v57, v58, v59
	global_store_dwordx2 v212, v[56:57], s[22:23] offset:0
	v_pk_mul_f32 v[60:61], v[60:61], v[210:211] op_sel_hi:[1,0]
	v_pk_mul_f32 v[62:63], v[62:63], v[210:211] op_sel_hi:[1,0]
	v_pk_mul_f32 v[60:61], v[60:61], v[44:45]
	v_pk_mul_f32 v[62:63], v[62:63], v[46:47]
	v_cvt_pk_f16_f32 v60, v60, v61
	v_cvt_pk_f16_f32 v61, v62, v63
	global_store_dwordx2 v212, v[60:61], s[22:23] offset:1024
	v_pk_mul_f32 v[64:65], v[64:65], v[210:211] op_sel_hi:[1,0]
	v_pk_mul_f32 v[66:67], v[66:67], v[210:211] op_sel_hi:[1,0]
	v_pk_mul_f32 v[64:65], v[64:65], v[48:49]
	v_pk_mul_f32 v[66:67], v[66:67], v[50:51]
	v_cvt_pk_f16_f32 v64, v64, v65
	v_cvt_pk_f16_f32 v65, v66, v67
	global_store_dwordx2 v212, v[64:65], s[22:23] offset:2048
	v_pk_mul_f32 v[68:69], v[68:69], v[210:211] op_sel_hi:[1,0]
	v_pk_mul_f32 v[70:71], v[70:71], v[210:211] op_sel_hi:[1,0]
	v_pk_mul_f32 v[68:69], v[68:69], v[52:53]
	v_pk_mul_f32 v[70:71], v[70:71], v[54:55]
	v_cvt_pk_f16_f32 v68, v68, v69
	v_cvt_pk_f16_f32 v69, v70, v71
	global_store_dwordx2 v212, v[68:69], s[22:23] offset:3072
	v_pk_add_f32 v[72:73], v[72:73], v[24:25]
	v_pk_add_f32 v[74:75], v[74:75], v[26:27]
	v_pk_add_f32 v[76:77], v[76:77], v[28:29]
	v_pk_add_f32 v[78:79], v[78:79], v[30:31]
	v_pk_add_f32 v[80:81], v[80:81], v[32:33]
	v_pk_add_f32 v[82:83], v[82:83], v[34:35]
	v_pk_add_f32 v[84:85], v[84:85], v[36:37]
	v_pk_add_f32 v[86:87], v[86:87], v[38:39]
	v_pk_mul_f32 v[208:209], v[72:73], v[72:73]
	v_pk_fma_f32 v[208:209], v[74:75], v[74:75], v[208:209]
	v_pk_fma_f32 v[208:209], v[76:77], v[76:77], v[208:209]
	v_pk_fma_f32 v[208:209], v[78:79], v[78:79], v[208:209]
	v_pk_fma_f32 v[208:209], v[80:81], v[80:81], v[208:209]
	v_pk_fma_f32 v[208:209], v[82:83], v[82:83], v[208:209]
	v_pk_fma_f32 v[208:209], v[84:85], v[84:85], v[208:209]
	v_pk_fma_f32 v[208:209], v[86:87], v[86:87], v[208:209]
	v_add_f32_e32 v208, v208, v209
	v_mov_b32_e32 v209, v208
	s_nop 1
	v_permlane16_swap_b32_e32 v208, v209
	v_add_f32_e32 v208, v208, v209
	v_mov_b32_e32 v209, v208
	s_nop 1
	v_permlane32_swap_b32_e32 v208, v209
	v_add_f32_e32 v208, v208, v209
	v_mov_b32_e32 v210, 0x358637bd
	v_fmac_f32_e32 v210, 0x3c800000, v208
	v_rsq_f32_e32 v210, v210
	s_add_u32 s24, s29, 1
	s_lshr_b32 s8, s24, 1
	s_lshl_b32 s8, s8, 12
	s_and_b32 s24, s24, 1
	s_lshl_b32 s24, s24, 8
	s_add_u32 s8, s8, s24
	v_mul_f32_e32 v210, v213, v210
	v_add_u32_e32 v212, s8, v23
	v_pk_mul_f32 v[72:73], v[72:73], v[210:211] op_sel_hi:[1,0]
	v_pk_mul_f32 v[74:75], v[74:75], v[210:211] op_sel_hi:[1,0]
	v_pk_mul_f32 v[72:73], v[72:73], v[40:41]
	v_pk_mul_f32 v[74:75], v[74:75], v[42:43]
	v_cvt_pk_f16_f32 v72, v72, v73
	v_cvt_pk_f16_f32 v73, v74, v75
	global_store_dwordx2 v212, v[72:73], s[22:23] offset:0
	v_pk_mul_f32 v[76:77], v[76:77], v[210:211] op_sel_hi:[1,0]
	v_pk_mul_f32 v[78:79], v[78:79], v[210:211] op_sel_hi:[1,0]
	v_pk_mul_f32 v[76:77], v[76:77], v[44:45]
	v_pk_mul_f32 v[78:79], v[78:79], v[46:47]
	v_cvt_pk_f16_f32 v76, v76, v77
	v_cvt_pk_f16_f32 v77, v78, v79
	global_store_dwordx2 v212, v[76:77], s[22:23] offset:1024
	v_pk_mul_f32 v[80:81], v[80:81], v[210:211] op_sel_hi:[1,0]
	v_pk_mul_f32 v[82:83], v[82:83], v[210:211] op_sel_hi:[1,0]
	v_pk_mul_f32 v[80:81], v[80:81], v[48:49]
	v_pk_mul_f32 v[82:83], v[82:83], v[50:51]
	v_cvt_pk_f16_f32 v80, v80, v81
	v_cvt_pk_f16_f32 v81, v82, v83
	global_store_dwordx2 v212, v[80:81], s[22:23] offset:2048
	v_pk_mul_f32 v[84:85], v[84:85], v[210:211] op_sel_hi:[1,0]
	v_pk_mul_f32 v[86:87], v[86:87], v[210:211] op_sel_hi:[1,0]
	v_pk_mul_f32 v[84:85], v[84:85], v[52:53]
	v_pk_mul_f32 v[86:87], v[86:87], v[54:55]
	v_cvt_pk_f16_f32 v84, v84, v85
	v_cvt_pk_f16_f32 v85, v86, v87
	global_store_dwordx2 v212, v[84:85], s[22:23] offset:3072
	v_pk_add_f32 v[88:89], v[88:89], v[24:25]
	v_pk_add_f32 v[90:91], v[90:91], v[26:27]
	v_pk_add_f32 v[92:93], v[92:93], v[28:29]
	v_pk_add_f32 v[94:95], v[94:95], v[30:31]
	v_pk_add_f32 v[96:97], v[96:97], v[32:33]
	v_pk_add_f32 v[98:99], v[98:99], v[34:35]
	v_pk_add_f32 v[100:101], v[100:101], v[36:37]
	v_pk_add_f32 v[102:103], v[102:103], v[38:39]
	v_pk_mul_f32 v[208:209], v[88:89], v[88:89]
	v_pk_fma_f32 v[208:209], v[90:91], v[90:91], v[208:209]
	v_pk_fma_f32 v[208:209], v[92:93], v[92:93], v[208:209]
	v_pk_fma_f32 v[208:209], v[94:95], v[94:95], v[208:209]
	v_pk_fma_f32 v[208:209], v[96:97], v[96:97], v[208:209]
	v_pk_fma_f32 v[208:209], v[98:99], v[98:99], v[208:209]
	v_pk_fma_f32 v[208:209], v[100:101], v[100:101], v[208:209]
	v_pk_fma_f32 v[208:209], v[102:103], v[102:103], v[208:209]
	v_add_f32_e32 v208, v208, v209
	v_mov_b32_e32 v209, v208
	s_nop 1
	v_permlane16_swap_b32_e32 v208, v209
	v_add_f32_e32 v208, v208, v209
	v_mov_b32_e32 v209, v208
	s_nop 1
	v_permlane32_swap_b32_e32 v208, v209
	v_add_f32_e32 v208, v208, v209
	v_mov_b32_e32 v210, 0x358637bd
	v_fmac_f32_e32 v210, 0x3c800000, v208
	v_rsq_f32_e32 v210, v210
	s_add_u32 s24, s29, 2
	s_lshr_b32 s8, s24, 1
	s_lshl_b32 s8, s8, 12
	s_and_b32 s24, s24, 1
	s_lshl_b32 s24, s24, 8
	s_add_u32 s8, s8, s24
	v_mul_f32_e32 v210, v213, v210
	v_add_u32_e32 v212, s8, v23
	v_pk_mul_f32 v[88:89], v[88:89], v[210:211] op_sel_hi:[1,0]
	v_pk_mul_f32 v[90:91], v[90:91], v[210:211] op_sel_hi:[1,0]
	v_pk_mul_f32 v[88:89], v[88:89], v[40:41]
	v_pk_mul_f32 v[90:91], v[90:91], v[42:43]
	v_cvt_pk_f16_f32 v88, v88, v89
	v_cvt_pk_f16_f32 v89, v90, v91
	global_store_dwordx2 v212, v[88:89], s[22:23] offset:0
	v_pk_mul_f32 v[92:93], v[92:93], v[210:211] op_sel_hi:[1,0]
	v_pk_mul_f32 v[94:95], v[94:95], v[210:211] op_sel_hi:[1,0]
	v_pk_mul_f32 v[92:93], v[92:93], v[44:45]
	v_pk_mul_f32 v[94:95], v[94:95], v[46:47]
	v_cvt_pk_f16_f32 v92, v92, v93
	v_cvt_pk_f16_f32 v93, v94, v95
	global_store_dwordx2 v212, v[92:93], s[22:23] offset:1024
	v_pk_mul_f32 v[96:97], v[96:97], v[210:211] op_sel_hi:[1,0]
	v_pk_mul_f32 v[98:99], v[98:99], v[210:211] op_sel_hi:[1,0]
	v_pk_mul_f32 v[96:97], v[96:97], v[48:49]
	v_pk_mul_f32 v[98:99], v[98:99], v[50:51]
	v_cvt_pk_f16_f32 v96, v96, v97
	v_cvt_pk_f16_f32 v97, v98, v99
	global_store_dwordx2 v212, v[96:97], s[22:23] offset:2048
	v_pk_mul_f32 v[100:101], v[100:101], v[210:211] op_sel_hi:[1,0]
	v_pk_mul_f32 v[102:103], v[102:103], v[210:211] op_sel_hi:[1,0]
	v_pk_mul_f32 v[100:101], v[100:101], v[52:53]
	v_pk_mul_f32 v[102:103], v[102:103], v[54:55]
	v_cvt_pk_f16_f32 v100, v100, v101
	v_cvt_pk_f16_f32 v101, v102, v103
	global_store_dwordx2 v212, v[100:101], s[22:23] offset:3072
	v_pk_add_f32 v[104:105], v[104:105], v[24:25]
	v_pk_add_f32 v[106:107], v[106:107], v[26:27]
	v_pk_add_f32 v[108:109], v[108:109], v[28:29]
	v_pk_add_f32 v[110:111], v[110:111], v[30:31]
	v_pk_add_f32 v[112:113], v[112:113], v[32:33]
	v_pk_add_f32 v[114:115], v[114:115], v[34:35]
	v_pk_add_f32 v[116:117], v[116:117], v[36:37]
	v_pk_add_f32 v[118:119], v[118:119], v[38:39]
	v_pk_mul_f32 v[208:209], v[104:105], v[104:105]
	v_pk_fma_f32 v[208:209], v[106:107], v[106:107], v[208:209]
	v_pk_fma_f32 v[208:209], v[108:109], v[108:109], v[208:209]
	v_pk_fma_f32 v[208:209], v[110:111], v[110:111], v[208:209]
	v_pk_fma_f32 v[208:209], v[112:113], v[112:113], v[208:209]
	v_pk_fma_f32 v[208:209], v[114:115], v[114:115], v[208:209]
	v_pk_fma_f32 v[208:209], v[116:117], v[116:117], v[208:209]
	v_pk_fma_f32 v[208:209], v[118:119], v[118:119], v[208:209]
	v_add_f32_e32 v208, v208, v209
	v_mov_b32_e32 v209, v208
	s_nop 1
	v_permlane16_swap_b32_e32 v208, v209
	v_add_f32_e32 v208, v208, v209
	v_mov_b32_e32 v209, v208
	s_nop 1
	v_permlane32_swap_b32_e32 v208, v209
	v_add_f32_e32 v208, v208, v209
	v_mov_b32_e32 v210, 0x358637bd
	v_fmac_f32_e32 v210, 0x3c800000, v208
	v_rsq_f32_e32 v210, v210
	s_add_u32 s24, s29, 3
	s_lshr_b32 s8, s24, 1
	s_lshl_b32 s8, s8, 12
	s_and_b32 s24, s24, 1
	s_lshl_b32 s24, s24, 8
	s_add_u32 s8, s8, s24
	v_mul_f32_e32 v210, v213, v210
	v_add_u32_e32 v212, s8, v23
	v_pk_mul_f32 v[104:105], v[104:105], v[210:211] op_sel_hi:[1,0]
	v_pk_mul_f32 v[106:107], v[106:107], v[210:211] op_sel_hi:[1,0]
	v_pk_mul_f32 v[104:105], v[104:105], v[40:41]
	v_pk_mul_f32 v[106:107], v[106:107], v[42:43]
	v_cvt_pk_f16_f32 v104, v104, v105
	v_cvt_pk_f16_f32 v105, v106, v107
	global_store_dwordx2 v212, v[104:105], s[22:23] offset:0
	v_pk_mul_f32 v[108:109], v[108:109], v[210:211] op_sel_hi:[1,0]
	v_pk_mul_f32 v[110:111], v[110:111], v[210:211] op_sel_hi:[1,0]
	v_pk_mul_f32 v[108:109], v[108:109], v[44:45]
	v_pk_mul_f32 v[110:111], v[110:111], v[46:47]
	v_cvt_pk_f16_f32 v108, v108, v109
	v_cvt_pk_f16_f32 v109, v110, v111
	global_store_dwordx2 v212, v[108:109], s[22:23] offset:1024
	v_pk_mul_f32 v[112:113], v[112:113], v[210:211] op_sel_hi:[1,0]
	v_pk_mul_f32 v[114:115], v[114:115], v[210:211] op_sel_hi:[1,0]
	v_pk_mul_f32 v[112:113], v[112:113], v[48:49]
	v_pk_mul_f32 v[114:115], v[114:115], v[50:51]
	v_cvt_pk_f16_f32 v112, v112, v113
	v_cvt_pk_f16_f32 v113, v114, v115
	global_store_dwordx2 v212, v[112:113], s[22:23] offset:2048
	v_pk_mul_f32 v[116:117], v[116:117], v[210:211] op_sel_hi:[1,0]
	v_pk_mul_f32 v[118:119], v[118:119], v[210:211] op_sel_hi:[1,0]
	v_pk_mul_f32 v[116:117], v[116:117], v[52:53]
	v_pk_mul_f32 v[118:119], v[118:119], v[54:55]
	v_cvt_pk_f16_f32 v116, v116, v117
	v_cvt_pk_f16_f32 v117, v118, v119
	global_store_dwordx2 v212, v[116:117], s[22:23] offset:3072
	s_branch .Lpf_done
.Lpf_vKA:
	s_mul_i32 s25, s25, 0x50
	s_add_u32 s29, s10, s25
	s_lshr_b32 s29, s29, 4
	v_add_u32_e32 v5, s25, v3
	v_lshlrev_b32_e32 v5, 7, v5
	v_add_u32_e32 v15, v5, v6
	v_add_u32_e32 v16, v5, v7
	v_add_u32_e32 v5, 0x9000, v9
	v_add_u32_e32 v17, v5, v6
	v_add_u32_e32 v18, v5, v7
	v_add_u32_e32 v19, 0x1a000, v15
	v_add_u32_e32 v20, 0x1a000, v16
	v_add_u32_e32 v21, 0x1a000, v17
	v_add_u32_e32 v22, 0x1a000, v18
	v_lshlrev_b32_e32 v5, 4, v4
	global_load_dwordx4 v[24:27], v5, s[14:15] offset:0
	global_load_dwordx4 v[28:31], v5, s[14:15] offset:64
	global_load_dwordx4 v[32:35], v5, s[14:15] offset:128
	global_load_dwordx4 v[36:39], v5, s[14:15] offset:192
	global_load_dwordx4 v[40:43], v5, s[16:17] offset:0
	global_load_dwordx4 v[44:47], v5, s[16:17] offset:64
	global_load_dwordx4 v[48:51], v5, s[16:17] offset:128
	global_load_dwordx4 v[52:55], v5, s[16:17] offset:192
	s_add_u32 m0, s28, 0x0
	s_nop 0
	global_load_lds_dwordx4 v10, s[4:5]
	s_add_u32 m0, s28, 0x2000
	s_nop 0
	global_load_lds_dwordx4 v11, s[4:5]
	s_add_u32 m0, s28, 0x4000
	s_nop 0
	global_load_lds_dwordx4 v12, s[4:5]
	s_add_u32 m0, s28, 0x6000
	s_nop 0
	global_load_lds_dwordx4 v13, s[4:5]
	s_add_u32 m0, s28, 0x8000
	s_nop 0
	global_load_lds_dwordx4 v14, s[4:5]
	s_add_u32 s4, s4, s20
	s_addc_u32 s5, s5, 0
	s_add_u32 m0, s28, 0x9000
	s_nop 0
	global_load_lds_dwordx4 v10, s[6:7]
	s_add_u32 m0, s28, 0xb000
	s_nop 0
	global_load_lds_dwordx4 v11, s[6:7]
	s_add_u32 s6, s6, s20
	s_addc_u32 s7, s7, 0
	s_add_u32 m0, s28, 0xd000
	s_nop 0
	global_load_lds_dwordx4 v10, s[4:5]
	s_add_u32 m0, s28, 0xf000
	s_nop 0
	global_load_lds_dwordx4 v11, s[4:5]
	s_add_u32 m0, s28, 0x11000
	s_nop 0
	global_load_lds_dwordx4 v12, s[4:5]
	s_add_u32 m0, s28, 0x13000
	s_nop 0
	global_load_lds_dwordx4 v13, s[4:5]
	s_add_u32 m0, s28, 0x15000
	s_nop 0
	global_load_lds_dwordx4 v14, s[4:5]
	s_add_u32 s4, s4, s20
	s_addc_u32 s5, s5, 0
	s_add_u32 m0, s28, 0x16000
	s_nop 0
	global_load_lds_dwordx4 v10, s[6:7]
	s_add_u32 m0, s28, 0x18000
	s_nop 0
	global_load_lds_dwordx4 v11, s[6:7]
	s_add_u32 s6, s6, s20
	s_addc_u32 s7, s7, 0
	s_add_u32 m0, s28, 0x1a000
	s_nop 0
	global_load_lds_dwordx4 v10, s[4:5]
	s_add_u32 m0, s28, 0x1c000
	s_nop 0
	global_load_lds_dwordx4 v11, s[4:5]
	s_add_u32 m0, s28, 0x1e000
	s_nop 0
	global_load_lds_dwordx4 v12, s[4:5]
	s_add_u32 m0, s28, 0x20000
	s_nop 0
	global_load_lds_dwordx4 v13, s[4:5]
	s_add_u32 m0, s28, 0x22000
	s_nop 0
	global_load_lds_dwordx4 v14, s[4:5]
	s_add_u32 s4, s4, s20
	s_addc_u32 s5, s5, 0
	s_add_u32 m0, s28, 0x23000
	s_nop 0
	global_load_lds_dwordx4 v10, s[6:7]
	s_add_u32 m0, s28, 0x25000
	s_nop 0
	global_load_lds_dwordx4 v11, s[6:7]
	s_add_u32 s6, s6, s20
	s_addc_u32 s7, s7, 0
	s_waitcnt vmcnt(14) lgkmcnt(0)
	s_barrier
	s_waitcnt lgkmcnt(6)
	ds_read_b128 v[136:139], v15
	ds_read_b128 v[156:159], v17
	ds_read_b128 v[160:163], v17 offset:2048
	ds_read_b128 v[164:167], v17 offset:4096
	ds_read_b128 v[168:171], v17 offset:6144
	ds_read_b128 v[140:143], v15 offset:2048
	ds_read_b128 v[144:147], v15 offset:4096
	ds_read_b128 v[148:151], v15 offset:6144
	ds_read_b128 v[152:155], v15 offset:8192
	s_waitcnt lgkmcnt(6)
	ds_read_b128 v[172:175], v16
	ds_read_b128 v[192:195], v18
	ds_read_b128 v[196:199], v18 offset:2048
	ds_read_b128 v[200:203], v18 offset:4096
	ds_read_b128 v[204:207], v18 offset:6144
	ds_read_b128 v[176:179], v16 offset:2048
	ds_read_b128 v[180:183], v16 offset:4096
	ds_read_b128 v[184:187], v16 offset:6144
	ds_read_b128 v[188:191], v16 offset:8192
	s_waitcnt lgkmcnt(9)
	v_mfma_f32_16x16x32_f16 v[56:59], v[156:159], v[136:139], 0
	v_mfma_f32_16x16x32_f16 v[60:63], v[160:163], v[136:139], 0
	v_mfma_f32_16x16x32_f16 v[64:67], v[164:167], v[136:139], 0
	v_mfma_f32_16x16x32_f16 v[68:71], v[168:171], v[136:139], 0
	v_mfma_f32_16x16x32_f16 v[72:75], v[156:159], v[140:143], 0
	v_mfma_f32_16x16x32_f16 v[76:79], v[160:163], v[140:143], 0
	v_mfma_f32_16x16x32_f16 v[80:83], v[164:167], v[140:143], 0
	v_mfma_f32_16x16x32_f16 v[84:87], v[168:171], v[140:143], 0
	v_mfma_f32_16x16x32_f16 v[88:91], v[156:159], v[144:147], 0
	v_mfma_f32_16x16x32_f16 v[92:95], v[160:163], v[144:147], 0
	v_mfma_f32_16x16x32_f16 v[96:99], v[164:167], v[144:147], 0
	v_mfma_f32_16x16x32_f16 v[100:103], v[168:171], v[144:147], 0
	v_mfma_f32_16x16x32_f16 v[104:107], v[156:159], v[148:151], 0
	v_mfma_f32_16x16x32_f16 v[108:111], v[160:163], v[148:151], 0
	v_mfma_f32_16x16x32_f16 v[112:115], v[164:167], v[148:151], 0
	v_mfma_f32_16x16x32_f16 v[116:119], v[168:171], v[148:151], 0
	v_mfma_f32_16x16x32_f16 v[120:123], v[156:159], v[152:155], 0
	v_mfma_f32_16x16x32_f16 v[124:127], v[160:163], v[152:155], 0
	v_mfma_f32_16x16x32_f16 v[128:131], v[164:167], v[152:155], 0
	v_mfma_f32_16x16x32_f16 v[132:135], v[168:171], v[152:155], 0
	s_waitcnt vmcnt(7) lgkmcnt(0)
	s_barrier
	s_waitcnt lgkmcnt(6)
	ds_read_b128 v[136:139], v15 offset:53248
	ds_read_b128 v[156:159], v17 offset:53248
	ds_read_b128 v[160:163], v17 offset:55296
	ds_read_b128 v[164:167], v17 offset:57344
	ds_read_b128 v[168:171], v17 offset:59392
	ds_read_b128 v[140:143], v15 offset:55296
	ds_read_b128 v[144:147], v15 offset:57344
	ds_read_b128 v[148:151], v15 offset:59392
	ds_read_b128 v[152:155], v15 offset:61440
	s_waitcnt lgkmcnt(9)
	v_mfma_f32_16x16x32_f16 v[56:59], v[192:195], v[172:175], v[56:59]
	s_add_u32 m0, s28, 0x0
	v_mfma_f32_16x16x32_f16 v[60:63], v[196:199], v[172:175], v[60:63]
	global_load_lds_dwordx4 v10, s[4:5]
	v_mfma_f32_16x16x32_f16 v[64:67], v[200:203], v[172:175], v[64:67]
	v_mfma_f32_16x16x32_f16 v[68:71], v[204:207], v[172:175], v[68:71]
	v_mfma_f32_16x16x32_f16 v[72:75], v[192:195], v[176:179], v[72:75]
	v_mfma_f32_16x16x32_f16 v[76:79], v[196:199], v[176:179], v[76:79]
	s_add_u32 m0, s28, 0x2000
	v_mfma_f32_16x16x32_f16 v[80:83], v[200:203], v[176:179], v[80:83]
	global_load_lds_dwordx4 v11, s[4:5]
	v_mfma_f32_16x16x32_f16 v[84:87], v[204:207], v[176:179], v[84:87]
	v_mfma_f32_16x16x32_f16 v[88:91], v[192:195], v[180:183], v[88:91]
	v_mfma_f32_16x16x32_f16 v[92:95], v[196:199], v[180:183], v[92:95]
	v_mfma_f32_16x16x32_f16 v[96:99], v[200:203], v[180:183], v[96:99]
	s_add_u32 m0, s28, 0x4000
	v_mfma_f32_16x16x32_f16 v[100:103], v[204:207], v[180:183], v[100:103]
	global_load_lds_dwordx4 v12, s[4:5]
	v_mfma_f32_16x16x32_f16 v[104:107], v[192:195], v[184:187], v[104:107]
	v_mfma_f32_16x16x32_f16 v[108:111], v[196:199], v[184:187], v[108:111]
	v_mfma_f32_16x16x32_f16 v[112:115], v[200:203], v[184:187], v[112:115]
	v_mfma_f32_16x16x32_f16 v[116:119], v[204:207], v[184:187], v[116:119]
	s_add_u32 m0, s28, 0x6000
	v_mfma_f32_16x16x32_f16 v[120:123], v[192:195], v[188:191], v[120:123]
	global_load_lds_dwordx4 v13, s[4:5]
	v_mfma_f32_16x16x32_f16 v[124:127], v[196:199], v[188:191], v[124:127]
	v_mfma_f32_16x16x32_f16 v[128:131], v[200:203], v[188:191], v[128:131]
	v_mfma_f32_16x16x32_f16 v[132:135], v[204:207], v[188:191], v[132:135]
	s_waitcnt lgkmcnt(6)
	ds_read_b128 v[172:175], v16 offset:53248
	ds_read_b128 v[192:195], v18 offset:53248
	ds_read_b128 v[196:199], v18 offset:55296
	ds_read_b128 v[200:203], v18 offset:57344
	ds_read_b128 v[204:207], v18 offset:59392
	ds_read_b128 v[176:179], v16 offset:55296
	ds_read_b128 v[180:183], v16 offset:57344
	ds_read_b128 v[184:187], v16 offset:59392
	ds_read_b128 v[188:191], v16 offset:61440
	s_waitcnt lgkmcnt(9)
	v_mfma_f32_16x16x32_f16 v[56:59], v[156:159], v[136:139], v[56:59]
	s_add_u32 m0, s28, 0x8000
	v_mfma_f32_16x16x32_f16 v[60:63], v[160:163], v[136:139], v[60:63]
	global_load_lds_dwordx4 v14, s[4:5]
	s_add_u32 s4, s4, s20
	s_addc_u32 s5, s5, 0
	v_mfma_f32_16x16x32_f16 v[64:67], v[164:167], v[136:139], v[64:67]
	v_mfma_f32_16x16x32_f16 v[68:71], v[168:171], v[136:139], v[68:71]
	v_mfma_f32_16x16x32_f16 v[72:75], v[156:159], v[140:143], v[72:75]
	v_mfma_f32_16x16x32_f16 v[76:79], v[160:163], v[140:143], v[76:79]
	v_mfma_f32_16x16x32_f16 v[80:83], v[164:167], v[140:143], v[80:83]
	s_add_u32 m0, s28, 0x9000
	v_mfma_f32_16x16x32_f16 v[84:87], v[168:171], v[140:143], v[84:87]
	global_load_lds_dwordx4 v10, s[6:7]
	v_mfma_f32_16x16x32_f16 v[88:91], v[156:159], v[144:147], v[88:91]
	v_mfma_f32_16x16x32_f16 v[92:95], v[160:163], v[144:147], v[92:95]
	v_mfma_f32_16x16x32_f16 v[96:99], v[164:167], v[144:147], v[96:99]
	v_mfma_f32_16x16x32_f16 v[100:103], v[168:171], v[144:147], v[100:103]
	v_mfma_f32_16x16x32_f16 v[104:107], v[156:159], v[148:151], v[104:107]
	v_mfma_f32_16x16x32_f16 v[108:111], v[160:163], v[148:151], v[108:111]
	s_add_u32 m0, s28, 0xb000
	v_mfma_f32_16x16x32_f16 v[112:115], v[164:167], v[148:151], v[112:115]
	global_load_lds_dwordx4 v11, s[6:7]
	s_add_u32 s6, s6, s20
	s_addc_u32 s7, s7, 0
	v_mfma_f32_16x16x32_f16 v[116:119], v[168:171], v[148:151], v[116:119]
	v_mfma_f32_16x16x32_f16 v[120:123], v[156:159], v[152:155], v[120:123]
	v_mfma_f32_16x16x32_f16 v[124:127], v[160:163], v[152:155], v[124:127]
	v_mfma_f32_16x16x32_f16 v[128:131], v[164:167], v[152:155], v[128:131]
	v_mfma_f32_16x16x32_f16 v[132:135], v[168:171], v[152:155], v[132:135]
	s_waitcnt vmcnt(7) lgkmcnt(0)
	s_barrier
	s_waitcnt lgkmcnt(6)
	ds_read_b128 v[136:139], v19
	ds_read_b128 v[156:159], v21
	ds_read_b128 v[160:163], v21 offset:2048
	ds_read_b128 v[164:167], v21 offset:4096
	ds_read_b128 v[168:171], v21 offset:6144
	ds_read_b128 v[140:143], v19 offset:2048
	ds_read_b128 v[144:147], v19 offset:4096
	ds_read_b128 v[148:151], v19 offset:6144
	ds_read_b128 v[152:155], v19 offset:8192
	s_waitcnt lgkmcnt(9)
	v_mfma_f32_16x16x32_f16 v[56:59], v[192:195], v[172:175], v[56:59]
	s_add_u32 m0, s28, 0xd000
	v_mfma_f32_16x16x32_f16 v[60:63], v[196:199], v[172:175], v[60:63]
	global_load_lds_dwordx4 v10, s[4:5]
	v_mfma_f32_16x16x32_f16 v[64:67], v[200:203], v[172:175], v[64:67]
	v_mfma_f32_16x16x32_f16 v[68:71], v[204:207], v[172:175], v[68:71]
	v_mfma_f32_16x16x32_f16 v[72:75], v[192:195], v[176:179], v[72:75]
	v_mfma_f32_16x16x32_f16 v[76:79], v[196:199], v[176:179], v[76:79]
	s_add_u32 m0, s28, 0xf000
	v_mfma_f32_16x16x32_f16 v[80:83], v[200:203], v[176:179], v[80:83]
	global_load_lds_dwordx4 v11, s[4:5]
	v_mfma_f32_16x16x32_f16 v[84:87], v[204:207], v[176:179], v[84:87]
	v_mfma_f32_16x16x32_f16 v[88:91], v[192:195], v[180:183], v[88:91]
	v_mfma_f32_16x16x32_f16 v[92:95], v[196:199], v[180:183], v[92:95]
	v_mfma_f32_16x16x32_f16 v[96:99], v[200:203], v[180:183], v[96:99]
	s_add_u32 m0, s28, 0x11000
	v_mfma_f32_16x16x32_f16 v[100:103], v[204:207], v[180:183], v[100:103]
	global_load_lds_dwordx4 v12, s[4:5]
	v_mfma_f32_16x16x32_f16 v[104:107], v[192:195], v[184:187], v[104:107]
	v_mfma_f32_16x16x32_f16 v[108:111], v[196:199], v[184:187], v[108:111]
	v_mfma_f32_16x16x32_f16 v[112:115], v[200:203], v[184:187], v[112:115]
	v_mfma_f32_16x16x32_f16 v[116:119], v[204:207], v[184:187], v[116:119]
	s_add_u32 m0, s28, 0x13000
	v_mfma_f32_16x16x32_f16 v[120:123], v[192:195], v[188:191], v[120:123]
	global_load_lds_dwordx4 v13, s[4:5]
	v_mfma_f32_16x16x32_f16 v[124:127], v[196:199], v[188:191], v[124:127]
	v_mfma_f32_16x16x32_f16 v[128:131], v[200:203], v[188:191], v[128:131]
	v_mfma_f32_16x16x32_f16 v[132:135], v[204:207], v[188:191], v[132:135]
	s_waitcnt lgkmcnt(6)
	ds_read_b128 v[172:175], v20
	ds_read_b128 v[192:195], v22
	ds_read_b128 v[196:199], v22 offset:2048
	ds_read_b128 v[200:203], v22 offset:4096
	ds_read_b128 v[204:207], v22 offset:6144
	ds_read_b128 v[176:179], v20 offset:2048
	ds_read_b128 v[180:183], v20 offset:4096
	ds_read_b128 v[184:187], v20 offset:6144
	ds_read_b128 v[188:191], v20 offset:8192
	s_waitcnt lgkmcnt(9)
	v_mfma_f32_16x16x32_f16 v[56:59], v[156:159], v[136:139], v[56:59]
	s_add_u32 m0, s28, 0x15000
	v_mfma_f32_16x16x32_f16 v[60:63], v[160:163], v[136:139], v[60:63]
	global_load_lds_dwordx4 v14, s[4:5]
	s_add_u32 s4, s4, s20
	s_addc_u32 s5, s5, 0
	v_mfma_f32_16x16x32_f16 v[64:67], v[164:167], v[136:139], v[64:67]
	v_mfma_f32_16x16x32_f16 v[68:71], v[168:171], v[136:139], v[68:71]
	v_mfma_f32_16x16x32_f16 v[72:75], v[156:159], v[140:143], v[72:75]
	v_mfma_f32_16x16x32_f16 v[76:79], v[160:163], v[140:143], v[76:79]
	v_mfma_f32_16x16x32_f16 v[80:83], v[164:167], v[140:143], v[80:83]
	s_add_u32 m0, s28, 0x16000
	v_mfma_f32_16x16x32_f16 v[84:87], v[168:171], v[140:143], v[84:87]
	global_load_lds_dwordx4 v10, s[6:7]
	v_mfma_f32_16x16x32_f16 v[88:91], v[156:159], v[144:147], v[88:91]
	v_mfma_f32_16x16x32_f16 v[92:95], v[160:163], v[144:147], v[92:95]
	v_mfma_f32_16x16x32_f16 v[96:99], v[164:167], v[144:147], v[96:99]
	v_mfma_f32_16x16x32_f16 v[100:103], v[168:171], v[144:147], v[100:103]
	v_mfma_f32_16x16x32_f16 v[104:107], v[156:159], v[148:151], v[104:107]
	v_mfma_f32_16x16x32_f16 v[108:111], v[160:163], v[148:151], v[108:111]
	s_add_u32 m0, s28, 0x18000
	v_mfma_f32_16x16x32_f16 v[112:115], v[164:167], v[148:151], v[112:115]
	global_load_lds_dwordx4 v11, s[6:7]
	s_add_u32 s6, s6, s20
	s_addc_u32 s7, s7, 0
	v_mfma_f32_16x16x32_f16 v[116:119], v[168:171], v[148:151], v[116:119]
	v_mfma_f32_16x16x32_f16 v[120:123], v[156:159], v[152:155], v[120:123]
	v_mfma_f32_16x16x32_f16 v[124:127], v[160:163], v[152:155], v[124:127]
	v_mfma_f32_16x16x32_f16 v[128:131], v[164:167], v[152:155], v[128:131]
	v_mfma_f32_16x16x32_f16 v[132:135], v[168:171], v[152:155], v[132:135]
	s_waitcnt vmcnt(7) lgkmcnt(0)
	s_barrier
	s_waitcnt lgkmcnt(6)
	ds_read_b128 v[136:139], v15
	ds_read_b128 v[156:159], v17
	ds_read_b128 v[160:163], v17 offset:2048
	ds_read_b128 v[164:167], v17 offset:4096
	ds_read_b128 v[168:171], v17 offset:6144
	ds_read_b128 v[140:143], v15 offset:2048
	ds_read_b128 v[144:147], v15 offset:4096
	ds_read_b128 v[148:151], v15 offset:6144
	ds_read_b128 v[152:155], v15 offset:8192
	s_waitcnt lgkmcnt(9)
	v_mfma_f32_16x16x32_f16 v[56:59], v[192:195], v[172:175], v[56:59]
	s_add_u32 m0, s28, 0x1a000
	v_mfma_f32_16x16x32_f16 v[60:63], v[196:199], v[172:175], v[60:63]
	global_load_lds_dwordx4 v10, s[4:5]
	v_mfma_f32_16x16x32_f16 v[64:67], v[200:203], v[172:175], v[64:67]
	v_mfma_f32_16x16x32_f16 v[68:71], v[204:207], v[172:175], v[68:71]
	v_mfma_f32_16x16x32_f16 v[72:75], v[192:195], v[176:179], v[72:75]
	v_mfma_f32_16x16x32_f16 v[76:79], v[196:199], v[176:179], v[76:79]
	s_add_u32 m0, s28, 0x1c000
	v_mfma_f32_16x16x32_f16 v[80:83], v[200:203], v[176:179], v[80:83]
	global_load_lds_dwordx4 v11, s[4:5]
	v_mfma_f32_16x16x32_f16 v[84:87], v[204:207], v[176:179], v[84:87]
	v_mfma_f32_16x16x32_f16 v[88:91], v[192:195], v[180:183], v[88:91]
	v_mfma_f32_16x16x32_f16 v[92:95], v[196:199], v[180:183], v[92:95]
	v_mfma_f32_16x16x32_f16 v[96:99], v[200:203], v[180:183], v[96:99]
	s_add_u32 m0, s28, 0x1e000
	v_mfma_f32_16x16x32_f16 v[100:103], v[204:207], v[180:183], v[100:103]
	global_load_lds_dwordx4 v12, s[4:5]
	v_mfma_f32_16x16x32_f16 v[104:107], v[192:195], v[184:187], v[104:107]
	v_mfma_f32_16x16x32_f16 v[108:111], v[196:199], v[184:187], v[108:111]
	v_mfma_f32_16x16x32_f16 v[112:115], v[200:203], v[184:187], v[112:115]
	v_mfma_f32_16x16x32_f16 v[116:119], v[204:207], v[184:187], v[116:119]
	s_add_u32 m0, s28, 0x20000
	v_mfma_f32_16x16x32_f16 v[120:123], v[192:195], v[188:191], v[120:123]
	global_load_lds_dwordx4 v13, s[4:5]
	v_mfma_f32_16x16x32_f16 v[124:127], v[196:199], v[188:191], v[124:127]
	v_mfma_f32_16x16x32_f16 v[128:131], v[200:203], v[188:191], v[128:131]
	v_mfma_f32_16x16x32_f16 v[132:135], v[204:207], v[188:191], v[132:135]
	s_waitcnt lgkmcnt(6)
	ds_read_b128 v[172:175], v16
	ds_read_b128 v[192:195], v18
	ds_read_b128 v[196:199], v18 offset:2048
	ds_read_b128 v[200:203], v18 offset:4096
	ds_read_b128 v[204:207], v18 offset:6144
	ds_read_b128 v[176:179], v16 offset:2048
	ds_read_b128 v[180:183], v16 offset:4096
	ds_read_b128 v[184:187], v16 offset:6144
	ds_read_b128 v[188:191], v16 offset:8192
	s_waitcnt lgkmcnt(9)
	v_mfma_f32_16x16x32_f16 v[56:59], v[156:159], v[136:139], v[56:59]
	s_add_u32 m0, s28, 0x22000
	v_mfma_f32_16x16x32_f16 v[60:63], v[160:163], v[136:139], v[60:63]
	global_load_lds_dwordx4 v14, s[4:5]
	s_add_u32 s4, s4, s20
	s_addc_u32 s5, s5, 0
	v_mfma_f32_16x16x32_f16 v[64:67], v[164:167], v[136:139], v[64:67]
	v_mfma_f32_16x16x32_f16 v[68:71], v[168:171], v[136:139], v[68:71]
	v_mfma_f32_16x16x32_f16 v[72:75], v[156:159], v[140:143], v[72:75]
	v_mfma_f32_16x16x32_f16 v[76:79], v[160:163], v[140:143], v[76:79]
	v_mfma_f32_16x16x32_f16 v[80:83], v[164:167], v[140:143], v[80:83]
	s_add_u32 m0, s28, 0x23000
	v_mfma_f32_16x16x32_f16 v[84:87], v[168:171], v[140:143], v[84:87]
	global_load_lds_dwordx4 v10, s[6:7]
	v_mfma_f32_16x16x32_f16 v[88:91], v[156:159], v[144:147], v[88:91]
	v_mfma_f32_16x16x32_f16 v[92:95], v[160:163], v[144:147], v[92:95]
	v_mfma_f32_16x16x32_f16 v[96:99], v[164:167], v[144:147], v[96:99]
	v_mfma_f32_16x16x32_f16 v[100:103], v[168:171], v[144:147], v[100:103]
	v_mfma_f32_16x16x32_f16 v[104:107], v[156:159], v[148:151], v[104:107]
	v_mfma_f32_16x16x32_f16 v[108:111], v[160:163], v[148:151], v[108:111]
	s_add_u32 m0, s28, 0x25000
	v_mfma_f32_16x16x32_f16 v[112:115], v[164:167], v[148:151], v[112:115]
	global_load_lds_dwordx4 v11, s[6:7]
	s_add_u32 s6, s6, s20
	s_addc_u32 s7, s7, 0
	v_mfma_f32_16x16x32_f16 v[116:119], v[168:171], v[148:151], v[116:119]
	v_mfma_f32_16x16x32_f16 v[120:123], v[156:159], v[152:155], v[120:123]
	v_mfma_f32_16x16x32_f16 v[124:127], v[160:163], v[152:155], v[124:127]
	v_mfma_f32_16x16x32_f16 v[128:131], v[164:167], v[152:155], v[128:131]
	v_mfma_f32_16x16x32_f16 v[132:135], v[168:171], v[152:155], v[132:135]
	s_waitcnt vmcnt(7) lgkmcnt(0)
	s_barrier
	s_waitcnt lgkmcnt(6)
	ds_read_b128 v[136:139], v15 offset:53248
	ds_read_b128 v[156:159], v17 offset:53248
	ds_read_b128 v[160:163], v17 offset:55296
	ds_read_b128 v[164:167], v17 offset:57344
	ds_read_b128 v[168:171], v17 offset:59392
	ds_read_b128 v[140:143], v15 offset:55296
	ds_read_b128 v[144:147], v15 offset:57344
	ds_read_b128 v[148:151], v15 offset:59392
	ds_read_b128 v[152:155], v15 offset:61440
	s_waitcnt lgkmcnt(9)
	v_mfma_f32_16x16x32_f16 v[56:59], v[192:195], v[172:175], v[56:59]
	s_add_u32 m0, s28, 0x0
	v_mfma_f32_16x16x32_f16 v[60:63], v[196:199], v[172:175], v[60:63]
	global_load_lds_dwordx4 v10, s[4:5]
	v_mfma_f32_16x16x32_f16 v[64:67], v[200:203], v[172:175], v[64:67]
	v_mfma_f32_16x16x32_f16 v[68:71], v[204:207], v[172:175], v[68:71]
	v_mfma_f32_16x16x32_f16 v[72:75], v[192:195], v[176:179], v[72:75]
	v_mfma_f32_16x16x32_f16 v[76:79], v[196:199], v[176:179], v[76:79]
	s_add_u32 m0, s28, 0x2000
	v_mfma_f32_16x16x32_f16 v[80:83], v[200:203], v[176:179], v[80:83]
	global_load_lds_dwordx4 v11, s[4:5]
	v_mfma_f32_16x16x32_f16 v[84:87], v[204:207], v[176:179], v[84:87]
	v_mfma_f32_16x16x32_f16 v[88:91], v[192:195], v[180:183], v[88:91]
	v_mfma_f32_16x16x32_f16 v[92:95], v[196:199], v[180:183], v[92:95]
	v_mfma_f32_16x16x32_f16 v[96:99], v[200:203], v[180:183], v[96:99]
	s_add_u32 m0, s28, 0x4000
	v_mfma_f32_16x16x32_f16 v[100:103], v[204:207], v[180:183], v[100:103]
	global_load_lds_dwordx4 v12, s[4:5]
	v_mfma_f32_16x16x32_f16 v[104:107], v[192:195], v[184:187], v[104:107]
	v_mfma_f32_16x16x32_f16 v[108:111], v[196:199], v[184:187], v[108:111]
	v_mfma_f32_16x16x32_f16 v[112:115], v[200:203], v[184:187], v[112:115]
	v_mfma_f32_16x16x32_f16 v[116:119], v[204:207], v[184:187], v[116:119]
	s_add_u32 m0, s28, 0x6000
	v_mfma_f32_16x16x32_f16 v[120:123], v[192:195], v[188:191], v[120:123]
	global_load_lds_dwordx4 v13, s[4:5]
	v_mfma_f32_16x16x32_f16 v[124:127], v[196:199], v[188:191], v[124:127]
	v_mfma_f32_16x16x32_f16 v[128:131], v[200:203], v[188:191], v[128:131]
	v_mfma_f32_16x16x32_f16 v[132:135], v[204:207], v[188:191], v[132:135]
	s_waitcnt lgkmcnt(6)
	ds_read_b128 v[172:175], v16 offset:53248
	ds_read_b128 v[192:195], v18 offset:53248
	ds_read_b128 v[196:199], v18 offset:55296
	ds_read_b128 v[200:203], v18 offset:57344
	ds_read_b128 v[204:207], v18 offset:59392
	ds_read_b128 v[176:179], v16 offset:55296
	ds_read_b128 v[180:183], v16 offset:57344
	ds_read_b128 v[184:187], v16 offset:59392
	ds_read_b128 v[188:191], v16 offset:61440
	s_waitcnt lgkmcnt(9)
	v_mfma_f32_16x16x32_f16 v[56:59], v[156:159], v[136:139], v[56:59]
	s_add_u32 m0, s28, 0x8000
	v_mfma_f32_16x16x32_f16 v[60:63], v[160:163], v[136:139], v[60:63]
	global_load_lds_dwordx4 v14, s[4:5]
	s_add_u32 s4, s4, s20
	s_addc_u32 s5, s5, 0
	v_mfma_f32_16x16x32_f16 v[64:67], v[164:167], v[136:139], v[64:67]
	v_mfma_f32_16x16x32_f16 v[68:71], v[168:171], v[136:139], v[68:71]
	v_mfma_f32_16x16x32_f16 v[72:75], v[156:159], v[140:143], v[72:75]
	v_mfma_f32_16x16x32_f16 v[76:79], v[160:163], v[140:143], v[76:79]
	v_mfma_f32_16x16x32_f16 v[80:83], v[164:167], v[140:143], v[80:83]
	s_add_u32 m0, s28, 0x9000
	v_mfma_f32_16x16x32_f16 v[84:87], v[168:171], v[140:143], v[84:87]
	global_load_lds_dwordx4 v10, s[6:7]
	v_mfma_f32_16x16x32_f16 v[88:91], v[156:159], v[144:147], v[88:91]
	v_mfma_f32_16x16x32_f16 v[92:95], v[160:163], v[144:147], v[92:95]
	v_mfma_f32_16x16x32_f16 v[96:99], v[164:167], v[144:147], v[96:99]
	v_mfma_f32_16x16x32_f16 v[100:103], v[168:171], v[144:147], v[100:103]
	v_mfma_f32_16x16x32_f16 v[104:107], v[156:159], v[148:151], v[104:107]
	v_mfma_f32_16x16x32_f16 v[108:111], v[160:163], v[148:151], v[108:111]
	s_add_u32 m0, s28, 0xb000
	v_mfma_f32_16x16x32_f16 v[112:115], v[164:167], v[148:151], v[112:115]
	global_load_lds_dwordx4 v11, s[6:7]
	s_add_u32 s6, s6, s20
	s_addc_u32 s7, s7, 0
	v_mfma_f32_16x16x32_f16 v[116:119], v[168:171], v[148:151], v[116:119]
	v_mfma_f32_16x16x32_f16 v[120:123], v[156:159], v[152:155], v[120:123]
	v_mfma_f32_16x16x32_f16 v[124:127], v[160:163], v[152:155], v[124:127]
	v_mfma_f32_16x16x32_f16 v[128:131], v[164:167], v[152:155], v[128:131]
	v_mfma_f32_16x16x32_f16 v[132:135], v[168:171], v[152:155], v[132:135]
	s_waitcnt vmcnt(7) lgkmcnt(0)
	s_barrier
	s_waitcnt lgkmcnt(6)
	ds_read_b128 v[136:139], v19
	ds_read_b128 v[156:159], v21
	ds_read_b128 v[160:163], v21 offset:2048
	ds_read_b128 v[164:167], v21 offset:4096
	ds_read_b128 v[168:171], v21 offset:6144
	ds_read_b128 v[140:143], v19 offset:2048
	ds_read_b128 v[144:147], v19 offset:4096
	ds_read_b128 v[148:151], v19 offset:6144
	ds_read_b128 v[152:155], v19 offset:8192
	s_waitcnt lgkmcnt(9)
	v_mfma_f32_16x16x32_f16 v[56:59], v[192:195], v[172:175], v[56:59]
	s_add_u32 m0, s28, 0xd000
	v_mfma_f32_16x16x32_f16 v[60:63], v[196:199], v[172:175], v[60:63]
	global_load_lds_dwordx4 v10, s[4:5]
	v_mfma_f32_16x16x32_f16 v[64:67], v[200:203], v[172:175], v[64:67]
	v_mfma_f32_16x16x32_f16 v[68:71], v[204:207], v[172:175], v[68:71]
	v_mfma_f32_16x16x32_f16 v[72:75], v[192:195], v[176:179], v[72:75]
	v_mfma_f32_16x16x32_f16 v[76:79], v[196:199], v[176:179], v[76:79]
	s_add_u32 m0, s28, 0xf000
	v_mfma_f32_16x16x32_f16 v[80:83], v[200:203], v[176:179], v[80:83]
	global_load_lds_dwordx4 v11, s[4:5]
	v_mfma_f32_16x16x32_f16 v[84:87], v[204:207], v[176:179], v[84:87]
	v_mfma_f32_16x16x32_f16 v[88:91], v[192:195], v[180:183], v[88:91]
	v_mfma_f32_16x16x32_f16 v[92:95], v[196:199], v[180:183], v[92:95]
	v_mfma_f32_16x16x32_f16 v[96:99], v[200:203], v[180:183], v[96:99]
	s_add_u32 m0, s28, 0x11000
	v_mfma_f32_16x16x32_f16 v[100:103], v[204:207], v[180:183], v[100:103]
	global_load_lds_dwordx4 v12, s[4:5]
	v_mfma_f32_16x16x32_f16 v[104:107], v[192:195], v[184:187], v[104:107]
	v_mfma_f32_16x16x32_f16 v[108:111], v[196:199], v[184:187], v[108:111]
	v_mfma_f32_16x16x32_f16 v[112:115], v[200:203], v[184:187], v[112:115]
	v_mfma_f32_16x16x32_f16 v[116:119], v[204:207], v[184:187], v[116:119]
	s_add_u32 m0, s28, 0x13000
	v_mfma_f32_16x16x32_f16 v[120:123], v[192:195], v[188:191], v[120:123]
	global_load_lds_dwordx4 v13, s[4:5]
	v_mfma_f32_16x16x32_f16 v[124:127], v[196:199], v[188:191], v[124:127]
	v_mfma_f32_16x16x32_f16 v[128:131], v[200:203], v[188:191], v[128:131]
	v_mfma_f32_16x16x32_f16 v[132:135], v[204:207], v[188:191], v[132:135]
	s_waitcnt lgkmcnt(6)
	ds_read_b128 v[172:175], v20
	ds_read_b128 v[192:195], v22
	ds_read_b128 v[196:199], v22 offset:2048
	ds_read_b128 v[200:203], v22 offset:4096
	ds_read_b128 v[204:207], v22 offset:6144
	ds_read_b128 v[176:179], v20 offset:2048
	ds_read_b128 v[180:183], v20 offset:4096
	ds_read_b128 v[184:187], v20 offset:6144
	ds_read_b128 v[188:191], v20 offset:8192
	s_waitcnt lgkmcnt(9)
	v_mfma_f32_16x16x32_f16 v[56:59], v[156:159], v[136:139], v[56:59]
	s_add_u32 m0, s28, 0x15000
	v_mfma_f32_16x16x32_f16 v[60:63], v[160:163], v[136:139], v[60:63]
	global_load_lds_dwordx4 v14, s[4:5]
	s_add_u32 s4, s4, s20
	s_addc_u32 s5, s5, 0
	v_mfma_f32_16x16x32_f16 v[64:67], v[164:167], v[136:139], v[64:67]
	v_mfma_f32_16x16x32_f16 v[68:71], v[168:171], v[136:139], v[68:71]
	v_mfma_f32_16x16x32_f16 v[72:75], v[156:159], v[140:143], v[72:75]
	v_mfma_f32_16x16x32_f16 v[76:79], v[160:163], v[140:143], v[76:79]
	v_mfma_f32_16x16x32_f16 v[80:83], v[164:167], v[140:143], v[80:83]
	s_add_u32 m0, s28, 0x16000
	v_mfma_f32_16x16x32_f16 v[84:87], v[168:171], v[140:143], v[84:87]
	global_load_lds_dwordx4 v10, s[6:7]
	v_mfma_f32_16x16x32_f16 v[88:91], v[156:159], v[144:147], v[88:91]
	v_mfma_f32_16x16x32_f16 v[92:95], v[160:163], v[144:147], v[92:95]
	v_mfma_f32_16x16x32_f16 v[96:99], v[164:167], v[144:147], v[96:99]
	v_mfma_f32_16x16x32_f16 v[100:103], v[168:171], v[144:147], v[100:103]
	v_mfma_f32_16x16x32_f16 v[104:107], v[156:159], v[148:151], v[104:107]
	v_mfma_f32_16x16x32_f16 v[108:111], v[160:163], v[148:151], v[108:111]
	s_add_u32 m0, s28, 0x18000
	v_mfma_f32_16x16x32_f16 v[112:115], v[164:167], v[148:151], v[112:115]
	global_load_lds_dwordx4 v11, s[6:7]
	s_add_u32 s6, s6, s20
	s_addc_u32 s7, s7, 0
	v_mfma_f32_16x16x32_f16 v[116:119], v[168:171], v[148:151], v[116:119]
	v_mfma_f32_16x16x32_f16 v[120:123], v[156:159], v[152:155], v[120:123]
	v_mfma_f32_16x16x32_f16 v[124:127], v[160:163], v[152:155], v[124:127]
	v_mfma_f32_16x16x32_f16 v[128:131], v[164:167], v[152:155], v[128:131]
	v_mfma_f32_16x16x32_f16 v[132:135], v[168:171], v[152:155], v[132:135]
	s_waitcnt vmcnt(7) lgkmcnt(0)
	s_barrier
	s_waitcnt lgkmcnt(6)
	ds_read_b128 v[136:139], v15
	ds_read_b128 v[156:159], v17
	ds_read_b128 v[160:163], v17 offset:2048
	ds_read_b128 v[164:167], v17 offset:4096
	ds_read_b128 v[168:171], v17 offset:6144
	ds_read_b128 v[140:143], v15 offset:2048
	ds_read_b128 v[144:147], v15 offset:4096
	ds_read_b128 v[148:151], v15 offset:6144
	ds_read_b128 v[152:155], v15 offset:8192
	s_waitcnt lgkmcnt(9)
	v_mfma_f32_16x16x32_f16 v[56:59], v[192:195], v[172:175], v[56:59]
	s_add_u32 m0, s28, 0x1a000
	v_mfma_f32_16x16x32_f16 v[60:63], v[196:199], v[172:175], v[60:63]
	global_load_lds_dwordx4 v10, s[4:5]
	v_mfma_f32_16x16x32_f16 v[64:67], v[200:203], v[172:175], v[64:67]
	v_mfma_f32_16x16x32_f16 v[68:71], v[204:207], v[172:175], v[68:71]
	v_mfma_f32_16x16x32_f16 v[72:75], v[192:195], v[176:179], v[72:75]
	v_mfma_f32_16x16x32_f16 v[76:79], v[196:199], v[176:179], v[76:79]
	s_add_u32 m0, s28, 0x1c000
	v_mfma_f32_16x16x32_f16 v[80:83], v[200:203], v[176:179], v[80:83]
	global_load_lds_dwordx4 v11, s[4:5]
	v_mfma_f32_16x16x32_f16 v[84:87], v[204:207], v[176:179], v[84:87]
	v_mfma_f32_16x16x32_f16 v[88:91], v[192:195], v[180:183], v[88:91]
	v_mfma_f32_16x16x32_f16 v[92:95], v[196:199], v[180:183], v[92:95]
	v_mfma_f32_16x16x32_f16 v[96:99], v[200:203], v[180:183], v[96:99]
	s_add_u32 m0, s28, 0x1e000
	v_mfma_f32_16x16x32_f16 v[100:103], v[204:207], v[180:183], v[100:103]
	global_load_lds_dwordx4 v12, s[4:5]
	v_mfma_f32_16x16x32_f16 v[104:107], v[192:195], v[184:187], v[104:107]
	v_mfma_f32_16x16x32_f16 v[108:111], v[196:199], v[184:187], v[108:111]
	v_mfma_f32_16x16x32_f16 v[112:115], v[200:203], v[184:187], v[112:115]
	v_mfma_f32_16x16x32_f16 v[116:119], v[204:207], v[184:187], v[116:119]
	s_add_u32 m0, s28, 0x20000
	v_mfma_f32_16x16x32_f16 v[120:123], v[192:195], v[188:191], v[120:123]
	global_load_lds_dwordx4 v13, s[4:5]
	v_mfma_f32_16x16x32_f16 v[124:127], v[196:199], v[188:191], v[124:127]
	v_mfma_f32_16x16x32_f16 v[128:131], v[200:203], v[188:191], v[128:131]
	v_mfma_f32_16x16x32_f16 v[132:135], v[204:207], v[188:191], v[132:135]
	s_waitcnt lgkmcnt(6)
	ds_read_b128 v[172:175], v16
	ds_read_b128 v[192:195], v18
	ds_read_b128 v[196:199], v18 offset:2048
	ds_read_b128 v[200:203], v18 offset:4096
	ds_read_b128 v[204:207], v18 offset:6144
	ds_read_b128 v[176:179], v16 offset:2048
	ds_read_b128 v[180:183], v16 offset:4096
	ds_read_b128 v[184:187], v16 offset:6144
	ds_read_b128 v[188:191], v16 offset:8192
	s_waitcnt lgkmcnt(9)
	v_mfma_f32_16x16x32_f16 v[56:59], v[156:159], v[136:139], v[56:59]
	s_add_u32 m0, s28, 0x22000
	v_mfma_f32_16x16x32_f16 v[60:63], v[160:163], v[136:139], v[60:63]
	global_load_lds_dwordx4 v14, s[4:5]
	s_add_u32 s4, s4, s20
	s_addc_u32 s5, s5, 0
	v_mfma_f32_16x16x32_f16 v[64:67], v[164:167], v[136:139], v[64:67]
	v_mfma_f32_16x16x32_f16 v[68:71], v[168:171], v[136:139], v[68:71]
	v_mfma_f32_16x16x32_f16 v[72:75], v[156:159], v[140:143], v[72:75]
	v_mfma_f32_16x16x32_f16 v[76:79], v[160:163], v[140:143], v[76:79]
	v_mfma_f32_16x16x32_f16 v[80:83], v[164:167], v[140:143], v[80:83]
	s_add_u32 m0, s28, 0x23000
	v_mfma_f32_16x16x32_f16 v[84:87], v[168:171], v[140:143], v[84:87]
	global_load_lds_dwordx4 v10, s[6:7]
	v_mfma_f32_16x16x32_f16 v[88:91], v[156:159], v[144:147], v[88:91]
	v_mfma_f32_16x16x32_f16 v[92:95], v[160:163], v[144:147], v[92:95]
	v_mfma_f32_16x16x32_f16 v[96:99], v[164:167], v[144:147], v[96:99]
	v_mfma_f32_16x16x32_f16 v[100:103], v[168:171], v[144:147], v[100:103]
	v_mfma_f32_16x16x32_f16 v[104:107], v[156:159], v[148:151], v[104:107]
	v_mfma_f32_16x16x32_f16 v[108:111], v[160:163], v[148:151], v[108:111]
	s_add_u32 m0, s28, 0x25000
	v_mfma_f32_16x16x32_f16 v[112:115], v[164:167], v[148:151], v[112:115]
	global_load_lds_dwordx4 v11, s[6:7]
	s_add_u32 s6, s6, s20
	s_addc_u32 s7, s7, 0
	v_mfma_f32_16x16x32_f16 v[116:119], v[168:171], v[148:151], v[116:119]
	v_mfma_f32_16x16x32_f16 v[120:123], v[156:159], v[152:155], v[120:123]
	v_mfma_f32_16x16x32_f16 v[124:127], v[160:163], v[152:155], v[124:127]
	v_mfma_f32_16x16x32_f16 v[128:131], v[164:167], v[152:155], v[128:131]
	v_mfma_f32_16x16x32_f16 v[132:135], v[168:171], v[152:155], v[132:135]
	s_waitcnt vmcnt(7) lgkmcnt(0)
	s_barrier
	s_waitcnt lgkmcnt(6)
	ds_read_b128 v[136:139], v15 offset:53248
	ds_read_b128 v[156:159], v17 offset:53248
	ds_read_b128 v[160:163], v17 offset:55296
	ds_read_b128 v[164:167], v17 offset:57344
	ds_read_b128 v[168:171], v17 offset:59392
	ds_read_b128 v[140:143], v15 offset:55296
	ds_read_b128 v[144:147], v15 offset:57344
	ds_read_b128 v[148:151], v15 offset:59392
	ds_read_b128 v[152:155], v15 offset:61440
	s_waitcnt lgkmcnt(9)
	v_mfma_f32_16x16x32_f16 v[56:59], v[192:195], v[172:175], v[56:59]
	s_add_u32 m0, s28, 0x0
	v_mfma_f32_16x16x32_f16 v[60:63], v[196:199], v[172:175], v[60:63]
	global_load_lds_dwordx4 v10, s[4:5]
	v_mfma_f32_16x16x32_f16 v[64:67], v[200:203], v[172:175], v[64:67]
	v_mfma_f32_16x16x32_f16 v[68:71], v[204:207], v[172:175], v[68:71]
	v_mfma_f32_16x16x32_f16 v[72:75], v[192:195], v[176:179], v[72:75]
	v_mfma_f32_16x16x32_f16 v[76:79], v[196:199], v[176:179], v[76:79]
	s_add_u32 m0, s28, 0x2000
	v_mfma_f32_16x16x32_f16 v[80:83], v[200:203], v[176:179], v[80:83]
	global_load_lds_dwordx4 v11, s[4:5]
	v_mfma_f32_16x16x32_f16 v[84:87], v[204:207], v[176:179], v[84:87]
	v_mfma_f32_16x16x32_f16 v[88:91], v[192:195], v[180:183], v[88:91]
	v_mfma_f32_16x16x32_f16 v[92:95], v[196:199], v[180:183], v[92:95]
	v_mfma_f32_16x16x32_f16 v[96:99], v[200:203], v[180:183], v[96:99]
	s_add_u32 m0, s28, 0x4000
	v_mfma_f32_16x16x32_f16 v[100:103], v[204:207], v[180:183], v[100:103]
	global_load_lds_dwordx4 v12, s[4:5]
	v_mfma_f32_16x16x32_f16 v[104:107], v[192:195], v[184:187], v[104:107]
	v_mfma_f32_16x16x32_f16 v[108:111], v[196:199], v[184:187], v[108:111]
	v_mfma_f32_16x16x32_f16 v[112:115], v[200:203], v[184:187], v[112:115]
	v_mfma_f32_16x16x32_f16 v[116:119], v[204:207], v[184:187], v[116:119]
	s_add_u32 m0, s28, 0x6000
	v_mfma_f32_16x16x32_f16 v[120:123], v[192:195], v[188:191], v[120:123]
	global_load_lds_dwordx4 v13, s[4:5]
	v_mfma_f32_16x16x32_f16 v[124:127], v[196:199], v[188:191], v[124:127]
	v_mfma_f32_16x16x32_f16 v[128:131], v[200:203], v[188:191], v[128:131]
	v_mfma_f32_16x16x32_f16 v[132:135], v[204:207], v[188:191], v[132:135]
	s_waitcnt lgkmcnt(6)
	ds_read_b128 v[172:175], v16 offset:53248
	ds_read_b128 v[192:195], v18 offset:53248
	ds_read_b128 v[196:199], v18 offset:55296
	ds_read_b128 v[200:203], v18 offset:57344
	ds_read_b128 v[204:207], v18 offset:59392
	ds_read_b128 v[176:179], v16 offset:55296
	ds_read_b128 v[180:183], v16 offset:57344
	ds_read_b128 v[184:187], v16 offset:59392
	ds_read_b128 v[188:191], v16 offset:61440
	s_waitcnt lgkmcnt(9)
	v_mfma_f32_16x16x32_f16 v[56:59], v[156:159], v[136:139], v[56:59]
	s_add_u32 m0, s28, 0x8000
	v_mfma_f32_16x16x32_f16 v[60:63], v[160:163], v[136:139], v[60:63]
	global_load_lds_dwordx4 v14, s[4:5]
	s_add_u32 s4, s4, s20
	s_addc_u32 s5, s5, 0
	v_mfma_f32_16x16x32_f16 v[64:67], v[164:167], v[136:139], v[64:67]
	v_mfma_f32_16x16x32_f16 v[68:71], v[168:171], v[136:139], v[68:71]
	v_mfma_f32_16x16x32_f16 v[72:75], v[156:159], v[140:143], v[72:75]
	v_mfma_f32_16x16x32_f16 v[76:79], v[160:163], v[140:143], v[76:79]
	v_mfma_f32_16x16x32_f16 v[80:83], v[164:167], v[140:143], v[80:83]
	s_add_u32 m0, s28, 0x9000
	v_mfma_f32_16x16x32_f16 v[84:87], v[168:171], v[140:143], v[84:87]
	global_load_lds_dwordx4 v10, s[6:7]
	v_mfma_f32_16x16x32_f16 v[88:91], v[156:159], v[144:147], v[88:91]
	v_mfma_f32_16x16x32_f16 v[92:95], v[160:163], v[144:147], v[92:95]
	v_mfma_f32_16x16x32_f16 v[96:99], v[164:167], v[144:147], v[96:99]
	v_mfma_f32_16x16x32_f16 v[100:103], v[168:171], v[144:147], v[100:103]
	v_mfma_f32_16x16x32_f16 v[104:107], v[156:159], v[148:151], v[104:107]
	v_mfma_f32_16x16x32_f16 v[108:111], v[160:163], v[148:151], v[108:111]
	s_add_u32 m0, s28, 0xb000
	v_mfma_f32_16x16x32_f16 v[112:115], v[164:167], v[148:151], v[112:115]
	global_load_lds_dwordx4 v11, s[6:7]
	s_add_u32 s6, s6, s20
	s_addc_u32 s7, s7, 0
	v_mfma_f32_16x16x32_f16 v[116:119], v[168:171], v[148:151], v[116:119]
	v_mfma_f32_16x16x32_f16 v[120:123], v[156:159], v[152:155], v[120:123]
	v_mfma_f32_16x16x32_f16 v[124:127], v[160:163], v[152:155], v[124:127]
	v_mfma_f32_16x16x32_f16 v[128:131], v[164:167], v[152:155], v[128:131]
	v_mfma_f32_16x16x32_f16 v[132:135], v[168:171], v[152:155], v[132:135]
	s_waitcnt vmcnt(7) lgkmcnt(0)
	s_barrier
	s_waitcnt lgkmcnt(6)
	ds_read_b128 v[136:139], v19
	ds_read_b128 v[156:159], v21
	ds_read_b128 v[160:163], v21 offset:2048
	ds_read_b128 v[164:167], v21 offset:4096
	ds_read_b128 v[168:171], v21 offset:6144
	ds_read_b128 v[140:143], v19 offset:2048
	ds_read_b128 v[144:147], v19 offset:4096
	ds_read_b128 v[148:151], v19 offset:6144
	ds_read_b128 v[152:155], v19 offset:8192
	s_waitcnt lgkmcnt(9)
	v_mfma_f32_16x16x32_f16 v[56:59], v[192:195], v[172:175], v[56:59]
	s_add_u32 m0, s28, 0xd000
	v_mfma_f32_16x16x32_f16 v[60:63], v[196:199], v[172:175], v[60:63]
	global_load_lds_dwordx4 v10, s[4:5]
	v_mfma_f32_16x16x32_f16 v[64:67], v[200:203], v[172:175], v[64:67]
	v_mfma_f32_16x16x32_f16 v[68:71], v[204:207], v[172:175], v[68:71]
	v_mfma_f32_16x16x32_f16 v[72:75], v[192:195], v[176:179], v[72:75]
	v_mfma_f32_16x16x32_f16 v[76:79], v[196:199], v[176:179], v[76:79]
	s_add_u32 m0, s28, 0xf000
	v_mfma_f32_16x16x32_f16 v[80:83], v[200:203], v[176:179], v[80:83]
	global_load_lds_dwordx4 v11, s[4:5]
	v_mfma_f32_16x16x32_f16 v[84:87], v[204:207], v[176:179], v[84:87]
	v_mfma_f32_16x16x32_f16 v[88:91], v[192:195], v[180:183], v[88:91]
	v_mfma_f32_16x16x32_f16 v[92:95], v[196:199], v[180:183], v[92:95]
	v_mfma_f32_16x16x32_f16 v[96:99], v[200:203], v[180:183], v[96:99]
	s_add_u32 m0, s28, 0x11000
	v_mfma_f32_16x16x32_f16 v[100:103], v[204:207], v[180:183], v[100:103]
	global_load_lds_dwordx4 v12, s[4:5]
	v_mfma_f32_16x16x32_f16 v[104:107], v[192:195], v[184:187], v[104:107]
	v_mfma_f32_16x16x32_f16 v[108:111], v[196:199], v[184:187], v[108:111]
	v_mfma_f32_16x16x32_f16 v[112:115], v[200:203], v[184:187], v[112:115]
	v_mfma_f32_16x16x32_f16 v[116:119], v[204:207], v[184:187], v[116:119]
	s_add_u32 m0, s28, 0x13000
	v_mfma_f32_16x16x32_f16 v[120:123], v[192:195], v[188:191], v[120:123]
	global_load_lds_dwordx4 v13, s[4:5]
	v_mfma_f32_16x16x32_f16 v[124:127], v[196:199], v[188:191], v[124:127]
	v_mfma_f32_16x16x32_f16 v[128:131], v[200:203], v[188:191], v[128:131]
	v_mfma_f32_16x16x32_f16 v[132:135], v[204:207], v[188:191], v[132:135]
	s_waitcnt lgkmcnt(6)
	ds_read_b128 v[172:175], v20
	ds_read_b128 v[192:195], v22
	ds_read_b128 v[196:199], v22 offset:2048
	ds_read_b128 v[200:203], v22 offset:4096
	ds_read_b128 v[204:207], v22 offset:6144
	ds_read_b128 v[176:179], v20 offset:2048
	ds_read_b128 v[180:183], v20 offset:4096
	ds_read_b128 v[184:187], v20 offset:6144
	ds_read_b128 v[188:191], v20 offset:8192
	s_waitcnt lgkmcnt(9)
	v_mfma_f32_16x16x32_f16 v[56:59], v[156:159], v[136:139], v[56:59]
	s_add_u32 m0, s28, 0x15000
	v_mfma_f32_16x16x32_f16 v[60:63], v[160:163], v[136:139], v[60:63]
	global_load_lds_dwordx4 v14, s[4:5]
	s_add_u32 s4, s4, s20
	s_addc_u32 s5, s5, 0
	v_mfma_f32_16x16x32_f16 v[64:67], v[164:167], v[136:139], v[64:67]
	v_mfma_f32_16x16x32_f16 v[68:71], v[168:171], v[136:139], v[68:71]
	v_mfma_f32_16x16x32_f16 v[72:75], v[156:159], v[140:143], v[72:75]
	v_mfma_f32_16x16x32_f16 v[76:79], v[160:163], v[140:143], v[76:79]
	v_mfma_f32_16x16x32_f16 v[80:83], v[164:167], v[140:143], v[80:83]
	s_add_u32 m0, s28, 0x16000
	v_mfma_f32_16x16x32_f16 v[84:87], v[168:171], v[140:143], v[84:87]
	global_load_lds_dwordx4 v10, s[6:7]
	v_mfma_f32_16x16x32_f16 v[88:91], v[156:159], v[144:147], v[88:91]
	v_mfma_f32_16x16x32_f16 v[92:95], v[160:163], v[144:147], v[92:95]
	v_mfma_f32_16x16x32_f16 v[96:99], v[164:167], v[144:147], v[96:99]
	v_mfma_f32_16x16x32_f16 v[100:103], v[168:171], v[144:147], v[100:103]
	v_mfma_f32_16x16x32_f16 v[104:107], v[156:159], v[148:151], v[104:107]
	v_mfma_f32_16x16x32_f16 v[108:111], v[160:163], v[148:151], v[108:111]
	s_add_u32 m0, s28, 0x18000
	v_mfma_f32_16x16x32_f16 v[112:115], v[164:167], v[148:151], v[112:115]
	global_load_lds_dwordx4 v11, s[6:7]
	s_add_u32 s6, s6, s20
	s_addc_u32 s7, s7, 0
	v_mfma_f32_16x16x32_f16 v[116:119], v[168:171], v[148:151], v[116:119]
	v_mfma_f32_16x16x32_f16 v[120:123], v[156:159], v[152:155], v[120:123]
	v_mfma_f32_16x16x32_f16 v[124:127], v[160:163], v[152:155], v[124:127]
	v_mfma_f32_16x16x32_f16 v[128:131], v[164:167], v[152:155], v[128:131]
	v_mfma_f32_16x16x32_f16 v[132:135], v[168:171], v[152:155], v[132:135]
	s_waitcnt vmcnt(7) lgkmcnt(0)
	s_barrier
	s_waitcnt lgkmcnt(6)
	ds_read_b128 v[136:139], v15
	ds_read_b128 v[156:159], v17
	ds_read_b128 v[160:163], v17 offset:2048
	ds_read_b128 v[164:167], v17 offset:4096
	ds_read_b128 v[168:171], v17 offset:6144
	ds_read_b128 v[140:143], v15 offset:2048
	ds_read_b128 v[144:147], v15 offset:4096
	ds_read_b128 v[148:151], v15 offset:6144
	ds_read_b128 v[152:155], v15 offset:8192
	s_waitcnt lgkmcnt(9)
	v_mfma_f32_16x16x32_f16 v[56:59], v[192:195], v[172:175], v[56:59]
	s_add_u32 m0, s28, 0x1a000
	v_mfma_f32_16x16x32_f16 v[60:63], v[196:199], v[172:175], v[60:63]
	global_load_lds_dwordx4 v10, s[4:5]
	v_mfma_f32_16x16x32_f16 v[64:67], v[200:203], v[172:175], v[64:67]
	v_mfma_f32_16x16x32_f16 v[68:71], v[204:207], v[172:175], v[68:71]
	v_mfma_f32_16x16x32_f16 v[72:75], v[192:195], v[176:179], v[72:75]
	v_mfma_f32_16x16x32_f16 v[76:79], v[196:199], v[176:179], v[76:79]
	s_add_u32 m0, s28, 0x1c000
	v_mfma_f32_16x16x32_f16 v[80:83], v[200:203], v[176:179], v[80:83]
	global_load_lds_dwordx4 v11, s[4:5]
	v_mfma_f32_16x16x32_f16 v[84:87], v[204:207], v[176:179], v[84:87]
	v_mfma_f32_16x16x32_f16 v[88:91], v[192:195], v[180:183], v[88:91]
	v_mfma_f32_16x16x32_f16 v[92:95], v[196:199], v[180:183], v[92:95]
	v_mfma_f32_16x16x32_f16 v[96:99], v[200:203], v[180:183], v[96:99]
	s_add_u32 m0, s28, 0x1e000
	v_mfma_f32_16x16x32_f16 v[100:103], v[204:207], v[180:183], v[100:103]
	global_load_lds_dwordx4 v12, s[4:5]
	v_mfma_f32_16x16x32_f16 v[104:107], v[192:195], v[184:187], v[104:107]
	v_mfma_f32_16x16x32_f16 v[108:111], v[196:199], v[184:187], v[108:111]
	v_mfma_f32_16x16x32_f16 v[112:115], v[200:203], v[184:187], v[112:115]
	v_mfma_f32_16x16x32_f16 v[116:119], v[204:207], v[184:187], v[116:119]
	s_add_u32 m0, s28, 0x20000
	v_mfma_f32_16x16x32_f16 v[120:123], v[192:195], v[188:191], v[120:123]
	global_load_lds_dwordx4 v13, s[4:5]
	v_mfma_f32_16x16x32_f16 v[124:127], v[196:199], v[188:191], v[124:127]
	v_mfma_f32_16x16x32_f16 v[128:131], v[200:203], v[188:191], v[128:131]
	v_mfma_f32_16x16x32_f16 v[132:135], v[204:207], v[188:191], v[132:135]
	s_waitcnt lgkmcnt(6)
	ds_read_b128 v[172:175], v16
	ds_read_b128 v[192:195], v18
	ds_read_b128 v[196:199], v18 offset:2048
	ds_read_b128 v[200:203], v18 offset:4096
	ds_read_b128 v[204:207], v18 offset:6144
	ds_read_b128 v[176:179], v16 offset:2048
	ds_read_b128 v[180:183], v16 offset:4096
	ds_read_b128 v[184:187], v16 offset:6144
	ds_read_b128 v[188:191], v16 offset:8192
	s_waitcnt lgkmcnt(9)
	v_mfma_f32_16x16x32_f16 v[56:59], v[156:159], v[136:139], v[56:59]
	s_add_u32 m0, s28, 0x22000
	v_mfma_f32_16x16x32_f16 v[60:63], v[160:163], v[136:139], v[60:63]
	global_load_lds_dwordx4 v14, s[4:5]
	s_add_u32 s4, s4, s20
	s_addc_u32 s5, s5, 0
	v_mfma_f32_16x16x32_f16 v[64:67], v[164:167], v[136:139], v[64:67]
	v_mfma_f32_16x16x32_f16 v[68:71], v[168:171], v[136:139], v[68:71]
	v_mfma_f32_16x16x32_f16 v[72:75], v[156:159], v[140:143], v[72:75]
	v_mfma_f32_16x16x32_f16 v[76:79], v[160:163], v[140:143], v[76:79]
	v_mfma_f32_16x16x32_f16 v[80:83], v[164:167], v[140:143], v[80:83]
	s_add_u32 m0, s28, 0x23000
	v_mfma_f32_16x16x32_f16 v[84:87], v[168:171], v[140:143], v[84:87]
	global_load_lds_dwordx4 v10, s[6:7]
	v_mfma_f32_16x16x32_f16 v[88:91], v[156:159], v[144:147], v[88:91]
	v_mfma_f32_16x16x32_f16 v[92:95], v[160:163], v[144:147], v[92:95]
	v_mfma_f32_16x16x32_f16 v[96:99], v[164:167], v[144:147], v[96:99]
	v_mfma_f32_16x16x32_f16 v[100:103], v[168:171], v[144:147], v[100:103]
	v_mfma_f32_16x16x32_f16 v[104:107], v[156:159], v[148:151], v[104:107]
	v_mfma_f32_16x16x32_f16 v[108:111], v[160:163], v[148:151], v[108:111]
	s_add_u32 m0, s28, 0x25000
	v_mfma_f32_16x16x32_f16 v[112:115], v[164:167], v[148:151], v[112:115]
	global_load_lds_dwordx4 v11, s[6:7]
	s_add_u32 s6, s6, s20
	s_addc_u32 s7, s7, 0
	v_mfma_f32_16x16x32_f16 v[116:119], v[168:171], v[148:151], v[116:119]
	v_mfma_f32_16x16x32_f16 v[120:123], v[156:159], v[152:155], v[120:123]
	v_mfma_f32_16x16x32_f16 v[124:127], v[160:163], v[152:155], v[124:127]
	v_mfma_f32_16x16x32_f16 v[128:131], v[164:167], v[152:155], v[128:131]
	v_mfma_f32_16x16x32_f16 v[132:135], v[168:171], v[152:155], v[132:135]
	s_waitcnt vmcnt(7) lgkmcnt(0)
	s_barrier
	s_waitcnt lgkmcnt(6)
	ds_read_b128 v[136:139], v15 offset:53248
	ds_read_b128 v[156:159], v17 offset:53248
	ds_read_b128 v[160:163], v17 offset:55296
	ds_read_b128 v[164:167], v17 offset:57344
	ds_read_b128 v[168:171], v17 offset:59392
	ds_read_b128 v[140:143], v15 offset:55296
	ds_read_b128 v[144:147], v15 offset:57344
	ds_read_b128 v[148:151], v15 offset:59392
	ds_read_b128 v[152:155], v15 offset:61440
	s_waitcnt lgkmcnt(9)
	v_mfma_f32_16x16x32_f16 v[56:59], v[192:195], v[172:175], v[56:59]
	s_add_u32 m0, s28, 0x0
	v_mfma_f32_16x16x32_f16 v[60:63], v[196:199], v[172:175], v[60:63]
	global_load_lds_dwordx4 v10, s[4:5]
	v_mfma_f32_16x16x32_f16 v[64:67], v[200:203], v[172:175], v[64:67]
	v_mfma_f32_16x16x32_f16 v[68:71], v[204:207], v[172:175], v[68:71]
	v_mfma_f32_16x16x32_f16 v[72:75], v[192:195], v[176:179], v[72:75]
	v_mfma_f32_16x16x32_f16 v[76:79], v[196:199], v[176:179], v[76:79]
	s_add_u32 m0, s28, 0x2000
	v_mfma_f32_16x16x32_f16 v[80:83], v[200:203], v[176:179], v[80:83]
	global_load_lds_dwordx4 v11, s[4:5]
	v_mfma_f32_16x16x32_f16 v[84:87], v[204:207], v[176:179], v[84:87]
	v_mfma_f32_16x16x32_f16 v[88:91], v[192:195], v[180:183], v[88:91]
	v_mfma_f32_16x16x32_f16 v[92:95], v[196:199], v[180:183], v[92:95]
	v_mfma_f32_16x16x32_f16 v[96:99], v[200:203], v[180:183], v[96:99]
	s_add_u32 m0, s28, 0x4000
	v_mfma_f32_16x16x32_f16 v[100:103], v[204:207], v[180:183], v[100:103]
	global_load_lds_dwordx4 v12, s[4:5]
	v_mfma_f32_16x16x32_f16 v[104:107], v[192:195], v[184:187], v[104:107]
	v_mfma_f32_16x16x32_f16 v[108:111], v[196:199], v[184:187], v[108:111]
	v_mfma_f32_16x16x32_f16 v[112:115], v[200:203], v[184:187], v[112:115]
	v_mfma_f32_16x16x32_f16 v[116:119], v[204:207], v[184:187], v[116:119]
	s_add_u32 m0, s28, 0x6000
	v_mfma_f32_16x16x32_f16 v[120:123], v[192:195], v[188:191], v[120:123]
	global_load_lds_dwordx4 v13, s[4:5]
	v_mfma_f32_16x16x32_f16 v[124:127], v[196:199], v[188:191], v[124:127]
	v_mfma_f32_16x16x32_f16 v[128:131], v[200:203], v[188:191], v[128:131]
	v_mfma_f32_16x16x32_f16 v[132:135], v[204:207], v[188:191], v[132:135]
	s_waitcnt lgkmcnt(6)
	ds_read_b128 v[172:175], v16 offset:53248
	ds_read_b128 v[192:195], v18 offset:53248
	ds_read_b128 v[196:199], v18 offset:55296
	ds_read_b128 v[200:203], v18 offset:57344
	ds_read_b128 v[204:207], v18 offset:59392
	ds_read_b128 v[176:179], v16 offset:55296
	ds_read_b128 v[180:183], v16 offset:57344
	ds_read_b128 v[184:187], v16 offset:59392
	ds_read_b128 v[188:191], v16 offset:61440
	s_waitcnt lgkmcnt(9)
	v_mfma_f32_16x16x32_f16 v[56:59], v[156:159], v[136:139], v[56:59]
	s_add_u32 m0, s28, 0x8000
	v_mfma_f32_16x16x32_f16 v[60:63], v[160:163], v[136:139], v[60:63]
	global_load_lds_dwordx4 v14, s[4:5]
	s_add_u32 s4, s4, s20
	s_addc_u32 s5, s5, 0
	v_mfma_f32_16x16x32_f16 v[64:67], v[164:167], v[136:139], v[64:67]
	v_mfma_f32_16x16x32_f16 v[68:71], v[168:171], v[136:139], v[68:71]
	v_mfma_f32_16x16x32_f16 v[72:75], v[156:159], v[140:143], v[72:75]
	v_mfma_f32_16x16x32_f16 v[76:79], v[160:163], v[140:143], v[76:79]
	v_mfma_f32_16x16x32_f16 v[80:83], v[164:167], v[140:143], v[80:83]
	s_add_u32 m0, s28, 0x9000
	v_mfma_f32_16x16x32_f16 v[84:87], v[168:171], v[140:143], v[84:87]
	global_load_lds_dwordx4 v10, s[6:7]
	v_mfma_f32_16x16x32_f16 v[88:91], v[156:159], v[144:147], v[88:91]
	v_mfma_f32_16x16x32_f16 v[92:95], v[160:163], v[144:147], v[92:95]
	v_mfma_f32_16x16x32_f16 v[96:99], v[164:167], v[144:147], v[96:99]
	v_mfma_f32_16x16x32_f16 v[100:103], v[168:171], v[144:147], v[100:103]
	v_mfma_f32_16x16x32_f16 v[104:107], v[156:159], v[148:151], v[104:107]
	v_mfma_f32_16x16x32_f16 v[108:111], v[160:163], v[148:151], v[108:111]
	s_add_u32 m0, s28, 0xb000
	v_mfma_f32_16x16x32_f16 v[112:115], v[164:167], v[148:151], v[112:115]
	global_load_lds_dwordx4 v11, s[6:7]
	s_add_u32 s6, s6, s20
	s_addc_u32 s7, s7, 0
	v_mfma_f32_16x16x32_f16 v[116:119], v[168:171], v[148:151], v[116:119]
	v_mfma_f32_16x16x32_f16 v[120:123], v[156:159], v[152:155], v[120:123]
	v_mfma_f32_16x16x32_f16 v[124:127], v[160:163], v[152:155], v[124:127]
	v_mfma_f32_16x16x32_f16 v[128:131], v[164:167], v[152:155], v[128:131]
	v_mfma_f32_16x16x32_f16 v[132:135], v[168:171], v[152:155], v[132:135]
	s_waitcnt vmcnt(7) lgkmcnt(0)
	s_barrier
	s_waitcnt lgkmcnt(6)
	ds_read_b128 v[136:139], v19
	ds_read_b128 v[156:159], v21
	ds_read_b128 v[160:163], v21 offset:2048
	ds_read_b128 v[164:167], v21 offset:4096
	ds_read_b128 v[168:171], v21 offset:6144
	ds_read_b128 v[140:143], v19 offset:2048
	ds_read_b128 v[144:147], v19 offset:4096
	ds_read_b128 v[148:151], v19 offset:6144
	ds_read_b128 v[152:155], v19 offset:8192
	s_waitcnt lgkmcnt(9)
	v_mfma_f32_16x16x32_f16 v[56:59], v[192:195], v[172:175], v[56:59]
	s_add_u32 m0, s28, 0xd000
	v_mfma_f32_16x16x32_f16 v[60:63], v[196:199], v[172:175], v[60:63]
	global_load_lds_dwordx4 v10, s[4:5]
	v_mfma_f32_16x16x32_f16 v[64:67], v[200:203], v[172:175], v[64:67]
	v_mfma_f32_16x16x32_f16 v[68:71], v[204:207], v[172:175], v[68:71]
	v_mfma_f32_16x16x32_f16 v[72:75], v[192:195], v[176:179], v[72:75]
	v_mfma_f32_16x16x32_f16 v[76:79], v[196:199], v[176:179], v[76:79]
	s_add_u32 m0, s28, 0xf000
	v_mfma_f32_16x16x32_f16 v[80:83], v[200:203], v[176:179], v[80:83]
	global_load_lds_dwordx4 v11, s[4:5]
	v_mfma_f32_16x16x32_f16 v[84:87], v[204:207], v[176:179], v[84:87]
	v_mfma_f32_16x16x32_f16 v[88:91], v[192:195], v[180:183], v[88:91]
	v_mfma_f32_16x16x32_f16 v[92:95], v[196:199], v[180:183], v[92:95]
	v_mfma_f32_16x16x32_f16 v[96:99], v[200:203], v[180:183], v[96:99]
	s_add_u32 m0, s28, 0x11000
	v_mfma_f32_16x16x32_f16 v[100:103], v[204:207], v[180:183], v[100:103]
	global_load_lds_dwordx4 v12, s[4:5]
	v_mfma_f32_16x16x32_f16 v[104:107], v[192:195], v[184:187], v[104:107]
	v_mfma_f32_16x16x32_f16 v[108:111], v[196:199], v[184:187], v[108:111]
	v_mfma_f32_16x16x32_f16 v[112:115], v[200:203], v[184:187], v[112:115]
	v_mfma_f32_16x16x32_f16 v[116:119], v[204:207], v[184:187], v[116:119]
	s_add_u32 m0, s28, 0x13000
	v_mfma_f32_16x16x32_f16 v[120:123], v[192:195], v[188:191], v[120:123]
	global_load_lds_dwordx4 v13, s[4:5]
	v_mfma_f32_16x16x32_f16 v[124:127], v[196:199], v[188:191], v[124:127]
	v_mfma_f32_16x16x32_f16 v[128:131], v[200:203], v[188:191], v[128:131]
	v_mfma_f32_16x16x32_f16 v[132:135], v[204:207], v[188:191], v[132:135]
	s_waitcnt lgkmcnt(6)
	ds_read_b128 v[172:175], v20
	ds_read_b128 v[192:195], v22
	ds_read_b128 v[196:199], v22 offset:2048
	ds_read_b128 v[200:203], v22 offset:4096
	ds_read_b128 v[204:207], v22 offset:6144
	ds_read_b128 v[176:179], v20 offset:2048
	ds_read_b128 v[180:183], v20 offset:4096
	ds_read_b128 v[184:187], v20 offset:6144
	ds_read_b128 v[188:191], v20 offset:8192
	s_waitcnt lgkmcnt(9)
	v_mfma_f32_16x16x32_f16 v[56:59], v[156:159], v[136:139], v[56:59]
	s_add_u32 m0, s28, 0x15000
	v_mfma_f32_16x16x32_f16 v[60:63], v[160:163], v[136:139], v[60:63]
	global_load_lds_dwordx4 v14, s[4:5]
	s_add_u32 s4, s4, s20
	s_addc_u32 s5, s5, 0
	v_mfma_f32_16x16x32_f16 v[64:67], v[164:167], v[136:139], v[64:67]
	v_mfma_f32_16x16x32_f16 v[68:71], v[168:171], v[136:139], v[68:71]
	v_mfma_f32_16x16x32_f16 v[72:75], v[156:159], v[140:143], v[72:75]
	v_mfma_f32_16x16x32_f16 v[76:79], v[160:163], v[140:143], v[76:79]
	v_mfma_f32_16x16x32_f16 v[80:83], v[164:167], v[140:143], v[80:83]
	s_add_u32 m0, s28, 0x16000
	v_mfma_f32_16x16x32_f16 v[84:87], v[168:171], v[140:143], v[84:87]
	global_load_lds_dwordx4 v10, s[6:7]
	v_mfma_f32_16x16x32_f16 v[88:91], v[156:159], v[144:147], v[88:91]
	v_mfma_f32_16x16x32_f16 v[92:95], v[160:163], v[144:147], v[92:95]
	v_mfma_f32_16x16x32_f16 v[96:99], v[164:167], v[144:147], v[96:99]
	v_mfma_f32_16x16x32_f16 v[100:103], v[168:171], v[144:147], v[100:103]
	v_mfma_f32_16x16x32_f16 v[104:107], v[156:159], v[148:151], v[104:107]
	v_mfma_f32_16x16x32_f16 v[108:111], v[160:163], v[148:151], v[108:111]
	s_add_u32 m0, s28, 0x18000
	v_mfma_f32_16x16x32_f16 v[112:115], v[164:167], v[148:151], v[112:115]
	global_load_lds_dwordx4 v11, s[6:7]
	s_add_u32 s6, s6, s20
	s_addc_u32 s7, s7, 0
	v_mfma_f32_16x16x32_f16 v[116:119], v[168:171], v[148:151], v[116:119]
	v_mfma_f32_16x16x32_f16 v[120:123], v[156:159], v[152:155], v[120:123]
	v_mfma_f32_16x16x32_f16 v[124:127], v[160:163], v[152:155], v[124:127]
	v_mfma_f32_16x16x32_f16 v[128:131], v[164:167], v[152:155], v[128:131]
	v_mfma_f32_16x16x32_f16 v[132:135], v[168:171], v[152:155], v[132:135]
	s_waitcnt vmcnt(7) lgkmcnt(0)
	s_barrier
	s_waitcnt lgkmcnt(6)
	ds_read_b128 v[136:139], v15
	ds_read_b128 v[156:159], v17
	ds_read_b128 v[160:163], v17 offset:2048
	ds_read_b128 v[164:167], v17 offset:4096
	ds_read_b128 v[168:171], v17 offset:6144
	ds_read_b128 v[140:143], v15 offset:2048
	ds_read_b128 v[144:147], v15 offset:4096
	ds_read_b128 v[148:151], v15 offset:6144
	ds_read_b128 v[152:155], v15 offset:8192
	s_waitcnt lgkmcnt(9)
	v_mfma_f32_16x16x32_f16 v[56:59], v[192:195], v[172:175], v[56:59]
	s_add_u32 m0, s28, 0x1a000
	v_mfma_f32_16x16x32_f16 v[60:63], v[196:199], v[172:175], v[60:63]
	global_load_lds_dwordx4 v10, s[4:5]
	v_mfma_f32_16x16x32_f16 v[64:67], v[200:203], v[172:175], v[64:67]
	v_mfma_f32_16x16x32_f16 v[68:71], v[204:207], v[172:175], v[68:71]
	v_mfma_f32_16x16x32_f16 v[72:75], v[192:195], v[176:179], v[72:75]
	v_mfma_f32_16x16x32_f16 v[76:79], v[196:199], v[176:179], v[76:79]
	s_add_u32 m0, s28, 0x1c000
	v_mfma_f32_16x16x32_f16 v[80:83], v[200:203], v[176:179], v[80:83]
	global_load_lds_dwordx4 v11, s[4:5]
	v_mfma_f32_16x16x32_f16 v[84:87], v[204:207], v[176:179], v[84:87]
	v_mfma_f32_16x16x32_f16 v[88:91], v[192:195], v[180:183], v[88:91]
	v_mfma_f32_16x16x32_f16 v[92:95], v[196:199], v[180:183], v[92:95]
	v_mfma_f32_16x16x32_f16 v[96:99], v[200:203], v[180:183], v[96:99]
	s_add_u32 m0, s28, 0x1e000
	v_mfma_f32_16x16x32_f16 v[100:103], v[204:207], v[180:183], v[100:103]
	global_load_lds_dwordx4 v12, s[4:5]
	v_mfma_f32_16x16x32_f16 v[104:107], v[192:195], v[184:187], v[104:107]
	v_mfma_f32_16x16x32_f16 v[108:111], v[196:199], v[184:187], v[108:111]
	v_mfma_f32_16x16x32_f16 v[112:115], v[200:203], v[184:187], v[112:115]
	v_mfma_f32_16x16x32_f16 v[116:119], v[204:207], v[184:187], v[116:119]
	s_add_u32 m0, s28, 0x20000
	v_mfma_f32_16x16x32_f16 v[120:123], v[192:195], v[188:191], v[120:123]
	global_load_lds_dwordx4 v13, s[4:5]
	v_mfma_f32_16x16x32_f16 v[124:127], v[196:199], v[188:191], v[124:127]
	v_mfma_f32_16x16x32_f16 v[128:131], v[200:203], v[188:191], v[128:131]
	v_mfma_f32_16x16x32_f16 v[132:135], v[204:207], v[188:191], v[132:135]
	s_waitcnt lgkmcnt(6)
	ds_read_b128 v[172:175], v16
	ds_read_b128 v[192:195], v18
	ds_read_b128 v[196:199], v18 offset:2048
	ds_read_b128 v[200:203], v18 offset:4096
	ds_read_b128 v[204:207], v18 offset:6144
	ds_read_b128 v[176:179], v16 offset:2048
	ds_read_b128 v[180:183], v16 offset:4096
	ds_read_b128 v[184:187], v16 offset:6144
	ds_read_b128 v[188:191], v16 offset:8192
	s_waitcnt lgkmcnt(9)
	v_mfma_f32_16x16x32_f16 v[56:59], v[156:159], v[136:139], v[56:59]
	s_add_u32 m0, s28, 0x22000
	v_mfma_f32_16x16x32_f16 v[60:63], v[160:163], v[136:139], v[60:63]
	global_load_lds_dwordx4 v14, s[4:5]
	s_add_u32 s4, s4, s20
	s_addc_u32 s5, s5, 0
	v_mfma_f32_16x16x32_f16 v[64:67], v[164:167], v[136:139], v[64:67]
	v_mfma_f32_16x16x32_f16 v[68:71], v[168:171], v[136:139], v[68:71]
	v_mfma_f32_16x16x32_f16 v[72:75], v[156:159], v[140:143], v[72:75]
	v_mfma_f32_16x16x32_f16 v[76:79], v[160:163], v[140:143], v[76:79]
	v_mfma_f32_16x16x32_f16 v[80:83], v[164:167], v[140:143], v[80:83]
	s_add_u32 m0, s28, 0x23000
	v_mfma_f32_16x16x32_f16 v[84:87], v[168:171], v[140:143], v[84:87]
	global_load_lds_dwordx4 v10, s[6:7]
	v_mfma_f32_16x16x32_f16 v[88:91], v[156:159], v[144:147], v[88:91]
	v_mfma_f32_16x16x32_f16 v[92:95], v[160:163], v[144:147], v[92:95]
	v_mfma_f32_16x16x32_f16 v[96:99], v[164:167], v[144:147], v[96:99]
	v_mfma_f32_16x16x32_f16 v[100:103], v[168:171], v[144:147], v[100:103]
	v_mfma_f32_16x16x32_f16 v[104:107], v[156:159], v[148:151], v[104:107]
	v_mfma_f32_16x16x32_f16 v[108:111], v[160:163], v[148:151], v[108:111]
	s_add_u32 m0, s28, 0x25000
	v_mfma_f32_16x16x32_f16 v[112:115], v[164:167], v[148:151], v[112:115]
	global_load_lds_dwordx4 v11, s[6:7]
	s_add_u32 s6, s6, s20
	s_addc_u32 s7, s7, 0
	v_mfma_f32_16x16x32_f16 v[116:119], v[168:171], v[148:151], v[116:119]
	v_mfma_f32_16x16x32_f16 v[120:123], v[156:159], v[152:155], v[120:123]
	v_mfma_f32_16x16x32_f16 v[124:127], v[160:163], v[152:155], v[124:127]
	v_mfma_f32_16x16x32_f16 v[128:131], v[164:167], v[152:155], v[128:131]
	v_mfma_f32_16x16x32_f16 v[132:135], v[168:171], v[152:155], v[132:135]
	s_waitcnt vmcnt(7) lgkmcnt(0)
	s_barrier
	s_waitcnt lgkmcnt(6)
	ds_read_b128 v[136:139], v15 offset:53248
	ds_read_b128 v[156:159], v17 offset:53248
	ds_read_b128 v[160:163], v17 offset:55296
	ds_read_b128 v[164:167], v17 offset:57344
	ds_read_b128 v[168:171], v17 offset:59392
	ds_read_b128 v[140:143], v15 offset:55296
	ds_read_b128 v[144:147], v15 offset:57344
	ds_read_b128 v[148:151], v15 offset:59392
	ds_read_b128 v[152:155], v15 offset:61440
	s_waitcnt lgkmcnt(9)
	v_mfma_f32_16x16x32_f16 v[56:59], v[192:195], v[172:175], v[56:59]
	s_add_u32 m0, s28, 0x0
	v_mfma_f32_16x16x32_f16 v[60:63], v[196:199], v[172:175], v[60:63]
	global_load_lds_dwordx4 v10, s[4:5]
	v_mfma_f32_16x16x32_f16 v[64:67], v[200:203], v[172:175], v[64:67]
	v_mfma_f32_16x16x32_f16 v[68:71], v[204:207], v[172:175], v[68:71]
	v_mfma_f32_16x16x32_f16 v[72:75], v[192:195], v[176:179], v[72:75]
	v_mfma_f32_16x16x32_f16 v[76:79], v[196:199], v[176:179], v[76:79]
	s_add_u32 m0, s28, 0x2000
	v_mfma_f32_16x16x32_f16 v[80:83], v[200:203], v[176:179], v[80:83]
	global_load_lds_dwordx4 v11, s[4:5]
	v_mfma_f32_16x16x32_f16 v[84:87], v[204:207], v[176:179], v[84:87]
	v_mfma_f32_16x16x32_f16 v[88:91], v[192:195], v[180:183], v[88:91]
	v_mfma_f32_16x16x32_f16 v[92:95], v[196:199], v[180:183], v[92:95]
	v_mfma_f32_16x16x32_f16 v[96:99], v[200:203], v[180:183], v[96:99]
	s_add_u32 m0, s28, 0x4000
	v_mfma_f32_16x16x32_f16 v[100:103], v[204:207], v[180:183], v[100:103]
	global_load_lds_dwordx4 v12, s[4:5]
	v_mfma_f32_16x16x32_f16 v[104:107], v[192:195], v[184:187], v[104:107]
	v_mfma_f32_16x16x32_f16 v[108:111], v[196:199], v[184:187], v[108:111]
	v_mfma_f32_16x16x32_f16 v[112:115], v[200:203], v[184:187], v[112:115]
	v_mfma_f32_16x16x32_f16 v[116:119], v[204:207], v[184:187], v[116:119]
	s_add_u32 m0, s28, 0x6000
	v_mfma_f32_16x16x32_f16 v[120:123], v[192:195], v[188:191], v[120:123]
	global_load_lds_dwordx4 v13, s[4:5]
	v_mfma_f32_16x16x32_f16 v[124:127], v[196:199], v[188:191], v[124:127]
	v_mfma_f32_16x16x32_f16 v[128:131], v[200:203], v[188:191], v[128:131]
	v_mfma_f32_16x16x32_f16 v[132:135], v[204:207], v[188:191], v[132:135]
	s_waitcnt lgkmcnt(6)
	ds_read_b128 v[172:175], v16 offset:53248
	ds_read_b128 v[192:195], v18 offset:53248
	ds_read_b128 v[196:199], v18 offset:55296
	ds_read_b128 v[200:203], v18 offset:57344
	ds_read_b128 v[204:207], v18 offset:59392
	ds_read_b128 v[176:179], v16 offset:55296
	ds_read_b128 v[180:183], v16 offset:57344
	ds_read_b128 v[184:187], v16 offset:59392
	ds_read_b128 v[188:191], v16 offset:61440
	s_waitcnt lgkmcnt(9)
	v_mfma_f32_16x16x32_f16 v[56:59], v[156:159], v[136:139], v[56:59]
	s_add_u32 m0, s28, 0x8000
	v_mfma_f32_16x16x32_f16 v[60:63], v[160:163], v[136:139], v[60:63]
	global_load_lds_dwordx4 v14, s[4:5]
	s_add_u32 s4, s4, s20
	s_addc_u32 s5, s5, 0
	v_mfma_f32_16x16x32_f16 v[64:67], v[164:167], v[136:139], v[64:67]
	v_mfma_f32_16x16x32_f16 v[68:71], v[168:171], v[136:139], v[68:71]
	v_mfma_f32_16x16x32_f16 v[72:75], v[156:159], v[140:143], v[72:75]
	v_mfma_f32_16x16x32_f16 v[76:79], v[160:163], v[140:143], v[76:79]
	v_mfma_f32_16x16x32_f16 v[80:83], v[164:167], v[140:143], v[80:83]
	s_add_u32 m0, s28, 0x9000
	v_mfma_f32_16x16x32_f16 v[84:87], v[168:171], v[140:143], v[84:87]
	global_load_lds_dwordx4 v10, s[6:7]
	v_mfma_f32_16x16x32_f16 v[88:91], v[156:159], v[144:147], v[88:91]
	v_mfma_f32_16x16x32_f16 v[92:95], v[160:163], v[144:147], v[92:95]
	v_mfma_f32_16x16x32_f16 v[96:99], v[164:167], v[144:147], v[96:99]
	v_mfma_f32_16x16x32_f16 v[100:103], v[168:171], v[144:147], v[100:103]
	v_mfma_f32_16x16x32_f16 v[104:107], v[156:159], v[148:151], v[104:107]
	v_mfma_f32_16x16x32_f16 v[108:111], v[160:163], v[148:151], v[108:111]
	s_add_u32 m0, s28, 0xb000
	v_mfma_f32_16x16x32_f16 v[112:115], v[164:167], v[148:151], v[112:115]
	global_load_lds_dwordx4 v11, s[6:7]
	s_add_u32 s6, s6, s20
	s_addc_u32 s7, s7, 0
	v_mfma_f32_16x16x32_f16 v[116:119], v[168:171], v[148:151], v[116:119]
	v_mfma_f32_16x16x32_f16 v[120:123], v[156:159], v[152:155], v[120:123]
	v_mfma_f32_16x16x32_f16 v[124:127], v[160:163], v[152:155], v[124:127]
	v_mfma_f32_16x16x32_f16 v[128:131], v[164:167], v[152:155], v[128:131]
	v_mfma_f32_16x16x32_f16 v[132:135], v[168:171], v[152:155], v[132:135]
	s_waitcnt vmcnt(7) lgkmcnt(0)
	s_barrier
	s_waitcnt lgkmcnt(6)
	ds_read_b128 v[136:139], v19
	ds_read_b128 v[156:159], v21
	ds_read_b128 v[160:163], v21 offset:2048
	ds_read_b128 v[164:167], v21 offset:4096
	ds_read_b128 v[168:171], v21 offset:6144
	ds_read_b128 v[140:143], v19 offset:2048
	ds_read_b128 v[144:147], v19 offset:4096
	ds_read_b128 v[148:151], v19 offset:6144
	ds_read_b128 v[152:155], v19 offset:8192
	s_waitcnt lgkmcnt(9)
	v_mfma_f32_16x16x32_f16 v[56:59], v[192:195], v[172:175], v[56:59]
	v_mfma_f32_16x16x32_f16 v[60:63], v[196:199], v[172:175], v[60:63]
	v_mfma_f32_16x16x32_f16 v[64:67], v[200:203], v[172:175], v[64:67]
	v_mfma_f32_16x16x32_f16 v[68:71], v[204:207], v[172:175], v[68:71]
	v_mfma_f32_16x16x32_f16 v[72:75], v[192:195], v[176:179], v[72:75]
	v_mfma_f32_16x16x32_f16 v[76:79], v[196:199], v[176:179], v[76:79]
	v_mfma_f32_16x16x32_f16 v[80:83], v[200:203], v[176:179], v[80:83]
	v_mfma_f32_16x16x32_f16 v[84:87], v[204:207], v[176:179], v[84:87]
	v_mfma_f32_16x16x32_f16 v[88:91], v[192:195], v[180:183], v[88:91]
	v_mfma_f32_16x16x32_f16 v[92:95], v[196:199], v[180:183], v[92:95]
	v_mfma_f32_16x16x32_f16 v[96:99], v[200:203], v[180:183], v[96:99]
	v_mfma_f32_16x16x32_f16 v[100:103], v[204:207], v[180:183], v[100:103]
	v_mfma_f32_16x16x32_f16 v[104:107], v[192:195], v[184:187], v[104:107]
	v_mfma_f32_16x16x32_f16 v[108:111], v[196:199], v[184:187], v[108:111]
	v_mfma_f32_16x16x32_f16 v[112:115], v[200:203], v[184:187], v[112:115]
	v_mfma_f32_16x16x32_f16 v[116:119], v[204:207], v[184:187], v[116:119]
	v_mfma_f32_16x16x32_f16 v[120:123], v[192:195], v[188:191], v[120:123]
	v_mfma_f32_16x16x32_f16 v[124:127], v[196:199], v[188:191], v[124:127]
	v_mfma_f32_16x16x32_f16 v[128:131], v[200:203], v[188:191], v[128:131]
	v_mfma_f32_16x16x32_f16 v[132:135], v[204:207], v[188:191], v[132:135]
	s_waitcnt lgkmcnt(6)
	ds_read_b128 v[172:175], v20
	ds_read_b128 v[192:195], v22
	ds_read_b128 v[196:199], v22 offset:2048
	ds_read_b128 v[200:203], v22 offset:4096
	ds_read_b128 v[204:207], v22 offset:6144
	ds_read_b128 v[176:179], v20 offset:2048
	ds_read_b128 v[180:183], v20 offset:4096
	ds_read_b128 v[184:187], v20 offset:6144
	ds_read_b128 v[188:191], v20 offset:8192
	s_waitcnt lgkmcnt(9)
	v_mfma_f32_16x16x32_f16 v[56:59], v[156:159], v[136:139], v[56:59]
	v_mfma_f32_16x16x32_f16 v[60:63], v[160:163], v[136:139], v[60:63]
	v_mfma_f32_16x16x32_f16 v[64:67], v[164:167], v[136:139], v[64:67]
	v_mfma_f32_16x16x32_f16 v[68:71], v[168:171], v[136:139], v[68:71]
	v_mfma_f32_16x16x32_f16 v[72:75], v[156:159], v[140:143], v[72:75]
	v_mfma_f32_16x16x32_f16 v[76:79], v[160:163], v[140:143], v[76:79]
	v_mfma_f32_16x16x32_f16 v[80:83], v[164:167], v[140:143], v[80:83]
	v_mfma_f32_16x16x32_f16 v[84:87], v[168:171], v[140:143], v[84:87]
	v_mfma_f32_16x16x32_f16 v[88:91], v[156:159], v[144:147], v[88:91]
	v_mfma_f32_16x16x32_f16 v[92:95], v[160:163], v[144:147], v[92:95]
	v_mfma_f32_16x16x32_f16 v[96:99], v[164:167], v[144:147], v[96:99]
	v_mfma_f32_16x16x32_f16 v[100:103], v[168:171], v[144:147], v[100:103]
	v_mfma_f32_16x16x32_f16 v[104:107], v[156:159], v[148:151], v[104:107]
	v_mfma_f32_16x16x32_f16 v[108:111], v[160:163], v[148:151], v[108:111]
	v_mfma_f32_16x16x32_f16 v[112:115], v[164:167], v[148:151], v[112:115]
	v_mfma_f32_16x16x32_f16 v[116:119], v[168:171], v[148:151], v[116:119]
	v_mfma_f32_16x16x32_f16 v[120:123], v[156:159], v[152:155], v[120:123]
	v_mfma_f32_16x16x32_f16 v[124:127], v[160:163], v[152:155], v[124:127]
	v_mfma_f32_16x16x32_f16 v[128:131], v[164:167], v[152:155], v[128:131]
	v_mfma_f32_16x16x32_f16 v[132:135], v[168:171], v[152:155], v[132:135]
	s_waitcnt vmcnt(0) lgkmcnt(0)
	s_barrier
	s_waitcnt lgkmcnt(6)
	ds_read_b128 v[136:139], v15
	ds_read_b128 v[156:159], v17
	ds_read_b128 v[160:163], v17 offset:2048
	ds_read_b128 v[164:167], v17 offset:4096
	ds_read_b128 v[168:171], v17 offset:6144
	ds_read_b128 v[140:143], v15 offset:2048
	ds_read_b128 v[144:147], v15 offset:4096
	ds_read_b128 v[148:151], v15 offset:6144
	ds_read_b128 v[152:155], v15 offset:8192
	s_waitcnt lgkmcnt(9)
	v_mfma_f32_16x16x32_f16 v[56:59], v[192:195], v[172:175], v[56:59]
	v_mfma_f32_16x16x32_f16 v[60:63], v[196:199], v[172:175], v[60:63]
	v_mfma_f32_16x16x32_f16 v[64:67], v[200:203], v[172:175], v[64:67]
	v_mfma_f32_16x16x32_f16 v[68:71], v[204:207], v[172:175], v[68:71]
	v_mfma_f32_16x16x32_f16 v[72:75], v[192:195], v[176:179], v[72:75]
	v_mfma_f32_16x16x32_f16 v[76:79], v[196:199], v[176:179], v[76:79]
	v_mfma_f32_16x16x32_f16 v[80:83], v[200:203], v[176:179], v[80:83]
	v_mfma_f32_16x16x32_f16 v[84:87], v[204:207], v[176:179], v[84:87]
	v_mfma_f32_16x16x32_f16 v[88:91], v[192:195], v[180:183], v[88:91]
	v_mfma_f32_16x16x32_f16 v[92:95], v[196:199], v[180:183], v[92:95]
	v_mfma_f32_16x16x32_f16 v[96:99], v[200:203], v[180:183], v[96:99]
	v_mfma_f32_16x16x32_f16 v[100:103], v[204:207], v[180:183], v[100:103]
	v_mfma_f32_16x16x32_f16 v[104:107], v[192:195], v[184:187], v[104:107]
	v_mfma_f32_16x16x32_f16 v[108:111], v[196:199], v[184:187], v[108:111]
	v_mfma_f32_16x16x32_f16 v[112:115], v[200:203], v[184:187], v[112:115]
	v_mfma_f32_16x16x32_f16 v[116:119], v[204:207], v[184:187], v[116:119]
	v_mfma_f32_16x16x32_f16 v[120:123], v[192:195], v[188:191], v[120:123]
	v_mfma_f32_16x16x32_f16 v[124:127], v[196:199], v[188:191], v[124:127]
	v_mfma_f32_16x16x32_f16 v[128:131], v[200:203], v[188:191], v[128:131]
	v_mfma_f32_16x16x32_f16 v[132:135], v[204:207], v[188:191], v[132:135]
	s_waitcnt lgkmcnt(6)
	ds_read_b128 v[172:175], v16
	ds_read_b128 v[192:195], v18
	ds_read_b128 v[196:199], v18 offset:2048
	ds_read_b128 v[200:203], v18 offset:4096
	ds_read_b128 v[204:207], v18 offset:6144
	ds_read_b128 v[176:179], v16 offset:2048
	ds_read_b128 v[180:183], v16 offset:4096
	ds_read_b128 v[184:187], v16 offset:6144
	ds_read_b128 v[188:191], v16 offset:8192
	s_waitcnt lgkmcnt(9)
	v_mfma_f32_16x16x32_f16 v[56:59], v[156:159], v[136:139], v[56:59]
	v_mfma_f32_16x16x32_f16 v[60:63], v[160:163], v[136:139], v[60:63]
	v_mfma_f32_16x16x32_f16 v[64:67], v[164:167], v[136:139], v[64:67]
	v_mfma_f32_16x16x32_f16 v[68:71], v[168:171], v[136:139], v[68:71]
	v_mfma_f32_16x16x32_f16 v[72:75], v[156:159], v[140:143], v[72:75]
	v_mfma_f32_16x16x32_f16 v[76:79], v[160:163], v[140:143], v[76:79]
	v_mfma_f32_16x16x32_f16 v[80:83], v[164:167], v[140:143], v[80:83]
	v_mfma_f32_16x16x32_f16 v[84:87], v[168:171], v[140:143], v[84:87]
	v_mfma_f32_16x16x32_f16 v[88:91], v[156:159], v[144:147], v[88:91]
	v_mfma_f32_16x16x32_f16 v[92:95], v[160:163], v[144:147], v[92:95]
	v_mfma_f32_16x16x32_f16 v[96:99], v[164:167], v[144:147], v[96:99]
	v_mfma_f32_16x16x32_f16 v[100:103], v[168:171], v[144:147], v[100:103]
	v_mfma_f32_16x16x32_f16 v[104:107], v[156:159], v[148:151], v[104:107]
	v_mfma_f32_16x16x32_f16 v[108:111], v[160:163], v[148:151], v[108:111]
	v_mfma_f32_16x16x32_f16 v[112:115], v[164:167], v[148:151], v[112:115]
	v_mfma_f32_16x16x32_f16 v[116:119], v[168:171], v[148:151], v[116:119]
	v_mfma_f32_16x16x32_f16 v[120:123], v[156:159], v[152:155], v[120:123]
	v_mfma_f32_16x16x32_f16 v[124:127], v[160:163], v[152:155], v[124:127]
	v_mfma_f32_16x16x32_f16 v[128:131], v[164:167], v[152:155], v[128:131]
	v_mfma_f32_16x16x32_f16 v[132:135], v[168:171], v[152:155], v[132:135]
	s_waitcnt lgkmcnt(0)
	v_mfma_f32_16x16x32_f16 v[56:59], v[192:195], v[172:175], v[56:59]
	v_mfma_f32_16x16x32_f16 v[60:63], v[196:199], v[172:175], v[60:63]
	v_mfma_f32_16x16x32_f16 v[64:67], v[200:203], v[172:175], v[64:67]
	v_mfma_f32_16x16x32_f16 v[68:71], v[204:207], v[172:175], v[68:71]
	v_mfma_f32_16x16x32_f16 v[72:75], v[192:195], v[176:179], v[72:75]
	v_mfma_f32_16x16x32_f16 v[76:79], v[196:199], v[176:179], v[76:79]
	v_mfma_f32_16x16x32_f16 v[80:83], v[200:203], v[176:179], v[80:83]
	v_mfma_f32_16x16x32_f16 v[84:87], v[204:207], v[176:179], v[84:87]
	v_mfma_f32_16x16x32_f16 v[88:91], v[192:195], v[180:183], v[88:91]
	v_mfma_f32_16x16x32_f16 v[92:95], v[196:199], v[180:183], v[92:95]
	v_mfma_f32_16x16x32_f16 v[96:99], v[200:203], v[180:183], v[96:99]
	v_mfma_f32_16x16x32_f16 v[100:103], v[204:207], v[180:183], v[100:103]
	v_mfma_f32_16x16x32_f16 v[104:107], v[192:195], v[184:187], v[104:107]
	v_mfma_f32_16x16x32_f16 v[108:111], v[196:199], v[184:187], v[108:111]
	v_mfma_f32_16x16x32_f16 v[112:115], v[200:203], v[184:187], v[112:115]
	v_mfma_f32_16x16x32_f16 v[116:119], v[204:207], v[184:187], v[116:119]
	v_mfma_f32_16x16x32_f16 v[120:123], v[192:195], v[188:191], v[120:123]
	v_mfma_f32_16x16x32_f16 v[124:127], v[196:199], v[188:191], v[124:127]
	v_mfma_f32_16x16x32_f16 v[128:131], v[200:203], v[188:191], v[128:131]
	v_mfma_f32_16x16x32_f16 v[132:135], v[204:207], v[188:191], v[132:135]
	s_nop 7
	s_nop 1
	v_mov_b32_e32 v213, s19
	v_pk_add_f32 v[56:57], v[56:57], v[24:25]
	v_pk_add_f32 v[58:59], v[58:59], v[26:27]
	v_pk_add_f32 v[60:61], v[60:61], v[28:29]
	v_pk_add_f32 v[62:63], v[62:63], v[30:31]
	v_pk_add_f32 v[64:65], v[64:65], v[32:33]
	v_pk_add_f32 v[66:67], v[66:67], v[34:35]
	v_pk_add_f32 v[68:69], v[68:69], v[36:37]
	v_pk_add_f32 v[70:71], v[70:71], v[38:39]
	v_pk_mul_f32 v[208:209], v[56:57], v[56:57]
	v_pk_fma_f32 v[208:209], v[58:59], v[58:59], v[208:209]
	v_pk_fma_f32 v[208:209], v[60:61], v[60:61], v[208:209]
	v_pk_fma_f32 v[208:209], v[62:63], v[62:63], v[208:209]
	v_pk_fma_f32 v[208:209], v[64:65], v[64:65], v[208:209]
	v_pk_fma_f32 v[208:209], v[66:67], v[66:67], v[208:209]
	v_pk_fma_f32 v[208:209], v[68:69], v[68:69], v[208:209]
	v_pk_fma_f32 v[208:209], v[70:71], v[70:71], v[208:209]
	v_add_f32_e32 v208, v208, v209
	v_mov_b32_e32 v209, v208
	s_nop 1
	v_permlane16_swap_b32_e32 v208, v209
	v_add_f32_e32 v208, v208, v209
	v_mov_b32_e32 v209, v208
	s_nop 1
	v_permlane32_swap_b32_e32 v208, v209
	v_add_f32_e32 v208, v208, v209
	v_mov_b32_e32 v210, 0x358637bd
	v_fmac_f32_e32 v210, 0x3c800000, v208
	v_rsq_f32_e32 v210, v210
	s_add_u32 s24, s29, 0
	s_lshr_b32 s8, s24, 1
	s_lshl_b32 s8, s8, 12
	s_and_b32 s24, s24, 1
	s_lshl_b32 s24, s24, 8
	s_add_u32 s8, s8, s24
	v_mul_f32_e32 v210, v213, v210
	v_add_u32_e32 v212, s8, v23
	v_pk_mul_f32 v[56:57], v[56:57], v[210:211] op_sel_hi:[1,0]
	v_pk_mul_f32 v[58:59], v[58:59], v[210:211] op_sel_hi:[1,0]
	v_pk_mul_f32 v[56:57], v[56:57], v[40:41]
	v_pk_mul_f32 v[58:59], v[58:59], v[42:43]
	v_cvt_pk_f16_f32 v56, v56, v57
	v_cvt_pk_f16_f32 v57, v58, v59
	global_store_dwordx2 v212, v[56:57], s[22:23] offset:0
	v_pk_mul_f32 v[60:61], v[60:61], v[210:211] op_sel_hi:[1,0]
	v_pk_mul_f32 v[62:63], v[62:63], v[210:211] op_sel_hi:[1,0]
	v_pk_mul_f32 v[60:61], v[60:61], v[44:45]
	v_pk_mul_f32 v[62:63], v[62:63], v[46:47]
	v_cvt_pk_f16_f32 v60, v60, v61
	v_cvt_pk_f16_f32 v61, v62, v63
	global_store_dwordx2 v212, v[60:61], s[22:23] offset:1024
	v_pk_mul_f32 v[64:65], v[64:65], v[210:211] op_sel_hi:[1,0]
	v_pk_mul_f32 v[66:67], v[66:67], v[210:211] op_sel_hi:[1,0]
	v_pk_mul_f32 v[64:65], v[64:65], v[48:49]
	v_pk_mul_f32 v[66:67], v[66:67], v[50:51]
	v_cvt_pk_f16_f32 v64, v64, v65
	v_cvt_pk_f16_f32 v65, v66, v67
	global_store_dwordx2 v212, v[64:65], s[22:23] offset:2048
	v_pk_mul_f32 v[68:69], v[68:69], v[210:211] op_sel_hi:[1,0]
	v_pk_mul_f32 v[70:71], v[70:71], v[210:211] op_sel_hi:[1,0]
	v_pk_mul_f32 v[68:69], v[68:69], v[52:53]
	v_pk_mul_f32 v[70:71], v[70:71], v[54:55]
	v_cvt_pk_f16_f32 v68, v68, v69
	v_cvt_pk_f16_f32 v69, v70, v71
	global_store_dwordx2 v212, v[68:69], s[22:23] offset:3072
	v_pk_add_f32 v[72:73], v[72:73], v[24:25]
	v_pk_add_f32 v[74:75], v[74:75], v[26:27]
	v_pk_add_f32 v[76:77], v[76:77], v[28:29]
	v_pk_add_f32 v[78:79], v[78:79], v[30:31]
	v_pk_add_f32 v[80:81], v[80:81], v[32:33]
	v_pk_add_f32 v[82:83], v[82:83], v[34:35]
	v_pk_add_f32 v[84:85], v[84:85], v[36:37]
	v_pk_add_f32 v[86:87], v[86:87], v[38:39]
	v_pk_mul_f32 v[208:209], v[72:73], v[72:73]
	v_pk_fma_f32 v[208:209], v[74:75], v[74:75], v[208:209]
	v_pk_fma_f32 v[208:209], v[76:77], v[76:77], v[208:209]
	v_pk_fma_f32 v[208:209], v[78:79], v[78:79], v[208:209]
	v_pk_fma_f32 v[208:209], v[80:81], v[80:81], v[208:209]
	v_pk_fma_f32 v[208:209], v[82:83], v[82:83], v[208:209]
	v_pk_fma_f32 v[208:209], v[84:85], v[84:85], v[208:209]
	v_pk_fma_f32 v[208:209], v[86:87], v[86:87], v[208:209]
	v_add_f32_e32 v208, v208, v209
	v_mov_b32_e32 v209, v208
	s_nop 1
	v_permlane16_swap_b32_e32 v208, v209
	v_add_f32_e32 v208, v208, v209
	v_mov_b32_e32 v209, v208
	s_nop 1
	v_permlane32_swap_b32_e32 v208, v209
	v_add_f32_e32 v208, v208, v209
	v_mov_b32_e32 v210, 0x358637bd
	v_fmac_f32_e32 v210, 0x3c800000, v208
	v_rsq_f32_e32 v210, v210
	s_add_u32 s24, s29, 1
	s_lshr_b32 s8, s24, 1
	s_lshl_b32 s8, s8, 12
	s_and_b32 s24, s24, 1
	s_lshl_b32 s24, s24, 8
	s_add_u32 s8, s8, s24
	v_mul_f32_e32 v210, v213, v210
	v_add_u32_e32 v212, s8, v23
	v_pk_mul_f32 v[72:73], v[72:73], v[210:211] op_sel_hi:[1,0]
	v_pk_mul_f32 v[74:75], v[74:75], v[210:211] op_sel_hi:[1,0]
	v_pk_mul_f32 v[72:73], v[72:73], v[40:41]
	v_pk_mul_f32 v[74:75], v[74:75], v[42:43]
	v_cvt_pk_f16_f32 v72, v72, v73
	v_cvt_pk_f16_f32 v73, v74, v75
	global_store_dwordx2 v212, v[72:73], s[22:23] offset:0
	v_pk_mul_f32 v[76:77], v[76:77], v[210:211] op_sel_hi:[1,0]
	v_pk_mul_f32 v[78:79], v[78:79], v[210:211] op_sel_hi:[1,0]
	v_pk_mul_f32 v[76:77], v[76:77], v[44:45]
	v_pk_mul_f32 v[78:79], v[78:79], v[46:47]
	v_cvt_pk_f16_f32 v76, v76, v77
	v_cvt_pk_f16_f32 v77, v78, v79
	global_store_dwordx2 v212, v[76:77], s[22:23] offset:1024
	v_pk_mul_f32 v[80:81], v[80:81], v[210:211] op_sel_hi:[1,0]
	v_pk_mul_f32 v[82:83], v[82:83], v[210:211] op_sel_hi:[1,0]
	v_pk_mul_f32 v[80:81], v[80:81], v[48:49]
	v_pk_mul_f32 v[82:83], v[82:83], v[50:51]
	v_cvt_pk_f16_f32 v80, v80, v81
	v_cvt_pk_f16_f32 v81, v82, v83
	global_store_dwordx2 v212, v[80:81], s[22:23] offset:2048
	v_pk_mul_f32 v[84:85], v[84:85], v[210:211] op_sel_hi:[1,0]
	v_pk_mul_f32 v[86:87], v[86:87], v[210:211] op_sel_hi:[1,0]
	v_pk_mul_f32 v[84:85], v[84:85], v[52:53]
	v_pk_mul_f32 v[86:87], v[86:87], v[54:55]
	v_cvt_pk_f16_f32 v84, v84, v85
	v_cvt_pk_f16_f32 v85, v86, v87
	global_store_dwordx2 v212, v[84:85], s[22:23] offset:3072
	v_pk_add_f32 v[88:89], v[88:89], v[24:25]
	v_pk_add_f32 v[90:91], v[90:91], v[26:27]
	v_pk_add_f32 v[92:93], v[92:93], v[28:29]
	v_pk_add_f32 v[94:95], v[94:95], v[30:31]
	v_pk_add_f32 v[96:97], v[96:97], v[32:33]
	v_pk_add_f32 v[98:99], v[98:99], v[34:35]
	v_pk_add_f32 v[100:101], v[100:101], v[36:37]
	v_pk_add_f32 v[102:103], v[102:103], v[38:39]
	v_pk_mul_f32 v[208:209], v[88:89], v[88:89]
	v_pk_fma_f32 v[208:209], v[90:91], v[90:91], v[208:209]
	v_pk_fma_f32 v[208:209], v[92:93], v[92:93], v[208:209]
	v_pk_fma_f32 v[208:209], v[94:95], v[94:95], v[208:209]
	v_pk_fma_f32 v[208:209], v[96:97], v[96:97], v[208:209]
	v_pk_fma_f32 v[208:209], v[98:99], v[98:99], v[208:209]
	v_pk_fma_f32 v[208:209], v[100:101], v[100:101], v[208:209]
	v_pk_fma_f32 v[208:209], v[102:103], v[102:103], v[208:209]
	v_add_f32_e32 v208, v208, v209
	v_mov_b32_e32 v209, v208
	s_nop 1
	v_permlane16_swap_b32_e32 v208, v209
	v_add_f32_e32 v208, v208, v209
	v_mov_b32_e32 v209, v208
	s_nop 1
	v_permlane32_swap_b32_e32 v208, v209
	v_add_f32_e32 v208, v208, v209
	v_mov_b32_e32 v210, 0x358637bd
	v_fmac_f32_e32 v210, 0x3c800000, v208
	v_rsq_f32_e32 v210, v210
	s_add_u32 s24, s29, 2
	s_lshr_b32 s8, s24, 1
	s_lshl_b32 s8, s8, 12
	s_and_b32 s24, s24, 1
	s_lshl_b32 s24, s24, 8
	s_add_u32 s8, s8, s24
	v_mul_f32_e32 v210, v213, v210
	v_add_u32_e32 v212, s8, v23
	v_pk_mul_f32 v[88:89], v[88:89], v[210:211] op_sel_hi:[1,0]
	v_pk_mul_f32 v[90:91], v[90:91], v[210:211] op_sel_hi:[1,0]
	v_pk_mul_f32 v[88:89], v[88:89], v[40:41]
	v_pk_mul_f32 v[90:91], v[90:91], v[42:43]
	v_cvt_pk_f16_f32 v88, v88, v89
	v_cvt_pk_f16_f32 v89, v90, v91
	global_store_dwordx2 v212, v[88:89], s[22:23] offset:0
	v_pk_mul_f32 v[92:93], v[92:93], v[210:211] op_sel_hi:[1,0]
	v_pk_mul_f32 v[94:95], v[94:95], v[210:211] op_sel_hi:[1,0]
	v_pk_mul_f32 v[92:93], v[92:93], v[44:45]
	v_pk_mul_f32 v[94:95], v[94:95], v[46:47]
	v_cvt_pk_f16_f32 v92, v92, v93
	v_cvt_pk_f16_f32 v93, v94, v95
	global_store_dwordx2 v212, v[92:93], s[22:23] offset:1024
	v_pk_mul_f32 v[96:97], v[96:97], v[210:211] op_sel_hi:[1,0]
	v_pk_mul_f32 v[98:99], v[98:99], v[210:211] op_sel_hi:[1,0]
	v_pk_mul_f32 v[96:97], v[96:97], v[48:49]
	v_pk_mul_f32 v[98:99], v[98:99], v[50:51]
	v_cvt_pk_f16_f32 v96, v96, v97
	v_cvt_pk_f16_f32 v97, v98, v99
	global_store_dwordx2 v212, v[96:97], s[22:23] offset:2048
	v_pk_mul_f32 v[100:101], v[100:101], v[210:211] op_sel_hi:[1,0]
	v_pk_mul_f32 v[102:103], v[102:103], v[210:211] op_sel_hi:[1,0]
	v_pk_mul_f32 v[100:101], v[100:101], v[52:53]
	v_pk_mul_f32 v[102:103], v[102:103], v[54:55]
	v_cvt_pk_f16_f32 v100, v100, v101
	v_cvt_pk_f16_f32 v101, v102, v103
	global_store_dwordx2 v212, v[100:101], s[22:23] offset:3072
	v_pk_add_f32 v[104:105], v[104:105], v[24:25]
	v_pk_add_f32 v[106:107], v[106:107], v[26:27]
	v_pk_add_f32 v[108:109], v[108:109], v[28:29]
	v_pk_add_f32 v[110:111], v[110:111], v[30:31]
	v_pk_add_f32 v[112:113], v[112:113], v[32:33]
	v_pk_add_f32 v[114:115], v[114:115], v[34:35]
	v_pk_add_f32 v[116:117], v[116:117], v[36:37]
	v_pk_add_f32 v[118:119], v[118:119], v[38:39]
	v_pk_mul_f32 v[208:209], v[104:105], v[104:105]
	v_pk_fma_f32 v[208:209], v[106:107], v[106:107], v[208:209]
	v_pk_fma_f32 v[208:209], v[108:109], v[108:109], v[208:209]
	v_pk_fma_f32 v[208:209], v[110:111], v[110:111], v[208:209]
	v_pk_fma_f32 v[208:209], v[112:113], v[112:113], v[208:209]
	v_pk_fma_f32 v[208:209], v[114:115], v[114:115], v[208:209]
	v_pk_fma_f32 v[208:209], v[116:117], v[116:117], v[208:209]
	v_pk_fma_f32 v[208:209], v[118:119], v[118:119], v[208:209]
	v_add_f32_e32 v208, v208, v209
	v_mov_b32_e32 v209, v208
	s_nop 1
	v_permlane16_swap_b32_e32 v208, v209
	v_add_f32_e32 v208, v208, v209
	v_mov_b32_e32 v209, v208
	s_nop 1
	v_permlane32_swap_b32_e32 v208, v209
	v_add_f32_e32 v208, v208, v209
	v_mov_b32_e32 v210, 0x358637bd
	v_fmac_f32_e32 v210, 0x3c800000, v208
	v_rsq_f32_e32 v210, v210
	s_add_u32 s24, s29, 3
	s_lshr_b32 s8, s24, 1
	s_lshl_b32 s8, s8, 12
	s_and_b32 s24, s24, 1
	s_lshl_b32 s24, s24, 8
	s_add_u32 s8, s8, s24
	v_mul_f32_e32 v210, v213, v210
	v_add_u32_e32 v212, s8, v23
	v_pk_mul_f32 v[104:105], v[104:105], v[210:211] op_sel_hi:[1,0]
	v_pk_mul_f32 v[106:107], v[106:107], v[210:211] op_sel_hi:[1,0]
	v_pk_mul_f32 v[104:105], v[104:105], v[40:41]
	v_pk_mul_f32 v[106:107], v[106:107], v[42:43]
	v_cvt_pk_f16_f32 v104, v104, v105
	v_cvt_pk_f16_f32 v105, v106, v107
	global_store_dwordx2 v212, v[104:105], s[22:23] offset:0
	v_pk_mul_f32 v[108:109], v[108:109], v[210:211] op_sel_hi:[1,0]
	v_pk_mul_f32 v[110:111], v[110:111], v[210:211] op_sel_hi:[1,0]
	v_pk_mul_f32 v[108:109], v[108:109], v[44:45]
	v_pk_mul_f32 v[110:111], v[110:111], v[46:47]
	v_cvt_pk_f16_f32 v108, v108, v109
	v_cvt_pk_f16_f32 v109, v110, v111
	global_store_dwordx2 v212, v[108:109], s[22:23] offset:1024
	v_pk_mul_f32 v[112:113], v[112:113], v[210:211] op_sel_hi:[1,0]
	v_pk_mul_f32 v[114:115], v[114:115], v[210:211] op_sel_hi:[1,0]
	v_pk_mul_f32 v[112:113], v[112:113], v[48:49]
	v_pk_mul_f32 v[114:115], v[114:115], v[50:51]
	v_cvt_pk_f16_f32 v112, v112, v113
	v_cvt_pk_f16_f32 v113, v114, v115
	global_store_dwordx2 v212, v[112:113], s[22:23] offset:2048
	v_pk_mul_f32 v[116:117], v[116:117], v[210:211] op_sel_hi:[1,0]
	v_pk_mul_f32 v[118:119], v[118:119], v[210:211] op_sel_hi:[1,0]
	v_pk_mul_f32 v[116:117], v[116:117], v[52:53]
	v_pk_mul_f32 v[118:119], v[118:119], v[54:55]
	v_cvt_pk_f16_f32 v116, v116, v117
	v_cvt_pk_f16_f32 v117, v118, v119
	global_store_dwordx2 v212, v[116:117], s[22:23] offset:3072
	v_pk_add_f32 v[120:121], v[120:121], v[24:25]
	v_pk_add_f32 v[122:123], v[122:123], v[26:27]
	v_pk_add_f32 v[124:125], v[124:125], v[28:29]
	v_pk_add_f32 v[126:127], v[126:127], v[30:31]
	v_pk_add_f32 v[128:129], v[128:129], v[32:33]
	v_pk_add_f32 v[130:131], v[130:131], v[34:35]
	v_pk_add_f32 v[132:133], v[132:133], v[36:37]
	v_pk_add_f32 v[134:135], v[134:135], v[38:39]
	v_pk_mul_f32 v[208:209], v[120:121], v[120:121]
	v_pk_fma_f32 v[208:209], v[122:123], v[122:123], v[208:209]
	v_pk_fma_f32 v[208:209], v[124:125], v[124:125], v[208:209]
	v_pk_fma_f32 v[208:209], v[126:127], v[126:127], v[208:209]
	v_pk_fma_f32 v[208:209], v[128:129], v[128:129], v[208:209]
	v_pk_fma_f32 v[208:209], v[130:131], v[130:131], v[208:209]
	v_pk_fma_f32 v[208:209], v[132:133], v[132:133], v[208:209]
	v_pk_fma_f32 v[208:209], v[134:135], v[134:135], v[208:209]
	v_add_f32_e32 v208, v208, v209
	v_mov_b32_e32 v209, v208
	s_nop 1
	v_permlane16_swap_b32_e32 v208, v209
	v_add_f32_e32 v208, v208, v209
	v_mov_b32_e32 v209, v208
	s_nop 1
	v_permlane32_swap_b32_e32 v208, v209
	v_add_f32_e32 v208, v208, v209
	v_mov_b32_e32 v210, 0x358637bd
	v_fmac_f32_e32 v210, 0x3c800000, v208
	v_rsq_f32_e32 v210, v210
	s_add_u32 s24, s29, 4
	s_lshr_b32 s8, s24, 1
	s_lshl_b32 s8, s8, 12
	s_and_b32 s24, s24, 1
	s_lshl_b32 s24, s24, 8
	s_add_u32 s8, s8, s24
	v_mul_f32_e32 v210, v213, v210
	v_add_u32_e32 v212, s8, v23
	v_pk_mul_f32 v[120:121], v[120:121], v[210:211] op_sel_hi:[1,0]
	v_pk_mul_f32 v[122:123], v[122:123], v[210:211] op_sel_hi:[1,0]
	v_pk_mul_f32 v[120:121], v[120:121], v[40:41]
	v_pk_mul_f32 v[122:123], v[122:123], v[42:43]
	v_cvt_pk_f16_f32 v120, v120, v121
	v_cvt_pk_f16_f32 v121, v122, v123
	global_store_dwordx2 v212, v[120:121], s[22:23] offset:0
	v_pk_mul_f32 v[124:125], v[124:125], v[210:211] op_sel_hi:[1,0]
	v_pk_mul_f32 v[126:127], v[126:127], v[210:211] op_sel_hi:[1,0]
	v_pk_mul_f32 v[124:125], v[124:125], v[44:45]
	v_pk_mul_f32 v[126:127], v[126:127], v[46:47]
	v_cvt_pk_f16_f32 v124, v124, v125
	v_cvt_pk_f16_f32 v125, v126, v127
	global_store_dwordx2 v212, v[124:125], s[22:23] offset:1024
	v_pk_mul_f32 v[128:129], v[128:129], v[210:211] op_sel_hi:[1,0]
	v_pk_mul_f32 v[130:131], v[130:131], v[210:211] op_sel_hi:[1,0]
	v_pk_mul_f32 v[128:129], v[128:129], v[48:49]
	v_pk_mul_f32 v[130:131], v[130:131], v[50:51]
	v_cvt_pk_f16_f32 v128, v128, v129
	v_cvt_pk_f16_f32 v129, v130, v131
	global_store_dwordx2 v212, v[128:129], s[22:23] offset:2048
	v_pk_mul_f32 v[132:133], v[132:133], v[210:211] op_sel_hi:[1,0]
	v_pk_mul_f32 v[134:135], v[134:135], v[210:211] op_sel_hi:[1,0]
	v_pk_mul_f32 v[132:133], v[132:133], v[52:53]
	v_pk_mul_f32 v[134:135], v[134:135], v[54:55]
	v_cvt_pk_f16_f32 v132, v132, v133
	v_cvt_pk_f16_f32 v133, v134, v135
	global_store_dwordx2 v212, v[132:133], s[22:23] offset:3072
	s_branch .Lpf_done
.Lpf_vKB:
	s_lshl_b32 s25, s25, 6
	s_add_u32 s25, s25, 32
	s_add_u32 s29, s10, s25
	s_lshr_b32 s29, s29, 4
	v_add_u32_e32 v5, s25, v3
	v_lshlrev_b32_e32 v5, 7, v5
	v_add_u32_e32 v15, v5, v6
	v_add_u32_e32 v16, v5, v7
	v_add_u32_e32 v5, 0x9000, v9
	v_add_u32_e32 v17, v5, v6
	v_add_u32_e32 v18, v5, v7
	v_add_u32_e32 v19, 0x1a000, v15
	v_add_u32_e32 v20, 0x1a000, v16
	v_add_u32_e32 v21, 0x1a000, v17
	v_add_u32_e32 v22, 0x1a000, v18
	v_lshlrev_b32_e32 v5, 4, v4
	global_load_dwordx4 v[24:27], v5, s[14:15] offset:0
	global_load_dwordx4 v[28:31], v5, s[14:15] offset:64
	global_load_dwordx4 v[32:35], v5, s[14:15] offset:128
	global_load_dwordx4 v[36:39], v5, s[14:15] offset:192
	global_load_dwordx4 v[40:43], v5, s[16:17] offset:0
	global_load_dwordx4 v[44:47], v5, s[16:17] offset:64
	global_load_dwordx4 v[48:51], v5, s[16:17] offset:128
	global_load_dwordx4 v[52:55], v5, s[16:17] offset:192
	s_add_u32 m0, s28, 0x0
	s_nop 0
	global_load_lds_dwordx4 v10, s[4:5]
	s_add_u32 m0, s28, 0x2000
	s_nop 0
	global_load_lds_dwordx4 v11, s[4:5]
	s_add_u32 m0, s28, 0x4000
	s_nop 0
	global_load_lds_dwordx4 v12, s[4:5]
	s_add_u32 m0, s28, 0x6000
	s_nop 0
	global_load_lds_dwordx4 v13, s[4:5]
	s_add_u32 s4, s4, s20
	s_addc_u32 s5, s5, 0
	s_add_u32 m0, s28, 0x9000
	s_nop 0
	global_load_lds_dwordx4 v10, s[6:7]
	s_add_u32 m0, s28, 0xb000
	s_nop 0
	global_load_lds_dwordx4 v11, s[6:7]
	s_add_u32 s6, s6, s20
	s_addc_u32 s7, s7, 0
	s_add_u32 m0, s28, 0xd000
	s_nop 0
	global_load_lds_dwordx4 v10, s[4:5]
	s_add_u32 m0, s28, 0xf000
	s_nop 0
	global_load_lds_dwordx4 v11, s[4:5]
	s_add_u32 m0, s28, 0x11000
	s_nop 0
	global_load_lds_dwordx4 v12, s[4:5]
	s_add_u32 m0, s28, 0x13000
	s_nop 0
	global_load_lds_dwordx4 v13, s[4:5]
	s_add_u32 s4, s4, s20
	s_addc_u32 s5, s5, 0
	s_add_u32 m0, s28, 0x16000
	s_nop 0
	global_load_lds_dwordx4 v10, s[6:7]
	s_add_u32 m0, s28, 0x18000
	s_nop 0
	global_load_lds_dwordx4 v11, s[6:7]
	s_add_u32 s6, s6, s20
	s_addc_u32 s7, s7, 0
	s_add_u32 m0, s28, 0x1a000
	s_nop 0
	global_load_lds_dwordx4 v10, s[4:5]
	s_add_u32 m0, s28, 0x1c000
	s_nop 0
	global_load_lds_dwordx4 v11, s[4:5]
	s_add_u32 m0, s28, 0x1e000
	s_nop 0
	global_load_lds_dwordx4 v12, s[4:5]
	s_add_u32 m0, s28, 0x20000
	s_nop 0
	global_load_lds_dwordx4 v13, s[4:5]
	s_add_u32 s4, s4, s20
	s_addc_u32 s5, s5, 0
	s_add_u32 m0, s28, 0x23000
	s_nop 0
	global_load_lds_dwordx4 v10, s[6:7]
	s_add_u32 m0, s28, 0x25000
	s_nop 0
	global_load_lds_dwordx4 v11, s[6:7]
	s_add_u32 s6, s6, s20
	s_addc_u32 s7, s7, 0
	s_waitcnt vmcnt(12) lgkmcnt(0)
	s_barrier
	s_waitcnt lgkmcnt(7)
	ds_read_b128 v[136:139], v15
	ds_read_b128 v[156:159], v17
	ds_read_b128 v[160:163], v17 offset:2048
	ds_read_b128 v[164:167], v17 offset:4096
	ds_read_b128 v[168:171], v17 offset:6144
	ds_read_b128 v[140:143], v15 offset:2048
	ds_read_b128 v[144:147], v15 offset:4096
	ds_read_b128 v[148:151], v15 offset:6144
	s_waitcnt lgkmcnt(7)
	ds_read_b128 v[172:175], v16
	ds_read_b128 v[192:195], v18
	ds_read_b128 v[196:199], v18 offset:2048
	ds_read_b128 v[200:203], v18 offset:4096
	ds_read_b128 v[204:207], v18 offset:6144
	ds_read_b128 v[176:179], v16 offset:2048
	ds_read_b128 v[180:183], v16 offset:4096
	ds_read_b128 v[184:187], v16 offset:6144
	s_waitcnt lgkmcnt(8)
	v_mfma_f32_16x16x32_f16 v[56:59], v[156:159], v[136:139], 0
	v_mfma_f32_16x16x32_f16 v[60:63], v[160:163], v[136:139], 0
	v_mfma_f32_16x16x32_f16 v[64:67], v[164:167], v[136:139], 0
	v_mfma_f32_16x16x32_f16 v[68:71], v[168:171], v[136:139], 0
	v_mfma_f32_16x16x32_f16 v[72:75], v[156:159], v[140:143], 0
	v_mfma_f32_16x16x32_f16 v[76:79], v[160:163], v[140:143], 0
	v_mfma_f32_16x16x32_f16 v[80:83], v[164:167], v[140:143], 0
	v_mfma_f32_16x16x32_f16 v[84:87], v[168:171], v[140:143], 0
	v_mfma_f32_16x16x32_f16 v[88:91], v[156:159], v[144:147], 0
	v_mfma_f32_16x16x32_f16 v[92:95], v[160:163], v[144:147], 0
	v_mfma_f32_16x16x32_f16 v[96:99], v[164:167], v[144:147], 0
	v_mfma_f32_16x16x32_f16 v[100:103], v[168:171], v[144:147], 0
	v_mfma_f32_16x16x32_f16 v[104:107], v[156:159], v[148:151], 0
	v_mfma_f32_16x16x32_f16 v[108:111], v[160:163], v[148:151], 0
	v_mfma_f32_16x16x32_f16 v[112:115], v[164:167], v[148:151], 0
	v_mfma_f32_16x16x32_f16 v[116:119], v[168:171], v[148:151], 0
	s_waitcnt vmcnt(6) lgkmcnt(0)
	s_barrier
	s_waitcnt lgkmcnt(7)
	ds_read_b128 v[136:139], v15 offset:53248
	ds_read_b128 v[156:159], v17 offset:53248
	ds_read_b128 v[160:163], v17 offset:55296
	ds_read_b128 v[164:167], v17 offset:57344
	ds_read_b128 v[168:171], v17 offset:59392
	ds_read_b128 v[140:143], v15 offset:55296
	ds_read_b128 v[144:147], v15 offset:57344
	ds_read_b128 v[148:151], v15 offset:59392
	s_waitcnt lgkmcnt(8)
	v_mfma_f32_16x16x32_f16 v[56:59], v[192:195], v[172:175], v[56:59]
	s_add_u32 m0, s28, 0x0
	v_mfma_f32_16x16x32_f16 v[60:63], v[196:199], v[172:175], v[60:63]
	global_load_lds_dwordx4 v10, s[4:5]
	v_mfma_f32_16x16x32_f16 v[64:67], v[200:203], v[172:175], v[64:67]
	v_mfma_f32_16x16x32_f16 v[68:71], v[204:207], v[172:175], v[68:71]
	v_mfma_f32_16x16x32_f16 v[72:75], v[192:195], v[176:179], v[72:75]
	v_mfma_f32_16x16x32_f16 v[76:79], v[196:199], v[176:179], v[76:79]
	s_add_u32 m0, s28, 0x2000
	v_mfma_f32_16x16x32_f16 v[80:83], v[200:203], v[176:179], v[80:83]
	global_load_lds_dwordx4 v11, s[4:5]
	v_mfma_f32_16x16x32_f16 v[84:87], v[204:207], v[176:179], v[84:87]
	v_mfma_f32_16x16x32_f16 v[88:91], v[192:195], v[180:183], v[88:91]
	v_mfma_f32_16x16x32_f16 v[92:95], v[196:199], v[180:183], v[92:95]
	v_mfma_f32_16x16x32_f16 v[96:99], v[200:203], v[180:183], v[96:99]
	s_add_u32 m0, s28, 0x4000
	v_mfma_f32_16x16x32_f16 v[100:103], v[204:207], v[180:183], v[100:103]
	global_load_lds_dwordx4 v12, s[4:5]
	v_mfma_f32_16x16x32_f16 v[104:107], v[192:195], v[184:187], v[104:107]
	v_mfma_f32_16x16x32_f16 v[108:111], v[196:199], v[184:187], v[108:111]
	v_mfma_f32_16x16x32_f16 v[112:115], v[200:203], v[184:187], v[112:115]
	v_mfma_f32_16x16x32_f16 v[116:119], v[204:207], v[184:187], v[116:119]
	s_waitcnt lgkmcnt(7)
	ds_read_b128 v[172:175], v16 offset:53248
	ds_read_b128 v[192:195], v18 offset:53248
	ds_read_b128 v[196:199], v18 offset:55296
	ds_read_b128 v[200:203], v18 offset:57344
	ds_read_b128 v[204:207], v18 offset:59392
	ds_read_b128 v[176:179], v16 offset:55296
	ds_read_b128 v[180:183], v16 offset:57344
	ds_read_b128 v[184:187], v16 offset:59392
	s_waitcnt lgkmcnt(8)
	v_mfma_f32_16x16x32_f16 v[56:59], v[156:159], v[136:139], v[56:59]
	s_add_u32 m0, s28, 0x6000
	v_mfma_f32_16x16x32_f16 v[60:63], v[160:163], v[136:139], v[60:63]
	global_load_lds_dwordx4 v13, s[4:5]
	s_add_u32 s4, s4, s20
	s_addc_u32 s5, s5, 0
	v_mfma_f32_16x16x32_f16 v[64:67], v[164:167], v[136:139], v[64:67]
	v_mfma_f32_16x16x32_f16 v[68:71], v[168:171], v[136:139], v[68:71]
	v_mfma_f32_16x16x32_f16 v[72:75], v[156:159], v[140:143], v[72:75]
	v_mfma_f32_16x16x32_f16 v[76:79], v[160:163], v[140:143], v[76:79]
	s_add_u32 m0, s28, 0x9000
	v_mfma_f32_16x16x32_f16 v[80:83], v[164:167], v[140:143], v[80:83]
	global_load_lds_dwordx4 v10, s[6:7]
	v_mfma_f32_16x16x32_f16 v[84:87], v[168:171], v[140:143], v[84:87]
	v_mfma_f32_16x16x32_f16 v[88:91], v[156:159], v[144:147], v[88:91]
	v_mfma_f32_16x16x32_f16 v[92:95], v[160:163], v[144:147], v[92:95]
	v_mfma_f32_16x16x32_f16 v[96:99], v[164:167], v[144:147], v[96:99]
	s_add_u32 m0, s28, 0xb000
	v_mfma_f32_16x16x32_f16 v[100:103], v[168:171], v[144:147], v[100:103]
	global_load_lds_dwordx4 v11, s[6:7]
	s_add_u32 s6, s6, s20
	s_addc_u32 s7, s7, 0
	v_mfma_f32_16x16x32_f16 v[104:107], v[156:159], v[148:151], v[104:107]
	v_mfma_f32_16x16x32_f16 v[108:111], v[160:163], v[148:151], v[108:111]
	v_mfma_f32_16x16x32_f16 v[112:115], v[164:167], v[148:151], v[112:115]
	v_mfma_f32_16x16x32_f16 v[116:119], v[168:171], v[148:151], v[116:119]
	s_waitcnt vmcnt(6) lgkmcnt(0)
	s_barrier
	s_waitcnt lgkmcnt(7)
	ds_read_b128 v[136:139], v19
	ds_read_b128 v[156:159], v21
	ds_read_b128 v[160:163], v21 offset:2048
	ds_read_b128 v[164:167], v21 offset:4096
	ds_read_b128 v[168:171], v21 offset:6144
	ds_read_b128 v[140:143], v19 offset:2048
	ds_read_b128 v[144:147], v19 offset:4096
	ds_read_b128 v[148:151], v19 offset:6144
	s_waitcnt lgkmcnt(8)
	v_mfma_f32_16x16x32_f16 v[56:59], v[192:195], v[172:175], v[56:59]
	s_add_u32 m0, s28, 0xd000
	v_mfma_f32_16x16x32_f16 v[60:63], v[196:199], v[172:175], v[60:63]
	global_load_lds_dwordx4 v10, s[4:5]
	v_mfma_f32_16x16x32_f16 v[64:67], v[200:203], v[172:175], v[64:67]
	v_mfma_f32_16x16x32_f16 v[68:71], v[204:207], v[172:175], v[68:71]
	v_mfma_f32_16x16x32_f16 v[72:75], v[192:195], v[176:179], v[72:75]
	v_mfma_f32_16x16x32_f16 v[76:79], v[196:199], v[176:179], v[76:79]
	s_add_u32 m0, s28, 0xf000
	v_mfma_f32_16x16x32_f16 v[80:83], v[200:203], v[176:179], v[80:83]
	global_load_lds_dwordx4 v11, s[4:5]
	v_mfma_f32_16x16x32_f16 v[84:87], v[204:207], v[176:179], v[84:87]
	v_mfma_f32_16x16x32_f16 v[88:91], v[192:195], v[180:183], v[88:91]
	v_mfma_f32_16x16x32_f16 v[92:95], v[196:199], v[180:183], v[92:95]
	v_mfma_f32_16x16x32_f16 v[96:99], v[200:203], v[180:183], v[96:99]
	s_add_u32 m0, s28, 0x11000
	v_mfma_f32_16x16x32_f16 v[100:103], v[204:207], v[180:183], v[100:103]
	global_load_lds_dwordx4 v12, s[4:5]
	v_mfma_f32_16x16x32_f16 v[104:107], v[192:195], v[184:187], v[104:107]
	v_mfma_f32_16x16x32_f16 v[108:111], v[196:199], v[184:187], v[108:111]
	v_mfma_f32_16x16x32_f16 v[112:115], v[200:203], v[184:187], v[112:115]
	v_mfma_f32_16x16x32_f16 v[116:119], v[204:207], v[184:187], v[116:119]
	s_waitcnt lgkmcnt(7)
	ds_read_b128 v[172:175], v20
	ds_read_b128 v[192:195], v22
	ds_read_b128 v[196:199], v22 offset:2048
	ds_read_b128 v[200:203], v22 offset:4096
	ds_read_b128 v[204:207], v22 offset:6144
	ds_read_b128 v[176:179], v20 offset:2048
	ds_read_b128 v[180:183], v20 offset:4096
	ds_read_b128 v[184:187], v20 offset:6144
	s_waitcnt lgkmcnt(8)
	v_mfma_f32_16x16x32_f16 v[56:59], v[156:159], v[136:139], v[56:59]
	s_add_u32 m0, s28, 0x13000
	v_mfma_f32_16x16x32_f16 v[60:63], v[160:163], v[136:139], v[60:63]
	global_load_lds_dwordx4 v13, s[4:5]
	s_add_u32 s4, s4, s20
	s_addc_u32 s5, s5, 0
	v_mfma_f32_16x16x32_f16 v[64:67], v[164:167], v[136:139], v[64:67]
	v_mfma_f32_16x16x32_f16 v[68:71], v[168:171], v[136:139], v[68:71]
	v_mfma_f32_16x16x32_f16 v[72:75], v[156:159], v[140:143], v[72:75]
	v_mfma_f32_16x16x32_f16 v[76:79], v[160:163], v[140:143], v[76:79]
	s_add_u32 m0, s28, 0x16000
	v_mfma_f32_16x16x32_f16 v[80:83], v[164:167], v[140:143], v[80:83]
	global_load_lds_dwordx4 v10, s[6:7]
	v_mfma_f32_16x16x32_f16 v[84:87], v[168:171], v[140:143], v[84:87]
	v_mfma_f32_16x16x32_f16 v[88:91], v[156:159], v[144:147], v[88:91]
	v_mfma_f32_16x16x32_f16 v[92:95], v[160:163], v[144:147], v[92:95]
	v_mfma_f32_16x16x32_f16 v[96:99], v[164:167], v[144:147], v[96:99]
	s_add_u32 m0, s28, 0x18000
	v_mfma_f32_16x16x32_f16 v[100:103], v[168:171], v[144:147], v[100:103]
	global_load_lds_dwordx4 v11, s[6:7]
	s_add_u32 s6, s6, s20
	s_addc_u32 s7, s7, 0
	v_mfma_f32_16x16x32_f16 v[104:107], v[156:159], v[148:151], v[104:107]
	v_mfma_f32_16x16x32_f16 v[108:111], v[160:163], v[148:151], v[108:111]
	v_mfma_f32_16x16x32_f16 v[112:115], v[164:167], v[148:151], v[112:115]
	v_mfma_f32_16x16x32_f16 v[116:119], v[168:171], v[148:151], v[116:119]
	s_waitcnt vmcnt(6) lgkmcnt(0)
	s_barrier
	s_waitcnt lgkmcnt(7)
	ds_read_b128 v[136:139], v15
	ds_read_b128 v[156:159], v17
	ds_read_b128 v[160:163], v17 offset:2048
	ds_read_b128 v[164:167], v17 offset:4096
	ds_read_b128 v[168:171], v17 offset:6144
	ds_read_b128 v[140:143], v15 offset:2048
	ds_read_b128 v[144:147], v15 offset:4096
	ds_read_b128 v[148:151], v15 offset:6144
	s_waitcnt lgkmcnt(8)
	v_mfma_f32_16x16x32_f16 v[56:59], v[192:195], v[172:175], v[56:59]
	s_add_u32 m0, s28, 0x1a000
	v_mfma_f32_16x16x32_f16 v[60:63], v[196:199], v[172:175], v[60:63]
	global_load_lds_dwordx4 v10, s[4:5]
	v_mfma_f32_16x16x32_f16 v[64:67], v[200:203], v[172:175], v[64:67]
	v_mfma_f32_16x16x32_f16 v[68:71], v[204:207], v[172:175], v[68:71]
	v_mfma_f32_16x16x32_f16 v[72:75], v[192:195], v[176:179], v[72:75]
	v_mfma_f32_16x16x32_f16 v[76:79], v[196:199], v[176:179], v[76:79]
	s_add_u32 m0, s28, 0x1c000
	v_mfma_f32_16x16x32_f16 v[80:83], v[200:203], v[176:179], v[80:83]
	global_load_lds_dwordx4 v11, s[4:5]
	v_mfma_f32_16x16x32_f16 v[84:87], v[204:207], v[176:179], v[84:87]
	v_mfma_f32_16x16x32_f16 v[88:91], v[192:195], v[180:183], v[88:91]
	v_mfma_f32_16x16x32_f16 v[92:95], v[196:199], v[180:183], v[92:95]
	v_mfma_f32_16x16x32_f16 v[96:99], v[200:203], v[180:183], v[96:99]
	s_add_u32 m0, s28, 0x1e000
	v_mfma_f32_16x16x32_f16 v[100:103], v[204:207], v[180:183], v[100:103]
	global_load_lds_dwordx4 v12, s[4:5]
	v_mfma_f32_16x16x32_f16 v[104:107], v[192:195], v[184:187], v[104:107]
	v_mfma_f32_16x16x32_f16 v[108:111], v[196:199], v[184:187], v[108:111]
	v_mfma_f32_16x16x32_f16 v[112:115], v[200:203], v[184:187], v[112:115]
	v_mfma_f32_16x16x32_f16 v[116:119], v[204:207], v[184:187], v[116:119]
	s_waitcnt lgkmcnt(7)
	ds_read_b128 v[172:175], v16
	ds_read_b128 v[192:195], v18
	ds_read_b128 v[196:199], v18 offset:2048
	ds_read_b128 v[200:203], v18 offset:4096
	ds_read_b128 v[204:207], v18 offset:6144
	ds_read_b128 v[176:179], v16 offset:2048
	ds_read_b128 v[180:183], v16 offset:4096
	ds_read_b128 v[184:187], v16 offset:6144
	s_waitcnt lgkmcnt(8)
	v_mfma_f32_16x16x32_f16 v[56:59], v[156:159], v[136:139], v[56:59]
	s_add_u32 m0, s28, 0x20000
	v_mfma_f32_16x16x32_f16 v[60:63], v[160:163], v[136:139], v[60:63]
	global_load_lds_dwordx4 v13, s[4:5]
	s_add_u32 s4, s4, s20
	s_addc_u32 s5, s5, 0
	v_mfma_f32_16x16x32_f16 v[64:67], v[164:167], v[136:139], v[64:67]
	v_mfma_f32_16x16x32_f16 v[68:71], v[168:171], v[136:139], v[68:71]
	v_mfma_f32_16x16x32_f16 v[72:75], v[156:159], v[140:143], v[72:75]
	v_mfma_f32_16x16x32_f16 v[76:79], v[160:163], v[140:143], v[76:79]
	s_add_u32 m0, s28, 0x23000
	v_mfma_f32_16x16x32_f16 v[80:83], v[164:167], v[140:143], v[80:83]
	global_load_lds_dwordx4 v10, s[6:7]
	v_mfma_f32_16x16x32_f16 v[84:87], v[168:171], v[140:143], v[84:87]
	v_mfma_f32_16x16x32_f16 v[88:91], v[156:159], v[144:147], v[88:91]
	v_mfma_f32_16x16x32_f16 v[92:95], v[160:163], v[144:147], v[92:95]
	v_mfma_f32_16x16x32_f16 v[96:99], v[164:167], v[144:147], v[96:99]
	s_add_u32 m0, s28, 0x25000
	v_mfma_f32_16x16x32_f16 v[100:103], v[168:171], v[144:147], v[100:103]
	global_load_lds_dwordx4 v11, s[6:7]
	s_add_u32 s6, s6, s20
	s_addc_u32 s7, s7, 0
	v_mfma_f32_16x16x32_f16 v[104:107], v[156:159], v[148:151], v[104:107]
	v_mfma_f32_16x16x32_f16 v[108:111], v[160:163], v[148:151], v[108:111]
	v_mfma_f32_16x16x32_f16 v[112:115], v[164:167], v[148:151], v[112:115]
	v_mfma_f32_16x16x32_f16 v[116:119], v[168:171], v[148:151], v[116:119]
	s_waitcnt vmcnt(6) lgkmcnt(0)
	s_barrier
	s_waitcnt lgkmcnt(7)
	ds_read_b128 v[136:139], v15 offset:53248
	ds_read_b128 v[156:159], v17 offset:53248
	ds_read_b128 v[160:163], v17 offset:55296
	ds_read_b128 v[164:167], v17 offset:57344
	ds_read_b128 v[168:171], v17 offset:59392
	ds_read_b128 v[140:143], v15 offset:55296
	ds_read_b128 v[144:147], v15 offset:57344
	ds_read_b128 v[148:151], v15 offset:59392
	s_waitcnt lgkmcnt(8)
	v_mfma_f32_16x16x32_f16 v[56:59], v[192:195], v[172:175], v[56:59]
	s_add_u32 m0, s28, 0x0
	v_mfma_f32_16x16x32_f16 v[60:63], v[196:199], v[172:175], v[60:63]
	global_load_lds_dwordx4 v10, s[4:5]
	v_mfma_f32_16x16x32_f16 v[64:67], v[200:203], v[172:175], v[64:67]
	v_mfma_f32_16x16x32_f16 v[68:71], v[204:207], v[172:175], v[68:71]
	v_mfma_f32_16x16x32_f16 v[72:75], v[192:195], v[176:179], v[72:75]
	v_mfma_f32_16x16x32_f16 v[76:79], v[196:199], v[176:179], v[76:79]
	s_add_u32 m0, s28, 0x2000
	v_mfma_f32_16x16x32_f16 v[80:83], v[200:203], v[176:179], v[80:83]
	global_load_lds_dwordx4 v11, s[4:5]
	v_mfma_f32_16x16x32_f16 v[84:87], v[204:207], v[176:179], v[84:87]
	v_mfma_f32_16x16x32_f16 v[88:91], v[192:195], v[180:183], v[88:91]
	v_mfma_f32_16x16x32_f16 v[92:95], v[196:199], v[180:183], v[92:95]
	v_mfma_f32_16x16x32_f16 v[96:99], v[200:203], v[180:183], v[96:99]
	s_add_u32 m0, s28, 0x4000
	v_mfma_f32_16x16x32_f16 v[100:103], v[204:207], v[180:183], v[100:103]
	global_load_lds_dwordx4 v12, s[4:5]
	v_mfma_f32_16x16x32_f16 v[104:107], v[192:195], v[184:187], v[104:107]
	v_mfma_f32_16x16x32_f16 v[108:111], v[196:199], v[184:187], v[108:111]
	v_mfma_f32_16x16x32_f16 v[112:115], v[200:203], v[184:187], v[112:115]
	v_mfma_f32_16x16x32_f16 v[116:119], v[204:207], v[184:187], v[116:119]
	s_waitcnt lgkmcnt(7)
	ds_read_b128 v[172:175], v16 offset:53248
	ds_read_b128 v[192:195], v18 offset:53248
	ds_read_b128 v[196:199], v18 offset:55296
	ds_read_b128 v[200:203], v18 offset:57344
	ds_read_b128 v[204:207], v18 offset:59392
	ds_read_b128 v[176:179], v16 offset:55296
	ds_read_b128 v[180:183], v16 offset:57344
	ds_read_b128 v[184:187], v16 offset:59392
	s_waitcnt lgkmcnt(8)
	v_mfma_f32_16x16x32_f16 v[56:59], v[156:159], v[136:139], v[56:59]
	s_add_u32 m0, s28, 0x6000
	v_mfma_f32_16x16x32_f16 v[60:63], v[160:163], v[136:139], v[60:63]
	global_load_lds_dwordx4 v13, s[4:5]
	s_add_u32 s4, s4, s20
	s_addc_u32 s5, s5, 0
	v_mfma_f32_16x16x32_f16 v[64:67], v[164:167], v[136:139], v[64:67]
	v_mfma_f32_16x16x32_f16 v[68:71], v[168:171], v[136:139], v[68:71]
	v_mfma_f32_16x16x32_f16 v[72:75], v[156:159], v[140:143], v[72:75]
	v_mfma_f32_16x16x32_f16 v[76:79], v[160:163], v[140:143], v[76:79]
	s_add_u32 m0, s28, 0x9000
	v_mfma_f32_16x16x32_f16 v[80:83], v[164:167], v[140:143], v[80:83]
	global_load_lds_dwordx4 v10, s[6:7]
	v_mfma_f32_16x16x32_f16 v[84:87], v[168:171], v[140:143], v[84:87]
	v_mfma_f32_16x16x32_f16 v[88:91], v[156:159], v[144:147], v[88:91]
	v_mfma_f32_16x16x32_f16 v[92:95], v[160:163], v[144:147], v[92:95]
	v_mfma_f32_16x16x32_f16 v[96:99], v[164:167], v[144:147], v[96:99]
	s_add_u32 m0, s28, 0xb000
	v_mfma_f32_16x16x32_f16 v[100:103], v[168:171], v[144:147], v[100:103]
	global_load_lds_dwordx4 v11, s[6:7]
	s_add_u32 s6, s6, s20
	s_addc_u32 s7, s7, 0
	v_mfma_f32_16x16x32_f16 v[104:107], v[156:159], v[148:151], v[104:107]
	v_mfma_f32_16x16x32_f16 v[108:111], v[160:163], v[148:151], v[108:111]
	v_mfma_f32_16x16x32_f16 v[112:115], v[164:167], v[148:151], v[112:115]
	v_mfma_f32_16x16x32_f16 v[116:119], v[168:171], v[148:151], v[116:119]
	s_waitcnt vmcnt(6) lgkmcnt(0)
	s_barrier
	s_waitcnt lgkmcnt(7)
	ds_read_b128 v[136:139], v19
	ds_read_b128 v[156:159], v21
	ds_read_b128 v[160:163], v21 offset:2048
	ds_read_b128 v[164:167], v21 offset:4096
	ds_read_b128 v[168:171], v21 offset:6144
	ds_read_b128 v[140:143], v19 offset:2048
	ds_read_b128 v[144:147], v19 offset:4096
	ds_read_b128 v[148:151], v19 offset:6144
	s_waitcnt lgkmcnt(8)
	v_mfma_f32_16x16x32_f16 v[56:59], v[192:195], v[172:175], v[56:59]
	s_add_u32 m0, s28, 0xd000
	v_mfma_f32_16x16x32_f16 v[60:63], v[196:199], v[172:175], v[60:63]
	global_load_lds_dwordx4 v10, s[4:5]
	v_mfma_f32_16x16x32_f16 v[64:67], v[200:203], v[172:175], v[64:67]
	v_mfma_f32_16x16x32_f16 v[68:71], v[204:207], v[172:175], v[68:71]
	v_mfma_f32_16x16x32_f16 v[72:75], v[192:195], v[176:179], v[72:75]
	v_mfma_f32_16x16x32_f16 v[76:79], v[196:199], v[176:179], v[76:79]
	s_add_u32 m0, s28, 0xf000
	v_mfma_f32_16x16x32_f16 v[80:83], v[200:203], v[176:179], v[80:83]
	global_load_lds_dwordx4 v11, s[4:5]
	v_mfma_f32_16x16x32_f16 v[84:87], v[204:207], v[176:179], v[84:87]
	v_mfma_f32_16x16x32_f16 v[88:91], v[192:195], v[180:183], v[88:91]
	v_mfma_f32_16x16x32_f16 v[92:95], v[196:199], v[180:183], v[92:95]
	v_mfma_f32_16x16x32_f16 v[96:99], v[200:203], v[180:183], v[96:99]
	s_add_u32 m0, s28, 0x11000
	v_mfma_f32_16x16x32_f16 v[100:103], v[204:207], v[180:183], v[100:103]
	global_load_lds_dwordx4 v12, s[4:5]
	v_mfma_f32_16x16x32_f16 v[104:107], v[192:195], v[184:187], v[104:107]
	v_mfma_f32_16x16x32_f16 v[108:111], v[196:199], v[184:187], v[108:111]
	v_mfma_f32_16x16x32_f16 v[112:115], v[200:203], v[184:187], v[112:115]
	v_mfma_f32_16x16x32_f16 v[116:119], v[204:207], v[184:187], v[116:119]
	s_waitcnt lgkmcnt(7)
	ds_read_b128 v[172:175], v20
	ds_read_b128 v[192:195], v22
	ds_read_b128 v[196:199], v22 offset:2048
	ds_read_b128 v[200:203], v22 offset:4096
	ds_read_b128 v[204:207], v22 offset:6144
	ds_read_b128 v[176:179], v20 offset:2048
	ds_read_b128 v[180:183], v20 offset:4096
	ds_read_b128 v[184:187], v20 offset:6144
	s_waitcnt lgkmcnt(8)
	v_mfma_f32_16x16x32_f16 v[56:59], v[156:159], v[136:139], v[56:59]
	s_add_u32 m0, s28, 0x13000
	v_mfma_f32_16x16x32_f16 v[60:63], v[160:163], v[136:139], v[60:63]
	global_load_lds_dwordx4 v13, s[4:5]
	s_add_u32 s4, s4, s20
	s_addc_u32 s5, s5, 0
	v_mfma_f32_16x16x32_f16 v[64:67], v[164:167], v[136:139], v[64:67]
	v_mfma_f32_16x16x32_f16 v[68:71], v[168:171], v[136:139], v[68:71]
	v_mfma_f32_16x16x32_f16 v[72:75], v[156:159], v[140:143], v[72:75]
	v_mfma_f32_16x16x32_f16 v[76:79], v[160:163], v[140:143], v[76:79]
	s_add_u32 m0, s28, 0x16000
	v_mfma_f32_16x16x32_f16 v[80:83], v[164:167], v[140:143], v[80:83]
	global_load_lds_dwordx4 v10, s[6:7]
	v_mfma_f32_16x16x32_f16 v[84:87], v[168:171], v[140:143], v[84:87]
	v_mfma_f32_16x16x32_f16 v[88:91], v[156:159], v[144:147], v[88:91]
	v_mfma_f32_16x16x32_f16 v[92:95], v[160:163], v[144:147], v[92:95]
	v_mfma_f32_16x16x32_f16 v[96:99], v[164:167], v[144:147], v[96:99]
	s_add_u32 m0, s28, 0x18000
	v_mfma_f32_16x16x32_f16 v[100:103], v[168:171], v[144:147], v[100:103]
	global_load_lds_dwordx4 v11, s[6:7]
	s_add_u32 s6, s6, s20
	s_addc_u32 s7, s7, 0
	v_mfma_f32_16x16x32_f16 v[104:107], v[156:159], v[148:151], v[104:107]
	v_mfma_f32_16x16x32_f16 v[108:111], v[160:163], v[148:151], v[108:111]
	v_mfma_f32_16x16x32_f16 v[112:115], v[164:167], v[148:151], v[112:115]
	v_mfma_f32_16x16x32_f16 v[116:119], v[168:171], v[148:151], v[116:119]
	s_waitcnt vmcnt(6) lgkmcnt(0)
	s_barrier
	s_waitcnt lgkmcnt(7)
	ds_read_b128 v[136:139], v15
	ds_read_b128 v[156:159], v17
	ds_read_b128 v[160:163], v17 offset:2048
	ds_read_b128 v[164:167], v17 offset:4096
	ds_read_b128 v[168:171], v17 offset:6144
	ds_read_b128 v[140:143], v15 offset:2048
	ds_read_b128 v[144:147], v15 offset:4096
	ds_read_b128 v[148:151], v15 offset:6144
	s_waitcnt lgkmcnt(8)
	v_mfma_f32_16x16x32_f16 v[56:59], v[192:195], v[172:175], v[56:59]
	s_add_u32 m0, s28, 0x1a000
	v_mfma_f32_16x16x32_f16 v[60:63], v[196:199], v[172:175], v[60:63]
	global_load_lds_dwordx4 v10, s[4:5]
	v_mfma_f32_16x16x32_f16 v[64:67], v[200:203], v[172:175], v[64:67]
	v_mfma_f32_16x16x32_f16 v[68:71], v[204:207], v[172:175], v[68:71]
	v_mfma_f32_16x16x32_f16 v[72:75], v[192:195], v[176:179], v[72:75]
	v_mfma_f32_16x16x32_f16 v[76:79], v[196:199], v[176:179], v[76:79]
	s_add_u32 m0, s28, 0x1c000
	v_mfma_f32_16x16x32_f16 v[80:83], v[200:203], v[176:179], v[80:83]
	global_load_lds_dwordx4 v11, s[4:5]
	v_mfma_f32_16x16x32_f16 v[84:87], v[204:207], v[176:179], v[84:87]
	v_mfma_f32_16x16x32_f16 v[88:91], v[192:195], v[180:183], v[88:91]
	v_mfma_f32_16x16x32_f16 v[92:95], v[196:199], v[180:183], v[92:95]
	v_mfma_f32_16x16x32_f16 v[96:99], v[200:203], v[180:183], v[96:99]
	s_add_u32 m0, s28, 0x1e000
	v_mfma_f32_16x16x32_f16 v[100:103], v[204:207], v[180:183], v[100:103]
	global_load_lds_dwordx4 v12, s[4:5]
	v_mfma_f32_16x16x32_f16 v[104:107], v[192:195], v[184:187], v[104:107]
	v_mfma_f32_16x16x32_f16 v[108:111], v[196:199], v[184:187], v[108:111]
	v_mfma_f32_16x16x32_f16 v[112:115], v[200:203], v[184:187], v[112:115]
	v_mfma_f32_16x16x32_f16 v[116:119], v[204:207], v[184:187], v[116:119]
	s_waitcnt lgkmcnt(7)
	ds_read_b128 v[172:175], v16
	ds_read_b128 v[192:195], v18
	ds_read_b128 v[196:199], v18 offset:2048
	ds_read_b128 v[200:203], v18 offset:4096
	ds_read_b128 v[204:207], v18 offset:6144
	ds_read_b128 v[176:179], v16 offset:2048
	ds_read_b128 v[180:183], v16 offset:4096
	ds_read_b128 v[184:187], v16 offset:6144
	s_waitcnt lgkmcnt(8)
	v_mfma_f32_16x16x32_f16 v[56:59], v[156:159], v[136:139], v[56:59]
	s_add_u32 m0, s28, 0x20000
	v_mfma_f32_16x16x32_f16 v[60:63], v[160:163], v[136:139], v[60:63]
	global_load_lds_dwordx4 v13, s[4:5]
	s_add_u32 s4, s4, s20
	s_addc_u32 s5, s5, 0
	v_mfma_f32_16x16x32_f16 v[64:67], v[164:167], v[136:139], v[64:67]
	v_mfma_f32_16x16x32_f16 v[68:71], v[168:171], v[136:139], v[68:71]
	v_mfma_f32_16x16x32_f16 v[72:75], v[156:159], v[140:143], v[72:75]
	v_mfma_f32_16x16x32_f16 v[76:79], v[160:163], v[140:143], v[76:79]
	s_add_u32 m0, s28, 0x23000
	v_mfma_f32_16x16x32_f16 v[80:83], v[164:167], v[140:143], v[80:83]
	global_load_lds_dwordx4 v10, s[6:7]
	v_mfma_f32_16x16x32_f16 v[84:87], v[168:171], v[140:143], v[84:87]
	v_mfma_f32_16x16x32_f16 v[88:91], v[156:159], v[144:147], v[88:91]
	v_mfma_f32_16x16x32_f16 v[92:95], v[160:163], v[144:147], v[92:95]
	v_mfma_f32_16x16x32_f16 v[96:99], v[164:167], v[144:147], v[96:99]
	s_add_u32 m0, s28, 0x25000
	v_mfma_f32_16x16x32_f16 v[100:103], v[168:171], v[144:147], v[100:103]
	global_load_lds_dwordx4 v11, s[6:7]
	s_add_u32 s6, s6, s20
	s_addc_u32 s7, s7, 0
	v_mfma_f32_16x16x32_f16 v[104:107], v[156:159], v[148:151], v[104:107]
	v_mfma_f32_16x16x32_f16 v[108:111], v[160:163], v[148:151], v[108:111]
	v_mfma_f32_16x16x32_f16 v[112:115], v[164:167], v[148:151], v[112:115]
	v_mfma_f32_16x16x32_f16 v[116:119], v[168:171], v[148:151], v[116:119]
	s_waitcnt vmcnt(6) lgkmcnt(0)
	s_barrier
	s_waitcnt lgkmcnt(7)
	ds_read_b128 v[136:139], v15 offset:53248
	ds_read_b128 v[156:159], v17 offset:53248
	ds_read_b128 v[160:163], v17 offset:55296
	ds_read_b128 v[164:167], v17 offset:57344
	ds_read_b128 v[168:171], v17 offset:59392
	ds_read_b128 v[140:143], v15 offset:55296
	ds_read_b128 v[144:147], v15 offset:57344
	ds_read_b128 v[148:151], v15 offset:59392
	s_waitcnt lgkmcnt(8)
	v_mfma_f32_16x16x32_f16 v[56:59], v[192:195], v[172:175], v[56:59]
	s_add_u32 m0, s28, 0x0
	v_mfma_f32_16x16x32_f16 v[60:63], v[196:199], v[172:175], v[60:63]
	global_load_lds_dwordx4 v10, s[4:5]
	v_mfma_f32_16x16x32_f16 v[64:67], v[200:203], v[172:175], v[64:67]
	v_mfma_f32_16x16x32_f16 v[68:71], v[204:207], v[172:175], v[68:71]
	v_mfma_f32_16x16x32_f16 v[72:75], v[192:195], v[176:179], v[72:75]
	v_mfma_f32_16x16x32_f16 v[76:79], v[196:199], v[176:179], v[76:79]
	s_add_u32 m0, s28, 0x2000
	v_mfma_f32_16x16x32_f16 v[80:83], v[200:203], v[176:179], v[80:83]
	global_load_lds_dwordx4 v11, s[4:5]
	v_mfma_f32_16x16x32_f16 v[84:87], v[204:207], v[176:179], v[84:87]
	v_mfma_f32_16x16x32_f16 v[88:91], v[192:195], v[180:183], v[88:91]
	v_mfma_f32_16x16x32_f16 v[92:95], v[196:199], v[180:183], v[92:95]
	v_mfma_f32_16x16x32_f16 v[96:99], v[200:203], v[180:183], v[96:99]
	s_add_u32 m0, s28, 0x4000
	v_mfma_f32_16x16x32_f16 v[100:103], v[204:207], v[180:183], v[100:103]
	global_load_lds_dwordx4 v12, s[4:5]
	v_mfma_f32_16x16x32_f16 v[104:107], v[192:195], v[184:187], v[104:107]
	v_mfma_f32_16x16x32_f16 v[108:111], v[196:199], v[184:187], v[108:111]
	v_mfma_f32_16x16x32_f16 v[112:115], v[200:203], v[184:187], v[112:115]
	v_mfma_f32_16x16x32_f16 v[116:119], v[204:207], v[184:187], v[116:119]
	s_waitcnt lgkmcnt(7)
	ds_read_b128 v[172:175], v16 offset:53248
	ds_read_b128 v[192:195], v18 offset:53248
	ds_read_b128 v[196:199], v18 offset:55296
	ds_read_b128 v[200:203], v18 offset:57344
	ds_read_b128 v[204:207], v18 offset:59392
	ds_read_b128 v[176:179], v16 offset:55296
	ds_read_b128 v[180:183], v16 offset:57344
	ds_read_b128 v[184:187], v16 offset:59392
	s_waitcnt lgkmcnt(8)
	v_mfma_f32_16x16x32_f16 v[56:59], v[156:159], v[136:139], v[56:59]
	s_add_u32 m0, s28, 0x6000
	v_mfma_f32_16x16x32_f16 v[60:63], v[160:163], v[136:139], v[60:63]
	global_load_lds_dwordx4 v13, s[4:5]
	s_add_u32 s4, s4, s20
	s_addc_u32 s5, s5, 0
	v_mfma_f32_16x16x32_f16 v[64:67], v[164:167], v[136:139], v[64:67]
	v_mfma_f32_16x16x32_f16 v[68:71], v[168:171], v[136:139], v[68:71]
	v_mfma_f32_16x16x32_f16 v[72:75], v[156:159], v[140:143], v[72:75]
	v_mfma_f32_16x16x32_f16 v[76:79], v[160:163], v[140:143], v[76:79]
	s_add_u32 m0, s28, 0x9000
	v_mfma_f32_16x16x32_f16 v[80:83], v[164:167], v[140:143], v[80:83]
	global_load_lds_dwordx4 v10, s[6:7]
	v_mfma_f32_16x16x32_f16 v[84:87], v[168:171], v[140:143], v[84:87]
	v_mfma_f32_16x16x32_f16 v[88:91], v[156:159], v[144:147], v[88:91]
	v_mfma_f32_16x16x32_f16 v[92:95], v[160:163], v[144:147], v[92:95]
	v_mfma_f32_16x16x32_f16 v[96:99], v[164:167], v[144:147], v[96:99]
	s_add_u32 m0, s28, 0xb000
	v_mfma_f32_16x16x32_f16 v[100:103], v[168:171], v[144:147], v[100:103]
	global_load_lds_dwordx4 v11, s[6:7]
	s_add_u32 s6, s6, s20
	s_addc_u32 s7, s7, 0
	v_mfma_f32_16x16x32_f16 v[104:107], v[156:159], v[148:151], v[104:107]
	v_mfma_f32_16x16x32_f16 v[108:111], v[160:163], v[148:151], v[108:111]
	v_mfma_f32_16x16x32_f16 v[112:115], v[164:167], v[148:151], v[112:115]
	v_mfma_f32_16x16x32_f16 v[116:119], v[168:171], v[148:151], v[116:119]
	s_waitcnt vmcnt(6) lgkmcnt(0)
	s_barrier
	s_waitcnt lgkmcnt(7)
	ds_read_b128 v[136:139], v19
	ds_read_b128 v[156:159], v21
	ds_read_b128 v[160:163], v21 offset:2048
	ds_read_b128 v[164:167], v21 offset:4096
	ds_read_b128 v[168:171], v21 offset:6144
	ds_read_b128 v[140:143], v19 offset:2048
	ds_read_b128 v[144:147], v19 offset:4096
	ds_read_b128 v[148:151], v19 offset:6144
	s_waitcnt lgkmcnt(8)
	v_mfma_f32_16x16x32_f16 v[56:59], v[192:195], v[172:175], v[56:59]
	s_add_u32 m0, s28, 0xd000
	v_mfma_f32_16x16x32_f16 v[60:63], v[196:199], v[172:175], v[60:63]
	global_load_lds_dwordx4 v10, s[4:5]
	v_mfma_f32_16x16x32_f16 v[64:67], v[200:203], v[172:175], v[64:67]
	v_mfma_f32_16x16x32_f16 v[68:71], v[204:207], v[172:175], v[68:71]
	v_mfma_f32_16x16x32_f16 v[72:75], v[192:195], v[176:179], v[72:75]
	v_mfma_f32_16x16x32_f16 v[76:79], v[196:199], v[176:179], v[76:79]
	s_add_u32 m0, s28, 0xf000
	v_mfma_f32_16x16x32_f16 v[80:83], v[200:203], v[176:179], v[80:83]
	global_load_lds_dwordx4 v11, s[4:5]
	v_mfma_f32_16x16x32_f16 v[84:87], v[204:207], v[176:179], v[84:87]
	v_mfma_f32_16x16x32_f16 v[88:91], v[192:195], v[180:183], v[88:91]
	v_mfma_f32_16x16x32_f16 v[92:95], v[196:199], v[180:183], v[92:95]
	v_mfma_f32_16x16x32_f16 v[96:99], v[200:203], v[180:183], v[96:99]
	s_add_u32 m0, s28, 0x11000
	v_mfma_f32_16x16x32_f16 v[100:103], v[204:207], v[180:183], v[100:103]
	global_load_lds_dwordx4 v12, s[4:5]
	v_mfma_f32_16x16x32_f16 v[104:107], v[192:195], v[184:187], v[104:107]
	v_mfma_f32_16x16x32_f16 v[108:111], v[196:199], v[184:187], v[108:111]
	v_mfma_f32_16x16x32_f16 v[112:115], v[200:203], v[184:187], v[112:115]
	v_mfma_f32_16x16x32_f16 v[116:119], v[204:207], v[184:187], v[116:119]
	s_waitcnt lgkmcnt(7)
	ds_read_b128 v[172:175], v20
	ds_read_b128 v[192:195], v22
	ds_read_b128 v[196:199], v22 offset:2048
	ds_read_b128 v[200:203], v22 offset:4096
	ds_read_b128 v[204:207], v22 offset:6144
	ds_read_b128 v[176:179], v20 offset:2048
	ds_read_b128 v[180:183], v20 offset:4096
	ds_read_b128 v[184:187], v20 offset:6144
	s_waitcnt lgkmcnt(8)
	v_mfma_f32_16x16x32_f16 v[56:59], v[156:159], v[136:139], v[56:59]
	s_add_u32 m0, s28, 0x13000
	v_mfma_f32_16x16x32_f16 v[60:63], v[160:163], v[136:139], v[60:63]
	global_load_lds_dwordx4 v13, s[4:5]
	s_add_u32 s4, s4, s20
	s_addc_u32 s5, s5, 0
	v_mfma_f32_16x16x32_f16 v[64:67], v[164:167], v[136:139], v[64:67]
	v_mfma_f32_16x16x32_f16 v[68:71], v[168:171], v[136:139], v[68:71]
	v_mfma_f32_16x16x32_f16 v[72:75], v[156:159], v[140:143], v[72:75]
	v_mfma_f32_16x16x32_f16 v[76:79], v[160:163], v[140:143], v[76:79]
	s_add_u32 m0, s28, 0x16000
	v_mfma_f32_16x16x32_f16 v[80:83], v[164:167], v[140:143], v[80:83]
	global_load_lds_dwordx4 v10, s[6:7]
	v_mfma_f32_16x16x32_f16 v[84:87], v[168:171], v[140:143], v[84:87]
	v_mfma_f32_16x16x32_f16 v[88:91], v[156:159], v[144:147], v[88:91]
	v_mfma_f32_16x16x32_f16 v[92:95], v[160:163], v[144:147], v[92:95]
	v_mfma_f32_16x16x32_f16 v[96:99], v[164:167], v[144:147], v[96:99]
	s_add_u32 m0, s28, 0x18000
	v_mfma_f32_16x16x32_f16 v[100:103], v[168:171], v[144:147], v[100:103]
	global_load_lds_dwordx4 v11, s[6:7]
	s_add_u32 s6, s6, s20
	s_addc_u32 s7, s7, 0
	v_mfma_f32_16x16x32_f16 v[104:107], v[156:159], v[148:151], v[104:107]
	v_mfma_f32_16x16x32_f16 v[108:111], v[160:163], v[148:151], v[108:111]
	v_mfma_f32_16x16x32_f16 v[112:115], v[164:167], v[148:151], v[112:115]
	v_mfma_f32_16x16x32_f16 v[116:119], v[168:171], v[148:151], v[116:119]
	s_waitcnt vmcnt(6) lgkmcnt(0)
	s_barrier
	s_waitcnt lgkmcnt(7)
	ds_read_b128 v[136:139], v15
	ds_read_b128 v[156:159], v17
	ds_read_b128 v[160:163], v17 offset:2048
	ds_read_b128 v[164:167], v17 offset:4096
	ds_read_b128 v[168:171], v17 offset:6144
	ds_read_b128 v[140:143], v15 offset:2048
	ds_read_b128 v[144:147], v15 offset:4096
	ds_read_b128 v[148:151], v15 offset:6144
	s_waitcnt lgkmcnt(8)
	v_mfma_f32_16x16x32_f16 v[56:59], v[192:195], v[172:175], v[56:59]
	s_add_u32 m0, s28, 0x1a000
	v_mfma_f32_16x16x32_f16 v[60:63], v[196:199], v[172:175], v[60:63]
	global_load_lds_dwordx4 v10, s[4:5]
	v_mfma_f32_16x16x32_f16 v[64:67], v[200:203], v[172:175], v[64:67]
	v_mfma_f32_16x16x32_f16 v[68:71], v[204:207], v[172:175], v[68:71]
	v_mfma_f32_16x16x32_f16 v[72:75], v[192:195], v[176:179], v[72:75]
	v_mfma_f32_16x16x32_f16 v[76:79], v[196:199], v[176:179], v[76:79]
	s_add_u32 m0, s28, 0x1c000
	v_mfma_f32_16x16x32_f16 v[80:83], v[200:203], v[176:179], v[80:83]
	global_load_lds_dwordx4 v11, s[4:5]
	v_mfma_f32_16x16x32_f16 v[84:87], v[204:207], v[176:179], v[84:87]
	v_mfma_f32_16x16x32_f16 v[88:91], v[192:195], v[180:183], v[88:91]
	v_mfma_f32_16x16x32_f16 v[92:95], v[196:199], v[180:183], v[92:95]
	v_mfma_f32_16x16x32_f16 v[96:99], v[200:203], v[180:183], v[96:99]
	s_add_u32 m0, s28, 0x1e000
	v_mfma_f32_16x16x32_f16 v[100:103], v[204:207], v[180:183], v[100:103]
	global_load_lds_dwordx4 v12, s[4:5]
	v_mfma_f32_16x16x32_f16 v[104:107], v[192:195], v[184:187], v[104:107]
	v_mfma_f32_16x16x32_f16 v[108:111], v[196:199], v[184:187], v[108:111]
	v_mfma_f32_16x16x32_f16 v[112:115], v[200:203], v[184:187], v[112:115]
	v_mfma_f32_16x16x32_f16 v[116:119], v[204:207], v[184:187], v[116:119]
	s_waitcnt lgkmcnt(7)
	ds_read_b128 v[172:175], v16
	ds_read_b128 v[192:195], v18
	ds_read_b128 v[196:199], v18 offset:2048
	ds_read_b128 v[200:203], v18 offset:4096
	ds_read_b128 v[204:207], v18 offset:6144
	ds_read_b128 v[176:179], v16 offset:2048
	ds_read_b128 v[180:183], v16 offset:4096
	ds_read_b128 v[184:187], v16 offset:6144
	s_waitcnt lgkmcnt(8)
	v_mfma_f32_16x16x32_f16 v[56:59], v[156:159], v[136:139], v[56:59]
	s_add_u32 m0, s28, 0x20000
	v_mfma_f32_16x16x32_f16 v[60:63], v[160:163], v[136:139], v[60:63]
	global_load_lds_dwordx4 v13, s[4:5]
	s_add_u32 s4, s4, s20
	s_addc_u32 s5, s5, 0
	v_mfma_f32_16x16x32_f16 v[64:67], v[164:167], v[136:139], v[64:67]
	v_mfma_f32_16x16x32_f16 v[68:71], v[168:171], v[136:139], v[68:71]
	v_mfma_f32_16x16x32_f16 v[72:75], v[156:159], v[140:143], v[72:75]
	v_mfma_f32_16x16x32_f16 v[76:79], v[160:163], v[140:143], v[76:79]
	s_add_u32 m0, s28, 0x23000
	v_mfma_f32_16x16x32_f16 v[80:83], v[164:167], v[140:143], v[80:83]
	global_load_lds_dwordx4 v10, s[6:7]
	v_mfma_f32_16x16x32_f16 v[84:87], v[168:171], v[140:143], v[84:87]
	v_mfma_f32_16x16x32_f16 v[88:91], v[156:159], v[144:147], v[88:91]
	v_mfma_f32_16x16x32_f16 v[92:95], v[160:163], v[144:147], v[92:95]
	v_mfma_f32_16x16x32_f16 v[96:99], v[164:167], v[144:147], v[96:99]
	s_add_u32 m0, s28, 0x25000
	v_mfma_f32_16x16x32_f16 v[100:103], v[168:171], v[144:147], v[100:103]
	global_load_lds_dwordx4 v11, s[6:7]
	s_add_u32 s6, s6, s20
	s_addc_u32 s7, s7, 0
	v_mfma_f32_16x16x32_f16 v[104:107], v[156:159], v[148:151], v[104:107]
	v_mfma_f32_16x16x32_f16 v[108:111], v[160:163], v[148:151], v[108:111]
	v_mfma_f32_16x16x32_f16 v[112:115], v[164:167], v[148:151], v[112:115]
	v_mfma_f32_16x16x32_f16 v[116:119], v[168:171], v[148:151], v[116:119]
	s_waitcnt vmcnt(6) lgkmcnt(0)
	s_barrier
	s_waitcnt lgkmcnt(7)
	ds_read_b128 v[136:139], v15 offset:53248
	ds_read_b128 v[156:159], v17 offset:53248
	ds_read_b128 v[160:163], v17 offset:55296
	ds_read_b128 v[164:167], v17 offset:57344
	ds_read_b128 v[168:171], v17 offset:59392
	ds_read_b128 v[140:143], v15 offset:55296
	ds_read_b128 v[144:147], v15 offset:57344
	ds_read_b128 v[148:151], v15 offset:59392
	s_waitcnt lgkmcnt(8)
	v_mfma_f32_16x16x32_f16 v[56:59], v[192:195], v[172:175], v[56:59]
	s_add_u32 m0, s28, 0x0
	v_mfma_f32_16x16x32_f16 v[60:63], v[196:199], v[172:175], v[60:63]
	global_load_lds_dwordx4 v10, s[4:5]
	v_mfma_f32_16x16x32_f16 v[64:67], v[200:203], v[172:175], v[64:67]
	v_mfma_f32_16x16x32_f16 v[68:71], v[204:207], v[172:175], v[68:71]
	v_mfma_f32_16x16x32_f16 v[72:75], v[192:195], v[176:179], v[72:75]
	v_mfma_f32_16x16x32_f16 v[76:79], v[196:199], v[176:179], v[76:79]
	s_add_u32 m0, s28, 0x2000
	v_mfma_f32_16x16x32_f16 v[80:83], v[200:203], v[176:179], v[80:83]
	global_load_lds_dwordx4 v11, s[4:5]
	v_mfma_f32_16x16x32_f16 v[84:87], v[204:207], v[176:179], v[84:87]
	v_mfma_f32_16x16x32_f16 v[88:91], v[192:195], v[180:183], v[88:91]
	v_mfma_f32_16x16x32_f16 v[92:95], v[196:199], v[180:183], v[92:95]
	v_mfma_f32_16x16x32_f16 v[96:99], v[200:203], v[180:183], v[96:99]
	s_add_u32 m0, s28, 0x4000
	v_mfma_f32_16x16x32_f16 v[100:103], v[204:207], v[180:183], v[100:103]
	global_load_lds_dwordx4 v12, s[4:5]
	v_mfma_f32_16x16x32_f16 v[104:107], v[192:195], v[184:187], v[104:107]
	v_mfma_f32_16x16x32_f16 v[108:111], v[196:199], v[184:187], v[108:111]
	v_mfma_f32_16x16x32_f16 v[112:115], v[200:203], v[184:187], v[112:115]
	v_mfma_f32_16x16x32_f16 v[116:119], v[204:207], v[184:187], v[116:119]
	s_waitcnt lgkmcnt(7)
	ds_read_b128 v[172:175], v16 offset:53248
	ds_read_b128 v[192:195], v18 offset:53248
	ds_read_b128 v[196:199], v18 offset:55296
	ds_read_b128 v[200:203], v18 offset:57344
	ds_read_b128 v[204:207], v18 offset:59392
	ds_read_b128 v[176:179], v16 offset:55296
	ds_read_b128 v[180:183], v16 offset:57344
	ds_read_b128 v[184:187], v16 offset:59392
	s_waitcnt lgkmcnt(8)
	v_mfma_f32_16x16x32_f16 v[56:59], v[156:159], v[136:139], v[56:59]
	s_add_u32 m0, s28, 0x6000
	v_mfma_f32_16x16x32_f16 v[60:63], v[160:163], v[136:139], v[60:63]
	global_load_lds_dwordx4 v13, s[4:5]
	s_add_u32 s4, s4, s20
	s_addc_u32 s5, s5, 0
	v_mfma_f32_16x16x32_f16 v[64:67], v[164:167], v[136:139], v[64:67]
	v_mfma_f32_16x16x32_f16 v[68:71], v[168:171], v[136:139], v[68:71]
	v_mfma_f32_16x16x32_f16 v[72:75], v[156:159], v[140:143], v[72:75]
	v_mfma_f32_16x16x32_f16 v[76:79], v[160:163], v[140:143], v[76:79]
	s_add_u32 m0, s28, 0x9000
	v_mfma_f32_16x16x32_f16 v[80:83], v[164:167], v[140:143], v[80:83]
	global_load_lds_dwordx4 v10, s[6:7]
	v_mfma_f32_16x16x32_f16 v[84:87], v[168:171], v[140:143], v[84:87]
	v_mfma_f32_16x16x32_f16 v[88:91], v[156:159], v[144:147], v[88:91]
	v_mfma_f32_16x16x32_f16 v[92:95], v[160:163], v[144:147], v[92:95]
	v_mfma_f32_16x16x32_f16 v[96:99], v[164:167], v[144:147], v[96:99]
	s_add_u32 m0, s28, 0xb000
	v_mfma_f32_16x16x32_f16 v[100:103], v[168:171], v[144:147], v[100:103]
	global_load_lds_dwordx4 v11, s[6:7]
	s_add_u32 s6, s6, s20
	s_addc_u32 s7, s7, 0
	v_mfma_f32_16x16x32_f16 v[104:107], v[156:159], v[148:151], v[104:107]
	v_mfma_f32_16x16x32_f16 v[108:111], v[160:163], v[148:151], v[108:111]
	v_mfma_f32_16x16x32_f16 v[112:115], v[164:167], v[148:151], v[112:115]
	v_mfma_f32_16x16x32_f16 v[116:119], v[168:171], v[148:151], v[116:119]
	s_waitcnt vmcnt(6) lgkmcnt(0)
	s_barrier
	s_waitcnt lgkmcnt(7)
	ds_read_b128 v[136:139], v19
	ds_read_b128 v[156:159], v21
	ds_read_b128 v[160:163], v21 offset:2048
	ds_read_b128 v[164:167], v21 offset:4096
	ds_read_b128 v[168:171], v21 offset:6144
	ds_read_b128 v[140:143], v19 offset:2048
	ds_read_b128 v[144:147], v19 offset:4096
	ds_read_b128 v[148:151], v19 offset:6144
	s_waitcnt lgkmcnt(8)
	v_mfma_f32_16x16x32_f16 v[56:59], v[192:195], v[172:175], v[56:59]
	s_add_u32 m0, s28, 0xd000
	v_mfma_f32_16x16x32_f16 v[60:63], v[196:199], v[172:175], v[60:63]
	global_load_lds_dwordx4 v10, s[4:5]
	v_mfma_f32_16x16x32_f16 v[64:67], v[200:203], v[172:175], v[64:67]
	v_mfma_f32_16x16x32_f16 v[68:71], v[204:207], v[172:175], v[68:71]
	v_mfma_f32_16x16x32_f16 v[72:75], v[192:195], v[176:179], v[72:75]
	v_mfma_f32_16x16x32_f16 v[76:79], v[196:199], v[176:179], v[76:79]
	s_add_u32 m0, s28, 0xf000
	v_mfma_f32_16x16x32_f16 v[80:83], v[200:203], v[176:179], v[80:83]
	global_load_lds_dwordx4 v11, s[4:5]
	v_mfma_f32_16x16x32_f16 v[84:87], v[204:207], v[176:179], v[84:87]
	v_mfma_f32_16x16x32_f16 v[88:91], v[192:195], v[180:183], v[88:91]
	v_mfma_f32_16x16x32_f16 v[92:95], v[196:199], v[180:183], v[92:95]
	v_mfma_f32_16x16x32_f16 v[96:99], v[200:203], v[180:183], v[96:99]
	s_add_u32 m0, s28, 0x11000
	v_mfma_f32_16x16x32_f16 v[100:103], v[204:207], v[180:183], v[100:103]
	global_load_lds_dwordx4 v12, s[4:5]
	v_mfma_f32_16x16x32_f16 v[104:107], v[192:195], v[184:187], v[104:107]
	v_mfma_f32_16x16x32_f16 v[108:111], v[196:199], v[184:187], v[108:111]
	v_mfma_f32_16x16x32_f16 v[112:115], v[200:203], v[184:187], v[112:115]
	v_mfma_f32_16x16x32_f16 v[116:119], v[204:207], v[184:187], v[116:119]
	s_waitcnt lgkmcnt(7)
	ds_read_b128 v[172:175], v20
	ds_read_b128 v[192:195], v22
	ds_read_b128 v[196:199], v22 offset:2048
	ds_read_b128 v[200:203], v22 offset:4096
	ds_read_b128 v[204:207], v22 offset:6144
	ds_read_b128 v[176:179], v20 offset:2048
	ds_read_b128 v[180:183], v20 offset:4096
	ds_read_b128 v[184:187], v20 offset:6144
	s_waitcnt lgkmcnt(8)
	v_mfma_f32_16x16x32_f16 v[56:59], v[156:159], v[136:139], v[56:59]
	s_add_u32 m0, s28, 0x13000
	v_mfma_f32_16x16x32_f16 v[60:63], v[160:163], v[136:139], v[60:63]
	global_load_lds_dwordx4 v13, s[4:5]
	s_add_u32 s4, s4, s20
	s_addc_u32 s5, s5, 0
	v_mfma_f32_16x16x32_f16 v[64:67], v[164:167], v[136:139], v[64:67]
	v_mfma_f32_16x16x32_f16 v[68:71], v[168:171], v[136:139], v[68:71]
	v_mfma_f32_16x16x32_f16 v[72:75], v[156:159], v[140:143], v[72:75]
	v_mfma_f32_16x16x32_f16 v[76:79], v[160:163], v[140:143], v[76:79]
	s_add_u32 m0, s28, 0x16000
	v_mfma_f32_16x16x32_f16 v[80:83], v[164:167], v[140:143], v[80:83]
	global_load_lds_dwordx4 v10, s[6:7]
	v_mfma_f32_16x16x32_f16 v[84:87], v[168:171], v[140:143], v[84:87]
	v_mfma_f32_16x16x32_f16 v[88:91], v[156:159], v[144:147], v[88:91]
	v_mfma_f32_16x16x32_f16 v[92:95], v[160:163], v[144:147], v[92:95]
	v_mfma_f32_16x16x32_f16 v[96:99], v[164:167], v[144:147], v[96:99]
	s_add_u32 m0, s28, 0x18000
	v_mfma_f32_16x16x32_f16 v[100:103], v[168:171], v[144:147], v[100:103]
	global_load_lds_dwordx4 v11, s[6:7]
	s_add_u32 s6, s6, s20
	s_addc_u32 s7, s7, 0
	v_mfma_f32_16x16x32_f16 v[104:107], v[156:159], v[148:151], v[104:107]
	v_mfma_f32_16x16x32_f16 v[108:111], v[160:163], v[148:151], v[108:111]
	v_mfma_f32_16x16x32_f16 v[112:115], v[164:167], v[148:151], v[112:115]
	v_mfma_f32_16x16x32_f16 v[116:119], v[168:171], v[148:151], v[116:119]
	s_waitcnt vmcnt(6) lgkmcnt(0)
	s_barrier
	s_waitcnt lgkmcnt(7)
	ds_read_b128 v[136:139], v15
	ds_read_b128 v[156:159], v17
	ds_read_b128 v[160:163], v17 offset:2048
	ds_read_b128 v[164:167], v17 offset:4096
	ds_read_b128 v[168:171], v17 offset:6144
	ds_read_b128 v[140:143], v15 offset:2048
	ds_read_b128 v[144:147], v15 offset:4096
	ds_read_b128 v[148:151], v15 offset:6144
	s_waitcnt lgkmcnt(8)
	v_mfma_f32_16x16x32_f16 v[56:59], v[192:195], v[172:175], v[56:59]
	s_add_u32 m0, s28, 0x1a000
	v_mfma_f32_16x16x32_f16 v[60:63], v[196:199], v[172:175], v[60:63]
	global_load_lds_dwordx4 v10, s[4:5]
	v_mfma_f32_16x16x32_f16 v[64:67], v[200:203], v[172:175], v[64:67]
	v_mfma_f32_16x16x32_f16 v[68:71], v[204:207], v[172:175], v[68:71]
	v_mfma_f32_16x16x32_f16 v[72:75], v[192:195], v[176:179], v[72:75]
	v_mfma_f32_16x16x32_f16 v[76:79], v[196:199], v[176:179], v[76:79]
	s_add_u32 m0, s28, 0x1c000
	v_mfma_f32_16x16x32_f16 v[80:83], v[200:203], v[176:179], v[80:83]
	global_load_lds_dwordx4 v11, s[4:5]
	v_mfma_f32_16x16x32_f16 v[84:87], v[204:207], v[176:179], v[84:87]
	v_mfma_f32_16x16x32_f16 v[88:91], v[192:195], v[180:183], v[88:91]
	v_mfma_f32_16x16x32_f16 v[92:95], v[196:199], v[180:183], v[92:95]
	v_mfma_f32_16x16x32_f16 v[96:99], v[200:203], v[180:183], v[96:99]
	s_add_u32 m0, s28, 0x1e000
	v_mfma_f32_16x16x32_f16 v[100:103], v[204:207], v[180:183], v[100:103]
	global_load_lds_dwordx4 v12, s[4:5]
	v_mfma_f32_16x16x32_f16 v[104:107], v[192:195], v[184:187], v[104:107]
	v_mfma_f32_16x16x32_f16 v[108:111], v[196:199], v[184:187], v[108:111]
	v_mfma_f32_16x16x32_f16 v[112:115], v[200:203], v[184:187], v[112:115]
	v_mfma_f32_16x16x32_f16 v[116:119], v[204:207], v[184:187], v[116:119]
	s_waitcnt lgkmcnt(7)
	ds_read_b128 v[172:175], v16
	ds_read_b128 v[192:195], v18
	ds_read_b128 v[196:199], v18 offset:2048
	ds_read_b128 v[200:203], v18 offset:4096
	ds_read_b128 v[204:207], v18 offset:6144
	ds_read_b128 v[176:179], v16 offset:2048
	ds_read_b128 v[180:183], v16 offset:4096
	ds_read_b128 v[184:187], v16 offset:6144
	s_waitcnt lgkmcnt(8)
	v_mfma_f32_16x16x32_f16 v[56:59], v[156:159], v[136:139], v[56:59]
	s_add_u32 m0, s28, 0x20000
	v_mfma_f32_16x16x32_f16 v[60:63], v[160:163], v[136:139], v[60:63]
	global_load_lds_dwordx4 v13, s[4:5]
	s_add_u32 s4, s4, s20
	s_addc_u32 s5, s5, 0
	v_mfma_f32_16x16x32_f16 v[64:67], v[164:167], v[136:139], v[64:67]
	v_mfma_f32_16x16x32_f16 v[68:71], v[168:171], v[136:139], v[68:71]
	v_mfma_f32_16x16x32_f16 v[72:75], v[156:159], v[140:143], v[72:75]
	v_mfma_f32_16x16x32_f16 v[76:79], v[160:163], v[140:143], v[76:79]
	s_add_u32 m0, s28, 0x23000
	v_mfma_f32_16x16x32_f16 v[80:83], v[164:167], v[140:143], v[80:83]
	global_load_lds_dwordx4 v10, s[6:7]
	v_mfma_f32_16x16x32_f16 v[84:87], v[168:171], v[140:143], v[84:87]
	v_mfma_f32_16x16x32_f16 v[88:91], v[156:159], v[144:147], v[88:91]
	v_mfma_f32_16x16x32_f16 v[92:95], v[160:163], v[144:147], v[92:95]
	v_mfma_f32_16x16x32_f16 v[96:99], v[164:167], v[144:147], v[96:99]
	s_add_u32 m0, s28, 0x25000
	v_mfma_f32_16x16x32_f16 v[100:103], v[168:171], v[144:147], v[100:103]
	global_load_lds_dwordx4 v11, s[6:7]
	s_add_u32 s6, s6, s20
	s_addc_u32 s7, s7, 0
	v_mfma_f32_16x16x32_f16 v[104:107], v[156:159], v[148:151], v[104:107]
	v_mfma_f32_16x16x32_f16 v[108:111], v[160:163], v[148:151], v[108:111]
	v_mfma_f32_16x16x32_f16 v[112:115], v[164:167], v[148:151], v[112:115]
	v_mfma_f32_16x16x32_f16 v[116:119], v[168:171], v[148:151], v[116:119]
	s_waitcnt vmcnt(6) lgkmcnt(0)
	s_barrier
	s_waitcnt lgkmcnt(7)
	ds_read_b128 v[136:139], v15 offset:53248
	ds_read_b128 v[156:159], v17 offset:53248
	ds_read_b128 v[160:163], v17 offset:55296
	ds_read_b128 v[164:167], v17 offset:57344
	ds_read_b128 v[168:171], v17 offset:59392
	ds_read_b128 v[140:143], v15 offset:55296
	ds_read_b128 v[144:147], v15 offset:57344
	ds_read_b128 v[148:151], v15 offset:59392
	s_waitcnt lgkmcnt(8)
	v_mfma_f32_16x16x32_f16 v[56:59], v[192:195], v[172:175], v[56:59]
	s_add_u32 m0, s28, 0x0
	v_mfma_f32_16x16x32_f16 v[60:63], v[196:199], v[172:175], v[60:63]
	global_load_lds_dwordx4 v10, s[4:5]
	v_mfma_f32_16x16x32_f16 v[64:67], v[200:203], v[172:175], v[64:67]
	v_mfma_f32_16x16x32_f16 v[68:71], v[204:207], v[172:175], v[68:71]
	v_mfma_f32_16x16x32_f16 v[72:75], v[192:195], v[176:179], v[72:75]
	v_mfma_f32_16x16x32_f16 v[76:79], v[196:199], v[176:179], v[76:79]
	s_add_u32 m0, s28, 0x2000
	v_mfma_f32_16x16x32_f16 v[80:83], v[200:203], v[176:179], v[80:83]
	global_load_lds_dwordx4 v11, s[4:5]
	v_mfma_f32_16x16x32_f16 v[84:87], v[204:207], v[176:179], v[84:87]
	v_mfma_f32_16x16x32_f16 v[88:91], v[192:195], v[180:183], v[88:91]
	v_mfma_f32_16x16x32_f16 v[92:95], v[196:199], v[180:183], v[92:95]
	v_mfma_f32_16x16x32_f16 v[96:99], v[200:203], v[180:183], v[96:99]
	s_add_u32 m0, s28, 0x4000
	v_mfma_f32_16x16x32_f16 v[100:103], v[204:207], v[180:183], v[100:103]
	global_load_lds_dwordx4 v12, s[4:5]
	v_mfma_f32_16x16x32_f16 v[104:107], v[192:195], v[184:187], v[104:107]
	v_mfma_f32_16x16x32_f16 v[108:111], v[196:199], v[184:187], v[108:111]
	v_mfma_f32_16x16x32_f16 v[112:115], v[200:203], v[184:187], v[112:115]
	v_mfma_f32_16x16x32_f16 v[116:119], v[204:207], v[184:187], v[116:119]
	s_waitcnt lgkmcnt(7)
	ds_read_b128 v[172:175], v16 offset:53248
	ds_read_b128 v[192:195], v18 offset:53248
	ds_read_b128 v[196:199], v18 offset:55296
	ds_read_b128 v[200:203], v18 offset:57344
	ds_read_b128 v[204:207], v18 offset:59392
	ds_read_b128 v[176:179], v16 offset:55296
	ds_read_b128 v[180:183], v16 offset:57344
	ds_read_b128 v[184:187], v16 offset:59392
	s_waitcnt lgkmcnt(8)
	v_mfma_f32_16x16x32_f16 v[56:59], v[156:159], v[136:139], v[56:59]
	s_add_u32 m0, s28, 0x6000
	v_mfma_f32_16x16x32_f16 v[60:63], v[160:163], v[136:139], v[60:63]
	global_load_lds_dwordx4 v13, s[4:5]
	s_add_u32 s4, s4, s20
	s_addc_u32 s5, s5, 0
	v_mfma_f32_16x16x32_f16 v[64:67], v[164:167], v[136:139], v[64:67]
	v_mfma_f32_16x16x32_f16 v[68:71], v[168:171], v[136:139], v[68:71]
	v_mfma_f32_16x16x32_f16 v[72:75], v[156:159], v[140:143], v[72:75]
	v_mfma_f32_16x16x32_f16 v[76:79], v[160:163], v[140:143], v[76:79]
	s_add_u32 m0, s28, 0x9000
	v_mfma_f32_16x16x32_f16 v[80:83], v[164:167], v[140:143], v[80:83]
	global_load_lds_dwordx4 v10, s[6:7]
	v_mfma_f32_16x16x32_f16 v[84:87], v[168:171], v[140:143], v[84:87]
	v_mfma_f32_16x16x32_f16 v[88:91], v[156:159], v[144:147], v[88:91]
	v_mfma_f32_16x16x32_f16 v[92:95], v[160:163], v[144:147], v[92:95]
	v_mfma_f32_16x16x32_f16 v[96:99], v[164:167], v[144:147], v[96:99]
	s_add_u32 m0, s28, 0xb000
	v_mfma_f32_16x16x32_f16 v[100:103], v[168:171], v[144:147], v[100:103]
	global_load_lds_dwordx4 v11, s[6:7]
	s_add_u32 s6, s6, s20
	s_addc_u32 s7, s7, 0
	v_mfma_f32_16x16x32_f16 v[104:107], v[156:159], v[148:151], v[104:107]
	v_mfma_f32_16x16x32_f16 v[108:111], v[160:163], v[148:151], v[108:111]
	v_mfma_f32_16x16x32_f16 v[112:115], v[164:167], v[148:151], v[112:115]
	v_mfma_f32_16x16x32_f16 v[116:119], v[168:171], v[148:151], v[116:119]
	s_waitcnt vmcnt(6) lgkmcnt(0)
	s_barrier
	s_waitcnt lgkmcnt(7)
	ds_read_b128 v[136:139], v19
	ds_read_b128 v[156:159], v21
	ds_read_b128 v[160:163], v21 offset:2048
	ds_read_b128 v[164:167], v21 offset:4096
	ds_read_b128 v[168:171], v21 offset:6144
	ds_read_b128 v[140:143], v19 offset:2048
	ds_read_b128 v[144:147], v19 offset:4096
	ds_read_b128 v[148:151], v19 offset:6144
	s_waitcnt lgkmcnt(8)
	v_mfma_f32_16x16x32_f16 v[56:59], v[192:195], v[172:175], v[56:59]
	v_mfma_f32_16x16x32_f16 v[60:63], v[196:199], v[172:175], v[60:63]
	v_mfma_f32_16x16x32_f16 v[64:67], v[200:203], v[172:175], v[64:67]
	v_mfma_f32_16x16x32_f16 v[68:71], v[204:207], v[172:175], v[68:71]
	v_mfma_f32_16x16x32_f16 v[72:75], v[192:195], v[176:179], v[72:75]
	v_mfma_f32_16x16x32_f16 v[76:79], v[196:199], v[176:179], v[76:79]
	v_mfma_f32_16x16x32_f16 v[80:83], v[200:203], v[176:179], v[80:83]
	v_mfma_f32_16x16x32_f16 v[84:87], v[204:207], v[176:179], v[84:87]
	v_mfma_f32_16x16x32_f16 v[88:91], v[192:195], v[180:183], v[88:91]
	v_mfma_f32_16x16x32_f16 v[92:95], v[196:199], v[180:183], v[92:95]
	v_mfma_f32_16x16x32_f16 v[96:99], v[200:203], v[180:183], v[96:99]
	v_mfma_f32_16x16x32_f16 v[100:103], v[204:207], v[180:183], v[100:103]
	v_mfma_f32_16x16x32_f16 v[104:107], v[192:195], v[184:187], v[104:107]
	v_mfma_f32_16x16x32_f16 v[108:111], v[196:199], v[184:187], v[108:111]
	v_mfma_f32_16x16x32_f16 v[112:115], v[200:203], v[184:187], v[112:115]
	v_mfma_f32_16x16x32_f16 v[116:119], v[204:207], v[184:187], v[116:119]
	s_waitcnt lgkmcnt(7)
	ds_read_b128 v[172:175], v20
	ds_read_b128 v[192:195], v22
	ds_read_b128 v[196:199], v22 offset:2048
	ds_read_b128 v[200:203], v22 offset:4096
	ds_read_b128 v[204:207], v22 offset:6144
	ds_read_b128 v[176:179], v20 offset:2048
	ds_read_b128 v[180:183], v20 offset:4096
	ds_read_b128 v[184:187], v20 offset:6144
	s_waitcnt lgkmcnt(8)
	v_mfma_f32_16x16x32_f16 v[56:59], v[156:159], v[136:139], v[56:59]
	v_mfma_f32_16x16x32_f16 v[60:63], v[160:163], v[136:139], v[60:63]
	v_mfma_f32_16x16x32_f16 v[64:67], v[164:167], v[136:139], v[64:67]
	v_mfma_f32_16x16x32_f16 v[68:71], v[168:171], v[136:139], v[68:71]
	v_mfma_f32_16x16x32_f16 v[72:75], v[156:159], v[140:143], v[72:75]
	v_mfma_f32_16x16x32_f16 v[76:79], v[160:163], v[140:143], v[76:79]
	v_mfma_f32_16x16x32_f16 v[80:83], v[164:167], v[140:143], v[80:83]
	v_mfma_f32_16x16x32_f16 v[84:87], v[168:171], v[140:143], v[84:87]
	v_mfma_f32_16x16x32_f16 v[88:91], v[156:159], v[144:147], v[88:91]
	v_mfma_f32_16x16x32_f16 v[92:95], v[160:163], v[144:147], v[92:95]
	v_mfma_f32_16x16x32_f16 v[96:99], v[164:167], v[144:147], v[96:99]
	v_mfma_f32_16x16x32_f16 v[100:103], v[168:171], v[144:147], v[100:103]
	v_mfma_f32_16x16x32_f16 v[104:107], v[156:159], v[148:151], v[104:107]
	v_mfma_f32_16x16x32_f16 v[108:111], v[160:163], v[148:151], v[108:111]
	v_mfma_f32_16x16x32_f16 v[112:115], v[164:167], v[148:151], v[112:115]
	v_mfma_f32_16x16x32_f16 v[116:119], v[168:171], v[148:151], v[116:119]
	s_waitcnt vmcnt(0) lgkmcnt(0)
	s_barrier
	s_waitcnt lgkmcnt(7)
	ds_read_b128 v[136:139], v15
	ds_read_b128 v[156:159], v17
	ds_read_b128 v[160:163], v17 offset:2048
	ds_read_b128 v[164:167], v17 offset:4096
	ds_read_b128 v[168:171], v17 offset:6144
	ds_read_b128 v[140:143], v15 offset:2048
	ds_read_b128 v[144:147], v15 offset:4096
	ds_read_b128 v[148:151], v15 offset:6144
	s_waitcnt lgkmcnt(8)
	v_mfma_f32_16x16x32_f16 v[56:59], v[192:195], v[172:175], v[56:59]
	v_mfma_f32_16x16x32_f16 v[60:63], v[196:199], v[172:175], v[60:63]
	v_mfma_f32_16x16x32_f16 v[64:67], v[200:203], v[172:175], v[64:67]
	v_mfma_f32_16x16x32_f16 v[68:71], v[204:207], v[172:175], v[68:71]
	v_mfma_f32_16x16x32_f16 v[72:75], v[192:195], v[176:179], v[72:75]
	v_mfma_f32_16x16x32_f16 v[76:79], v[196:199], v[176:179], v[76:79]
	v_mfma_f32_16x16x32_f16 v[80:83], v[200:203], v[176:179], v[80:83]
	v_mfma_f32_16x16x32_f16 v[84:87], v[204:207], v[176:179], v[84:87]
	v_mfma_f32_16x16x32_f16 v[88:91], v[192:195], v[180:183], v[88:91]
	v_mfma_f32_16x16x32_f16 v[92:95], v[196:199], v[180:183], v[92:95]
	v_mfma_f32_16x16x32_f16 v[96:99], v[200:203], v[180:183], v[96:99]
	v_mfma_f32_16x16x32_f16 v[100:103], v[204:207], v[180:183], v[100:103]
	v_mfma_f32_16x16x32_f16 v[104:107], v[192:195], v[184:187], v[104:107]
	v_mfma_f32_16x16x32_f16 v[108:111], v[196:199], v[184:187], v[108:111]
	v_mfma_f32_16x16x32_f16 v[112:115], v[200:203], v[184:187], v[112:115]
	v_mfma_f32_16x16x32_f16 v[116:119], v[204:207], v[184:187], v[116:119]
	s_waitcnt lgkmcnt(7)
	ds_read_b128 v[172:175], v16
	ds_read_b128 v[192:195], v18
	ds_read_b128 v[196:199], v18 offset:2048
	ds_read_b128 v[200:203], v18 offset:4096
	ds_read_b128 v[204:207], v18 offset:6144
	ds_read_b128 v[176:179], v16 offset:2048
	ds_read_b128 v[180:183], v16 offset:4096
	ds_read_b128 v[184:187], v16 offset:6144
	s_waitcnt lgkmcnt(8)
	v_mfma_f32_16x16x32_f16 v[56:59], v[156:159], v[136:139], v[56:59]
	v_mfma_f32_16x16x32_f16 v[60:63], v[160:163], v[136:139], v[60:63]
	v_mfma_f32_16x16x32_f16 v[64:67], v[164:167], v[136:139], v[64:67]
	v_mfma_f32_16x16x32_f16 v[68:71], v[168:171], v[136:139], v[68:71]
	v_mfma_f32_16x16x32_f16 v[72:75], v[156:159], v[140:143], v[72:75]
	v_mfma_f32_16x16x32_f16 v[76:79], v[160:163], v[140:143], v[76:79]
	v_mfma_f32_16x16x32_f16 v[80:83], v[164:167], v[140:143], v[80:83]
	v_mfma_f32_16x16x32_f16 v[84:87], v[168:171], v[140:143], v[84:87]
	v_mfma_f32_16x16x32_f16 v[88:91], v[156:159], v[144:147], v[88:91]
	v_mfma_f32_16x16x32_f16 v[92:95], v[160:163], v[144:147], v[92:95]
	v_mfma_f32_16x16x32_f16 v[96:99], v[164:167], v[144:147], v[96:99]
	v_mfma_f32_16x16x32_f16 v[100:103], v[168:171], v[144:147], v[100:103]
	v_mfma_f32_16x16x32_f16 v[104:107], v[156:159], v[148:151], v[104:107]
	v_mfma_f32_16x16x32_f16 v[108:111], v[160:163], v[148:151], v[108:111]
	v_mfma_f32_16x16x32_f16 v[112:115], v[164:167], v[148:151], v[112:115]
	v_mfma_f32_16x16x32_f16 v[116:119], v[168:171], v[148:151], v[116:119]
	s_waitcnt lgkmcnt(0)
	v_mfma_f32_16x16x32_f16 v[56:59], v[192:195], v[172:175], v[56:59]
	v_mfma_f32_16x16x32_f16 v[60:63], v[196:199], v[172:175], v[60:63]
	v_mfma_f32_16x16x32_f16 v[64:67], v[200:203], v[172:175], v[64:67]
	v_mfma_f32_16x16x32_f16 v[68:71], v[204:207], v[172:175], v[68:71]
	v_mfma_f32_16x16x32_f16 v[72:75], v[192:195], v[176:179], v[72:75]
	v_mfma_f32_16x16x32_f16 v[76:79], v[196:199], v[176:179], v[76:79]
	v_mfma_f32_16x16x32_f16 v[80:83], v[200:203], v[176:179], v[80:83]
	v_mfma_f32_16x16x32_f16 v[84:87], v[204:207], v[176:179], v[84:87]
	v_mfma_f32_16x16x32_f16 v[88:91], v[192:195], v[180:183], v[88:91]
	v_mfma_f32_16x16x32_f16 v[92:95], v[196:199], v[180:183], v[92:95]
	v_mfma_f32_16x16x32_f16 v[96:99], v[200:203], v[180:183], v[96:99]
	v_mfma_f32_16x16x32_f16 v[100:103], v[204:207], v[180:183], v[100:103]
	v_mfma_f32_16x16x32_f16 v[104:107], v[192:195], v[184:187], v[104:107]
	v_mfma_f32_16x16x32_f16 v[108:111], v[196:199], v[184:187], v[108:111]
	v_mfma_f32_16x16x32_f16 v[112:115], v[200:203], v[184:187], v[112:115]
	v_mfma_f32_16x16x32_f16 v[116:119], v[204:207], v[184:187], v[116:119]
	s_nop 7
	s_nop 1
	v_mov_b32_e32 v213, s19
	v_pk_add_f32 v[56:57], v[56:57], v[24:25]
	v_pk_add_f32 v[58:59], v[58:59], v[26:27]
	v_pk_add_f32 v[60:61], v[60:61], v[28:29]
	v_pk_add_f32 v[62:63], v[62:63], v[30:31]
	v_pk_add_f32 v[64:65], v[64:65], v[32:33]
	v_pk_add_f32 v[66:67], v[66:67], v[34:35]
	v_pk_add_f32 v[68:69], v[68:69], v[36:37]
	v_pk_add_f32 v[70:71], v[70:71], v[38:39]
	v_pk_mul_f32 v[208:209], v[56:57], v[56:57]
	v_pk_fma_f32 v[208:209], v[58:59], v[58:59], v[208:209]
	v_pk_fma_f32 v[208:209], v[60:61], v[60:61], v[208:209]
	v_pk_fma_f32 v[208:209], v[62:63], v[62:63], v[208:209]
	v_pk_fma_f32 v[208:209], v[64:65], v[64:65], v[208:209]
	v_pk_fma_f32 v[208:209], v[66:67], v[66:67], v[208:209]
	v_pk_fma_f32 v[208:209], v[68:69], v[68:69], v[208:209]
	v_pk_fma_f32 v[208:209], v[70:71], v[70:71], v[208:209]
	v_add_f32_e32 v208, v208, v209
	v_mov_b32_e32 v209, v208
	s_nop 1
	v_permlane16_swap_b32_e32 v208, v209
	v_add_f32_e32 v208, v208, v209
	v_mov_b32_e32 v209, v208
	s_nop 1
	v_permlane32_swap_b32_e32 v208, v209
	v_add_f32_e32 v208, v208, v209
	v_mov_b32_e32 v210, 0x358637bd
	v_fmac_f32_e32 v210, 0x3c800000, v208
	v_rsq_f32_e32 v210, v210
	s_add_u32 s24, s29, 0
	s_lshr_b32 s8, s24, 1
	s_lshl_b32 s8, s8, 12
	s_and_b32 s24, s24, 1
	s_lshl_b32 s24, s24, 8
	s_add_u32 s8, s8, s24
	v_mul_f32_e32 v210, v213, v210
	v_add_u32_e32 v212, s8, v23
	v_pk_mul_f32 v[56:57], v[56:57], v[210:211] op_sel_hi:[1,0]
	v_pk_mul_f32 v[58:59], v[58:59], v[210:211] op_sel_hi:[1,0]
	v_pk_mul_f32 v[56:57], v[56:57], v[40:41]
	v_pk_mul_f32 v[58:59], v[58:59], v[42:43]
	v_cvt_pk_f16_f32 v56, v56, v57
	v_cvt_pk_f16_f32 v57, v58, v59
	global_store_dwordx2 v212, v[56:57], s[22:23] offset:0
	v_pk_mul_f32 v[60:61], v[60:61], v[210:211] op_sel_hi:[1,0]
	v_pk_mul_f32 v[62:63], v[62:63], v[210:211] op_sel_hi:[1,0]
	v_pk_mul_f32 v[60:61], v[60:61], v[44:45]
	v_pk_mul_f32 v[62:63], v[62:63], v[46:47]
	v_cvt_pk_f16_f32 v60, v60, v61
	v_cvt_pk_f16_f32 v61, v62, v63
	global_store_dwordx2 v212, v[60:61], s[22:23] offset:1024
	v_pk_mul_f32 v[64:65], v[64:65], v[210:211] op_sel_hi:[1,0]
	v_pk_mul_f32 v[66:67], v[66:67], v[210:211] op_sel_hi:[1,0]
	v_pk_mul_f32 v[64:65], v[64:65], v[48:49]
	v_pk_mul_f32 v[66:67], v[66:67], v[50:51]
	v_cvt_pk_f16_f32 v64, v64, v65
	v_cvt_pk_f16_f32 v65, v66, v67
	global_store_dwordx2 v212, v[64:65], s[22:23] offset:2048
	v_pk_mul_f32 v[68:69], v[68:69], v[210:211] op_sel_hi:[1,0]
	v_pk_mul_f32 v[70:71], v[70:71], v[210:211] op_sel_hi:[1,0]
	v_pk_mul_f32 v[68:69], v[68:69], v[52:53]
	v_pk_mul_f32 v[70:71], v[70:71], v[54:55]
	v_cvt_pk_f16_f32 v68, v68, v69
	v_cvt_pk_f16_f32 v69, v70, v71
	global_store_dwordx2 v212, v[68:69], s[22:23] offset:3072
	v_pk_add_f32 v[72:73], v[72:73], v[24:25]
	v_pk_add_f32 v[74:75], v[74:75], v[26:27]
	v_pk_add_f32 v[76:77], v[76:77], v[28:29]
	v_pk_add_f32 v[78:79], v[78:79], v[30:31]
	v_pk_add_f32 v[80:81], v[80:81], v[32:33]
	v_pk_add_f32 v[82:83], v[82:83], v[34:35]
	v_pk_add_f32 v[84:85], v[84:85], v[36:37]
	v_pk_add_f32 v[86:87], v[86:87], v[38:39]
	v_pk_mul_f32 v[208:209], v[72:73], v[72:73]
	v_pk_fma_f32 v[208:209], v[74:75], v[74:75], v[208:209]
	v_pk_fma_f32 v[208:209], v[76:77], v[76:77], v[208:209]
	v_pk_fma_f32 v[208:209], v[78:79], v[78:79], v[208:209]
	v_pk_fma_f32 v[208:209], v[80:81], v[80:81], v[208:209]
	v_pk_fma_f32 v[208:209], v[82:83], v[82:83], v[208:209]
	v_pk_fma_f32 v[208:209], v[84:85], v[84:85], v[208:209]
	v_pk_fma_f32 v[208:209], v[86:87], v[86:87], v[208:209]
	v_add_f32_e32 v208, v208, v209
	v_mov_b32_e32 v209, v208
	s_nop 1
	v_permlane16_swap_b32_e32 v208, v209
	v_add_f32_e32 v208, v208, v209
	v_mov_b32_e32 v209, v208
	s_nop 1
	v_permlane32_swap_b32_e32 v208, v209
	v_add_f32_e32 v208, v208, v209
	v_mov_b32_e32 v210, 0x358637bd
	v_fmac_f32_e32 v210, 0x3c800000, v208
	v_rsq_f32_e32 v210, v210
	s_add_u32 s24, s29, 1
	s_lshr_b32 s8, s24, 1
	s_lshl_b32 s8, s8, 12
	s_and_b32 s24, s24, 1
	s_lshl_b32 s24, s24, 8
	s_add_u32 s8, s8, s24
	v_mul_f32_e32 v210, v213, v210
	v_add_u32_e32 v212, s8, v23
	v_pk_mul_f32 v[72:73], v[72:73], v[210:211] op_sel_hi:[1,0]
	v_pk_mul_f32 v[74:75], v[74:75], v[210:211] op_sel_hi:[1,0]
	v_pk_mul_f32 v[72:73], v[72:73], v[40:41]
	v_pk_mul_f32 v[74:75], v[74:75], v[42:43]
	v_cvt_pk_f16_f32 v72, v72, v73
	v_cvt_pk_f16_f32 v73, v74, v75
	global_store_dwordx2 v212, v[72:73], s[22:23] offset:0
	v_pk_mul_f32 v[76:77], v[76:77], v[210:211] op_sel_hi:[1,0]
	v_pk_mul_f32 v[78:79], v[78:79], v[210:211] op_sel_hi:[1,0]
	v_pk_mul_f32 v[76:77], v[76:77], v[44:45]
	v_pk_mul_f32 v[78:79], v[78:79], v[46:47]
	v_cvt_pk_f16_f32 v76, v76, v77
	v_cvt_pk_f16_f32 v77, v78, v79
	global_store_dwordx2 v212, v[76:77], s[22:23] offset:1024
	v_pk_mul_f32 v[80:81], v[80:81], v[210:211] op_sel_hi:[1,0]
	v_pk_mul_f32 v[82:83], v[82:83], v[210:211] op_sel_hi:[1,0]
	v_pk_mul_f32 v[80:81], v[80:81], v[48:49]
	v_pk_mul_f32 v[82:83], v[82:83], v[50:51]
	v_cvt_pk_f16_f32 v80, v80, v81
	v_cvt_pk_f16_f32 v81, v82, v83
	global_store_dwordx2 v212, v[80:81], s[22:23] offset:2048
	v_pk_mul_f32 v[84:85], v[84:85], v[210:211] op_sel_hi:[1,0]
	v_pk_mul_f32 v[86:87], v[86:87], v[210:211] op_sel_hi:[1,0]
	v_pk_mul_f32 v[84:85], v[84:85], v[52:53]
	v_pk_mul_f32 v[86:87], v[86:87], v[54:55]
	v_cvt_pk_f16_f32 v84, v84, v85
	v_cvt_pk_f16_f32 v85, v86, v87
	global_store_dwordx2 v212, v[84:85], s[22:23] offset:3072
	v_pk_add_f32 v[88:89], v[88:89], v[24:25]
	v_pk_add_f32 v[90:91], v[90:91], v[26:27]
	v_pk_add_f32 v[92:93], v[92:93], v[28:29]
	v_pk_add_f32 v[94:95], v[94:95], v[30:31]
	v_pk_add_f32 v[96:97], v[96:97], v[32:33]
	v_pk_add_f32 v[98:99], v[98:99], v[34:35]
	v_pk_add_f32 v[100:101], v[100:101], v[36:37]
	v_pk_add_f32 v[102:103], v[102:103], v[38:39]
	v_pk_mul_f32 v[208:209], v[88:89], v[88:89]
	v_pk_fma_f32 v[208:209], v[90:91], v[90:91], v[208:209]
	v_pk_fma_f32 v[208:209], v[92:93], v[92:93], v[208:209]
	v_pk_fma_f32 v[208:209], v[94:95], v[94:95], v[208:209]
	v_pk_fma_f32 v[208:209], v[96:97], v[96:97], v[208:209]
	v_pk_fma_f32 v[208:209], v[98:99], v[98:99], v[208:209]
	v_pk_fma_f32 v[208:209], v[100:101], v[100:101], v[208:209]
	v_pk_fma_f32 v[208:209], v[102:103], v[102:103], v[208:209]
	v_add_f32_e32 v208, v208, v209
	v_mov_b32_e32 v209, v208
	s_nop 1
	v_permlane16_swap_b32_e32 v208, v209
	v_add_f32_e32 v208, v208, v209
	v_mov_b32_e32 v209, v208
	s_nop 1
	v_permlane32_swap_b32_e32 v208, v209
	v_add_f32_e32 v208, v208, v209
	v_mov_b32_e32 v210, 0x358637bd
	v_fmac_f32_e32 v210, 0x3c800000, v208
	v_rsq_f32_e32 v210, v210
	s_add_u32 s24, s29, 2
	s_lshr_b32 s8, s24, 1
	s_lshl_b32 s8, s8, 12
	s_and_b32 s24, s24, 1
	s_lshl_b32 s24, s24, 8
	s_add_u32 s8, s8, s24
	v_mul_f32_e32 v210, v213, v210
	v_add_u32_e32 v212, s8, v23
	v_pk_mul_f32 v[88:89], v[88:89], v[210:211] op_sel_hi:[1,0]
	v_pk_mul_f32 v[90:91], v[90:91], v[210:211] op_sel_hi:[1,0]
	v_pk_mul_f32 v[88:89], v[88:89], v[40:41]
	v_pk_mul_f32 v[90:91], v[90:91], v[42:43]
	v_cvt_pk_f16_f32 v88, v88, v89
	v_cvt_pk_f16_f32 v89, v90, v91
	global_store_dwordx2 v212, v[88:89], s[22:23] offset:0
	v_pk_mul_f32 v[92:93], v[92:93], v[210:211] op_sel_hi:[1,0]
	v_pk_mul_f32 v[94:95], v[94:95], v[210:211] op_sel_hi:[1,0]
	v_pk_mul_f32 v[92:93], v[92:93], v[44:45]
	v_pk_mul_f32 v[94:95], v[94:95], v[46:47]
	v_cvt_pk_f16_f32 v92, v92, v93
	v_cvt_pk_f16_f32 v93, v94, v95
	global_store_dwordx2 v212, v[92:93], s[22:23] offset:1024
	v_pk_mul_f32 v[96:97], v[96:97], v[210:211] op_sel_hi:[1,0]
	v_pk_mul_f32 v[98:99], v[98:99], v[210:211] op_sel_hi:[1,0]
	v_pk_mul_f32 v[96:97], v[96:97], v[48:49]
	v_pk_mul_f32 v[98:99], v[98:99], v[50:51]
	v_cvt_pk_f16_f32 v96, v96, v97
	v_cvt_pk_f16_f32 v97, v98, v99
	global_store_dwordx2 v212, v[96:97], s[22:23] offset:2048
	v_pk_mul_f32 v[100:101], v[100:101], v[210:211] op_sel_hi:[1,0]
	v_pk_mul_f32 v[102:103], v[102:103], v[210:211] op_sel_hi:[1,0]
	v_pk_mul_f32 v[100:101], v[100:101], v[52:53]
	v_pk_mul_f32 v[102:103], v[102:103], v[54:55]
	v_cvt_pk_f16_f32 v100, v100, v101
	v_cvt_pk_f16_f32 v101, v102, v103
	global_store_dwordx2 v212, v[100:101], s[22:23] offset:3072
	v_pk_add_f32 v[104:105], v[104:105], v[24:25]
	v_pk_add_f32 v[106:107], v[106:107], v[26:27]
	v_pk_add_f32 v[108:109], v[108:109], v[28:29]
	v_pk_add_f32 v[110:111], v[110:111], v[30:31]
	v_pk_add_f32 v[112:113], v[112:113], v[32:33]
	v_pk_add_f32 v[114:115], v[114:115], v[34:35]
	v_pk_add_f32 v[116:117], v[116:117], v[36:37]
	v_pk_add_f32 v[118:119], v[118:119], v[38:39]
	v_pk_mul_f32 v[208:209], v[104:105], v[104:105]
	v_pk_fma_f32 v[208:209], v[106:107], v[106:107], v[208:209]
	v_pk_fma_f32 v[208:209], v[108:109], v[108:109], v[208:209]
	v_pk_fma_f32 v[208:209], v[110:111], v[110:111], v[208:209]
	v_pk_fma_f32 v[208:209], v[112:113], v[112:113], v[208:209]
	v_pk_fma_f32 v[208:209], v[114:115], v[114:115], v[208:209]
	v_pk_fma_f32 v[208:209], v[116:117], v[116:117], v[208:209]
	v_pk_fma_f32 v[208:209], v[118:119], v[118:119], v[208:209]
	v_add_f32_e32 v208, v208, v209
	v_mov_b32_e32 v209, v208
	s_nop 1
	v_permlane16_swap_b32_e32 v208, v209
	v_add_f32_e32 v208, v208, v209
	v_mov_b32_e32 v209, v208
	s_nop 1
	v_permlane32_swap_b32_e32 v208, v209
	v_add_f32_e32 v208, v208, v209
	v_mov_b32_e32 v210, 0x358637bd
	v_fmac_f32_e32 v210, 0x3c800000, v208
	v_rsq_f32_e32 v210, v210
	s_add_u32 s24, s29, 3
	s_lshr_b32 s8, s24, 1
	s_lshl_b32 s8, s8, 12
	s_and_b32 s24, s24, 1
	s_lshl_b32 s24, s24, 8
	s_add_u32 s8, s8, s24
	v_mul_f32_e32 v210, v213, v210
	v_add_u32_e32 v212, s8, v23
	v_pk_mul_f32 v[104:105], v[104:105], v[210:211] op_sel_hi:[1,0]
	v_pk_mul_f32 v[106:107], v[106:107], v[210:211] op_sel_hi:[1,0]
	v_pk_mul_f32 v[104:105], v[104:105], v[40:41]
	v_pk_mul_f32 v[106:107], v[106:107], v[42:43]
	v_cvt_pk_f16_f32 v104, v104, v105
	v_cvt_pk_f16_f32 v105, v106, v107
	global_store_dwordx2 v212, v[104:105], s[22:23] offset:0
	v_pk_mul_f32 v[108:109], v[108:109], v[210:211] op_sel_hi:[1,0]
	v_pk_mul_f32 v[110:111], v[110:111], v[210:211] op_sel_hi:[1,0]
	v_pk_mul_f32 v[108:109], v[108:109], v[44:45]
	v_pk_mul_f32 v[110:111], v[110:111], v[46:47]
	v_cvt_pk_f16_f32 v108, v108, v109
	v_cvt_pk_f16_f32 v109, v110, v111
	global_store_dwordx2 v212, v[108:109], s[22:23] offset:1024
	v_pk_mul_f32 v[112:113], v[112:113], v[210:211] op_sel_hi:[1,0]
	v_pk_mul_f32 v[114:115], v[114:115], v[210:211] op_sel_hi:[1,0]
	v_pk_mul_f32 v[112:113], v[112:113], v[48:49]
	v_pk_mul_f32 v[114:115], v[114:115], v[50:51]
	v_cvt_pk_f16_f32 v112, v112, v113
	v_cvt_pk_f16_f32 v113, v114, v115
	global_store_dwordx2 v212, v[112:113], s[22:23] offset:2048
	v_pk_mul_f32 v[116:117], v[116:117], v[210:211] op_sel_hi:[1,0]
	v_pk_mul_f32 v[118:119], v[118:119], v[210:211] op_sel_hi:[1,0]
	v_pk_mul_f32 v[116:117], v[116:117], v[52:53]
	v_pk_mul_f32 v[118:119], v[118:119], v[54:55]
	v_cvt_pk_f16_f32 v116, v116, v117
	v_cvt_pk_f16_f32 v117, v118, v119
	global_store_dwordx2 v212, v[116:117], s[22:23] offset:3072
	s_branch .Lpf_done
.Lpf_vVA:
	s_mul_i32 s25, s25, 0x50
	s_add_u32 s29, s10, s25
	s_lshr_b32 s29, s29, 4
	v_add_u32_e32 v5, s25, v3
	v_lshlrev_b32_e32 v5, 7, v5
	v_add_u32_e32 v15, v5, v6
	v_add_u32_e32 v16, v5, v7
	v_add_u32_e32 v5, 0x9000, v9
	v_add_u32_e32 v17, v5, v6
	v_add_u32_e32 v18, v5, v7
	v_add_u32_e32 v19, 0x1a000, v15
	v_add_u32_e32 v20, 0x1a000, v16
	v_add_u32_e32 v21, 0x1a000, v17
	v_add_u32_e32 v22, 0x1a000, v18
	v_lshlrev_b32_e32 v5, 2, v3
	global_load_dword v24, v5, s[14:15] offset:0
	global_load_dword v26, v5, s[14:15] offset:64
	global_load_dword v28, v5, s[14:15] offset:128
	global_load_dword v30, v5, s[14:15] offset:192
	s_add_u32 m0, s28, 0x0
	s_nop 0
	global_load_lds_dwordx4 v10, s[4:5]
	s_add_u32 m0, s28, 0x2000
	s_nop 0
	global_load_lds_dwordx4 v11, s[4:5]
	s_add_u32 m0, s28, 0x4000
	s_nop 0
	global_load_lds_dwordx4 v12, s[4:5]
	s_add_u32 m0, s28, 0x6000
	s_nop 0
	global_load_lds_dwordx4 v13, s[4:5]
	s_add_u32 m0, s28, 0x8000
	s_nop 0
	global_load_lds_dwordx4 v14, s[4:5]
	s_add_u32 s4, s4, s20
	s_addc_u32 s5, s5, 0
	s_add_u32 m0, s28, 0x9000
	s_nop 0
	global_load_lds_dwordx4 v10, s[6:7]
	s_add_u32 m0, s28, 0xb000
	s_nop 0
	global_load_lds_dwordx4 v11, s[6:7]
	s_add_u32 s6, s6, s20
	s_addc_u32 s7, s7, 0
	s_add_u32 m0, s28, 0xd000
	s_nop 0
	global_load_lds_dwordx4 v10, s[4:5]
	s_add_u32 m0, s28, 0xf000
	s_nop 0
	global_load_lds_dwordx4 v11, s[4:5]
	s_add_u32 m0, s28, 0x11000
	s_nop 0
	global_load_lds_dwordx4 v12, s[4:5]
	s_add_u32 m0, s28, 0x13000
	s_nop 0
	global_load_lds_dwordx4 v13, s[4:5]
	s_add_u32 m0, s28, 0x15000
	s_nop 0
	global_load_lds_dwordx4 v14, s[4:5]
	s_add_u32 s4, s4, s20
	s_addc_u32 s5, s5, 0
	s_add_u32 m0, s28, 0x16000
	s_nop 0
	global_load_lds_dwordx4 v10, s[6:7]
	s_add_u32 m0, s28, 0x18000
	s_nop 0
	global_load_lds_dwordx4 v11, s[6:7]
	s_add_u32 s6, s6, s20
	s_addc_u32 s7, s7, 0
	s_add_u32 m0, s28, 0x1a000
	s_nop 0
	global_load_lds_dwordx4 v10, s[4:5]
	s_add_u32 m0, s28, 0x1c000
	s_nop 0
	global_load_lds_dwordx4 v11, s[4:5]
	s_add_u32 m0, s28, 0x1e000
	s_nop 0
	global_load_lds_dwordx4 v12, s[4:5]
	s_add_u32 m0, s28, 0x20000
	s_nop 0
	global_load_lds_dwordx4 v13, s[4:5]
	s_add_u32 m0, s28, 0x22000
	s_nop 0
	global_load_lds_dwordx4 v14, s[4:5]
	s_add_u32 s4, s4, s20
	s_addc_u32 s5, s5, 0
	s_add_u32 m0, s28, 0x23000
	s_nop 0
	global_load_lds_dwordx4 v10, s[6:7]
	s_add_u32 m0, s28, 0x25000
	s_nop 0
	global_load_lds_dwordx4 v11, s[6:7]
	s_add_u32 s6, s6, s20
	s_addc_u32 s7, s7, 0
	s_waitcnt vmcnt(14) lgkmcnt(0)
	s_barrier
	s_waitcnt lgkmcnt(6)
	ds_read_b128 v[136:139], v15
	ds_read_b128 v[156:159], v17
	ds_read_b128 v[160:163], v17 offset:2048
	ds_read_b128 v[164:167], v17 offset:4096
	ds_read_b128 v[168:171], v17 offset:6144
	ds_read_b128 v[140:143], v15 offset:2048
	ds_read_b128 v[144:147], v15 offset:4096
	ds_read_b128 v[148:151], v15 offset:6144
	ds_read_b128 v[152:155], v15 offset:8192
	s_waitcnt lgkmcnt(6)
	ds_read_b128 v[172:175], v16
	ds_read_b128 v[192:195], v18
	ds_read_b128 v[196:199], v18 offset:2048
	ds_read_b128 v[200:203], v18 offset:4096
	ds_read_b128 v[204:207], v18 offset:6144
	ds_read_b128 v[176:179], v16 offset:2048
	ds_read_b128 v[180:183], v16 offset:4096
	ds_read_b128 v[184:187], v16 offset:6144
	ds_read_b128 v[188:191], v16 offset:8192
	s_waitcnt lgkmcnt(9)
	v_mfma_f32_16x16x32_f16 v[56:59], v[136:139], v[156:159], 0
	v_mfma_f32_16x16x32_f16 v[60:63], v[136:139], v[160:163], 0
	v_mfma_f32_16x16x32_f16 v[64:67], v[136:139], v[164:167], 0
	v_mfma_f32_16x16x32_f16 v[68:71], v[136:139], v[168:171], 0
	v_mfma_f32_16x16x32_f16 v[72:75], v[140:143], v[156:159], 0
	v_mfma_f32_16x16x32_f16 v[76:79], v[140:143], v[160:163], 0
	v_mfma_f32_16x16x32_f16 v[80:83], v[140:143], v[164:167], 0
	v_mfma_f32_16x16x32_f16 v[84:87], v[140:143], v[168:171], 0
	v_mfma_f32_16x16x32_f16 v[88:91], v[144:147], v[156:159], 0
	v_mfma_f32_16x16x32_f16 v[92:95], v[144:147], v[160:163], 0
	v_mfma_f32_16x16x32_f16 v[96:99], v[144:147], v[164:167], 0
	v_mfma_f32_16x16x32_f16 v[100:103], v[144:147], v[168:171], 0
	v_mfma_f32_16x16x32_f16 v[104:107], v[148:151], v[156:159], 0
	v_mfma_f32_16x16x32_f16 v[108:111], v[148:151], v[160:163], 0
	v_mfma_f32_16x16x32_f16 v[112:115], v[148:151], v[164:167], 0
	v_mfma_f32_16x16x32_f16 v[116:119], v[148:151], v[168:171], 0
	v_mfma_f32_16x16x32_f16 v[120:123], v[152:155], v[156:159], 0
	v_mfma_f32_16x16x32_f16 v[124:127], v[152:155], v[160:163], 0
	v_mfma_f32_16x16x32_f16 v[128:131], v[152:155], v[164:167], 0
	v_mfma_f32_16x16x32_f16 v[132:135], v[152:155], v[168:171], 0
	s_waitcnt vmcnt(7) lgkmcnt(0)
	s_barrier
	s_waitcnt lgkmcnt(6)
	ds_read_b128 v[136:139], v15 offset:53248
	ds_read_b128 v[156:159], v17 offset:53248
	ds_read_b128 v[160:163], v17 offset:55296
	ds_read_b128 v[164:167], v17 offset:57344
	ds_read_b128 v[168:171], v17 offset:59392
	ds_read_b128 v[140:143], v15 offset:55296
	ds_read_b128 v[144:147], v15 offset:57344
	ds_read_b128 v[148:151], v15 offset:59392
	ds_read_b128 v[152:155], v15 offset:61440
	s_waitcnt lgkmcnt(9)
	v_mfma_f32_16x16x32_f16 v[56:59], v[172:175], v[192:195], v[56:59]
	s_add_u32 m0, s28, 0x0
	v_mfma_f32_16x16x32_f16 v[60:63], v[172:175], v[196:199], v[60:63]
	global_load_lds_dwordx4 v10, s[4:5]
	v_mfma_f32_16x16x32_f16 v[64:67], v[172:175], v[200:203], v[64:67]
	v_mfma_f32_16x16x32_f16 v[68:71], v[172:175], v[204:207], v[68:71]
	v_mfma_f32_16x16x32_f16 v[72:75], v[176:179], v[192:195], v[72:75]
	v_mfma_f32_16x16x32_f16 v[76:79], v[176:179], v[196:199], v[76:79]
	s_add_u32 m0, s28, 0x2000
	v_mfma_f32_16x16x32_f16 v[80:83], v[176:179], v[200:203], v[80:83]
	global_load_lds_dwordx4 v11, s[4:5]
	v_mfma_f32_16x16x32_f16 v[84:87], v[176:179], v[204:207], v[84:87]
	v_mfma_f32_16x16x32_f16 v[88:91], v[180:183], v[192:195], v[88:91]
	v_mfma_f32_16x16x32_f16 v[92:95], v[180:183], v[196:199], v[92:95]
	v_mfma_f32_16x16x32_f16 v[96:99], v[180:183], v[200:203], v[96:99]
	s_add_u32 m0, s28, 0x4000
	v_mfma_f32_16x16x32_f16 v[100:103], v[180:183], v[204:207], v[100:103]
	global_load_lds_dwordx4 v12, s[4:5]
	v_mfma_f32_16x16x32_f16 v[104:107], v[184:187], v[192:195], v[104:107]
	v_mfma_f32_16x16x32_f16 v[108:111], v[184:187], v[196:199], v[108:111]
	v_mfma_f32_16x16x32_f16 v[112:115], v[184:187], v[200:203], v[112:115]
	v_mfma_f32_16x16x32_f16 v[116:119], v[184:187], v[204:207], v[116:119]
	s_add_u32 m0, s28, 0x6000
	v_mfma_f32_16x16x32_f16 v[120:123], v[188:191], v[192:195], v[120:123]
	global_load_lds_dwordx4 v13, s[4:5]
	v_mfma_f32_16x16x32_f16 v[124:127], v[188:191], v[196:199], v[124:127]
	v_mfma_f32_16x16x32_f16 v[128:131], v[188:191], v[200:203], v[128:131]
	v_mfma_f32_16x16x32_f16 v[132:135], v[188:191], v[204:207], v[132:135]
	s_waitcnt lgkmcnt(6)
	ds_read_b128 v[172:175], v16 offset:53248
	ds_read_b128 v[192:195], v18 offset:53248
	ds_read_b128 v[196:199], v18 offset:55296
	ds_read_b128 v[200:203], v18 offset:57344
	ds_read_b128 v[204:207], v18 offset:59392
	ds_read_b128 v[176:179], v16 offset:55296
	ds_read_b128 v[180:183], v16 offset:57344
	ds_read_b128 v[184:187], v16 offset:59392
	ds_read_b128 v[188:191], v16 offset:61440
	s_waitcnt lgkmcnt(9)
	v_mfma_f32_16x16x32_f16 v[56:59], v[136:139], v[156:159], v[56:59]
	s_add_u32 m0, s28, 0x8000
	v_mfma_f32_16x16x32_f16 v[60:63], v[136:139], v[160:163], v[60:63]
	global_load_lds_dwordx4 v14, s[4:5]
	s_add_u32 s4, s4, s20
	s_addc_u32 s5, s5, 0
	v_mfma_f32_16x16x32_f16 v[64:67], v[136:139], v[164:167], v[64:67]
	v_mfma_f32_16x16x32_f16 v[68:71], v[136:139], v[168:171], v[68:71]
	v_mfma_f32_16x16x32_f16 v[72:75], v[140:143], v[156:159], v[72:75]
	v_mfma_f32_16x16x32_f16 v[76:79], v[140:143], v[160:163], v[76:79]
	v_mfma_f32_16x16x32_f16 v[80:83], v[140:143], v[164:167], v[80:83]
	s_add_u32 m0, s28, 0x9000
	v_mfma_f32_16x16x32_f16 v[84:87], v[140:143], v[168:171], v[84:87]
	global_load_lds_dwordx4 v10, s[6:7]
	v_mfma_f32_16x16x32_f16 v[88:91], v[144:147], v[156:159], v[88:91]
	v_mfma_f32_16x16x32_f16 v[92:95], v[144:147], v[160:163], v[92:95]
	v_mfma_f32_16x16x32_f16 v[96:99], v[144:147], v[164:167], v[96:99]
	v_mfma_f32_16x16x32_f16 v[100:103], v[144:147], v[168:171], v[100:103]
	v_mfma_f32_16x16x32_f16 v[104:107], v[148:151], v[156:159], v[104:107]
	v_mfma_f32_16x16x32_f16 v[108:111], v[148:151], v[160:163], v[108:111]
	s_add_u32 m0, s28, 0xb000
	v_mfma_f32_16x16x32_f16 v[112:115], v[148:151], v[164:167], v[112:115]
	global_load_lds_dwordx4 v11, s[6:7]
	s_add_u32 s6, s6, s20
	s_addc_u32 s7, s7, 0
	v_mfma_f32_16x16x32_f16 v[116:119], v[148:151], v[168:171], v[116:119]
	v_mfma_f32_16x16x32_f16 v[120:123], v[152:155], v[156:159], v[120:123]
	v_mfma_f32_16x16x32_f16 v[124:127], v[152:155], v[160:163], v[124:127]
	v_mfma_f32_16x16x32_f16 v[128:131], v[152:155], v[164:167], v[128:131]
	v_mfma_f32_16x16x32_f16 v[132:135], v[152:155], v[168:171], v[132:135]
	s_waitcnt vmcnt(7) lgkmcnt(0)
	s_barrier
	s_waitcnt lgkmcnt(6)
	ds_read_b128 v[136:139], v19
	ds_read_b128 v[156:159], v21
	ds_read_b128 v[160:163], v21 offset:2048
	ds_read_b128 v[164:167], v21 offset:4096
	ds_read_b128 v[168:171], v21 offset:6144
	ds_read_b128 v[140:143], v19 offset:2048
	ds_read_b128 v[144:147], v19 offset:4096
	ds_read_b128 v[148:151], v19 offset:6144
	ds_read_b128 v[152:155], v19 offset:8192
	s_waitcnt lgkmcnt(9)
	v_mfma_f32_16x16x32_f16 v[56:59], v[172:175], v[192:195], v[56:59]
	s_add_u32 m0, s28, 0xd000
	v_mfma_f32_16x16x32_f16 v[60:63], v[172:175], v[196:199], v[60:63]
	global_load_lds_dwordx4 v10, s[4:5]
	v_mfma_f32_16x16x32_f16 v[64:67], v[172:175], v[200:203], v[64:67]
	v_mfma_f32_16x16x32_f16 v[68:71], v[172:175], v[204:207], v[68:71]
	v_mfma_f32_16x16x32_f16 v[72:75], v[176:179], v[192:195], v[72:75]
	v_mfma_f32_16x16x32_f16 v[76:79], v[176:179], v[196:199], v[76:79]
	s_add_u32 m0, s28, 0xf000
	v_mfma_f32_16x16x32_f16 v[80:83], v[176:179], v[200:203], v[80:83]
	global_load_lds_dwordx4 v11, s[4:5]
	v_mfma_f32_16x16x32_f16 v[84:87], v[176:179], v[204:207], v[84:87]
	v_mfma_f32_16x16x32_f16 v[88:91], v[180:183], v[192:195], v[88:91]
	v_mfma_f32_16x16x32_f16 v[92:95], v[180:183], v[196:199], v[92:95]
	v_mfma_f32_16x16x32_f16 v[96:99], v[180:183], v[200:203], v[96:99]
	s_add_u32 m0, s28, 0x11000
	v_mfma_f32_16x16x32_f16 v[100:103], v[180:183], v[204:207], v[100:103]
	global_load_lds_dwordx4 v12, s[4:5]
	v_mfma_f32_16x16x32_f16 v[104:107], v[184:187], v[192:195], v[104:107]
	v_mfma_f32_16x16x32_f16 v[108:111], v[184:187], v[196:199], v[108:111]
	v_mfma_f32_16x16x32_f16 v[112:115], v[184:187], v[200:203], v[112:115]
	v_mfma_f32_16x16x32_f16 v[116:119], v[184:187], v[204:207], v[116:119]
	s_add_u32 m0, s28, 0x13000
	v_mfma_f32_16x16x32_f16 v[120:123], v[188:191], v[192:195], v[120:123]
	global_load_lds_dwordx4 v13, s[4:5]
	v_mfma_f32_16x16x32_f16 v[124:127], v[188:191], v[196:199], v[124:127]
	v_mfma_f32_16x16x32_f16 v[128:131], v[188:191], v[200:203], v[128:131]
	v_mfma_f32_16x16x32_f16 v[132:135], v[188:191], v[204:207], v[132:135]
	s_waitcnt lgkmcnt(6)
	ds_read_b128 v[172:175], v20
	ds_read_b128 v[192:195], v22
	ds_read_b128 v[196:199], v22 offset:2048
	ds_read_b128 v[200:203], v22 offset:4096
	ds_read_b128 v[204:207], v22 offset:6144
	ds_read_b128 v[176:179], v20 offset:2048
	ds_read_b128 v[180:183], v20 offset:4096
	ds_read_b128 v[184:187], v20 offset:6144
	ds_read_b128 v[188:191], v20 offset:8192
	s_waitcnt lgkmcnt(9)
	v_mfma_f32_16x16x32_f16 v[56:59], v[136:139], v[156:159], v[56:59]
	s_add_u32 m0, s28, 0x15000
	v_mfma_f32_16x16x32_f16 v[60:63], v[136:139], v[160:163], v[60:63]
	global_load_lds_dwordx4 v14, s[4:5]
	s_add_u32 s4, s4, s20
	s_addc_u32 s5, s5, 0
	v_mfma_f32_16x16x32_f16 v[64:67], v[136:139], v[164:167], v[64:67]
	v_mfma_f32_16x16x32_f16 v[68:71], v[136:139], v[168:171], v[68:71]
	v_mfma_f32_16x16x32_f16 v[72:75], v[140:143], v[156:159], v[72:75]
	v_mfma_f32_16x16x32_f16 v[76:79], v[140:143], v[160:163], v[76:79]
	v_mfma_f32_16x16x32_f16 v[80:83], v[140:143], v[164:167], v[80:83]
	s_add_u32 m0, s28, 0x16000
	v_mfma_f32_16x16x32_f16 v[84:87], v[140:143], v[168:171], v[84:87]
	global_load_lds_dwordx4 v10, s[6:7]
	v_mfma_f32_16x16x32_f16 v[88:91], v[144:147], v[156:159], v[88:91]
	v_mfma_f32_16x16x32_f16 v[92:95], v[144:147], v[160:163], v[92:95]
	v_mfma_f32_16x16x32_f16 v[96:99], v[144:147], v[164:167], v[96:99]
	v_mfma_f32_16x16x32_f16 v[100:103], v[144:147], v[168:171], v[100:103]
	v_mfma_f32_16x16x32_f16 v[104:107], v[148:151], v[156:159], v[104:107]
	v_mfma_f32_16x16x32_f16 v[108:111], v[148:151], v[160:163], v[108:111]
	s_add_u32 m0, s28, 0x18000
	v_mfma_f32_16x16x32_f16 v[112:115], v[148:151], v[164:167], v[112:115]
	global_load_lds_dwordx4 v11, s[6:7]
	s_add_u32 s6, s6, s20
	s_addc_u32 s7, s7, 0
	v_mfma_f32_16x16x32_f16 v[116:119], v[148:151], v[168:171], v[116:119]
	v_mfma_f32_16x16x32_f16 v[120:123], v[152:155], v[156:159], v[120:123]
	v_mfma_f32_16x16x32_f16 v[124:127], v[152:155], v[160:163], v[124:127]
	v_mfma_f32_16x16x32_f16 v[128:131], v[152:155], v[164:167], v[128:131]
	v_mfma_f32_16x16x32_f16 v[132:135], v[152:155], v[168:171], v[132:135]
	s_waitcnt vmcnt(7) lgkmcnt(0)
	s_barrier
	s_waitcnt lgkmcnt(6)
	ds_read_b128 v[136:139], v15
	ds_read_b128 v[156:159], v17
	ds_read_b128 v[160:163], v17 offset:2048
	ds_read_b128 v[164:167], v17 offset:4096
	ds_read_b128 v[168:171], v17 offset:6144
	ds_read_b128 v[140:143], v15 offset:2048
	ds_read_b128 v[144:147], v15 offset:4096
	ds_read_b128 v[148:151], v15 offset:6144
	ds_read_b128 v[152:155], v15 offset:8192
	s_waitcnt lgkmcnt(9)
	v_mfma_f32_16x16x32_f16 v[56:59], v[172:175], v[192:195], v[56:59]
	s_add_u32 m0, s28, 0x1a000
	v_mfma_f32_16x16x32_f16 v[60:63], v[172:175], v[196:199], v[60:63]
	global_load_lds_dwordx4 v10, s[4:5]
	v_mfma_f32_16x16x32_f16 v[64:67], v[172:175], v[200:203], v[64:67]
	v_mfma_f32_16x16x32_f16 v[68:71], v[172:175], v[204:207], v[68:71]
	v_mfma_f32_16x16x32_f16 v[72:75], v[176:179], v[192:195], v[72:75]
	v_mfma_f32_16x16x32_f16 v[76:79], v[176:179], v[196:199], v[76:79]
	s_add_u32 m0, s28, 0x1c000
	v_mfma_f32_16x16x32_f16 v[80:83], v[176:179], v[200:203], v[80:83]
	global_load_lds_dwordx4 v11, s[4:5]
	v_mfma_f32_16x16x32_f16 v[84:87], v[176:179], v[204:207], v[84:87]
	v_mfma_f32_16x16x32_f16 v[88:91], v[180:183], v[192:195], v[88:91]
	v_mfma_f32_16x16x32_f16 v[92:95], v[180:183], v[196:199], v[92:95]
	v_mfma_f32_16x16x32_f16 v[96:99], v[180:183], v[200:203], v[96:99]
	s_add_u32 m0, s28, 0x1e000
	v_mfma_f32_16x16x32_f16 v[100:103], v[180:183], v[204:207], v[100:103]
	global_load_lds_dwordx4 v12, s[4:5]
	v_mfma_f32_16x16x32_f16 v[104:107], v[184:187], v[192:195], v[104:107]
	v_mfma_f32_16x16x32_f16 v[108:111], v[184:187], v[196:199], v[108:111]
	v_mfma_f32_16x16x32_f16 v[112:115], v[184:187], v[200:203], v[112:115]
	v_mfma_f32_16x16x32_f16 v[116:119], v[184:187], v[204:207], v[116:119]
	s_add_u32 m0, s28, 0x20000
	v_mfma_f32_16x16x32_f16 v[120:123], v[188:191], v[192:195], v[120:123]
	global_load_lds_dwordx4 v13, s[4:5]
	v_mfma_f32_16x16x32_f16 v[124:127], v[188:191], v[196:199], v[124:127]
	v_mfma_f32_16x16x32_f16 v[128:131], v[188:191], v[200:203], v[128:131]
	v_mfma_f32_16x16x32_f16 v[132:135], v[188:191], v[204:207], v[132:135]
	s_waitcnt lgkmcnt(6)
	ds_read_b128 v[172:175], v16
	ds_read_b128 v[192:195], v18
	ds_read_b128 v[196:199], v18 offset:2048
	ds_read_b128 v[200:203], v18 offset:4096
	ds_read_b128 v[204:207], v18 offset:6144
	ds_read_b128 v[176:179], v16 offset:2048
	ds_read_b128 v[180:183], v16 offset:4096
	ds_read_b128 v[184:187], v16 offset:6144
	ds_read_b128 v[188:191], v16 offset:8192
	s_waitcnt lgkmcnt(9)
	v_mfma_f32_16x16x32_f16 v[56:59], v[136:139], v[156:159], v[56:59]
	s_add_u32 m0, s28, 0x22000
	v_mfma_f32_16x16x32_f16 v[60:63], v[136:139], v[160:163], v[60:63]
	global_load_lds_dwordx4 v14, s[4:5]
	s_add_u32 s4, s4, s20
	s_addc_u32 s5, s5, 0
	v_mfma_f32_16x16x32_f16 v[64:67], v[136:139], v[164:167], v[64:67]
	v_mfma_f32_16x16x32_f16 v[68:71], v[136:139], v[168:171], v[68:71]
	v_mfma_f32_16x16x32_f16 v[72:75], v[140:143], v[156:159], v[72:75]
	v_mfma_f32_16x16x32_f16 v[76:79], v[140:143], v[160:163], v[76:79]
	v_mfma_f32_16x16x32_f16 v[80:83], v[140:143], v[164:167], v[80:83]
	s_add_u32 m0, s28, 0x23000
	v_mfma_f32_16x16x32_f16 v[84:87], v[140:143], v[168:171], v[84:87]
	global_load_lds_dwordx4 v10, s[6:7]
	v_mfma_f32_16x16x32_f16 v[88:91], v[144:147], v[156:159], v[88:91]
	v_mfma_f32_16x16x32_f16 v[92:95], v[144:147], v[160:163], v[92:95]
	v_mfma_f32_16x16x32_f16 v[96:99], v[144:147], v[164:167], v[96:99]
	v_mfma_f32_16x16x32_f16 v[100:103], v[144:147], v[168:171], v[100:103]
	v_mfma_f32_16x16x32_f16 v[104:107], v[148:151], v[156:159], v[104:107]
	v_mfma_f32_16x16x32_f16 v[108:111], v[148:151], v[160:163], v[108:111]
	s_add_u32 m0, s28, 0x25000
	v_mfma_f32_16x16x32_f16 v[112:115], v[148:151], v[164:167], v[112:115]
	global_load_lds_dwordx4 v11, s[6:7]
	s_add_u32 s6, s6, s20
	s_addc_u32 s7, s7, 0
	v_mfma_f32_16x16x32_f16 v[116:119], v[148:151], v[168:171], v[116:119]
	v_mfma_f32_16x16x32_f16 v[120:123], v[152:155], v[156:159], v[120:123]
	v_mfma_f32_16x16x32_f16 v[124:127], v[152:155], v[160:163], v[124:127]
	v_mfma_f32_16x16x32_f16 v[128:131], v[152:155], v[164:167], v[128:131]
	v_mfma_f32_16x16x32_f16 v[132:135], v[152:155], v[168:171], v[132:135]
	s_waitcnt vmcnt(7) lgkmcnt(0)
	s_barrier
	s_waitcnt lgkmcnt(6)
	ds_read_b128 v[136:139], v15 offset:53248
	ds_read_b128 v[156:159], v17 offset:53248
	ds_read_b128 v[160:163], v17 offset:55296
	ds_read_b128 v[164:167], v17 offset:57344
	ds_read_b128 v[168:171], v17 offset:59392
	ds_read_b128 v[140:143], v15 offset:55296
	ds_read_b128 v[144:147], v15 offset:57344
	ds_read_b128 v[148:151], v15 offset:59392
	ds_read_b128 v[152:155], v15 offset:61440
	s_waitcnt lgkmcnt(9)
	v_mfma_f32_16x16x32_f16 v[56:59], v[172:175], v[192:195], v[56:59]
	s_add_u32 m0, s28, 0x0
	v_mfma_f32_16x16x32_f16 v[60:63], v[172:175], v[196:199], v[60:63]
	global_load_lds_dwordx4 v10, s[4:5]
	v_mfma_f32_16x16x32_f16 v[64:67], v[172:175], v[200:203], v[64:67]
	v_mfma_f32_16x16x32_f16 v[68:71], v[172:175], v[204:207], v[68:71]
	v_mfma_f32_16x16x32_f16 v[72:75], v[176:179], v[192:195], v[72:75]
	v_mfma_f32_16x16x32_f16 v[76:79], v[176:179], v[196:199], v[76:79]
	s_add_u32 m0, s28, 0x2000
	v_mfma_f32_16x16x32_f16 v[80:83], v[176:179], v[200:203], v[80:83]
	global_load_lds_dwordx4 v11, s[4:5]
	v_mfma_f32_16x16x32_f16 v[84:87], v[176:179], v[204:207], v[84:87]
	v_mfma_f32_16x16x32_f16 v[88:91], v[180:183], v[192:195], v[88:91]
	v_mfma_f32_16x16x32_f16 v[92:95], v[180:183], v[196:199], v[92:95]
	v_mfma_f32_16x16x32_f16 v[96:99], v[180:183], v[200:203], v[96:99]
	s_add_u32 m0, s28, 0x4000
	v_mfma_f32_16x16x32_f16 v[100:103], v[180:183], v[204:207], v[100:103]
	global_load_lds_dwordx4 v12, s[4:5]
	v_mfma_f32_16x16x32_f16 v[104:107], v[184:187], v[192:195], v[104:107]
	v_mfma_f32_16x16x32_f16 v[108:111], v[184:187], v[196:199], v[108:111]
	v_mfma_f32_16x16x32_f16 v[112:115], v[184:187], v[200:203], v[112:115]
	v_mfma_f32_16x16x32_f16 v[116:119], v[184:187], v[204:207], v[116:119]
	s_add_u32 m0, s28, 0x6000
	v_mfma_f32_16x16x32_f16 v[120:123], v[188:191], v[192:195], v[120:123]
	global_load_lds_dwordx4 v13, s[4:5]
	v_mfma_f32_16x16x32_f16 v[124:127], v[188:191], v[196:199], v[124:127]
	v_mfma_f32_16x16x32_f16 v[128:131], v[188:191], v[200:203], v[128:131]
	v_mfma_f32_16x16x32_f16 v[132:135], v[188:191], v[204:207], v[132:135]
	s_waitcnt lgkmcnt(6)
	ds_read_b128 v[172:175], v16 offset:53248
	ds_read_b128 v[192:195], v18 offset:53248
	ds_read_b128 v[196:199], v18 offset:55296
	ds_read_b128 v[200:203], v18 offset:57344
	ds_read_b128 v[204:207], v18 offset:59392
	ds_read_b128 v[176:179], v16 offset:55296
	ds_read_b128 v[180:183], v16 offset:57344
	ds_read_b128 v[184:187], v16 offset:59392
	ds_read_b128 v[188:191], v16 offset:61440
	s_waitcnt lgkmcnt(9)
	v_mfma_f32_16x16x32_f16 v[56:59], v[136:139], v[156:159], v[56:59]
	s_add_u32 m0, s28, 0x8000
	v_mfma_f32_16x16x32_f16 v[60:63], v[136:139], v[160:163], v[60:63]
	global_load_lds_dwordx4 v14, s[4:5]
	s_add_u32 s4, s4, s20
	s_addc_u32 s5, s5, 0
	v_mfma_f32_16x16x32_f16 v[64:67], v[136:139], v[164:167], v[64:67]
	v_mfma_f32_16x16x32_f16 v[68:71], v[136:139], v[168:171], v[68:71]
	v_mfma_f32_16x16x32_f16 v[72:75], v[140:143], v[156:159], v[72:75]
	v_mfma_f32_16x16x32_f16 v[76:79], v[140:143], v[160:163], v[76:79]
	v_mfma_f32_16x16x32_f16 v[80:83], v[140:143], v[164:167], v[80:83]
	s_add_u32 m0, s28, 0x9000
	v_mfma_f32_16x16x32_f16 v[84:87], v[140:143], v[168:171], v[84:87]
	global_load_lds_dwordx4 v10, s[6:7]
	v_mfma_f32_16x16x32_f16 v[88:91], v[144:147], v[156:159], v[88:91]
	v_mfma_f32_16x16x32_f16 v[92:95], v[144:147], v[160:163], v[92:95]
	v_mfma_f32_16x16x32_f16 v[96:99], v[144:147], v[164:167], v[96:99]
	v_mfma_f32_16x16x32_f16 v[100:103], v[144:147], v[168:171], v[100:103]
	v_mfma_f32_16x16x32_f16 v[104:107], v[148:151], v[156:159], v[104:107]
	v_mfma_f32_16x16x32_f16 v[108:111], v[148:151], v[160:163], v[108:111]
	s_add_u32 m0, s28, 0xb000
	v_mfma_f32_16x16x32_f16 v[112:115], v[148:151], v[164:167], v[112:115]
	global_load_lds_dwordx4 v11, s[6:7]
	s_add_u32 s6, s6, s20
	s_addc_u32 s7, s7, 0
	v_mfma_f32_16x16x32_f16 v[116:119], v[148:151], v[168:171], v[116:119]
	v_mfma_f32_16x16x32_f16 v[120:123], v[152:155], v[156:159], v[120:123]
	v_mfma_f32_16x16x32_f16 v[124:127], v[152:155], v[160:163], v[124:127]
	v_mfma_f32_16x16x32_f16 v[128:131], v[152:155], v[164:167], v[128:131]
	v_mfma_f32_16x16x32_f16 v[132:135], v[152:155], v[168:171], v[132:135]
	s_waitcnt vmcnt(7) lgkmcnt(0)
	s_barrier
	s_waitcnt lgkmcnt(6)
	ds_read_b128 v[136:139], v19
	ds_read_b128 v[156:159], v21
	ds_read_b128 v[160:163], v21 offset:2048
	ds_read_b128 v[164:167], v21 offset:4096
	ds_read_b128 v[168:171], v21 offset:6144
	ds_read_b128 v[140:143], v19 offset:2048
	ds_read_b128 v[144:147], v19 offset:4096
	ds_read_b128 v[148:151], v19 offset:6144
	ds_read_b128 v[152:155], v19 offset:8192
	s_waitcnt lgkmcnt(9)
	v_mfma_f32_16x16x32_f16 v[56:59], v[172:175], v[192:195], v[56:59]
	s_add_u32 m0, s28, 0xd000
	v_mfma_f32_16x16x32_f16 v[60:63], v[172:175], v[196:199], v[60:63]
	global_load_lds_dwordx4 v10, s[4:5]
	v_mfma_f32_16x16x32_f16 v[64:67], v[172:175], v[200:203], v[64:67]
	v_mfma_f32_16x16x32_f16 v[68:71], v[172:175], v[204:207], v[68:71]
	v_mfma_f32_16x16x32_f16 v[72:75], v[176:179], v[192:195], v[72:75]
	v_mfma_f32_16x16x32_f16 v[76:79], v[176:179], v[196:199], v[76:79]
	s_add_u32 m0, s28, 0xf000
	v_mfma_f32_16x16x32_f16 v[80:83], v[176:179], v[200:203], v[80:83]
	global_load_lds_dwordx4 v11, s[4:5]
	v_mfma_f32_16x16x32_f16 v[84:87], v[176:179], v[204:207], v[84:87]
	v_mfma_f32_16x16x32_f16 v[88:91], v[180:183], v[192:195], v[88:91]
	v_mfma_f32_16x16x32_f16 v[92:95], v[180:183], v[196:199], v[92:95]
	v_mfma_f32_16x16x32_f16 v[96:99], v[180:183], v[200:203], v[96:99]
	s_add_u32 m0, s28, 0x11000
	v_mfma_f32_16x16x32_f16 v[100:103], v[180:183], v[204:207], v[100:103]
	global_load_lds_dwordx4 v12, s[4:5]
	v_mfma_f32_16x16x32_f16 v[104:107], v[184:187], v[192:195], v[104:107]
	v_mfma_f32_16x16x32_f16 v[108:111], v[184:187], v[196:199], v[108:111]
	v_mfma_f32_16x16x32_f16 v[112:115], v[184:187], v[200:203], v[112:115]
	v_mfma_f32_16x16x32_f16 v[116:119], v[184:187], v[204:207], v[116:119]
	s_add_u32 m0, s28, 0x13000
	v_mfma_f32_16x16x32_f16 v[120:123], v[188:191], v[192:195], v[120:123]
	global_load_lds_dwordx4 v13, s[4:5]
	v_mfma_f32_16x16x32_f16 v[124:127], v[188:191], v[196:199], v[124:127]
	v_mfma_f32_16x16x32_f16 v[128:131], v[188:191], v[200:203], v[128:131]
	v_mfma_f32_16x16x32_f16 v[132:135], v[188:191], v[204:207], v[132:135]
	s_waitcnt lgkmcnt(6)
	ds_read_b128 v[172:175], v20
	ds_read_b128 v[192:195], v22
	ds_read_b128 v[196:199], v22 offset:2048
	ds_read_b128 v[200:203], v22 offset:4096
	ds_read_b128 v[204:207], v22 offset:6144
	ds_read_b128 v[176:179], v20 offset:2048
	ds_read_b128 v[180:183], v20 offset:4096
	ds_read_b128 v[184:187], v20 offset:6144
	ds_read_b128 v[188:191], v20 offset:8192
	s_waitcnt lgkmcnt(9)
	v_mfma_f32_16x16x32_f16 v[56:59], v[136:139], v[156:159], v[56:59]
	s_add_u32 m0, s28, 0x15000
	v_mfma_f32_16x16x32_f16 v[60:63], v[136:139], v[160:163], v[60:63]
	global_load_lds_dwordx4 v14, s[4:5]
	s_add_u32 s4, s4, s20
	s_addc_u32 s5, s5, 0
	v_mfma_f32_16x16x32_f16 v[64:67], v[136:139], v[164:167], v[64:67]
	v_mfma_f32_16x16x32_f16 v[68:71], v[136:139], v[168:171], v[68:71]
	v_mfma_f32_16x16x32_f16 v[72:75], v[140:143], v[156:159], v[72:75]
	v_mfma_f32_16x16x32_f16 v[76:79], v[140:143], v[160:163], v[76:79]
	v_mfma_f32_16x16x32_f16 v[80:83], v[140:143], v[164:167], v[80:83]
	s_add_u32 m0, s28, 0x16000
	v_mfma_f32_16x16x32_f16 v[84:87], v[140:143], v[168:171], v[84:87]
	global_load_lds_dwordx4 v10, s[6:7]
	v_mfma_f32_16x16x32_f16 v[88:91], v[144:147], v[156:159], v[88:91]
	v_mfma_f32_16x16x32_f16 v[92:95], v[144:147], v[160:163], v[92:95]
	v_mfma_f32_16x16x32_f16 v[96:99], v[144:147], v[164:167], v[96:99]
	v_mfma_f32_16x16x32_f16 v[100:103], v[144:147], v[168:171], v[100:103]
	v_mfma_f32_16x16x32_f16 v[104:107], v[148:151], v[156:159], v[104:107]
	v_mfma_f32_16x16x32_f16 v[108:111], v[148:151], v[160:163], v[108:111]
	s_add_u32 m0, s28, 0x18000
	v_mfma_f32_16x16x32_f16 v[112:115], v[148:151], v[164:167], v[112:115]
	global_load_lds_dwordx4 v11, s[6:7]
	s_add_u32 s6, s6, s20
	s_addc_u32 s7, s7, 0
	v_mfma_f32_16x16x32_f16 v[116:119], v[148:151], v[168:171], v[116:119]
	v_mfma_f32_16x16x32_f16 v[120:123], v[152:155], v[156:159], v[120:123]
	v_mfma_f32_16x16x32_f16 v[124:127], v[152:155], v[160:163], v[124:127]
	v_mfma_f32_16x16x32_f16 v[128:131], v[152:155], v[164:167], v[128:131]
	v_mfma_f32_16x16x32_f16 v[132:135], v[152:155], v[168:171], v[132:135]
	s_waitcnt vmcnt(7) lgkmcnt(0)
	s_barrier
	s_waitcnt lgkmcnt(6)
	ds_read_b128 v[136:139], v15
	ds_read_b128 v[156:159], v17
	ds_read_b128 v[160:163], v17 offset:2048
	ds_read_b128 v[164:167], v17 offset:4096
	ds_read_b128 v[168:171], v17 offset:6144
	ds_read_b128 v[140:143], v15 offset:2048
	ds_read_b128 v[144:147], v15 offset:4096
	ds_read_b128 v[148:151], v15 offset:6144
	ds_read_b128 v[152:155], v15 offset:8192
	s_waitcnt lgkmcnt(9)
	v_mfma_f32_16x16x32_f16 v[56:59], v[172:175], v[192:195], v[56:59]
	s_add_u32 m0, s28, 0x1a000
	v_mfma_f32_16x16x32_f16 v[60:63], v[172:175], v[196:199], v[60:63]
	global_load_lds_dwordx4 v10, s[4:5]
	v_mfma_f32_16x16x32_f16 v[64:67], v[172:175], v[200:203], v[64:67]
	v_mfma_f32_16x16x32_f16 v[68:71], v[172:175], v[204:207], v[68:71]
	v_mfma_f32_16x16x32_f16 v[72:75], v[176:179], v[192:195], v[72:75]
	v_mfma_f32_16x16x32_f16 v[76:79], v[176:179], v[196:199], v[76:79]
	s_add_u32 m0, s28, 0x1c000
	v_mfma_f32_16x16x32_f16 v[80:83], v[176:179], v[200:203], v[80:83]
	global_load_lds_dwordx4 v11, s[4:5]
	v_mfma_f32_16x16x32_f16 v[84:87], v[176:179], v[204:207], v[84:87]
	v_mfma_f32_16x16x32_f16 v[88:91], v[180:183], v[192:195], v[88:91]
	v_mfma_f32_16x16x32_f16 v[92:95], v[180:183], v[196:199], v[92:95]
	v_mfma_f32_16x16x32_f16 v[96:99], v[180:183], v[200:203], v[96:99]
	s_add_u32 m0, s28, 0x1e000
	v_mfma_f32_16x16x32_f16 v[100:103], v[180:183], v[204:207], v[100:103]
	global_load_lds_dwordx4 v12, s[4:5]
	v_mfma_f32_16x16x32_f16 v[104:107], v[184:187], v[192:195], v[104:107]
	v_mfma_f32_16x16x32_f16 v[108:111], v[184:187], v[196:199], v[108:111]
	v_mfma_f32_16x16x32_f16 v[112:115], v[184:187], v[200:203], v[112:115]
	v_mfma_f32_16x16x32_f16 v[116:119], v[184:187], v[204:207], v[116:119]
	s_add_u32 m0, s28, 0x20000
	v_mfma_f32_16x16x32_f16 v[120:123], v[188:191], v[192:195], v[120:123]
	global_load_lds_dwordx4 v13, s[4:5]
	v_mfma_f32_16x16x32_f16 v[124:127], v[188:191], v[196:199], v[124:127]
	v_mfma_f32_16x16x32_f16 v[128:131], v[188:191], v[200:203], v[128:131]
	v_mfma_f32_16x16x32_f16 v[132:135], v[188:191], v[204:207], v[132:135]
	s_waitcnt lgkmcnt(6)
	ds_read_b128 v[172:175], v16
	ds_read_b128 v[192:195], v18
	ds_read_b128 v[196:199], v18 offset:2048
	ds_read_b128 v[200:203], v18 offset:4096
	ds_read_b128 v[204:207], v18 offset:6144
	ds_read_b128 v[176:179], v16 offset:2048
	ds_read_b128 v[180:183], v16 offset:4096
	ds_read_b128 v[184:187], v16 offset:6144
	ds_read_b128 v[188:191], v16 offset:8192
	s_waitcnt lgkmcnt(9)
	v_mfma_f32_16x16x32_f16 v[56:59], v[136:139], v[156:159], v[56:59]
	s_add_u32 m0, s28, 0x22000
	v_mfma_f32_16x16x32_f16 v[60:63], v[136:139], v[160:163], v[60:63]
	global_load_lds_dwordx4 v14, s[4:5]
	s_add_u32 s4, s4, s20
	s_addc_u32 s5, s5, 0
	v_mfma_f32_16x16x32_f16 v[64:67], v[136:139], v[164:167], v[64:67]
	v_mfma_f32_16x16x32_f16 v[68:71], v[136:139], v[168:171], v[68:71]
	v_mfma_f32_16x16x32_f16 v[72:75], v[140:143], v[156:159], v[72:75]
	v_mfma_f32_16x16x32_f16 v[76:79], v[140:143], v[160:163], v[76:79]
	v_mfma_f32_16x16x32_f16 v[80:83], v[140:143], v[164:167], v[80:83]
	s_add_u32 m0, s28, 0x23000
	v_mfma_f32_16x16x32_f16 v[84:87], v[140:143], v[168:171], v[84:87]
	global_load_lds_dwordx4 v10, s[6:7]
	v_mfma_f32_16x16x32_f16 v[88:91], v[144:147], v[156:159], v[88:91]
	v_mfma_f32_16x16x32_f16 v[92:95], v[144:147], v[160:163], v[92:95]
	v_mfma_f32_16x16x32_f16 v[96:99], v[144:147], v[164:167], v[96:99]
	v_mfma_f32_16x16x32_f16 v[100:103], v[144:147], v[168:171], v[100:103]
	v_mfma_f32_16x16x32_f16 v[104:107], v[148:151], v[156:159], v[104:107]
	v_mfma_f32_16x16x32_f16 v[108:111], v[148:151], v[160:163], v[108:111]
	s_add_u32 m0, s28, 0x25000
	v_mfma_f32_16x16x32_f16 v[112:115], v[148:151], v[164:167], v[112:115]
	global_load_lds_dwordx4 v11, s[6:7]
	s_add_u32 s6, s6, s20
	s_addc_u32 s7, s7, 0
	v_mfma_f32_16x16x32_f16 v[116:119], v[148:151], v[168:171], v[116:119]
	v_mfma_f32_16x16x32_f16 v[120:123], v[152:155], v[156:159], v[120:123]
	v_mfma_f32_16x16x32_f16 v[124:127], v[152:155], v[160:163], v[124:127]
	v_mfma_f32_16x16x32_f16 v[128:131], v[152:155], v[164:167], v[128:131]
	v_mfma_f32_16x16x32_f16 v[132:135], v[152:155], v[168:171], v[132:135]
	s_waitcnt vmcnt(7) lgkmcnt(0)
	s_barrier
	s_waitcnt lgkmcnt(6)
	ds_read_b128 v[136:139], v15 offset:53248
	ds_read_b128 v[156:159], v17 offset:53248
	ds_read_b128 v[160:163], v17 offset:55296
	ds_read_b128 v[164:167], v17 offset:57344
	ds_read_b128 v[168:171], v17 offset:59392
	ds_read_b128 v[140:143], v15 offset:55296
	ds_read_b128 v[144:147], v15 offset:57344
	ds_read_b128 v[148:151], v15 offset:59392
	ds_read_b128 v[152:155], v15 offset:61440
	s_waitcnt lgkmcnt(9)
	v_mfma_f32_16x16x32_f16 v[56:59], v[172:175], v[192:195], v[56:59]
	s_add_u32 m0, s28, 0x0
	v_mfma_f32_16x16x32_f16 v[60:63], v[172:175], v[196:199], v[60:63]
	global_load_lds_dwordx4 v10, s[4:5]
	v_mfma_f32_16x16x32_f16 v[64:67], v[172:175], v[200:203], v[64:67]
	v_mfma_f32_16x16x32_f16 v[68:71], v[172:175], v[204:207], v[68:71]
	v_mfma_f32_16x16x32_f16 v[72:75], v[176:179], v[192:195], v[72:75]
	v_mfma_f32_16x16x32_f16 v[76:79], v[176:179], v[196:199], v[76:79]
	s_add_u32 m0, s28, 0x2000
	v_mfma_f32_16x16x32_f16 v[80:83], v[176:179], v[200:203], v[80:83]
	global_load_lds_dwordx4 v11, s[4:5]
	v_mfma_f32_16x16x32_f16 v[84:87], v[176:179], v[204:207], v[84:87]
	v_mfma_f32_16x16x32_f16 v[88:91], v[180:183], v[192:195], v[88:91]
	v_mfma_f32_16x16x32_f16 v[92:95], v[180:183], v[196:199], v[92:95]
	v_mfma_f32_16x16x32_f16 v[96:99], v[180:183], v[200:203], v[96:99]
	s_add_u32 m0, s28, 0x4000
	v_mfma_f32_16x16x32_f16 v[100:103], v[180:183], v[204:207], v[100:103]
	global_load_lds_dwordx4 v12, s[4:5]
	v_mfma_f32_16x16x32_f16 v[104:107], v[184:187], v[192:195], v[104:107]
	v_mfma_f32_16x16x32_f16 v[108:111], v[184:187], v[196:199], v[108:111]
	v_mfma_f32_16x16x32_f16 v[112:115], v[184:187], v[200:203], v[112:115]
	v_mfma_f32_16x16x32_f16 v[116:119], v[184:187], v[204:207], v[116:119]
	s_add_u32 m0, s28, 0x6000
	v_mfma_f32_16x16x32_f16 v[120:123], v[188:191], v[192:195], v[120:123]
	global_load_lds_dwordx4 v13, s[4:5]
	v_mfma_f32_16x16x32_f16 v[124:127], v[188:191], v[196:199], v[124:127]
	v_mfma_f32_16x16x32_f16 v[128:131], v[188:191], v[200:203], v[128:131]
	v_mfma_f32_16x16x32_f16 v[132:135], v[188:191], v[204:207], v[132:135]
	s_waitcnt lgkmcnt(6)
	ds_read_b128 v[172:175], v16 offset:53248
	ds_read_b128 v[192:195], v18 offset:53248
	ds_read_b128 v[196:199], v18 offset:55296
	ds_read_b128 v[200:203], v18 offset:57344
	ds_read_b128 v[204:207], v18 offset:59392
	ds_read_b128 v[176:179], v16 offset:55296
	ds_read_b128 v[180:183], v16 offset:57344
	ds_read_b128 v[184:187], v16 offset:59392
	ds_read_b128 v[188:191], v16 offset:61440
	s_waitcnt lgkmcnt(9)
	v_mfma_f32_16x16x32_f16 v[56:59], v[136:139], v[156:159], v[56:59]
	s_add_u32 m0, s28, 0x8000
	v_mfma_f32_16x16x32_f16 v[60:63], v[136:139], v[160:163], v[60:63]
	global_load_lds_dwordx4 v14, s[4:5]
	s_add_u32 s4, s4, s20
	s_addc_u32 s5, s5, 0
	v_mfma_f32_16x16x32_f16 v[64:67], v[136:139], v[164:167], v[64:67]
	v_mfma_f32_16x16x32_f16 v[68:71], v[136:139], v[168:171], v[68:71]
	v_mfma_f32_16x16x32_f16 v[72:75], v[140:143], v[156:159], v[72:75]
	v_mfma_f32_16x16x32_f16 v[76:79], v[140:143], v[160:163], v[76:79]
	v_mfma_f32_16x16x32_f16 v[80:83], v[140:143], v[164:167], v[80:83]
	s_add_u32 m0, s28, 0x9000
	v_mfma_f32_16x16x32_f16 v[84:87], v[140:143], v[168:171], v[84:87]
	global_load_lds_dwordx4 v10, s[6:7]
	v_mfma_f32_16x16x32_f16 v[88:91], v[144:147], v[156:159], v[88:91]
	v_mfma_f32_16x16x32_f16 v[92:95], v[144:147], v[160:163], v[92:95]
	v_mfma_f32_16x16x32_f16 v[96:99], v[144:147], v[164:167], v[96:99]
	v_mfma_f32_16x16x32_f16 v[100:103], v[144:147], v[168:171], v[100:103]
	v_mfma_f32_16x16x32_f16 v[104:107], v[148:151], v[156:159], v[104:107]
	v_mfma_f32_16x16x32_f16 v[108:111], v[148:151], v[160:163], v[108:111]
	s_add_u32 m0, s28, 0xb000
	v_mfma_f32_16x16x32_f16 v[112:115], v[148:151], v[164:167], v[112:115]
	global_load_lds_dwordx4 v11, s[6:7]
	s_add_u32 s6, s6, s20
	s_addc_u32 s7, s7, 0
	v_mfma_f32_16x16x32_f16 v[116:119], v[148:151], v[168:171], v[116:119]
	v_mfma_f32_16x16x32_f16 v[120:123], v[152:155], v[156:159], v[120:123]
	v_mfma_f32_16x16x32_f16 v[124:127], v[152:155], v[160:163], v[124:127]
	v_mfma_f32_16x16x32_f16 v[128:131], v[152:155], v[164:167], v[128:131]
	v_mfma_f32_16x16x32_f16 v[132:135], v[152:155], v[168:171], v[132:135]
	s_waitcnt vmcnt(7) lgkmcnt(0)
	s_barrier
	s_waitcnt lgkmcnt(6)
	ds_read_b128 v[136:139], v19
	ds_read_b128 v[156:159], v21
	ds_read_b128 v[160:163], v21 offset:2048
	ds_read_b128 v[164:167], v21 offset:4096
	ds_read_b128 v[168:171], v21 offset:6144
	ds_read_b128 v[140:143], v19 offset:2048
	ds_read_b128 v[144:147], v19 offset:4096
	ds_read_b128 v[148:151], v19 offset:6144
	ds_read_b128 v[152:155], v19 offset:8192
	s_waitcnt lgkmcnt(9)
	v_mfma_f32_16x16x32_f16 v[56:59], v[172:175], v[192:195], v[56:59]
	s_add_u32 m0, s28, 0xd000
	v_mfma_f32_16x16x32_f16 v[60:63], v[172:175], v[196:199], v[60:63]
	global_load_lds_dwordx4 v10, s[4:5]
	v_mfma_f32_16x16x32_f16 v[64:67], v[172:175], v[200:203], v[64:67]
	v_mfma_f32_16x16x32_f16 v[68:71], v[172:175], v[204:207], v[68:71]
	v_mfma_f32_16x16x32_f16 v[72:75], v[176:179], v[192:195], v[72:75]
	v_mfma_f32_16x16x32_f16 v[76:79], v[176:179], v[196:199], v[76:79]
	s_add_u32 m0, s28, 0xf000
	v_mfma_f32_16x16x32_f16 v[80:83], v[176:179], v[200:203], v[80:83]
	global_load_lds_dwordx4 v11, s[4:5]
	v_mfma_f32_16x16x32_f16 v[84:87], v[176:179], v[204:207], v[84:87]
	v_mfma_f32_16x16x32_f16 v[88:91], v[180:183], v[192:195], v[88:91]
	v_mfma_f32_16x16x32_f16 v[92:95], v[180:183], v[196:199], v[92:95]
	v_mfma_f32_16x16x32_f16 v[96:99], v[180:183], v[200:203], v[96:99]
	s_add_u32 m0, s28, 0x11000
	v_mfma_f32_16x16x32_f16 v[100:103], v[180:183], v[204:207], v[100:103]
	global_load_lds_dwordx4 v12, s[4:5]
	v_mfma_f32_16x16x32_f16 v[104:107], v[184:187], v[192:195], v[104:107]
	v_mfma_f32_16x16x32_f16 v[108:111], v[184:187], v[196:199], v[108:111]
	v_mfma_f32_16x16x32_f16 v[112:115], v[184:187], v[200:203], v[112:115]
	v_mfma_f32_16x16x32_f16 v[116:119], v[184:187], v[204:207], v[116:119]
	s_add_u32 m0, s28, 0x13000
	v_mfma_f32_16x16x32_f16 v[120:123], v[188:191], v[192:195], v[120:123]
	global_load_lds_dwordx4 v13, s[4:5]
	v_mfma_f32_16x16x32_f16 v[124:127], v[188:191], v[196:199], v[124:127]
	v_mfma_f32_16x16x32_f16 v[128:131], v[188:191], v[200:203], v[128:131]
	v_mfma_f32_16x16x32_f16 v[132:135], v[188:191], v[204:207], v[132:135]
	s_waitcnt lgkmcnt(6)
	ds_read_b128 v[172:175], v20
	ds_read_b128 v[192:195], v22
	ds_read_b128 v[196:199], v22 offset:2048
	ds_read_b128 v[200:203], v22 offset:4096
	ds_read_b128 v[204:207], v22 offset:6144
	ds_read_b128 v[176:179], v20 offset:2048
	ds_read_b128 v[180:183], v20 offset:4096
	ds_read_b128 v[184:187], v20 offset:6144
	ds_read_b128 v[188:191], v20 offset:8192
	s_waitcnt lgkmcnt(9)
	v_mfma_f32_16x16x32_f16 v[56:59], v[136:139], v[156:159], v[56:59]
	s_add_u32 m0, s28, 0x15000
	v_mfma_f32_16x16x32_f16 v[60:63], v[136:139], v[160:163], v[60:63]
	global_load_lds_dwordx4 v14, s[4:5]
	s_add_u32 s4, s4, s20
	s_addc_u32 s5, s5, 0
	v_mfma_f32_16x16x32_f16 v[64:67], v[136:139], v[164:167], v[64:67]
	v_mfma_f32_16x16x32_f16 v[68:71], v[136:139], v[168:171], v[68:71]
	v_mfma_f32_16x16x32_f16 v[72:75], v[140:143], v[156:159], v[72:75]
	v_mfma_f32_16x16x32_f16 v[76:79], v[140:143], v[160:163], v[76:79]
	v_mfma_f32_16x16x32_f16 v[80:83], v[140:143], v[164:167], v[80:83]
	s_add_u32 m0, s28, 0x16000
	v_mfma_f32_16x16x32_f16 v[84:87], v[140:143], v[168:171], v[84:87]
	global_load_lds_dwordx4 v10, s[6:7]
	v_mfma_f32_16x16x32_f16 v[88:91], v[144:147], v[156:159], v[88:91]
	v_mfma_f32_16x16x32_f16 v[92:95], v[144:147], v[160:163], v[92:95]
	v_mfma_f32_16x16x32_f16 v[96:99], v[144:147], v[164:167], v[96:99]
	v_mfma_f32_16x16x32_f16 v[100:103], v[144:147], v[168:171], v[100:103]
	v_mfma_f32_16x16x32_f16 v[104:107], v[148:151], v[156:159], v[104:107]
	v_mfma_f32_16x16x32_f16 v[108:111], v[148:151], v[160:163], v[108:111]
	s_add_u32 m0, s28, 0x18000
	v_mfma_f32_16x16x32_f16 v[112:115], v[148:151], v[164:167], v[112:115]
	global_load_lds_dwordx4 v11, s[6:7]
	s_add_u32 s6, s6, s20
	s_addc_u32 s7, s7, 0
	v_mfma_f32_16x16x32_f16 v[116:119], v[148:151], v[168:171], v[116:119]
	v_mfma_f32_16x16x32_f16 v[120:123], v[152:155], v[156:159], v[120:123]
	v_mfma_f32_16x16x32_f16 v[124:127], v[152:155], v[160:163], v[124:127]
	v_mfma_f32_16x16x32_f16 v[128:131], v[152:155], v[164:167], v[128:131]
	v_mfma_f32_16x16x32_f16 v[132:135], v[152:155], v[168:171], v[132:135]
	s_waitcnt vmcnt(7) lgkmcnt(0)
	s_barrier
	s_waitcnt lgkmcnt(6)
	ds_read_b128 v[136:139], v15
	ds_read_b128 v[156:159], v17
	ds_read_b128 v[160:163], v17 offset:2048
	ds_read_b128 v[164:167], v17 offset:4096
	ds_read_b128 v[168:171], v17 offset:6144
	ds_read_b128 v[140:143], v15 offset:2048
	ds_read_b128 v[144:147], v15 offset:4096
	ds_read_b128 v[148:151], v15 offset:6144
	ds_read_b128 v[152:155], v15 offset:8192
	s_waitcnt lgkmcnt(9)
	v_mfma_f32_16x16x32_f16 v[56:59], v[172:175], v[192:195], v[56:59]
	s_add_u32 m0, s28, 0x1a000
	v_mfma_f32_16x16x32_f16 v[60:63], v[172:175], v[196:199], v[60:63]
	global_load_lds_dwordx4 v10, s[4:5]
	v_mfma_f32_16x16x32_f16 v[64:67], v[172:175], v[200:203], v[64:67]
	v_mfma_f32_16x16x32_f16 v[68:71], v[172:175], v[204:207], v[68:71]
	v_mfma_f32_16x16x32_f16 v[72:75], v[176:179], v[192:195], v[72:75]
	v_mfma_f32_16x16x32_f16 v[76:79], v[176:179], v[196:199], v[76:79]
	s_add_u32 m0, s28, 0x1c000
	v_mfma_f32_16x16x32_f16 v[80:83], v[176:179], v[200:203], v[80:83]
	global_load_lds_dwordx4 v11, s[4:5]
	v_mfma_f32_16x16x32_f16 v[84:87], v[176:179], v[204:207], v[84:87]
	v_mfma_f32_16x16x32_f16 v[88:91], v[180:183], v[192:195], v[88:91]
	v_mfma_f32_16x16x32_f16 v[92:95], v[180:183], v[196:199], v[92:95]
	v_mfma_f32_16x16x32_f16 v[96:99], v[180:183], v[200:203], v[96:99]
	s_add_u32 m0, s28, 0x1e000
	v_mfma_f32_16x16x32_f16 v[100:103], v[180:183], v[204:207], v[100:103]
	global_load_lds_dwordx4 v12, s[4:5]
	v_mfma_f32_16x16x32_f16 v[104:107], v[184:187], v[192:195], v[104:107]
	v_mfma_f32_16x16x32_f16 v[108:111], v[184:187], v[196:199], v[108:111]
	v_mfma_f32_16x16x32_f16 v[112:115], v[184:187], v[200:203], v[112:115]
	v_mfma_f32_16x16x32_f16 v[116:119], v[184:187], v[204:207], v[116:119]
	s_add_u32 m0, s28, 0x20000
	v_mfma_f32_16x16x32_f16 v[120:123], v[188:191], v[192:195], v[120:123]
	global_load_lds_dwordx4 v13, s[4:5]
	v_mfma_f32_16x16x32_f16 v[124:127], v[188:191], v[196:199], v[124:127]
	v_mfma_f32_16x16x32_f16 v[128:131], v[188:191], v[200:203], v[128:131]
	v_mfma_f32_16x16x32_f16 v[132:135], v[188:191], v[204:207], v[132:135]
	s_waitcnt lgkmcnt(6)
	ds_read_b128 v[172:175], v16
	ds_read_b128 v[192:195], v18
	ds_read_b128 v[196:199], v18 offset:2048
	ds_read_b128 v[200:203], v18 offset:4096
	ds_read_b128 v[204:207], v18 offset:6144
	ds_read_b128 v[176:179], v16 offset:2048
	ds_read_b128 v[180:183], v16 offset:4096
	ds_read_b128 v[184:187], v16 offset:6144
	ds_read_b128 v[188:191], v16 offset:8192
	s_waitcnt lgkmcnt(9)
	v_mfma_f32_16x16x32_f16 v[56:59], v[136:139], v[156:159], v[56:59]
	s_add_u32 m0, s28, 0x22000
	v_mfma_f32_16x16x32_f16 v[60:63], v[136:139], v[160:163], v[60:63]
	global_load_lds_dwordx4 v14, s[4:5]
	s_add_u32 s4, s4, s20
	s_addc_u32 s5, s5, 0
	v_mfma_f32_16x16x32_f16 v[64:67], v[136:139], v[164:167], v[64:67]
	v_mfma_f32_16x16x32_f16 v[68:71], v[136:139], v[168:171], v[68:71]
	v_mfma_f32_16x16x32_f16 v[72:75], v[140:143], v[156:159], v[72:75]
	v_mfma_f32_16x16x32_f16 v[76:79], v[140:143], v[160:163], v[76:79]
	v_mfma_f32_16x16x32_f16 v[80:83], v[140:143], v[164:167], v[80:83]
	s_add_u32 m0, s28, 0x23000
	v_mfma_f32_16x16x32_f16 v[84:87], v[140:143], v[168:171], v[84:87]
	global_load_lds_dwordx4 v10, s[6:7]
	v_mfma_f32_16x16x32_f16 v[88:91], v[144:147], v[156:159], v[88:91]
	v_mfma_f32_16x16x32_f16 v[92:95], v[144:147], v[160:163], v[92:95]
	v_mfma_f32_16x16x32_f16 v[96:99], v[144:147], v[164:167], v[96:99]
	v_mfma_f32_16x16x32_f16 v[100:103], v[144:147], v[168:171], v[100:103]
	v_mfma_f32_16x16x32_f16 v[104:107], v[148:151], v[156:159], v[104:107]
	v_mfma_f32_16x16x32_f16 v[108:111], v[148:151], v[160:163], v[108:111]
	s_add_u32 m0, s28, 0x25000
	v_mfma_f32_16x16x32_f16 v[112:115], v[148:151], v[164:167], v[112:115]
	global_load_lds_dwordx4 v11, s[6:7]
	s_add_u32 s6, s6, s20
	s_addc_u32 s7, s7, 0
	v_mfma_f32_16x16x32_f16 v[116:119], v[148:151], v[168:171], v[116:119]
	v_mfma_f32_16x16x32_f16 v[120:123], v[152:155], v[156:159], v[120:123]
	v_mfma_f32_16x16x32_f16 v[124:127], v[152:155], v[160:163], v[124:127]
	v_mfma_f32_16x16x32_f16 v[128:131], v[152:155], v[164:167], v[128:131]
	v_mfma_f32_16x16x32_f16 v[132:135], v[152:155], v[168:171], v[132:135]
	s_waitcnt vmcnt(7) lgkmcnt(0)
	s_barrier
	s_waitcnt lgkmcnt(6)
	ds_read_b128 v[136:139], v15 offset:53248
	ds_read_b128 v[156:159], v17 offset:53248
	ds_read_b128 v[160:163], v17 offset:55296
	ds_read_b128 v[164:167], v17 offset:57344
	ds_read_b128 v[168:171], v17 offset:59392
	ds_read_b128 v[140:143], v15 offset:55296
	ds_read_b128 v[144:147], v15 offset:57344
	ds_read_b128 v[148:151], v15 offset:59392
	ds_read_b128 v[152:155], v15 offset:61440
	s_waitcnt lgkmcnt(9)
	v_mfma_f32_16x16x32_f16 v[56:59], v[172:175], v[192:195], v[56:59]
	s_add_u32 m0, s28, 0x0
	v_mfma_f32_16x16x32_f16 v[60:63], v[172:175], v[196:199], v[60:63]
	global_load_lds_dwordx4 v10, s[4:5]
	v_mfma_f32_16x16x32_f16 v[64:67], v[172:175], v[200:203], v[64:67]
	v_mfma_f32_16x16x32_f16 v[68:71], v[172:175], v[204:207], v[68:71]
	v_mfma_f32_16x16x32_f16 v[72:75], v[176:179], v[192:195], v[72:75]
	v_mfma_f32_16x16x32_f16 v[76:79], v[176:179], v[196:199], v[76:79]
	s_add_u32 m0, s28, 0x2000
	v_mfma_f32_16x16x32_f16 v[80:83], v[176:179], v[200:203], v[80:83]
	global_load_lds_dwordx4 v11, s[4:5]
	v_mfma_f32_16x16x32_f16 v[84:87], v[176:179], v[204:207], v[84:87]
	v_mfma_f32_16x16x32_f16 v[88:91], v[180:183], v[192:195], v[88:91]
	v_mfma_f32_16x16x32_f16 v[92:95], v[180:183], v[196:199], v[92:95]
	v_mfma_f32_16x16x32_f16 v[96:99], v[180:183], v[200:203], v[96:99]
	s_add_u32 m0, s28, 0x4000
	v_mfma_f32_16x16x32_f16 v[100:103], v[180:183], v[204:207], v[100:103]
	global_load_lds_dwordx4 v12, s[4:5]
	v_mfma_f32_16x16x32_f16 v[104:107], v[184:187], v[192:195], v[104:107]
	v_mfma_f32_16x16x32_f16 v[108:111], v[184:187], v[196:199], v[108:111]
	v_mfma_f32_16x16x32_f16 v[112:115], v[184:187], v[200:203], v[112:115]
	v_mfma_f32_16x16x32_f16 v[116:119], v[184:187], v[204:207], v[116:119]
	s_add_u32 m0, s28, 0x6000
	v_mfma_f32_16x16x32_f16 v[120:123], v[188:191], v[192:195], v[120:123]
	global_load_lds_dwordx4 v13, s[4:5]
	v_mfma_f32_16x16x32_f16 v[124:127], v[188:191], v[196:199], v[124:127]
	v_mfma_f32_16x16x32_f16 v[128:131], v[188:191], v[200:203], v[128:131]
	v_mfma_f32_16x16x32_f16 v[132:135], v[188:191], v[204:207], v[132:135]
	s_waitcnt lgkmcnt(6)
	ds_read_b128 v[172:175], v16 offset:53248
	ds_read_b128 v[192:195], v18 offset:53248
	ds_read_b128 v[196:199], v18 offset:55296
	ds_read_b128 v[200:203], v18 offset:57344
	ds_read_b128 v[204:207], v18 offset:59392
	ds_read_b128 v[176:179], v16 offset:55296
	ds_read_b128 v[180:183], v16 offset:57344
	ds_read_b128 v[184:187], v16 offset:59392
	ds_read_b128 v[188:191], v16 offset:61440
	s_waitcnt lgkmcnt(9)
	v_mfma_f32_16x16x32_f16 v[56:59], v[136:139], v[156:159], v[56:59]
	s_add_u32 m0, s28, 0x8000
	v_mfma_f32_16x16x32_f16 v[60:63], v[136:139], v[160:163], v[60:63]
	global_load_lds_dwordx4 v14, s[4:5]
	s_add_u32 s4, s4, s20
	s_addc_u32 s5, s5, 0
	v_mfma_f32_16x16x32_f16 v[64:67], v[136:139], v[164:167], v[64:67]
	v_mfma_f32_16x16x32_f16 v[68:71], v[136:139], v[168:171], v[68:71]
	v_mfma_f32_16x16x32_f16 v[72:75], v[140:143], v[156:159], v[72:75]
	v_mfma_f32_16x16x32_f16 v[76:79], v[140:143], v[160:163], v[76:79]
	v_mfma_f32_16x16x32_f16 v[80:83], v[140:143], v[164:167], v[80:83]
	s_add_u32 m0, s28, 0x9000
	v_mfma_f32_16x16x32_f16 v[84:87], v[140:143], v[168:171], v[84:87]
	global_load_lds_dwordx4 v10, s[6:7]
	v_mfma_f32_16x16x32_f16 v[88:91], v[144:147], v[156:159], v[88:91]
	v_mfma_f32_16x16x32_f16 v[92:95], v[144:147], v[160:163], v[92:95]
	v_mfma_f32_16x16x32_f16 v[96:99], v[144:147], v[164:167], v[96:99]
	v_mfma_f32_16x16x32_f16 v[100:103], v[144:147], v[168:171], v[100:103]
	v_mfma_f32_16x16x32_f16 v[104:107], v[148:151], v[156:159], v[104:107]
	v_mfma_f32_16x16x32_f16 v[108:111], v[148:151], v[160:163], v[108:111]
	s_add_u32 m0, s28, 0xb000
	v_mfma_f32_16x16x32_f16 v[112:115], v[148:151], v[164:167], v[112:115]
	global_load_lds_dwordx4 v11, s[6:7]
	s_add_u32 s6, s6, s20
	s_addc_u32 s7, s7, 0
	v_mfma_f32_16x16x32_f16 v[116:119], v[148:151], v[168:171], v[116:119]
	v_mfma_f32_16x16x32_f16 v[120:123], v[152:155], v[156:159], v[120:123]
	v_mfma_f32_16x16x32_f16 v[124:127], v[152:155], v[160:163], v[124:127]
	v_mfma_f32_16x16x32_f16 v[128:131], v[152:155], v[164:167], v[128:131]
	v_mfma_f32_16x16x32_f16 v[132:135], v[152:155], v[168:171], v[132:135]
	s_waitcnt vmcnt(7) lgkmcnt(0)
	s_barrier
	s_waitcnt lgkmcnt(6)
	ds_read_b128 v[136:139], v19
	ds_read_b128 v[156:159], v21
	ds_read_b128 v[160:163], v21 offset:2048
	ds_read_b128 v[164:167], v21 offset:4096
	ds_read_b128 v[168:171], v21 offset:6144
	ds_read_b128 v[140:143], v19 offset:2048
	ds_read_b128 v[144:147], v19 offset:4096
	ds_read_b128 v[148:151], v19 offset:6144
	ds_read_b128 v[152:155], v19 offset:8192
	s_waitcnt lgkmcnt(9)
	v_mfma_f32_16x16x32_f16 v[56:59], v[172:175], v[192:195], v[56:59]
	s_add_u32 m0, s28, 0xd000
	v_mfma_f32_16x16x32_f16 v[60:63], v[172:175], v[196:199], v[60:63]
	global_load_lds_dwordx4 v10, s[4:5]
	v_mfma_f32_16x16x32_f16 v[64:67], v[172:175], v[200:203], v[64:67]
	v_mfma_f32_16x16x32_f16 v[68:71], v[172:175], v[204:207], v[68:71]
	v_mfma_f32_16x16x32_f16 v[72:75], v[176:179], v[192:195], v[72:75]
	v_mfma_f32_16x16x32_f16 v[76:79], v[176:179], v[196:199], v[76:79]
	s_add_u32 m0, s28, 0xf000
	v_mfma_f32_16x16x32_f16 v[80:83], v[176:179], v[200:203], v[80:83]
	global_load_lds_dwordx4 v11, s[4:5]
	v_mfma_f32_16x16x32_f16 v[84:87], v[176:179], v[204:207], v[84:87]
	v_mfma_f32_16x16x32_f16 v[88:91], v[180:183], v[192:195], v[88:91]
	v_mfma_f32_16x16x32_f16 v[92:95], v[180:183], v[196:199], v[92:95]
	v_mfma_f32_16x16x32_f16 v[96:99], v[180:183], v[200:203], v[96:99]
	s_add_u32 m0, s28, 0x11000
	v_mfma_f32_16x16x32_f16 v[100:103], v[180:183], v[204:207], v[100:103]
	global_load_lds_dwordx4 v12, s[4:5]
	v_mfma_f32_16x16x32_f16 v[104:107], v[184:187], v[192:195], v[104:107]
	v_mfma_f32_16x16x32_f16 v[108:111], v[184:187], v[196:199], v[108:111]
	v_mfma_f32_16x16x32_f16 v[112:115], v[184:187], v[200:203], v[112:115]
	v_mfma_f32_16x16x32_f16 v[116:119], v[184:187], v[204:207], v[116:119]
	s_add_u32 m0, s28, 0x13000
	v_mfma_f32_16x16x32_f16 v[120:123], v[188:191], v[192:195], v[120:123]
	global_load_lds_dwordx4 v13, s[4:5]
	v_mfma_f32_16x16x32_f16 v[124:127], v[188:191], v[196:199], v[124:127]
	v_mfma_f32_16x16x32_f16 v[128:131], v[188:191], v[200:203], v[128:131]
	v_mfma_f32_16x16x32_f16 v[132:135], v[188:191], v[204:207], v[132:135]
	s_waitcnt lgkmcnt(6)
	ds_read_b128 v[172:175], v20
	ds_read_b128 v[192:195], v22
	ds_read_b128 v[196:199], v22 offset:2048
	ds_read_b128 v[200:203], v22 offset:4096
	ds_read_b128 v[204:207], v22 offset:6144
	ds_read_b128 v[176:179], v20 offset:2048
	ds_read_b128 v[180:183], v20 offset:4096
	ds_read_b128 v[184:187], v20 offset:6144
	ds_read_b128 v[188:191], v20 offset:8192
	s_waitcnt lgkmcnt(9)
	v_mfma_f32_16x16x32_f16 v[56:59], v[136:139], v[156:159], v[56:59]
	s_add_u32 m0, s28, 0x15000
	v_mfma_f32_16x16x32_f16 v[60:63], v[136:139], v[160:163], v[60:63]
	global_load_lds_dwordx4 v14, s[4:5]
	s_add_u32 s4, s4, s20
	s_addc_u32 s5, s5, 0
	v_mfma_f32_16x16x32_f16 v[64:67], v[136:139], v[164:167], v[64:67]
	v_mfma_f32_16x16x32_f16 v[68:71], v[136:139], v[168:171], v[68:71]
	v_mfma_f32_16x16x32_f16 v[72:75], v[140:143], v[156:159], v[72:75]
	v_mfma_f32_16x16x32_f16 v[76:79], v[140:143], v[160:163], v[76:79]
	v_mfma_f32_16x16x32_f16 v[80:83], v[140:143], v[164:167], v[80:83]
	s_add_u32 m0, s28, 0x16000
	v_mfma_f32_16x16x32_f16 v[84:87], v[140:143], v[168:171], v[84:87]
	global_load_lds_dwordx4 v10, s[6:7]
	v_mfma_f32_16x16x32_f16 v[88:91], v[144:147], v[156:159], v[88:91]
	v_mfma_f32_16x16x32_f16 v[92:95], v[144:147], v[160:163], v[92:95]
	v_mfma_f32_16x16x32_f16 v[96:99], v[144:147], v[164:167], v[96:99]
	v_mfma_f32_16x16x32_f16 v[100:103], v[144:147], v[168:171], v[100:103]
	v_mfma_f32_16x16x32_f16 v[104:107], v[148:151], v[156:159], v[104:107]
	v_mfma_f32_16x16x32_f16 v[108:111], v[148:151], v[160:163], v[108:111]
	s_add_u32 m0, s28, 0x18000
	v_mfma_f32_16x16x32_f16 v[112:115], v[148:151], v[164:167], v[112:115]
	global_load_lds_dwordx4 v11, s[6:7]
	s_add_u32 s6, s6, s20
	s_addc_u32 s7, s7, 0
	v_mfma_f32_16x16x32_f16 v[116:119], v[148:151], v[168:171], v[116:119]
	v_mfma_f32_16x16x32_f16 v[120:123], v[152:155], v[156:159], v[120:123]
	v_mfma_f32_16x16x32_f16 v[124:127], v[152:155], v[160:163], v[124:127]
	v_mfma_f32_16x16x32_f16 v[128:131], v[152:155], v[164:167], v[128:131]
	v_mfma_f32_16x16x32_f16 v[132:135], v[152:155], v[168:171], v[132:135]
	s_waitcnt vmcnt(7) lgkmcnt(0)
	s_barrier
	s_waitcnt lgkmcnt(6)
	ds_read_b128 v[136:139], v15
	ds_read_b128 v[156:159], v17
	ds_read_b128 v[160:163], v17 offset:2048
	ds_read_b128 v[164:167], v17 offset:4096
	ds_read_b128 v[168:171], v17 offset:6144
	ds_read_b128 v[140:143], v15 offset:2048
	ds_read_b128 v[144:147], v15 offset:4096
	ds_read_b128 v[148:151], v15 offset:6144
	ds_read_b128 v[152:155], v15 offset:8192
	s_waitcnt lgkmcnt(9)
	v_mfma_f32_16x16x32_f16 v[56:59], v[172:175], v[192:195], v[56:59]
	s_add_u32 m0, s28, 0x1a000
	v_mfma_f32_16x16x32_f16 v[60:63], v[172:175], v[196:199], v[60:63]
	global_load_lds_dwordx4 v10, s[4:5]
	v_mfma_f32_16x16x32_f16 v[64:67], v[172:175], v[200:203], v[64:67]
	v_mfma_f32_16x16x32_f16 v[68:71], v[172:175], v[204:207], v[68:71]
	v_mfma_f32_16x16x32_f16 v[72:75], v[176:179], v[192:195], v[72:75]
	v_mfma_f32_16x16x32_f16 v[76:79], v[176:179], v[196:199], v[76:79]
	s_add_u32 m0, s28, 0x1c000
	v_mfma_f32_16x16x32_f16 v[80:83], v[176:179], v[200:203], v[80:83]
	global_load_lds_dwordx4 v11, s[4:5]
	v_mfma_f32_16x16x32_f16 v[84:87], v[176:179], v[204:207], v[84:87]
	v_mfma_f32_16x16x32_f16 v[88:91], v[180:183], v[192:195], v[88:91]
	v_mfma_f32_16x16x32_f16 v[92:95], v[180:183], v[196:199], v[92:95]
	v_mfma_f32_16x16x32_f16 v[96:99], v[180:183], v[200:203], v[96:99]
	s_add_u32 m0, s28, 0x1e000
	v_mfma_f32_16x16x32_f16 v[100:103], v[180:183], v[204:207], v[100:103]
	global_load_lds_dwordx4 v12, s[4:5]
	v_mfma_f32_16x16x32_f16 v[104:107], v[184:187], v[192:195], v[104:107]
	v_mfma_f32_16x16x32_f16 v[108:111], v[184:187], v[196:199], v[108:111]
	v_mfma_f32_16x16x32_f16 v[112:115], v[184:187], v[200:203], v[112:115]
	v_mfma_f32_16x16x32_f16 v[116:119], v[184:187], v[204:207], v[116:119]
	s_add_u32 m0, s28, 0x20000
	v_mfma_f32_16x16x32_f16 v[120:123], v[188:191], v[192:195], v[120:123]
	global_load_lds_dwordx4 v13, s[4:5]
	v_mfma_f32_16x16x32_f16 v[124:127], v[188:191], v[196:199], v[124:127]
	v_mfma_f32_16x16x32_f16 v[128:131], v[188:191], v[200:203], v[128:131]
	v_mfma_f32_16x16x32_f16 v[132:135], v[188:191], v[204:207], v[132:135]
	s_waitcnt lgkmcnt(6)
	ds_read_b128 v[172:175], v16
	ds_read_b128 v[192:195], v18
	ds_read_b128 v[196:199], v18 offset:2048
	ds_read_b128 v[200:203], v18 offset:4096
	ds_read_b128 v[204:207], v18 offset:6144
	ds_read_b128 v[176:179], v16 offset:2048
	ds_read_b128 v[180:183], v16 offset:4096
	ds_read_b128 v[184:187], v16 offset:6144
	ds_read_b128 v[188:191], v16 offset:8192
	s_waitcnt lgkmcnt(9)
	v_mfma_f32_16x16x32_f16 v[56:59], v[136:139], v[156:159], v[56:59]
	s_add_u32 m0, s28, 0x22000
	v_mfma_f32_16x16x32_f16 v[60:63], v[136:139], v[160:163], v[60:63]
	global_load_lds_dwordx4 v14, s[4:5]
	s_add_u32 s4, s4, s20
	s_addc_u32 s5, s5, 0
	v_mfma_f32_16x16x32_f16 v[64:67], v[136:139], v[164:167], v[64:67]
	v_mfma_f32_16x16x32_f16 v[68:71], v[136:139], v[168:171], v[68:71]
	v_mfma_f32_16x16x32_f16 v[72:75], v[140:143], v[156:159], v[72:75]
	v_mfma_f32_16x16x32_f16 v[76:79], v[140:143], v[160:163], v[76:79]
	v_mfma_f32_16x16x32_f16 v[80:83], v[140:143], v[164:167], v[80:83]
	s_add_u32 m0, s28, 0x23000
	v_mfma_f32_16x16x32_f16 v[84:87], v[140:143], v[168:171], v[84:87]
	global_load_lds_dwordx4 v10, s[6:7]
	v_mfma_f32_16x16x32_f16 v[88:91], v[144:147], v[156:159], v[88:91]
	v_mfma_f32_16x16x32_f16 v[92:95], v[144:147], v[160:163], v[92:95]
	v_mfma_f32_16x16x32_f16 v[96:99], v[144:147], v[164:167], v[96:99]
	v_mfma_f32_16x16x32_f16 v[100:103], v[144:147], v[168:171], v[100:103]
	v_mfma_f32_16x16x32_f16 v[104:107], v[148:151], v[156:159], v[104:107]
	v_mfma_f32_16x16x32_f16 v[108:111], v[148:151], v[160:163], v[108:111]
	s_add_u32 m0, s28, 0x25000
	v_mfma_f32_16x16x32_f16 v[112:115], v[148:151], v[164:167], v[112:115]
	global_load_lds_dwordx4 v11, s[6:7]
	s_add_u32 s6, s6, s20
	s_addc_u32 s7, s7, 0
	v_mfma_f32_16x16x32_f16 v[116:119], v[148:151], v[168:171], v[116:119]
	v_mfma_f32_16x16x32_f16 v[120:123], v[152:155], v[156:159], v[120:123]
	v_mfma_f32_16x16x32_f16 v[124:127], v[152:155], v[160:163], v[124:127]
	v_mfma_f32_16x16x32_f16 v[128:131], v[152:155], v[164:167], v[128:131]
	v_mfma_f32_16x16x32_f16 v[132:135], v[152:155], v[168:171], v[132:135]
	s_waitcnt vmcnt(7) lgkmcnt(0)
	s_barrier
	s_waitcnt lgkmcnt(6)
	ds_read_b128 v[136:139], v15 offset:53248
	ds_read_b128 v[156:159], v17 offset:53248
	ds_read_b128 v[160:163], v17 offset:55296
	ds_read_b128 v[164:167], v17 offset:57344
	ds_read_b128 v[168:171], v17 offset:59392
	ds_read_b128 v[140:143], v15 offset:55296
	ds_read_b128 v[144:147], v15 offset:57344
	ds_read_b128 v[148:151], v15 offset:59392
	ds_read_b128 v[152:155], v15 offset:61440
	s_waitcnt lgkmcnt(9)
	v_mfma_f32_16x16x32_f16 v[56:59], v[172:175], v[192:195], v[56:59]
	s_add_u32 m0, s28, 0x0
	v_mfma_f32_16x16x32_f16 v[60:63], v[172:175], v[196:199], v[60:63]
	global_load_lds_dwordx4 v10, s[4:5]
	v_mfma_f32_16x16x32_f16 v[64:67], v[172:175], v[200:203], v[64:67]
	v_mfma_f32_16x16x32_f16 v[68:71], v[172:175], v[204:207], v[68:71]
	v_mfma_f32_16x16x32_f16 v[72:75], v[176:179], v[192:195], v[72:75]
	v_mfma_f32_16x16x32_f16 v[76:79], v[176:179], v[196:199], v[76:79]
	s_add_u32 m0, s28, 0x2000
	v_mfma_f32_16x16x32_f16 v[80:83], v[176:179], v[200:203], v[80:83]
	global_load_lds_dwordx4 v11, s[4:5]
	v_mfma_f32_16x16x32_f16 v[84:87], v[176:179], v[204:207], v[84:87]
	v_mfma_f32_16x16x32_f16 v[88:91], v[180:183], v[192:195], v[88:91]
	v_mfma_f32_16x16x32_f16 v[92:95], v[180:183], v[196:199], v[92:95]
	v_mfma_f32_16x16x32_f16 v[96:99], v[180:183], v[200:203], v[96:99]
	s_add_u32 m0, s28, 0x4000
	v_mfma_f32_16x16x32_f16 v[100:103], v[180:183], v[204:207], v[100:103]
	global_load_lds_dwordx4 v12, s[4:5]
	v_mfma_f32_16x16x32_f16 v[104:107], v[184:187], v[192:195], v[104:107]
	v_mfma_f32_16x16x32_f16 v[108:111], v[184:187], v[196:199], v[108:111]
	v_mfma_f32_16x16x32_f16 v[112:115], v[184:187], v[200:203], v[112:115]
	v_mfma_f32_16x16x32_f16 v[116:119], v[184:187], v[204:207], v[116:119]
	s_add_u32 m0, s28, 0x6000
	v_mfma_f32_16x16x32_f16 v[120:123], v[188:191], v[192:195], v[120:123]
	global_load_lds_dwordx4 v13, s[4:5]
	v_mfma_f32_16x16x32_f16 v[124:127], v[188:191], v[196:199], v[124:127]
	v_mfma_f32_16x16x32_f16 v[128:131], v[188:191], v[200:203], v[128:131]
	v_mfma_f32_16x16x32_f16 v[132:135], v[188:191], v[204:207], v[132:135]
	s_waitcnt lgkmcnt(6)
	ds_read_b128 v[172:175], v16 offset:53248
	ds_read_b128 v[192:195], v18 offset:53248
	ds_read_b128 v[196:199], v18 offset:55296
	ds_read_b128 v[200:203], v18 offset:57344
	ds_read_b128 v[204:207], v18 offset:59392
	ds_read_b128 v[176:179], v16 offset:55296
	ds_read_b128 v[180:183], v16 offset:57344
	ds_read_b128 v[184:187], v16 offset:59392
	ds_read_b128 v[188:191], v16 offset:61440
	s_waitcnt lgkmcnt(9)
	v_mfma_f32_16x16x32_f16 v[56:59], v[136:139], v[156:159], v[56:59]
	s_add_u32 m0, s28, 0x8000
	v_mfma_f32_16x16x32_f16 v[60:63], v[136:139], v[160:163], v[60:63]
	global_load_lds_dwordx4 v14, s[4:5]
	s_add_u32 s4, s4, s20
	s_addc_u32 s5, s5, 0
	v_mfma_f32_16x16x32_f16 v[64:67], v[136:139], v[164:167], v[64:67]
	v_mfma_f32_16x16x32_f16 v[68:71], v[136:139], v[168:171], v[68:71]
	v_mfma_f32_16x16x32_f16 v[72:75], v[140:143], v[156:159], v[72:75]
	v_mfma_f32_16x16x32_f16 v[76:79], v[140:143], v[160:163], v[76:79]
	v_mfma_f32_16x16x32_f16 v[80:83], v[140:143], v[164:167], v[80:83]
	s_add_u32 m0, s28, 0x9000
	v_mfma_f32_16x16x32_f16 v[84:87], v[140:143], v[168:171], v[84:87]
	global_load_lds_dwordx4 v10, s[6:7]
	v_mfma_f32_16x16x32_f16 v[88:91], v[144:147], v[156:159], v[88:91]
	v_mfma_f32_16x16x32_f16 v[92:95], v[144:147], v[160:163], v[92:95]
	v_mfma_f32_16x16x32_f16 v[96:99], v[144:147], v[164:167], v[96:99]
	v_mfma_f32_16x16x32_f16 v[100:103], v[144:147], v[168:171], v[100:103]
	v_mfma_f32_16x16x32_f16 v[104:107], v[148:151], v[156:159], v[104:107]
	v_mfma_f32_16x16x32_f16 v[108:111], v[148:151], v[160:163], v[108:111]
	s_add_u32 m0, s28, 0xb000
	v_mfma_f32_16x16x32_f16 v[112:115], v[148:151], v[164:167], v[112:115]
	global_load_lds_dwordx4 v11, s[6:7]
	s_add_u32 s6, s6, s20
	s_addc_u32 s7, s7, 0
	v_mfma_f32_16x16x32_f16 v[116:119], v[148:151], v[168:171], v[116:119]
	v_mfma_f32_16x16x32_f16 v[120:123], v[152:155], v[156:159], v[120:123]
	v_mfma_f32_16x16x32_f16 v[124:127], v[152:155], v[160:163], v[124:127]
	v_mfma_f32_16x16x32_f16 v[128:131], v[152:155], v[164:167], v[128:131]
	v_mfma_f32_16x16x32_f16 v[132:135], v[152:155], v[168:171], v[132:135]
	s_waitcnt vmcnt(7) lgkmcnt(0)
	s_barrier
	s_waitcnt lgkmcnt(6)
	ds_read_b128 v[136:139], v19
	ds_read_b128 v[156:159], v21
	ds_read_b128 v[160:163], v21 offset:2048
	ds_read_b128 v[164:167], v21 offset:4096
	ds_read_b128 v[168:171], v21 offset:6144
	ds_read_b128 v[140:143], v19 offset:2048
	ds_read_b128 v[144:147], v19 offset:4096
	ds_read_b128 v[148:151], v19 offset:6144
	ds_read_b128 v[152:155], v19 offset:8192
	s_waitcnt lgkmcnt(9)
	v_mfma_f32_16x16x32_f16 v[56:59], v[172:175], v[192:195], v[56:59]
	v_mfma_f32_16x16x32_f16 v[60:63], v[172:175], v[196:199], v[60:63]
	v_mfma_f32_16x16x32_f16 v[64:67], v[172:175], v[200:203], v[64:67]
	v_mfma_f32_16x16x32_f16 v[68:71], v[172:175], v[204:207], v[68:71]
	v_mfma_f32_16x16x32_f16 v[72:75], v[176:179], v[192:195], v[72:75]
	v_mfma_f32_16x16x32_f16 v[76:79], v[176:179], v[196:199], v[76:79]
	v_mfma_f32_16x16x32_f16 v[80:83], v[176:179], v[200:203], v[80:83]
	v_mfma_f32_16x16x32_f16 v[84:87], v[176:179], v[204:207], v[84:87]
	v_mfma_f32_16x16x32_f16 v[88:91], v[180:183], v[192:195], v[88:91]
	v_mfma_f32_16x16x32_f16 v[92:95], v[180:183], v[196:199], v[92:95]
	v_mfma_f32_16x16x32_f16 v[96:99], v[180:183], v[200:203], v[96:99]
	v_mfma_f32_16x16x32_f16 v[100:103], v[180:183], v[204:207], v[100:103]
	v_mfma_f32_16x16x32_f16 v[104:107], v[184:187], v[192:195], v[104:107]
	v_mfma_f32_16x16x32_f16 v[108:111], v[184:187], v[196:199], v[108:111]
	v_mfma_f32_16x16x32_f16 v[112:115], v[184:187], v[200:203], v[112:115]
	v_mfma_f32_16x16x32_f16 v[116:119], v[184:187], v[204:207], v[116:119]
	v_mfma_f32_16x16x32_f16 v[120:123], v[188:191], v[192:195], v[120:123]
	v_mfma_f32_16x16x32_f16 v[124:127], v[188:191], v[196:199], v[124:127]
	v_mfma_f32_16x16x32_f16 v[128:131], v[188:191], v[200:203], v[128:131]
	v_mfma_f32_16x16x32_f16 v[132:135], v[188:191], v[204:207], v[132:135]
	s_waitcnt lgkmcnt(6)
	ds_read_b128 v[172:175], v20
	ds_read_b128 v[192:195], v22
	ds_read_b128 v[196:199], v22 offset:2048
	ds_read_b128 v[200:203], v22 offset:4096
	ds_read_b128 v[204:207], v22 offset:6144
	ds_read_b128 v[176:179], v20 offset:2048
	ds_read_b128 v[180:183], v20 offset:4096
	ds_read_b128 v[184:187], v20 offset:6144
	ds_read_b128 v[188:191], v20 offset:8192
	s_waitcnt lgkmcnt(9)
	v_mfma_f32_16x16x32_f16 v[56:59], v[136:139], v[156:159], v[56:59]
	v_mfma_f32_16x16x32_f16 v[60:63], v[136:139], v[160:163], v[60:63]
	v_mfma_f32_16x16x32_f16 v[64:67], v[136:139], v[164:167], v[64:67]
	v_mfma_f32_16x16x32_f16 v[68:71], v[136:139], v[168:171], v[68:71]
	v_mfma_f32_16x16x32_f16 v[72:75], v[140:143], v[156:159], v[72:75]
	v_mfma_f32_16x16x32_f16 v[76:79], v[140:143], v[160:163], v[76:79]
	v_mfma_f32_16x16x32_f16 v[80:83], v[140:143], v[164:167], v[80:83]
	v_mfma_f32_16x16x32_f16 v[84:87], v[140:143], v[168:171], v[84:87]
	v_mfma_f32_16x16x32_f16 v[88:91], v[144:147], v[156:159], v[88:91]
	v_mfma_f32_16x16x32_f16 v[92:95], v[144:147], v[160:163], v[92:95]
	v_mfma_f32_16x16x32_f16 v[96:99], v[144:147], v[164:167], v[96:99]
	v_mfma_f32_16x16x32_f16 v[100:103], v[144:147], v[168:171], v[100:103]
	v_mfma_f32_16x16x32_f16 v[104:107], v[148:151], v[156:159], v[104:107]
	v_mfma_f32_16x16x32_f16 v[108:111], v[148:151], v[160:163], v[108:111]
	v_mfma_f32_16x16x32_f16 v[112:115], v[148:151], v[164:167], v[112:115]
	v_mfma_f32_16x16x32_f16 v[116:119], v[148:151], v[168:171], v[116:119]
	v_mfma_f32_16x16x32_f16 v[120:123], v[152:155], v[156:159], v[120:123]
	v_mfma_f32_16x16x32_f16 v[124:127], v[152:155], v[160:163], v[124:127]
	v_mfma_f32_16x16x32_f16 v[128:131], v[152:155], v[164:167], v[128:131]
	v_mfma_f32_16x16x32_f16 v[132:135], v[152:155], v[168:171], v[132:135]
	s_waitcnt vmcnt(0) lgkmcnt(0)
	s_barrier
	s_waitcnt lgkmcnt(6)
	ds_read_b128 v[136:139], v15
	ds_read_b128 v[156:159], v17
	ds_read_b128 v[160:163], v17 offset:2048
	ds_read_b128 v[164:167], v17 offset:4096
	ds_read_b128 v[168:171], v17 offset:6144
	ds_read_b128 v[140:143], v15 offset:2048
	ds_read_b128 v[144:147], v15 offset:4096
	ds_read_b128 v[148:151], v15 offset:6144
	ds_read_b128 v[152:155], v15 offset:8192
	s_waitcnt lgkmcnt(9)
	v_mfma_f32_16x16x32_f16 v[56:59], v[172:175], v[192:195], v[56:59]
	v_mfma_f32_16x16x32_f16 v[60:63], v[172:175], v[196:199], v[60:63]
	v_mfma_f32_16x16x32_f16 v[64:67], v[172:175], v[200:203], v[64:67]
	v_mfma_f32_16x16x32_f16 v[68:71], v[172:175], v[204:207], v[68:71]
	v_mfma_f32_16x16x32_f16 v[72:75], v[176:179], v[192:195], v[72:75]
	v_mfma_f32_16x16x32_f16 v[76:79], v[176:179], v[196:199], v[76:79]
	v_mfma_f32_16x16x32_f16 v[80:83], v[176:179], v[200:203], v[80:83]
	v_mfma_f32_16x16x32_f16 v[84:87], v[176:179], v[204:207], v[84:87]
	v_mfma_f32_16x16x32_f16 v[88:91], v[180:183], v[192:195], v[88:91]
	v_mfma_f32_16x16x32_f16 v[92:95], v[180:183], v[196:199], v[92:95]
	v_mfma_f32_16x16x32_f16 v[96:99], v[180:183], v[200:203], v[96:99]
	v_mfma_f32_16x16x32_f16 v[100:103], v[180:183], v[204:207], v[100:103]
	v_mfma_f32_16x16x32_f16 v[104:107], v[184:187], v[192:195], v[104:107]
	v_mfma_f32_16x16x32_f16 v[108:111], v[184:187], v[196:199], v[108:111]
	v_mfma_f32_16x16x32_f16 v[112:115], v[184:187], v[200:203], v[112:115]
	v_mfma_f32_16x16x32_f16 v[116:119], v[184:187], v[204:207], v[116:119]
	v_mfma_f32_16x16x32_f16 v[120:123], v[188:191], v[192:195], v[120:123]
	v_mfma_f32_16x16x32_f16 v[124:127], v[188:191], v[196:199], v[124:127]
	v_mfma_f32_16x16x32_f16 v[128:131], v[188:191], v[200:203], v[128:131]
	v_mfma_f32_16x16x32_f16 v[132:135], v[188:191], v[204:207], v[132:135]
	s_waitcnt lgkmcnt(6)
	ds_read_b128 v[172:175], v16
	ds_read_b128 v[192:195], v18
	ds_read_b128 v[196:199], v18 offset:2048
	ds_read_b128 v[200:203], v18 offset:4096
	ds_read_b128 v[204:207], v18 offset:6144
	ds_read_b128 v[176:179], v16 offset:2048
	ds_read_b128 v[180:183], v16 offset:4096
	ds_read_b128 v[184:187], v16 offset:6144
	ds_read_b128 v[188:191], v16 offset:8192
	s_waitcnt lgkmcnt(9)
	v_mfma_f32_16x16x32_f16 v[56:59], v[136:139], v[156:159], v[56:59]
	v_mfma_f32_16x16x32_f16 v[60:63], v[136:139], v[160:163], v[60:63]
	v_mfma_f32_16x16x32_f16 v[64:67], v[136:139], v[164:167], v[64:67]
	v_mfma_f32_16x16x32_f16 v[68:71], v[136:139], v[168:171], v[68:71]
	v_mfma_f32_16x16x32_f16 v[72:75], v[140:143], v[156:159], v[72:75]
	v_mfma_f32_16x16x32_f16 v[76:79], v[140:143], v[160:163], v[76:79]
	v_mfma_f32_16x16x32_f16 v[80:83], v[140:143], v[164:167], v[80:83]
	v_mfma_f32_16x16x32_f16 v[84:87], v[140:143], v[168:171], v[84:87]
	v_mfma_f32_16x16x32_f16 v[88:91], v[144:147], v[156:159], v[88:91]
	v_mfma_f32_16x16x32_f16 v[92:95], v[144:147], v[160:163], v[92:95]
	v_mfma_f32_16x16x32_f16 v[96:99], v[144:147], v[164:167], v[96:99]
	v_mfma_f32_16x16x32_f16 v[100:103], v[144:147], v[168:171], v[100:103]
	v_mfma_f32_16x16x32_f16 v[104:107], v[148:151], v[156:159], v[104:107]
	v_mfma_f32_16x16x32_f16 v[108:111], v[148:151], v[160:163], v[108:111]
	v_mfma_f32_16x16x32_f16 v[112:115], v[148:151], v[164:167], v[112:115]
	v_mfma_f32_16x16x32_f16 v[116:119], v[148:151], v[168:171], v[116:119]
	v_mfma_f32_16x16x32_f16 v[120:123], v[152:155], v[156:159], v[120:123]
	v_mfma_f32_16x16x32_f16 v[124:127], v[152:155], v[160:163], v[124:127]
	v_mfma_f32_16x16x32_f16 v[128:131], v[152:155], v[164:167], v[128:131]
	v_mfma_f32_16x16x32_f16 v[132:135], v[152:155], v[168:171], v[132:135]
	s_waitcnt lgkmcnt(0)
	v_mfma_f32_16x16x32_f16 v[56:59], v[172:175], v[192:195], v[56:59]
	v_mfma_f32_16x16x32_f16 v[60:63], v[172:175], v[196:199], v[60:63]
	v_mfma_f32_16x16x32_f16 v[64:67], v[172:175], v[200:203], v[64:67]
	v_mfma_f32_16x16x32_f16 v[68:71], v[172:175], v[204:207], v[68:71]
	v_mfma_f32_16x16x32_f16 v[72:75], v[176:179], v[192:195], v[72:75]
	v_mfma_f32_16x16x32_f16 v[76:79], v[176:179], v[196:199], v[76:79]
	v_mfma_f32_16x16x32_f16 v[80:83], v[176:179], v[200:203], v[80:83]
	v_mfma_f32_16x16x32_f16 v[84:87], v[176:179], v[204:207], v[84:87]
	v_mfma_f32_16x16x32_f16 v[88:91], v[180:183], v[192:195], v[88:91]
	v_mfma_f32_16x16x32_f16 v[92:95], v[180:183], v[196:199], v[92:95]
	v_mfma_f32_16x16x32_f16 v[96:99], v[180:183], v[200:203], v[96:99]
	v_mfma_f32_16x16x32_f16 v[100:103], v[180:183], v[204:207], v[100:103]
	v_mfma_f32_16x16x32_f16 v[104:107], v[184:187], v[192:195], v[104:107]
	v_mfma_f32_16x16x32_f16 v[108:111], v[184:187], v[196:199], v[108:111]
	v_mfma_f32_16x16x32_f16 v[112:115], v[184:187], v[200:203], v[112:115]
	v_mfma_f32_16x16x32_f16 v[116:119], v[184:187], v[204:207], v[116:119]
	v_mfma_f32_16x16x32_f16 v[120:123], v[188:191], v[192:195], v[120:123]
	v_mfma_f32_16x16x32_f16 v[124:127], v[188:191], v[196:199], v[124:127]
	v_mfma_f32_16x16x32_f16 v[128:131], v[188:191], v[200:203], v[128:131]
	v_mfma_f32_16x16x32_f16 v[132:135], v[188:191], v[204:207], v[132:135]
	s_nop 7
	s_nop 1
	s_add_u32 s24, s29, 0
	s_lshl_b32 s8, s24, 11
	v_add_u32_e32 v212, s8, v23
	v_pk_add_f32 v[56:57], v[56:57], v[24:25] op_sel_hi:[1,0]
	v_pk_add_f32 v[58:59], v[58:59], v[24:25] op_sel_hi:[1,0]
	v_cvt_pk_f16_f32 v56, v56, v57
	v_cvt_pk_f16_f32 v57, v58, v59
	global_store_dwordx2 v212, v[56:57], s[22:23] offset:0
	v_pk_add_f32 v[60:61], v[60:61], v[26:27] op_sel_hi:[1,0]
	v_pk_add_f32 v[62:63], v[62:63], v[26:27] op_sel_hi:[1,0]
	v_cvt_pk_f16_f32 v60, v60, v61
	v_cvt_pk_f16_f32 v61, v62, v63
	global_store_dwordx2 v212, v[60:61], s[22:23] offset:256
	v_pk_add_f32 v[64:65], v[64:65], v[28:29] op_sel_hi:[1,0]
	v_pk_add_f32 v[66:67], v[66:67], v[28:29] op_sel_hi:[1,0]
	v_cvt_pk_f16_f32 v64, v64, v65
	v_cvt_pk_f16_f32 v65, v66, v67
	global_store_dwordx2 v212, v[64:65], s[22:23] offset:1024
	v_pk_add_f32 v[68:69], v[68:69], v[30:31] op_sel_hi:[1,0]
	v_pk_add_f32 v[70:71], v[70:71], v[30:31] op_sel_hi:[1,0]
	v_cvt_pk_f16_f32 v68, v68, v69
	v_cvt_pk_f16_f32 v69, v70, v71
	global_store_dwordx2 v212, v[68:69], s[22:23] offset:1280
	s_add_u32 s24, s29, 1
	s_lshl_b32 s8, s24, 11
	v_add_u32_e32 v212, s8, v23
	v_pk_add_f32 v[72:73], v[72:73], v[24:25] op_sel_hi:[1,0]
	v_pk_add_f32 v[74:75], v[74:75], v[24:25] op_sel_hi:[1,0]
	v_cvt_pk_f16_f32 v72, v72, v73
	v_cvt_pk_f16_f32 v73, v74, v75
	global_store_dwordx2 v212, v[72:73], s[22:23] offset:0
	v_pk_add_f32 v[76:77], v[76:77], v[26:27] op_sel_hi:[1,0]
	v_pk_add_f32 v[78:79], v[78:79], v[26:27] op_sel_hi:[1,0]
	v_cvt_pk_f16_f32 v76, v76, v77
	v_cvt_pk_f16_f32 v77, v78, v79
	global_store_dwordx2 v212, v[76:77], s[22:23] offset:256
	v_pk_add_f32 v[80:81], v[80:81], v[28:29] op_sel_hi:[1,0]
	v_pk_add_f32 v[82:83], v[82:83], v[28:29] op_sel_hi:[1,0]
	v_cvt_pk_f16_f32 v80, v80, v81
	v_cvt_pk_f16_f32 v81, v82, v83
	global_store_dwordx2 v212, v[80:81], s[22:23] offset:1024
	v_pk_add_f32 v[84:85], v[84:85], v[30:31] op_sel_hi:[1,0]
	v_pk_add_f32 v[86:87], v[86:87], v[30:31] op_sel_hi:[1,0]
	v_cvt_pk_f16_f32 v84, v84, v85
	v_cvt_pk_f16_f32 v85, v86, v87
	global_store_dwordx2 v212, v[84:85], s[22:23] offset:1280
	s_add_u32 s24, s29, 2
	s_lshl_b32 s8, s24, 11
	v_add_u32_e32 v212, s8, v23
	v_pk_add_f32 v[88:89], v[88:89], v[24:25] op_sel_hi:[1,0]
	v_pk_add_f32 v[90:91], v[90:91], v[24:25] op_sel_hi:[1,0]
	v_cvt_pk_f16_f32 v88, v88, v89
	v_cvt_pk_f16_f32 v89, v90, v91
	global_store_dwordx2 v212, v[88:89], s[22:23] offset:0
	v_pk_add_f32 v[92:93], v[92:93], v[26:27] op_sel_hi:[1,0]
	v_pk_add_f32 v[94:95], v[94:95], v[26:27] op_sel_hi:[1,0]
	v_cvt_pk_f16_f32 v92, v92, v93
	v_cvt_pk_f16_f32 v93, v94, v95
	global_store_dwordx2 v212, v[92:93], s[22:23] offset:256
	v_pk_add_f32 v[96:97], v[96:97], v[28:29] op_sel_hi:[1,0]
	v_pk_add_f32 v[98:99], v[98:99], v[28:29] op_sel_hi:[1,0]
	v_cvt_pk_f16_f32 v96, v96, v97
	v_cvt_pk_f16_f32 v97, v98, v99
	global_store_dwordx2 v212, v[96:97], s[22:23] offset:1024
	v_pk_add_f32 v[100:101], v[100:101], v[30:31] op_sel_hi:[1,0]
	v_pk_add_f32 v[102:103], v[102:103], v[30:31] op_sel_hi:[1,0]
	v_cvt_pk_f16_f32 v100, v100, v101
	v_cvt_pk_f16_f32 v101, v102, v103
	global_store_dwordx2 v212, v[100:101], s[22:23] offset:1280
	s_add_u32 s24, s29, 3
	s_lshl_b32 s8, s24, 11
	v_add_u32_e32 v212, s8, v23
	v_pk_add_f32 v[104:105], v[104:105], v[24:25] op_sel_hi:[1,0]
	v_pk_add_f32 v[106:107], v[106:107], v[24:25] op_sel_hi:[1,0]
	v_cvt_pk_f16_f32 v104, v104, v105
	v_cvt_pk_f16_f32 v105, v106, v107
	global_store_dwordx2 v212, v[104:105], s[22:23] offset:0
	v_pk_add_f32 v[108:109], v[108:109], v[26:27] op_sel_hi:[1,0]
	v_pk_add_f32 v[110:111], v[110:111], v[26:27] op_sel_hi:[1,0]
	v_cvt_pk_f16_f32 v108, v108, v109
	v_cvt_pk_f16_f32 v109, v110, v111
	global_store_dwordx2 v212, v[108:109], s[22:23] offset:256
	v_pk_add_f32 v[112:113], v[112:113], v[28:29] op_sel_hi:[1,0]
	v_pk_add_f32 v[114:115], v[114:115], v[28:29] op_sel_hi:[1,0]
	v_cvt_pk_f16_f32 v112, v112, v113
	v_cvt_pk_f16_f32 v113, v114, v115
	global_store_dwordx2 v212, v[112:113], s[22:23] offset:1024
	v_pk_add_f32 v[116:117], v[116:117], v[30:31] op_sel_hi:[1,0]
	v_pk_add_f32 v[118:119], v[118:119], v[30:31] op_sel_hi:[1,0]
	v_cvt_pk_f16_f32 v116, v116, v117
	v_cvt_pk_f16_f32 v117, v118, v119
	global_store_dwordx2 v212, v[116:117], s[22:23] offset:1280
	s_add_u32 s24, s29, 4
	s_lshl_b32 s8, s24, 11
	v_add_u32_e32 v212, s8, v23
	v_pk_add_f32 v[120:121], v[120:121], v[24:25] op_sel_hi:[1,0]
	v_pk_add_f32 v[122:123], v[122:123], v[24:25] op_sel_hi:[1,0]
	v_cvt_pk_f16_f32 v120, v120, v121
	v_cvt_pk_f16_f32 v121, v122, v123
	global_store_dwordx2 v212, v[120:121], s[22:23] offset:0
	v_pk_add_f32 v[124:125], v[124:125], v[26:27] op_sel_hi:[1,0]
	v_pk_add_f32 v[126:127], v[126:127], v[26:27] op_sel_hi:[1,0]
	v_cvt_pk_f16_f32 v124, v124, v125
	v_cvt_pk_f16_f32 v125, v126, v127
	global_store_dwordx2 v212, v[124:125], s[22:23] offset:256
	v_pk_add_f32 v[128:129], v[128:129], v[28:29] op_sel_hi:[1,0]
	v_pk_add_f32 v[130:131], v[130:131], v[28:29] op_sel_hi:[1,0]
	v_cvt_pk_f16_f32 v128, v128, v129
	v_cvt_pk_f16_f32 v129, v130, v131
	global_store_dwordx2 v212, v[128:129], s[22:23] offset:1024
	v_pk_add_f32 v[132:133], v[132:133], v[30:31] op_sel_hi:[1,0]
	v_pk_add_f32 v[134:135], v[134:135], v[30:31] op_sel_hi:[1,0]
	v_cvt_pk_f16_f32 v132, v132, v133
	v_cvt_pk_f16_f32 v133, v134, v135
	global_store_dwordx2 v212, v[132:133], s[22:23] offset:1280
	s_branch .Lpf_done
.Lpf_vVB:
	s_lshl_b32 s25, s25, 6
	s_add_u32 s25, s25, 32
	s_add_u32 s29, s10, s25
	s_lshr_b32 s29, s29, 4
	v_add_u32_e32 v5, s25, v3
	v_lshlrev_b32_e32 v5, 7, v5
	v_add_u32_e32 v15, v5, v6
	v_add_u32_e32 v16, v5, v7
	v_add_u32_e32 v5, 0x9000, v9
	v_add_u32_e32 v17, v5, v6
	v_add_u32_e32 v18, v5, v7
	v_add_u32_e32 v19, 0x1a000, v15
	v_add_u32_e32 v20, 0x1a000, v16
	v_add_u32_e32 v21, 0x1a000, v17
	v_add_u32_e32 v22, 0x1a000, v18
	v_lshlrev_b32_e32 v5, 2, v3
	global_load_dword v24, v5, s[14:15] offset:0
	global_load_dword v26, v5, s[14:15] offset:64
	global_load_dword v28, v5, s[14:15] offset:128
	global_load_dword v30, v5, s[14:15] offset:192
	s_add_u32 m0, s28, 0x0
	s_nop 0
	global_load_lds_dwordx4 v10, s[4:5]
	s_add_u32 m0, s28, 0x2000
	s_nop 0
	global_load_lds_dwordx4 v11, s[4:5]
	s_add_u32 m0, s28, 0x4000
	s_nop 0
	global_load_lds_dwordx4 v12, s[4:5]
	s_add_u32 m0, s28, 0x6000
	s_nop 0
	global_load_lds_dwordx4 v13, s[4:5]
	s_add_u32 s4, s4, s20
	s_addc_u32 s5, s5, 0
	s_add_u32 m0, s28, 0x9000
	s_nop 0
	global_load_lds_dwordx4 v10, s[6:7]
	s_add_u32 m0, s28, 0xb000
	s_nop 0
	global_load_lds_dwordx4 v11, s[6:7]
	s_add_u32 s6, s6, s20
	s_addc_u32 s7, s7, 0
	s_add_u32 m0, s28, 0xd000
	s_nop 0
	global_load_lds_dwordx4 v10, s[4:5]
	s_add_u32 m0, s28, 0xf000
	s_nop 0
	global_load_lds_dwordx4 v11, s[4:5]
	s_add_u32 m0, s28, 0x11000
	s_nop 0
	global_load_lds_dwordx4 v12, s[4:5]
	s_add_u32 m0, s28, 0x13000
	s_nop 0
	global_load_lds_dwordx4 v13, s[4:5]
	s_add_u32 s4, s4, s20
	s_addc_u32 s5, s5, 0
	s_add_u32 m0, s28, 0x16000
	s_nop 0
	global_load_lds_dwordx4 v10, s[6:7]
	s_add_u32 m0, s28, 0x18000
	s_nop 0
	global_load_lds_dwordx4 v11, s[6:7]
	s_add_u32 s6, s6, s20
	s_addc_u32 s7, s7, 0
	s_add_u32 m0, s28, 0x1a000
	s_nop 0
	global_load_lds_dwordx4 v10, s[4:5]
	s_add_u32 m0, s28, 0x1c000
	s_nop 0
	global_load_lds_dwordx4 v11, s[4:5]
	s_add_u32 m0, s28, 0x1e000
	s_nop 0
	global_load_lds_dwordx4 v12, s[4:5]
	s_add_u32 m0, s28, 0x20000
	s_nop 0
	global_load_lds_dwordx4 v13, s[4:5]
	s_add_u32 s4, s4, s20
	s_addc_u32 s5, s5, 0
	s_add_u32 m0, s28, 0x23000
	s_nop 0
	global_load_lds_dwordx4 v10, s[6:7]
	s_add_u32 m0, s28, 0x25000
	s_nop 0
	global_load_lds_dwordx4 v11, s[6:7]
	s_add_u32 s6, s6, s20
	s_addc_u32 s7, s7, 0
	s_waitcnt vmcnt(12) lgkmcnt(0)
	s_barrier
	s_waitcnt lgkmcnt(7)
	ds_read_b128 v[136:139], v15
	ds_read_b128 v[156:159], v17
	ds_read_b128 v[160:163], v17 offset:2048
	ds_read_b128 v[164:167], v17 offset:4096
	ds_read_b128 v[168:171], v17 offset:6144
	ds_read_b128 v[140:143], v15 offset:2048
	ds_read_b128 v[144:147], v15 offset:4096
	ds_read_b128 v[148:151], v15 offset:6144
	s_waitcnt lgkmcnt(7)
	ds_read_b128 v[172:175], v16
	ds_read_b128 v[192:195], v18
	ds_read_b128 v[196:199], v18 offset:2048
	ds_read_b128 v[200:203], v18 offset:4096
	ds_read_b128 v[204:207], v18 offset:6144
	ds_read_b128 v[176:179], v16 offset:2048
	ds_read_b128 v[180:183], v16 offset:4096
	ds_read_b128 v[184:187], v16 offset:6144
	s_waitcnt lgkmcnt(8)
	v_mfma_f32_16x16x32_f16 v[56:59], v[136:139], v[156:159], 0
	v_mfma_f32_16x16x32_f16 v[60:63], v[136:139], v[160:163], 0
	v_mfma_f32_16x16x32_f16 v[64:67], v[136:139], v[164:167], 0
	v_mfma_f32_16x16x32_f16 v[68:71], v[136:139], v[168:171], 0
	v_mfma_f32_16x16x32_f16 v[72:75], v[140:143], v[156:159], 0
	v_mfma_f32_16x16x32_f16 v[76:79], v[140:143], v[160:163], 0
	v_mfma_f32_16x16x32_f16 v[80:83], v[140:143], v[164:167], 0
	v_mfma_f32_16x16x32_f16 v[84:87], v[140:143], v[168:171], 0
	v_mfma_f32_16x16x32_f16 v[88:91], v[144:147], v[156:159], 0
	v_mfma_f32_16x16x32_f16 v[92:95], v[144:147], v[160:163], 0
	v_mfma_f32_16x16x32_f16 v[96:99], v[144:147], v[164:167], 0
	v_mfma_f32_16x16x32_f16 v[100:103], v[144:147], v[168:171], 0
	v_mfma_f32_16x16x32_f16 v[104:107], v[148:151], v[156:159], 0
	v_mfma_f32_16x16x32_f16 v[108:111], v[148:151], v[160:163], 0
	v_mfma_f32_16x16x32_f16 v[112:115], v[148:151], v[164:167], 0
	v_mfma_f32_16x16x32_f16 v[116:119], v[148:151], v[168:171], 0
	s_waitcnt vmcnt(6) lgkmcnt(0)
	s_barrier
	s_waitcnt lgkmcnt(7)
	ds_read_b128 v[136:139], v15 offset:53248
	ds_read_b128 v[156:159], v17 offset:53248
	ds_read_b128 v[160:163], v17 offset:55296
	ds_read_b128 v[164:167], v17 offset:57344
	ds_read_b128 v[168:171], v17 offset:59392
	ds_read_b128 v[140:143], v15 offset:55296
	ds_read_b128 v[144:147], v15 offset:57344
	ds_read_b128 v[148:151], v15 offset:59392
	s_waitcnt lgkmcnt(8)
	v_mfma_f32_16x16x32_f16 v[56:59], v[172:175], v[192:195], v[56:59]
	s_add_u32 m0, s28, 0x0
	v_mfma_f32_16x16x32_f16 v[60:63], v[172:175], v[196:199], v[60:63]
	global_load_lds_dwordx4 v10, s[4:5]
	v_mfma_f32_16x16x32_f16 v[64:67], v[172:175], v[200:203], v[64:67]
	v_mfma_f32_16x16x32_f16 v[68:71], v[172:175], v[204:207], v[68:71]
	v_mfma_f32_16x16x32_f16 v[72:75], v[176:179], v[192:195], v[72:75]
	v_mfma_f32_16x16x32_f16 v[76:79], v[176:179], v[196:199], v[76:79]
	s_add_u32 m0, s28, 0x2000
	v_mfma_f32_16x16x32_f16 v[80:83], v[176:179], v[200:203], v[80:83]
	global_load_lds_dwordx4 v11, s[4:5]
	v_mfma_f32_16x16x32_f16 v[84:87], v[176:179], v[204:207], v[84:87]
	v_mfma_f32_16x16x32_f16 v[88:91], v[180:183], v[192:195], v[88:91]
	v_mfma_f32_16x16x32_f16 v[92:95], v[180:183], v[196:199], v[92:95]
	v_mfma_f32_16x16x32_f16 v[96:99], v[180:183], v[200:203], v[96:99]
	s_add_u32 m0, s28, 0x4000
	v_mfma_f32_16x16x32_f16 v[100:103], v[180:183], v[204:207], v[100:103]
	global_load_lds_dwordx4 v12, s[4:5]
	v_mfma_f32_16x16x32_f16 v[104:107], v[184:187], v[192:195], v[104:107]
	v_mfma_f32_16x16x32_f16 v[108:111], v[184:187], v[196:199], v[108:111]
	v_mfma_f32_16x16x32_f16 v[112:115], v[184:187], v[200:203], v[112:115]
	v_mfma_f32_16x16x32_f16 v[116:119], v[184:187], v[204:207], v[116:119]
	s_waitcnt lgkmcnt(7)
	ds_read_b128 v[172:175], v16 offset:53248
	ds_read_b128 v[192:195], v18 offset:53248
	ds_read_b128 v[196:199], v18 offset:55296
	ds_read_b128 v[200:203], v18 offset:57344
	ds_read_b128 v[204:207], v18 offset:59392
	ds_read_b128 v[176:179], v16 offset:55296
	ds_read_b128 v[180:183], v16 offset:57344
	ds_read_b128 v[184:187], v16 offset:59392
	s_waitcnt lgkmcnt(8)
	v_mfma_f32_16x16x32_f16 v[56:59], v[136:139], v[156:159], v[56:59]
	s_add_u32 m0, s28, 0x6000
	v_mfma_f32_16x16x32_f16 v[60:63], v[136:139], v[160:163], v[60:63]
	global_load_lds_dwordx4 v13, s[4:5]
	s_add_u32 s4, s4, s20
	s_addc_u32 s5, s5, 0
	v_mfma_f32_16x16x32_f16 v[64:67], v[136:139], v[164:167], v[64:67]
	v_mfma_f32_16x16x32_f16 v[68:71], v[136:139], v[168:171], v[68:71]
	v_mfma_f32_16x16x32_f16 v[72:75], v[140:143], v[156:159], v[72:75]
	v_mfma_f32_16x16x32_f16 v[76:79], v[140:143], v[160:163], v[76:79]
	s_add_u32 m0, s28, 0x9000
	v_mfma_f32_16x16x32_f16 v[80:83], v[140:143], v[164:167], v[80:83]
	global_load_lds_dwordx4 v10, s[6:7]
	v_mfma_f32_16x16x32_f16 v[84:87], v[140:143], v[168:171], v[84:87]
	v_mfma_f32_16x16x32_f16 v[88:91], v[144:147], v[156:159], v[88:91]
	v_mfma_f32_16x16x32_f16 v[92:95], v[144:147], v[160:163], v[92:95]
	v_mfma_f32_16x16x32_f16 v[96:99], v[144:147], v[164:167], v[96:99]
	s_add_u32 m0, s28, 0xb000
	v_mfma_f32_16x16x32_f16 v[100:103], v[144:147], v[168:171], v[100:103]
	global_load_lds_dwordx4 v11, s[6:7]
	s_add_u32 s6, s6, s20
	s_addc_u32 s7, s7, 0
	v_mfma_f32_16x16x32_f16 v[104:107], v[148:151], v[156:159], v[104:107]
	v_mfma_f32_16x16x32_f16 v[108:111], v[148:151], v[160:163], v[108:111]
	v_mfma_f32_16x16x32_f16 v[112:115], v[148:151], v[164:167], v[112:115]
	v_mfma_f32_16x16x32_f16 v[116:119], v[148:151], v[168:171], v[116:119]
	s_waitcnt vmcnt(6) lgkmcnt(0)
	s_barrier
	s_waitcnt lgkmcnt(7)
	ds_read_b128 v[136:139], v19
	ds_read_b128 v[156:159], v21
	ds_read_b128 v[160:163], v21 offset:2048
	ds_read_b128 v[164:167], v21 offset:4096
	ds_read_b128 v[168:171], v21 offset:6144
	ds_read_b128 v[140:143], v19 offset:2048
	ds_read_b128 v[144:147], v19 offset:4096
	ds_read_b128 v[148:151], v19 offset:6144
	s_waitcnt lgkmcnt(8)
	v_mfma_f32_16x16x32_f16 v[56:59], v[172:175], v[192:195], v[56:59]
	s_add_u32 m0, s28, 0xd000
	v_mfma_f32_16x16x32_f16 v[60:63], v[172:175], v[196:199], v[60:63]
	global_load_lds_dwordx4 v10, s[4:5]
	v_mfma_f32_16x16x32_f16 v[64:67], v[172:175], v[200:203], v[64:67]
	v_mfma_f32_16x16x32_f16 v[68:71], v[172:175], v[204:207], v[68:71]
	v_mfma_f32_16x16x32_f16 v[72:75], v[176:179], v[192:195], v[72:75]
	v_mfma_f32_16x16x32_f16 v[76:79], v[176:179], v[196:199], v[76:79]
	s_add_u32 m0, s28, 0xf000
	v_mfma_f32_16x16x32_f16 v[80:83], v[176:179], v[200:203], v[80:83]
	global_load_lds_dwordx4 v11, s[4:5]
	v_mfma_f32_16x16x32_f16 v[84:87], v[176:179], v[204:207], v[84:87]
	v_mfma_f32_16x16x32_f16 v[88:91], v[180:183], v[192:195], v[88:91]
	v_mfma_f32_16x16x32_f16 v[92:95], v[180:183], v[196:199], v[92:95]
	v_mfma_f32_16x16x32_f16 v[96:99], v[180:183], v[200:203], v[96:99]
	s_add_u32 m0, s28, 0x11000
	v_mfma_f32_16x16x32_f16 v[100:103], v[180:183], v[204:207], v[100:103]
	global_load_lds_dwordx4 v12, s[4:5]
	v_mfma_f32_16x16x32_f16 v[104:107], v[184:187], v[192:195], v[104:107]
	v_mfma_f32_16x16x32_f16 v[108:111], v[184:187], v[196:199], v[108:111]
	v_mfma_f32_16x16x32_f16 v[112:115], v[184:187], v[200:203], v[112:115]
	v_mfma_f32_16x16x32_f16 v[116:119], v[184:187], v[204:207], v[116:119]
	s_waitcnt lgkmcnt(7)
	ds_read_b128 v[172:175], v20
	ds_read_b128 v[192:195], v22
	ds_read_b128 v[196:199], v22 offset:2048
	ds_read_b128 v[200:203], v22 offset:4096
	ds_read_b128 v[204:207], v22 offset:6144
	ds_read_b128 v[176:179], v20 offset:2048
	ds_read_b128 v[180:183], v20 offset:4096
	ds_read_b128 v[184:187], v20 offset:6144
	s_waitcnt lgkmcnt(8)
	v_mfma_f32_16x16x32_f16 v[56:59], v[136:139], v[156:159], v[56:59]
	s_add_u32 m0, s28, 0x13000
	v_mfma_f32_16x16x32_f16 v[60:63], v[136:139], v[160:163], v[60:63]
	global_load_lds_dwordx4 v13, s[4:5]
	s_add_u32 s4, s4, s20
	s_addc_u32 s5, s5, 0
	v_mfma_f32_16x16x32_f16 v[64:67], v[136:139], v[164:167], v[64:67]
	v_mfma_f32_16x16x32_f16 v[68:71], v[136:139], v[168:171], v[68:71]
	v_mfma_f32_16x16x32_f16 v[72:75], v[140:143], v[156:159], v[72:75]
	v_mfma_f32_16x16x32_f16 v[76:79], v[140:143], v[160:163], v[76:79]
	s_add_u32 m0, s28, 0x16000
	v_mfma_f32_16x16x32_f16 v[80:83], v[140:143], v[164:167], v[80:83]
	global_load_lds_dwordx4 v10, s[6:7]
	v_mfma_f32_16x16x32_f16 v[84:87], v[140:143], v[168:171], v[84:87]
	v_mfma_f32_16x16x32_f16 v[88:91], v[144:147], v[156:159], v[88:91]
	v_mfma_f32_16x16x32_f16 v[92:95], v[144:147], v[160:163], v[92:95]
	v_mfma_f32_16x16x32_f16 v[96:99], v[144:147], v[164:167], v[96:99]
	s_add_u32 m0, s28, 0x18000
	v_mfma_f32_16x16x32_f16 v[100:103], v[144:147], v[168:171], v[100:103]
	global_load_lds_dwordx4 v11, s[6:7]
	s_add_u32 s6, s6, s20
	s_addc_u32 s7, s7, 0
	v_mfma_f32_16x16x32_f16 v[104:107], v[148:151], v[156:159], v[104:107]
	v_mfma_f32_16x16x32_f16 v[108:111], v[148:151], v[160:163], v[108:111]
	v_mfma_f32_16x16x32_f16 v[112:115], v[148:151], v[164:167], v[112:115]
	v_mfma_f32_16x16x32_f16 v[116:119], v[148:151], v[168:171], v[116:119]
	s_waitcnt vmcnt(6) lgkmcnt(0)
	s_barrier
	s_waitcnt lgkmcnt(7)
	ds_read_b128 v[136:139], v15
	ds_read_b128 v[156:159], v17
	ds_read_b128 v[160:163], v17 offset:2048
	ds_read_b128 v[164:167], v17 offset:4096
	ds_read_b128 v[168:171], v17 offset:6144
	ds_read_b128 v[140:143], v15 offset:2048
	ds_read_b128 v[144:147], v15 offset:4096
	ds_read_b128 v[148:151], v15 offset:6144
	s_waitcnt lgkmcnt(8)
	v_mfma_f32_16x16x32_f16 v[56:59], v[172:175], v[192:195], v[56:59]
	s_add_u32 m0, s28, 0x1a000
	v_mfma_f32_16x16x32_f16 v[60:63], v[172:175], v[196:199], v[60:63]
	global_load_lds_dwordx4 v10, s[4:5]
	v_mfma_f32_16x16x32_f16 v[64:67], v[172:175], v[200:203], v[64:67]
	v_mfma_f32_16x16x32_f16 v[68:71], v[172:175], v[204:207], v[68:71]
	v_mfma_f32_16x16x32_f16 v[72:75], v[176:179], v[192:195], v[72:75]
	v_mfma_f32_16x16x32_f16 v[76:79], v[176:179], v[196:199], v[76:79]
	s_add_u32 m0, s28, 0x1c000
	v_mfma_f32_16x16x32_f16 v[80:83], v[176:179], v[200:203], v[80:83]
	global_load_lds_dwordx4 v11, s[4:5]
	v_mfma_f32_16x16x32_f16 v[84:87], v[176:179], v[204:207], v[84:87]
	v_mfma_f32_16x16x32_f16 v[88:91], v[180:183], v[192:195], v[88:91]
	v_mfma_f32_16x16x32_f16 v[92:95], v[180:183], v[196:199], v[92:95]
	v_mfma_f32_16x16x32_f16 v[96:99], v[180:183], v[200:203], v[96:99]
	s_add_u32 m0, s28, 0x1e000
	v_mfma_f32_16x16x32_f16 v[100:103], v[180:183], v[204:207], v[100:103]
	global_load_lds_dwordx4 v12, s[4:5]
	v_mfma_f32_16x16x32_f16 v[104:107], v[184:187], v[192:195], v[104:107]
	v_mfma_f32_16x16x32_f16 v[108:111], v[184:187], v[196:199], v[108:111]
	v_mfma_f32_16x16x32_f16 v[112:115], v[184:187], v[200:203], v[112:115]
	v_mfma_f32_16x16x32_f16 v[116:119], v[184:187], v[204:207], v[116:119]
	s_waitcnt lgkmcnt(7)
	ds_read_b128 v[172:175], v16
	ds_read_b128 v[192:195], v18
	ds_read_b128 v[196:199], v18 offset:2048
	ds_read_b128 v[200:203], v18 offset:4096
	ds_read_b128 v[204:207], v18 offset:6144
	ds_read_b128 v[176:179], v16 offset:2048
	ds_read_b128 v[180:183], v16 offset:4096
	ds_read_b128 v[184:187], v16 offset:6144
	s_waitcnt lgkmcnt(8)
	v_mfma_f32_16x16x32_f16 v[56:59], v[136:139], v[156:159], v[56:59]
	s_add_u32 m0, s28, 0x20000
	v_mfma_f32_16x16x32_f16 v[60:63], v[136:139], v[160:163], v[60:63]
	global_load_lds_dwordx4 v13, s[4:5]
	s_add_u32 s4, s4, s20
	s_addc_u32 s5, s5, 0
	v_mfma_f32_16x16x32_f16 v[64:67], v[136:139], v[164:167], v[64:67]
	v_mfma_f32_16x16x32_f16 v[68:71], v[136:139], v[168:171], v[68:71]
	v_mfma_f32_16x16x32_f16 v[72:75], v[140:143], v[156:159], v[72:75]
	v_mfma_f32_16x16x32_f16 v[76:79], v[140:143], v[160:163], v[76:79]
	s_add_u32 m0, s28, 0x23000
	v_mfma_f32_16x16x32_f16 v[80:83], v[140:143], v[164:167], v[80:83]
	global_load_lds_dwordx4 v10, s[6:7]
	v_mfma_f32_16x16x32_f16 v[84:87], v[140:143], v[168:171], v[84:87]
	v_mfma_f32_16x16x32_f16 v[88:91], v[144:147], v[156:159], v[88:91]
	v_mfma_f32_16x16x32_f16 v[92:95], v[144:147], v[160:163], v[92:95]
	v_mfma_f32_16x16x32_f16 v[96:99], v[144:147], v[164:167], v[96:99]
	s_add_u32 m0, s28, 0x25000
	v_mfma_f32_16x16x32_f16 v[100:103], v[144:147], v[168:171], v[100:103]
	global_load_lds_dwordx4 v11, s[6:7]
	s_add_u32 s6, s6, s20
	s_addc_u32 s7, s7, 0
	v_mfma_f32_16x16x32_f16 v[104:107], v[148:151], v[156:159], v[104:107]
	v_mfma_f32_16x16x32_f16 v[108:111], v[148:151], v[160:163], v[108:111]
	v_mfma_f32_16x16x32_f16 v[112:115], v[148:151], v[164:167], v[112:115]
	v_mfma_f32_16x16x32_f16 v[116:119], v[148:151], v[168:171], v[116:119]
	s_waitcnt vmcnt(6) lgkmcnt(0)
	s_barrier
	s_waitcnt lgkmcnt(7)
	ds_read_b128 v[136:139], v15 offset:53248
	ds_read_b128 v[156:159], v17 offset:53248
	ds_read_b128 v[160:163], v17 offset:55296
	ds_read_b128 v[164:167], v17 offset:57344
	ds_read_b128 v[168:171], v17 offset:59392
	ds_read_b128 v[140:143], v15 offset:55296
	ds_read_b128 v[144:147], v15 offset:57344
	ds_read_b128 v[148:151], v15 offset:59392
	s_waitcnt lgkmcnt(8)
	v_mfma_f32_16x16x32_f16 v[56:59], v[172:175], v[192:195], v[56:59]
	s_add_u32 m0, s28, 0x0
	v_mfma_f32_16x16x32_f16 v[60:63], v[172:175], v[196:199], v[60:63]
	global_load_lds_dwordx4 v10, s[4:5]
	v_mfma_f32_16x16x32_f16 v[64:67], v[172:175], v[200:203], v[64:67]
	v_mfma_f32_16x16x32_f16 v[68:71], v[172:175], v[204:207], v[68:71]
	v_mfma_f32_16x16x32_f16 v[72:75], v[176:179], v[192:195], v[72:75]
	v_mfma_f32_16x16x32_f16 v[76:79], v[176:179], v[196:199], v[76:79]
	s_add_u32 m0, s28, 0x2000
	v_mfma_f32_16x16x32_f16 v[80:83], v[176:179], v[200:203], v[80:83]
	global_load_lds_dwordx4 v11, s[4:5]
	v_mfma_f32_16x16x32_f16 v[84:87], v[176:179], v[204:207], v[84:87]
	v_mfma_f32_16x16x32_f16 v[88:91], v[180:183], v[192:195], v[88:91]
	v_mfma_f32_16x16x32_f16 v[92:95], v[180:183], v[196:199], v[92:95]
	v_mfma_f32_16x16x32_f16 v[96:99], v[180:183], v[200:203], v[96:99]
	s_add_u32 m0, s28, 0x4000
	v_mfma_f32_16x16x32_f16 v[100:103], v[180:183], v[204:207], v[100:103]
	global_load_lds_dwordx4 v12, s[4:5]
	v_mfma_f32_16x16x32_f16 v[104:107], v[184:187], v[192:195], v[104:107]
	v_mfma_f32_16x16x32_f16 v[108:111], v[184:187], v[196:199], v[108:111]
	v_mfma_f32_16x16x32_f16 v[112:115], v[184:187], v[200:203], v[112:115]
	v_mfma_f32_16x16x32_f16 v[116:119], v[184:187], v[204:207], v[116:119]
	s_waitcnt lgkmcnt(7)
	ds_read_b128 v[172:175], v16 offset:53248
	ds_read_b128 v[192:195], v18 offset:53248
	ds_read_b128 v[196:199], v18 offset:55296
	ds_read_b128 v[200:203], v18 offset:57344
	ds_read_b128 v[204:207], v18 offset:59392
	ds_read_b128 v[176:179], v16 offset:55296
	ds_read_b128 v[180:183], v16 offset:57344
	ds_read_b128 v[184:187], v16 offset:59392
	s_waitcnt lgkmcnt(8)
	v_mfma_f32_16x16x32_f16 v[56:59], v[136:139], v[156:159], v[56:59]
	s_add_u32 m0, s28, 0x6000
	v_mfma_f32_16x16x32_f16 v[60:63], v[136:139], v[160:163], v[60:63]
	global_load_lds_dwordx4 v13, s[4:5]
	s_add_u32 s4, s4, s20
	s_addc_u32 s5, s5, 0
	v_mfma_f32_16x16x32_f16 v[64:67], v[136:139], v[164:167], v[64:67]
	v_mfma_f32_16x16x32_f16 v[68:71], v[136:139], v[168:171], v[68:71]
	v_mfma_f32_16x16x32_f16 v[72:75], v[140:143], v[156:159], v[72:75]
	v_mfma_f32_16x16x32_f16 v[76:79], v[140:143], v[160:163], v[76:79]
	s_add_u32 m0, s28, 0x9000
	v_mfma_f32_16x16x32_f16 v[80:83], v[140:143], v[164:167], v[80:83]
	global_load_lds_dwordx4 v10, s[6:7]
	v_mfma_f32_16x16x32_f16 v[84:87], v[140:143], v[168:171], v[84:87]
	v_mfma_f32_16x16x32_f16 v[88:91], v[144:147], v[156:159], v[88:91]
	v_mfma_f32_16x16x32_f16 v[92:95], v[144:147], v[160:163], v[92:95]
	v_mfma_f32_16x16x32_f16 v[96:99], v[144:147], v[164:167], v[96:99]
	s_add_u32 m0, s28, 0xb000
	v_mfma_f32_16x16x32_f16 v[100:103], v[144:147], v[168:171], v[100:103]
	global_load_lds_dwordx4 v11, s[6:7]
	s_add_u32 s6, s6, s20
	s_addc_u32 s7, s7, 0
	v_mfma_f32_16x16x32_f16 v[104:107], v[148:151], v[156:159], v[104:107]
	v_mfma_f32_16x16x32_f16 v[108:111], v[148:151], v[160:163], v[108:111]
	v_mfma_f32_16x16x32_f16 v[112:115], v[148:151], v[164:167], v[112:115]
	v_mfma_f32_16x16x32_f16 v[116:119], v[148:151], v[168:171], v[116:119]
	s_waitcnt vmcnt(6) lgkmcnt(0)
	s_barrier
	s_waitcnt lgkmcnt(7)
	ds_read_b128 v[136:139], v19
	ds_read_b128 v[156:159], v21
	ds_read_b128 v[160:163], v21 offset:2048
	ds_read_b128 v[164:167], v21 offset:4096
	ds_read_b128 v[168:171], v21 offset:6144
	ds_read_b128 v[140:143], v19 offset:2048
	ds_read_b128 v[144:147], v19 offset:4096
	ds_read_b128 v[148:151], v19 offset:6144
	s_waitcnt lgkmcnt(8)
	v_mfma_f32_16x16x32_f16 v[56:59], v[172:175], v[192:195], v[56:59]
	s_add_u32 m0, s28, 0xd000
	v_mfma_f32_16x16x32_f16 v[60:63], v[172:175], v[196:199], v[60:63]
	global_load_lds_dwordx4 v10, s[4:5]
	v_mfma_f32_16x16x32_f16 v[64:67], v[172:175], v[200:203], v[64:67]
	v_mfma_f32_16x16x32_f16 v[68:71], v[172:175], v[204:207], v[68:71]
	v_mfma_f32_16x16x32_f16 v[72:75], v[176:179], v[192:195], v[72:75]
	v_mfma_f32_16x16x32_f16 v[76:79], v[176:179], v[196:199], v[76:79]
	s_add_u32 m0, s28, 0xf000
	v_mfma_f32_16x16x32_f16 v[80:83], v[176:179], v[200:203], v[80:83]
	global_load_lds_dwordx4 v11, s[4:5]
	v_mfma_f32_16x16x32_f16 v[84:87], v[176:179], v[204:207], v[84:87]
	v_mfma_f32_16x16x32_f16 v[88:91], v[180:183], v[192:195], v[88:91]
	v_mfma_f32_16x16x32_f16 v[92:95], v[180:183], v[196:199], v[92:95]
	v_mfma_f32_16x16x32_f16 v[96:99], v[180:183], v[200:203], v[96:99]
	s_add_u32 m0, s28, 0x11000
	v_mfma_f32_16x16x32_f16 v[100:103], v[180:183], v[204:207], v[100:103]
	global_load_lds_dwordx4 v12, s[4:5]
	v_mfma_f32_16x16x32_f16 v[104:107], v[184:187], v[192:195], v[104:107]
	v_mfma_f32_16x16x32_f16 v[108:111], v[184:187], v[196:199], v[108:111]
	v_mfma_f32_16x16x32_f16 v[112:115], v[184:187], v[200:203], v[112:115]
	v_mfma_f32_16x16x32_f16 v[116:119], v[184:187], v[204:207], v[116:119]
	s_waitcnt lgkmcnt(7)
	ds_read_b128 v[172:175], v20
	ds_read_b128 v[192:195], v22
	ds_read_b128 v[196:199], v22 offset:2048
	ds_read_b128 v[200:203], v22 offset:4096
	ds_read_b128 v[204:207], v22 offset:6144
	ds_read_b128 v[176:179], v20 offset:2048
	ds_read_b128 v[180:183], v20 offset:4096
	ds_read_b128 v[184:187], v20 offset:6144
	s_waitcnt lgkmcnt(8)
	v_mfma_f32_16x16x32_f16 v[56:59], v[136:139], v[156:159], v[56:59]
	s_add_u32 m0, s28, 0x13000
	v_mfma_f32_16x16x32_f16 v[60:63], v[136:139], v[160:163], v[60:63]
	global_load_lds_dwordx4 v13, s[4:5]
	s_add_u32 s4, s4, s20
	s_addc_u32 s5, s5, 0
	v_mfma_f32_16x16x32_f16 v[64:67], v[136:139], v[164:167], v[64:67]
	v_mfma_f32_16x16x32_f16 v[68:71], v[136:139], v[168:171], v[68:71]
	v_mfma_f32_16x16x32_f16 v[72:75], v[140:143], v[156:159], v[72:75]
	v_mfma_f32_16x16x32_f16 v[76:79], v[140:143], v[160:163], v[76:79]
	s_add_u32 m0, s28, 0x16000
	v_mfma_f32_16x16x32_f16 v[80:83], v[140:143], v[164:167], v[80:83]
	global_load_lds_dwordx4 v10, s[6:7]
	v_mfma_f32_16x16x32_f16 v[84:87], v[140:143], v[168:171], v[84:87]
	v_mfma_f32_16x16x32_f16 v[88:91], v[144:147], v[156:159], v[88:91]
	v_mfma_f32_16x16x32_f16 v[92:95], v[144:147], v[160:163], v[92:95]
	v_mfma_f32_16x16x32_f16 v[96:99], v[144:147], v[164:167], v[96:99]
	s_add_u32 m0, s28, 0x18000
	v_mfma_f32_16x16x32_f16 v[100:103], v[144:147], v[168:171], v[100:103]
	global_load_lds_dwordx4 v11, s[6:7]
	s_add_u32 s6, s6, s20
	s_addc_u32 s7, s7, 0
	v_mfma_f32_16x16x32_f16 v[104:107], v[148:151], v[156:159], v[104:107]
	v_mfma_f32_16x16x32_f16 v[108:111], v[148:151], v[160:163], v[108:111]
	v_mfma_f32_16x16x32_f16 v[112:115], v[148:151], v[164:167], v[112:115]
	v_mfma_f32_16x16x32_f16 v[116:119], v[148:151], v[168:171], v[116:119]
	s_waitcnt vmcnt(6) lgkmcnt(0)
	s_barrier
	s_waitcnt lgkmcnt(7)
	ds_read_b128 v[136:139], v15
	ds_read_b128 v[156:159], v17
	ds_read_b128 v[160:163], v17 offset:2048
	ds_read_b128 v[164:167], v17 offset:4096
	ds_read_b128 v[168:171], v17 offset:6144
	ds_read_b128 v[140:143], v15 offset:2048
	ds_read_b128 v[144:147], v15 offset:4096
	ds_read_b128 v[148:151], v15 offset:6144
	s_waitcnt lgkmcnt(8)
	v_mfma_f32_16x16x32_f16 v[56:59], v[172:175], v[192:195], v[56:59]
	s_add_u32 m0, s28, 0x1a000
	v_mfma_f32_16x16x32_f16 v[60:63], v[172:175], v[196:199], v[60:63]
	global_load_lds_dwordx4 v10, s[4:5]
	v_mfma_f32_16x16x32_f16 v[64:67], v[172:175], v[200:203], v[64:67]
	v_mfma_f32_16x16x32_f16 v[68:71], v[172:175], v[204:207], v[68:71]
	v_mfma_f32_16x16x32_f16 v[72:75], v[176:179], v[192:195], v[72:75]
	v_mfma_f32_16x16x32_f16 v[76:79], v[176:179], v[196:199], v[76:79]
	s_add_u32 m0, s28, 0x1c000
	v_mfma_f32_16x16x32_f16 v[80:83], v[176:179], v[200:203], v[80:83]
	global_load_lds_dwordx4 v11, s[4:5]
	v_mfma_f32_16x16x32_f16 v[84:87], v[176:179], v[204:207], v[84:87]
	v_mfma_f32_16x16x32_f16 v[88:91], v[180:183], v[192:195], v[88:91]
	v_mfma_f32_16x16x32_f16 v[92:95], v[180:183], v[196:199], v[92:95]
	v_mfma_f32_16x16x32_f16 v[96:99], v[180:183], v[200:203], v[96:99]
	s_add_u32 m0, s28, 0x1e000
	v_mfma_f32_16x16x32_f16 v[100:103], v[180:183], v[204:207], v[100:103]
	global_load_lds_dwordx4 v12, s[4:5]
	v_mfma_f32_16x16x32_f16 v[104:107], v[184:187], v[192:195], v[104:107]
	v_mfma_f32_16x16x32_f16 v[108:111], v[184:187], v[196:199], v[108:111]
	v_mfma_f32_16x16x32_f16 v[112:115], v[184:187], v[200:203], v[112:115]
	v_mfma_f32_16x16x32_f16 v[116:119], v[184:187], v[204:207], v[116:119]
	s_waitcnt lgkmcnt(7)
	ds_read_b128 v[172:175], v16
	ds_read_b128 v[192:195], v18
	ds_read_b128 v[196:199], v18 offset:2048
	ds_read_b128 v[200:203], v18 offset:4096
	ds_read_b128 v[204:207], v18 offset:6144
	ds_read_b128 v[176:179], v16 offset:2048
	ds_read_b128 v[180:183], v16 offset:4096
	ds_read_b128 v[184:187], v16 offset:6144
	s_waitcnt lgkmcnt(8)
	v_mfma_f32_16x16x32_f16 v[56:59], v[136:139], v[156:159], v[56:59]
	s_add_u32 m0, s28, 0x20000
	v_mfma_f32_16x16x32_f16 v[60:63], v[136:139], v[160:163], v[60:63]
	global_load_lds_dwordx4 v13, s[4:5]
	s_add_u32 s4, s4, s20
	s_addc_u32 s5, s5, 0
	v_mfma_f32_16x16x32_f16 v[64:67], v[136:139], v[164:167], v[64:67]
	v_mfma_f32_16x16x32_f16 v[68:71], v[136:139], v[168:171], v[68:71]
	v_mfma_f32_16x16x32_f16 v[72:75], v[140:143], v[156:159], v[72:75]
	v_mfma_f32_16x16x32_f16 v[76:79], v[140:143], v[160:163], v[76:79]
	s_add_u32 m0, s28, 0x23000
	v_mfma_f32_16x16x32_f16 v[80:83], v[140:143], v[164:167], v[80:83]
	global_load_lds_dwordx4 v10, s[6:7]
	v_mfma_f32_16x16x32_f16 v[84:87], v[140:143], v[168:171], v[84:87]
	v_mfma_f32_16x16x32_f16 v[88:91], v[144:147], v[156:159], v[88:91]
	v_mfma_f32_16x16x32_f16 v[92:95], v[144:147], v[160:163], v[92:95]
	v_mfma_f32_16x16x32_f16 v[96:99], v[144:147], v[164:167], v[96:99]
	s_add_u32 m0, s28, 0x25000
	v_mfma_f32_16x16x32_f16 v[100:103], v[144:147], v[168:171], v[100:103]
	global_load_lds_dwordx4 v11, s[6:7]
	s_add_u32 s6, s6, s20
	s_addc_u32 s7, s7, 0
	v_mfma_f32_16x16x32_f16 v[104:107], v[148:151], v[156:159], v[104:107]
	v_mfma_f32_16x16x32_f16 v[108:111], v[148:151], v[160:163], v[108:111]
	v_mfma_f32_16x16x32_f16 v[112:115], v[148:151], v[164:167], v[112:115]
	v_mfma_f32_16x16x32_f16 v[116:119], v[148:151], v[168:171], v[116:119]
	s_waitcnt vmcnt(6) lgkmcnt(0)
	s_barrier
	s_waitcnt lgkmcnt(7)
	ds_read_b128 v[136:139], v15 offset:53248
	ds_read_b128 v[156:159], v17 offset:53248
	ds_read_b128 v[160:163], v17 offset:55296
	ds_read_b128 v[164:167], v17 offset:57344
	ds_read_b128 v[168:171], v17 offset:59392
	ds_read_b128 v[140:143], v15 offset:55296
	ds_read_b128 v[144:147], v15 offset:57344
	ds_read_b128 v[148:151], v15 offset:59392
	s_waitcnt lgkmcnt(8)
	v_mfma_f32_16x16x32_f16 v[56:59], v[172:175], v[192:195], v[56:59]
	s_add_u32 m0, s28, 0x0
	v_mfma_f32_16x16x32_f16 v[60:63], v[172:175], v[196:199], v[60:63]
	global_load_lds_dwordx4 v10, s[4:5]
	v_mfma_f32_16x16x32_f16 v[64:67], v[172:175], v[200:203], v[64:67]
	v_mfma_f32_16x16x32_f16 v[68:71], v[172:175], v[204:207], v[68:71]
	v_mfma_f32_16x16x32_f16 v[72:75], v[176:179], v[192:195], v[72:75]
	v_mfma_f32_16x16x32_f16 v[76:79], v[176:179], v[196:199], v[76:79]
	s_add_u32 m0, s28, 0x2000
	v_mfma_f32_16x16x32_f16 v[80:83], v[176:179], v[200:203], v[80:83]
	global_load_lds_dwordx4 v11, s[4:5]
	v_mfma_f32_16x16x32_f16 v[84:87], v[176:179], v[204:207], v[84:87]
	v_mfma_f32_16x16x32_f16 v[88:91], v[180:183], v[192:195], v[88:91]
	v_mfma_f32_16x16x32_f16 v[92:95], v[180:183], v[196:199], v[92:95]
	v_mfma_f32_16x16x32_f16 v[96:99], v[180:183], v[200:203], v[96:99]
	s_add_u32 m0, s28, 0x4000
	v_mfma_f32_16x16x32_f16 v[100:103], v[180:183], v[204:207], v[100:103]
	global_load_lds_dwordx4 v12, s[4:5]
	v_mfma_f32_16x16x32_f16 v[104:107], v[184:187], v[192:195], v[104:107]
	v_mfma_f32_16x16x32_f16 v[108:111], v[184:187], v[196:199], v[108:111]
	v_mfma_f32_16x16x32_f16 v[112:115], v[184:187], v[200:203], v[112:115]
	v_mfma_f32_16x16x32_f16 v[116:119], v[184:187], v[204:207], v[116:119]
	s_waitcnt lgkmcnt(7)
	ds_read_b128 v[172:175], v16 offset:53248
	ds_read_b128 v[192:195], v18 offset:53248
	ds_read_b128 v[196:199], v18 offset:55296
	ds_read_b128 v[200:203], v18 offset:57344
	ds_read_b128 v[204:207], v18 offset:59392
	ds_read_b128 v[176:179], v16 offset:55296
	ds_read_b128 v[180:183], v16 offset:57344
	ds_read_b128 v[184:187], v16 offset:59392
	s_waitcnt lgkmcnt(8)
	v_mfma_f32_16x16x32_f16 v[56:59], v[136:139], v[156:159], v[56:59]
	s_add_u32 m0, s28, 0x6000
	v_mfma_f32_16x16x32_f16 v[60:63], v[136:139], v[160:163], v[60:63]
	global_load_lds_dwordx4 v13, s[4:5]
	s_add_u32 s4, s4, s20
	s_addc_u32 s5, s5, 0
	v_mfma_f32_16x16x32_f16 v[64:67], v[136:139], v[164:167], v[64:67]
	v_mfma_f32_16x16x32_f16 v[68:71], v[136:139], v[168:171], v[68:71]
	v_mfma_f32_16x16x32_f16 v[72:75], v[140:143], v[156:159], v[72:75]
	v_mfma_f32_16x16x32_f16 v[76:79], v[140:143], v[160:163], v[76:79]
	s_add_u32 m0, s28, 0x9000
	v_mfma_f32_16x16x32_f16 v[80:83], v[140:143], v[164:167], v[80:83]
	global_load_lds_dwordx4 v10, s[6:7]
	v_mfma_f32_16x16x32_f16 v[84:87], v[140:143], v[168:171], v[84:87]
	v_mfma_f32_16x16x32_f16 v[88:91], v[144:147], v[156:159], v[88:91]
	v_mfma_f32_16x16x32_f16 v[92:95], v[144:147], v[160:163], v[92:95]
	v_mfma_f32_16x16x32_f16 v[96:99], v[144:147], v[164:167], v[96:99]
	s_add_u32 m0, s28, 0xb000
	v_mfma_f32_16x16x32_f16 v[100:103], v[144:147], v[168:171], v[100:103]
	global_load_lds_dwordx4 v11, s[6:7]
	s_add_u32 s6, s6, s20
	s_addc_u32 s7, s7, 0
	v_mfma_f32_16x16x32_f16 v[104:107], v[148:151], v[156:159], v[104:107]
	v_mfma_f32_16x16x32_f16 v[108:111], v[148:151], v[160:163], v[108:111]
	v_mfma_f32_16x16x32_f16 v[112:115], v[148:151], v[164:167], v[112:115]
	v_mfma_f32_16x16x32_f16 v[116:119], v[148:151], v[168:171], v[116:119]
	s_waitcnt vmcnt(6) lgkmcnt(0)
	s_barrier
	s_waitcnt lgkmcnt(7)
	ds_read_b128 v[136:139], v19
	ds_read_b128 v[156:159], v21
	ds_read_b128 v[160:163], v21 offset:2048
	ds_read_b128 v[164:167], v21 offset:4096
	ds_read_b128 v[168:171], v21 offset:6144
	ds_read_b128 v[140:143], v19 offset:2048
	ds_read_b128 v[144:147], v19 offset:4096
	ds_read_b128 v[148:151], v19 offset:6144
	s_waitcnt lgkmcnt(8)
	v_mfma_f32_16x16x32_f16 v[56:59], v[172:175], v[192:195], v[56:59]
	s_add_u32 m0, s28, 0xd000
	v_mfma_f32_16x16x32_f16 v[60:63], v[172:175], v[196:199], v[60:63]
	global_load_lds_dwordx4 v10, s[4:5]
	v_mfma_f32_16x16x32_f16 v[64:67], v[172:175], v[200:203], v[64:67]
	v_mfma_f32_16x16x32_f16 v[68:71], v[172:175], v[204:207], v[68:71]
	v_mfma_f32_16x16x32_f16 v[72:75], v[176:179], v[192:195], v[72:75]
	v_mfma_f32_16x16x32_f16 v[76:79], v[176:179], v[196:199], v[76:79]
	s_add_u32 m0, s28, 0xf000
	v_mfma_f32_16x16x32_f16 v[80:83], v[176:179], v[200:203], v[80:83]
	global_load_lds_dwordx4 v11, s[4:5]
	v_mfma_f32_16x16x32_f16 v[84:87], v[176:179], v[204:207], v[84:87]
	v_mfma_f32_16x16x32_f16 v[88:91], v[180:183], v[192:195], v[88:91]
	v_mfma_f32_16x16x32_f16 v[92:95], v[180:183], v[196:199], v[92:95]
	v_mfma_f32_16x16x32_f16 v[96:99], v[180:183], v[200:203], v[96:99]
	s_add_u32 m0, s28, 0x11000
	v_mfma_f32_16x16x32_f16 v[100:103], v[180:183], v[204:207], v[100:103]
	global_load_lds_dwordx4 v12, s[4:5]
	v_mfma_f32_16x16x32_f16 v[104:107], v[184:187], v[192:195], v[104:107]
	v_mfma_f32_16x16x32_f16 v[108:111], v[184:187], v[196:199], v[108:111]
	v_mfma_f32_16x16x32_f16 v[112:115], v[184:187], v[200:203], v[112:115]
	v_mfma_f32_16x16x32_f16 v[116:119], v[184:187], v[204:207], v[116:119]
	s_waitcnt lgkmcnt(7)
	ds_read_b128 v[172:175], v20
	ds_read_b128 v[192:195], v22
	ds_read_b128 v[196:199], v22 offset:2048
	ds_read_b128 v[200:203], v22 offset:4096
	ds_read_b128 v[204:207], v22 offset:6144
	ds_read_b128 v[176:179], v20 offset:2048
	ds_read_b128 v[180:183], v20 offset:4096
	ds_read_b128 v[184:187], v20 offset:6144
	s_waitcnt lgkmcnt(8)
	v_mfma_f32_16x16x32_f16 v[56:59], v[136:139], v[156:159], v[56:59]
	s_add_u32 m0, s28, 0x13000
	v_mfma_f32_16x16x32_f16 v[60:63], v[136:139], v[160:163], v[60:63]
	global_load_lds_dwordx4 v13, s[4:5]
	s_add_u32 s4, s4, s20
	s_addc_u32 s5, s5, 0
	v_mfma_f32_16x16x32_f16 v[64:67], v[136:139], v[164:167], v[64:67]
	v_mfma_f32_16x16x32_f16 v[68:71], v[136:139], v[168:171], v[68:71]
	v_mfma_f32_16x16x32_f16 v[72:75], v[140:143], v[156:159], v[72:75]
	v_mfma_f32_16x16x32_f16 v[76:79], v[140:143], v[160:163], v[76:79]
	s_add_u32 m0, s28, 0x16000
	v_mfma_f32_16x16x32_f16 v[80:83], v[140:143], v[164:167], v[80:83]
	global_load_lds_dwordx4 v10, s[6:7]
	v_mfma_f32_16x16x32_f16 v[84:87], v[140:143], v[168:171], v[84:87]
	v_mfma_f32_16x16x32_f16 v[88:91], v[144:147], v[156:159], v[88:91]
	v_mfma_f32_16x16x32_f16 v[92:95], v[144:147], v[160:163], v[92:95]
	v_mfma_f32_16x16x32_f16 v[96:99], v[144:147], v[164:167], v[96:99]
	s_add_u32 m0, s28, 0x18000
	v_mfma_f32_16x16x32_f16 v[100:103], v[144:147], v[168:171], v[100:103]
	global_load_lds_dwordx4 v11, s[6:7]
	s_add_u32 s6, s6, s20
	s_addc_u32 s7, s7, 0
	v_mfma_f32_16x16x32_f16 v[104:107], v[148:151], v[156:159], v[104:107]
	v_mfma_f32_16x16x32_f16 v[108:111], v[148:151], v[160:163], v[108:111]
	v_mfma_f32_16x16x32_f16 v[112:115], v[148:151], v[164:167], v[112:115]
	v_mfma_f32_16x16x32_f16 v[116:119], v[148:151], v[168:171], v[116:119]
	s_waitcnt vmcnt(6) lgkmcnt(0)
	s_barrier
	s_waitcnt lgkmcnt(7)
	ds_read_b128 v[136:139], v15
	ds_read_b128 v[156:159], v17
	ds_read_b128 v[160:163], v17 offset:2048
	ds_read_b128 v[164:167], v17 offset:4096
	ds_read_b128 v[168:171], v17 offset:6144
	ds_read_b128 v[140:143], v15 offset:2048
	ds_read_b128 v[144:147], v15 offset:4096
	ds_read_b128 v[148:151], v15 offset:6144
	s_waitcnt lgkmcnt(8)
	v_mfma_f32_16x16x32_f16 v[56:59], v[172:175], v[192:195], v[56:59]
	s_add_u32 m0, s28, 0x1a000
	v_mfma_f32_16x16x32_f16 v[60:63], v[172:175], v[196:199], v[60:63]
	global_load_lds_dwordx4 v10, s[4:5]
	v_mfma_f32_16x16x32_f16 v[64:67], v[172:175], v[200:203], v[64:67]
	v_mfma_f32_16x16x32_f16 v[68:71], v[172:175], v[204:207], v[68:71]
	v_mfma_f32_16x16x32_f16 v[72:75], v[176:179], v[192:195], v[72:75]
	v_mfma_f32_16x16x32_f16 v[76:79], v[176:179], v[196:199], v[76:79]
	s_add_u32 m0, s28, 0x1c000
	v_mfma_f32_16x16x32_f16 v[80:83], v[176:179], v[200:203], v[80:83]
	global_load_lds_dwordx4 v11, s[4:5]
	v_mfma_f32_16x16x32_f16 v[84:87], v[176:179], v[204:207], v[84:87]
	v_mfma_f32_16x16x32_f16 v[88:91], v[180:183], v[192:195], v[88:91]
	v_mfma_f32_16x16x32_f16 v[92:95], v[180:183], v[196:199], v[92:95]
	v_mfma_f32_16x16x32_f16 v[96:99], v[180:183], v[200:203], v[96:99]
	s_add_u32 m0, s28, 0x1e000
	v_mfma_f32_16x16x32_f16 v[100:103], v[180:183], v[204:207], v[100:103]
	global_load_lds_dwordx4 v12, s[4:5]
	v_mfma_f32_16x16x32_f16 v[104:107], v[184:187], v[192:195], v[104:107]
	v_mfma_f32_16x16x32_f16 v[108:111], v[184:187], v[196:199], v[108:111]
	v_mfma_f32_16x16x32_f16 v[112:115], v[184:187], v[200:203], v[112:115]
	v_mfma_f32_16x16x32_f16 v[116:119], v[184:187], v[204:207], v[116:119]
	s_waitcnt lgkmcnt(7)
	ds_read_b128 v[172:175], v16
	ds_read_b128 v[192:195], v18
	ds_read_b128 v[196:199], v18 offset:2048
	ds_read_b128 v[200:203], v18 offset:4096
	ds_read_b128 v[204:207], v18 offset:6144
	ds_read_b128 v[176:179], v16 offset:2048
	ds_read_b128 v[180:183], v16 offset:4096
	ds_read_b128 v[184:187], v16 offset:6144
	s_waitcnt lgkmcnt(8)
	v_mfma_f32_16x16x32_f16 v[56:59], v[136:139], v[156:159], v[56:59]
	s_add_u32 m0, s28, 0x20000
	v_mfma_f32_16x16x32_f16 v[60:63], v[136:139], v[160:163], v[60:63]
	global_load_lds_dwordx4 v13, s[4:5]
	s_add_u32 s4, s4, s20
	s_addc_u32 s5, s5, 0
	v_mfma_f32_16x16x32_f16 v[64:67], v[136:139], v[164:167], v[64:67]
	v_mfma_f32_16x16x32_f16 v[68:71], v[136:139], v[168:171], v[68:71]
	v_mfma_f32_16x16x32_f16 v[72:75], v[140:143], v[156:159], v[72:75]
	v_mfma_f32_16x16x32_f16 v[76:79], v[140:143], v[160:163], v[76:79]
	s_add_u32 m0, s28, 0x23000
	v_mfma_f32_16x16x32_f16 v[80:83], v[140:143], v[164:167], v[80:83]
	global_load_lds_dwordx4 v10, s[6:7]
	v_mfma_f32_16x16x32_f16 v[84:87], v[140:143], v[168:171], v[84:87]
	v_mfma_f32_16x16x32_f16 v[88:91], v[144:147], v[156:159], v[88:91]
	v_mfma_f32_16x16x32_f16 v[92:95], v[144:147], v[160:163], v[92:95]
	v_mfma_f32_16x16x32_f16 v[96:99], v[144:147], v[164:167], v[96:99]
	s_add_u32 m0, s28, 0x25000
	v_mfma_f32_16x16x32_f16 v[100:103], v[144:147], v[168:171], v[100:103]
	global_load_lds_dwordx4 v11, s[6:7]
	s_add_u32 s6, s6, s20
	s_addc_u32 s7, s7, 0
	v_mfma_f32_16x16x32_f16 v[104:107], v[148:151], v[156:159], v[104:107]
	v_mfma_f32_16x16x32_f16 v[108:111], v[148:151], v[160:163], v[108:111]
	v_mfma_f32_16x16x32_f16 v[112:115], v[148:151], v[164:167], v[112:115]
	v_mfma_f32_16x16x32_f16 v[116:119], v[148:151], v[168:171], v[116:119]
	s_waitcnt vmcnt(6) lgkmcnt(0)
	s_barrier
	s_waitcnt lgkmcnt(7)
	ds_read_b128 v[136:139], v15 offset:53248
	ds_read_b128 v[156:159], v17 offset:53248
	ds_read_b128 v[160:163], v17 offset:55296
	ds_read_b128 v[164:167], v17 offset:57344
	ds_read_b128 v[168:171], v17 offset:59392
	ds_read_b128 v[140:143], v15 offset:55296
	ds_read_b128 v[144:147], v15 offset:57344
	ds_read_b128 v[148:151], v15 offset:59392
	s_waitcnt lgkmcnt(8)
	v_mfma_f32_16x16x32_f16 v[56:59], v[172:175], v[192:195], v[56:59]
	s_add_u32 m0, s28, 0x0
	v_mfma_f32_16x16x32_f16 v[60:63], v[172:175], v[196:199], v[60:63]
	global_load_lds_dwordx4 v10, s[4:5]
	v_mfma_f32_16x16x32_f16 v[64:67], v[172:175], v[200:203], v[64:67]
	v_mfma_f32_16x16x32_f16 v[68:71], v[172:175], v[204:207], v[68:71]
	v_mfma_f32_16x16x32_f16 v[72:75], v[176:179], v[192:195], v[72:75]
	v_mfma_f32_16x16x32_f16 v[76:79], v[176:179], v[196:199], v[76:79]
	s_add_u32 m0, s28, 0x2000
	v_mfma_f32_16x16x32_f16 v[80:83], v[176:179], v[200:203], v[80:83]
	global_load_lds_dwordx4 v11, s[4:5]
	v_mfma_f32_16x16x32_f16 v[84:87], v[176:179], v[204:207], v[84:87]
	v_mfma_f32_16x16x32_f16 v[88:91], v[180:183], v[192:195], v[88:91]
	v_mfma_f32_16x16x32_f16 v[92:95], v[180:183], v[196:199], v[92:95]
	v_mfma_f32_16x16x32_f16 v[96:99], v[180:183], v[200:203], v[96:99]
	s_add_u32 m0, s28, 0x4000
	v_mfma_f32_16x16x32_f16 v[100:103], v[180:183], v[204:207], v[100:103]
	global_load_lds_dwordx4 v12, s[4:5]
	v_mfma_f32_16x16x32_f16 v[104:107], v[184:187], v[192:195], v[104:107]
	v_mfma_f32_16x16x32_f16 v[108:111], v[184:187], v[196:199], v[108:111]
	v_mfma_f32_16x16x32_f16 v[112:115], v[184:187], v[200:203], v[112:115]
	v_mfma_f32_16x16x32_f16 v[116:119], v[184:187], v[204:207], v[116:119]
	s_waitcnt lgkmcnt(7)
	ds_read_b128 v[172:175], v16 offset:53248
	ds_read_b128 v[192:195], v18 offset:53248
	ds_read_b128 v[196:199], v18 offset:55296
	ds_read_b128 v[200:203], v18 offset:57344
	ds_read_b128 v[204:207], v18 offset:59392
	ds_read_b128 v[176:179], v16 offset:55296
	ds_read_b128 v[180:183], v16 offset:57344
	ds_read_b128 v[184:187], v16 offset:59392
	s_waitcnt lgkmcnt(8)
	v_mfma_f32_16x16x32_f16 v[56:59], v[136:139], v[156:159], v[56:59]
	s_add_u32 m0, s28, 0x6000
	v_mfma_f32_16x16x32_f16 v[60:63], v[136:139], v[160:163], v[60:63]
	global_load_lds_dwordx4 v13, s[4:5]
	s_add_u32 s4, s4, s20
	s_addc_u32 s5, s5, 0
	v_mfma_f32_16x16x32_f16 v[64:67], v[136:139], v[164:167], v[64:67]
	v_mfma_f32_16x16x32_f16 v[68:71], v[136:139], v[168:171], v[68:71]
	v_mfma_f32_16x16x32_f16 v[72:75], v[140:143], v[156:159], v[72:75]
	v_mfma_f32_16x16x32_f16 v[76:79], v[140:143], v[160:163], v[76:79]
	s_add_u32 m0, s28, 0x9000
	v_mfma_f32_16x16x32_f16 v[80:83], v[140:143], v[164:167], v[80:83]
	global_load_lds_dwordx4 v10, s[6:7]
	v_mfma_f32_16x16x32_f16 v[84:87], v[140:143], v[168:171], v[84:87]
	v_mfma_f32_16x16x32_f16 v[88:91], v[144:147], v[156:159], v[88:91]
	v_mfma_f32_16x16x32_f16 v[92:95], v[144:147], v[160:163], v[92:95]
	v_mfma_f32_16x16x32_f16 v[96:99], v[144:147], v[164:167], v[96:99]
	s_add_u32 m0, s28, 0xb000
	v_mfma_f32_16x16x32_f16 v[100:103], v[144:147], v[168:171], v[100:103]
	global_load_lds_dwordx4 v11, s[6:7]
	s_add_u32 s6, s6, s20
	s_addc_u32 s7, s7, 0
	v_mfma_f32_16x16x32_f16 v[104:107], v[148:151], v[156:159], v[104:107]
	v_mfma_f32_16x16x32_f16 v[108:111], v[148:151], v[160:163], v[108:111]
	v_mfma_f32_16x16x32_f16 v[112:115], v[148:151], v[164:167], v[112:115]
	v_mfma_f32_16x16x32_f16 v[116:119], v[148:151], v[168:171], v[116:119]
	s_waitcnt vmcnt(6) lgkmcnt(0)
	s_barrier
	s_waitcnt lgkmcnt(7)
	ds_read_b128 v[136:139], v19
	ds_read_b128 v[156:159], v21
	ds_read_b128 v[160:163], v21 offset:2048
	ds_read_b128 v[164:167], v21 offset:4096
	ds_read_b128 v[168:171], v21 offset:6144
	ds_read_b128 v[140:143], v19 offset:2048
	ds_read_b128 v[144:147], v19 offset:4096
	ds_read_b128 v[148:151], v19 offset:6144
	s_waitcnt lgkmcnt(8)
	v_mfma_f32_16x16x32_f16 v[56:59], v[172:175], v[192:195], v[56:59]
	s_add_u32 m0, s28, 0xd000
	v_mfma_f32_16x16x32_f16 v[60:63], v[172:175], v[196:199], v[60:63]
	global_load_lds_dwordx4 v10, s[4:5]
	v_mfma_f32_16x16x32_f16 v[64:67], v[172:175], v[200:203], v[64:67]
	v_mfma_f32_16x16x32_f16 v[68:71], v[172:175], v[204:207], v[68:71]
	v_mfma_f32_16x16x32_f16 v[72:75], v[176:179], v[192:195], v[72:75]
	v_mfma_f32_16x16x32_f16 v[76:79], v[176:179], v[196:199], v[76:79]
	s_add_u32 m0, s28, 0xf000
	v_mfma_f32_16x16x32_f16 v[80:83], v[176:179], v[200:203], v[80:83]
	global_load_lds_dwordx4 v11, s[4:5]
	v_mfma_f32_16x16x32_f16 v[84:87], v[176:179], v[204:207], v[84:87]
	v_mfma_f32_16x16x32_f16 v[88:91], v[180:183], v[192:195], v[88:91]
	v_mfma_f32_16x16x32_f16 v[92:95], v[180:183], v[196:199], v[92:95]
	v_mfma_f32_16x16x32_f16 v[96:99], v[180:183], v[200:203], v[96:99]
	s_add_u32 m0, s28, 0x11000
	v_mfma_f32_16x16x32_f16 v[100:103], v[180:183], v[204:207], v[100:103]
	global_load_lds_dwordx4 v12, s[4:5]
	v_mfma_f32_16x16x32_f16 v[104:107], v[184:187], v[192:195], v[104:107]
	v_mfma_f32_16x16x32_f16 v[108:111], v[184:187], v[196:199], v[108:111]
	v_mfma_f32_16x16x32_f16 v[112:115], v[184:187], v[200:203], v[112:115]
	v_mfma_f32_16x16x32_f16 v[116:119], v[184:187], v[204:207], v[116:119]
	s_waitcnt lgkmcnt(7)
	ds_read_b128 v[172:175], v20
	ds_read_b128 v[192:195], v22
	ds_read_b128 v[196:199], v22 offset:2048
	ds_read_b128 v[200:203], v22 offset:4096
	ds_read_b128 v[204:207], v22 offset:6144
	ds_read_b128 v[176:179], v20 offset:2048
	ds_read_b128 v[180:183], v20 offset:4096
	ds_read_b128 v[184:187], v20 offset:6144
	s_waitcnt lgkmcnt(8)
	v_mfma_f32_16x16x32_f16 v[56:59], v[136:139], v[156:159], v[56:59]
	s_add_u32 m0, s28, 0x13000
	v_mfma_f32_16x16x32_f16 v[60:63], v[136:139], v[160:163], v[60:63]
	global_load_lds_dwordx4 v13, s[4:5]
	s_add_u32 s4, s4, s20
	s_addc_u32 s5, s5, 0
	v_mfma_f32_16x16x32_f16 v[64:67], v[136:139], v[164:167], v[64:67]
	v_mfma_f32_16x16x32_f16 v[68:71], v[136:139], v[168:171], v[68:71]
	v_mfma_f32_16x16x32_f16 v[72:75], v[140:143], v[156:159], v[72:75]
	v_mfma_f32_16x16x32_f16 v[76:79], v[140:143], v[160:163], v[76:79]
	s_add_u32 m0, s28, 0x16000
	v_mfma_f32_16x16x32_f16 v[80:83], v[140:143], v[164:167], v[80:83]
	global_load_lds_dwordx4 v10, s[6:7]
	v_mfma_f32_16x16x32_f16 v[84:87], v[140:143], v[168:171], v[84:87]
	v_mfma_f32_16x16x32_f16 v[88:91], v[144:147], v[156:159], v[88:91]
	v_mfma_f32_16x16x32_f16 v[92:95], v[144:147], v[160:163], v[92:95]
	v_mfma_f32_16x16x32_f16 v[96:99], v[144:147], v[164:167], v[96:99]
	s_add_u32 m0, s28, 0x18000
	v_mfma_f32_16x16x32_f16 v[100:103], v[144:147], v[168:171], v[100:103]
	global_load_lds_dwordx4 v11, s[6:7]
	s_add_u32 s6, s6, s20
	s_addc_u32 s7, s7, 0
	v_mfma_f32_16x16x32_f16 v[104:107], v[148:151], v[156:159], v[104:107]
	v_mfma_f32_16x16x32_f16 v[108:111], v[148:151], v[160:163], v[108:111]
	v_mfma_f32_16x16x32_f16 v[112:115], v[148:151], v[164:167], v[112:115]
	v_mfma_f32_16x16x32_f16 v[116:119], v[148:151], v[168:171], v[116:119]
	s_waitcnt vmcnt(6) lgkmcnt(0)
	s_barrier
	s_waitcnt lgkmcnt(7)
	ds_read_b128 v[136:139], v15
	ds_read_b128 v[156:159], v17
	ds_read_b128 v[160:163], v17 offset:2048
	ds_read_b128 v[164:167], v17 offset:4096
	ds_read_b128 v[168:171], v17 offset:6144
	ds_read_b128 v[140:143], v15 offset:2048
	ds_read_b128 v[144:147], v15 offset:4096
	ds_read_b128 v[148:151], v15 offset:6144
	s_waitcnt lgkmcnt(8)
	v_mfma_f32_16x16x32_f16 v[56:59], v[172:175], v[192:195], v[56:59]
	s_add_u32 m0, s28, 0x1a000
	v_mfma_f32_16x16x32_f16 v[60:63], v[172:175], v[196:199], v[60:63]
	global_load_lds_dwordx4 v10, s[4:5]
	v_mfma_f32_16x16x32_f16 v[64:67], v[172:175], v[200:203], v[64:67]
	v_mfma_f32_16x16x32_f16 v[68:71], v[172:175], v[204:207], v[68:71]
	v_mfma_f32_16x16x32_f16 v[72:75], v[176:179], v[192:195], v[72:75]
	v_mfma_f32_16x16x32_f16 v[76:79], v[176:179], v[196:199], v[76:79]
	s_add_u32 m0, s28, 0x1c000
	v_mfma_f32_16x16x32_f16 v[80:83], v[176:179], v[200:203], v[80:83]
	global_load_lds_dwordx4 v11, s[4:5]
	v_mfma_f32_16x16x32_f16 v[84:87], v[176:179], v[204:207], v[84:87]
	v_mfma_f32_16x16x32_f16 v[88:91], v[180:183], v[192:195], v[88:91]
	v_mfma_f32_16x16x32_f16 v[92:95], v[180:183], v[196:199], v[92:95]
	v_mfma_f32_16x16x32_f16 v[96:99], v[180:183], v[200:203], v[96:99]
	s_add_u32 m0, s28, 0x1e000
	v_mfma_f32_16x16x32_f16 v[100:103], v[180:183], v[204:207], v[100:103]
	global_load_lds_dwordx4 v12, s[4:5]
	v_mfma_f32_16x16x32_f16 v[104:107], v[184:187], v[192:195], v[104:107]
	v_mfma_f32_16x16x32_f16 v[108:111], v[184:187], v[196:199], v[108:111]
	v_mfma_f32_16x16x32_f16 v[112:115], v[184:187], v[200:203], v[112:115]
	v_mfma_f32_16x16x32_f16 v[116:119], v[184:187], v[204:207], v[116:119]
	s_waitcnt lgkmcnt(7)
	ds_read_b128 v[172:175], v16
	ds_read_b128 v[192:195], v18
	ds_read_b128 v[196:199], v18 offset:2048
	ds_read_b128 v[200:203], v18 offset:4096
	ds_read_b128 v[204:207], v18 offset:6144
	ds_read_b128 v[176:179], v16 offset:2048
	ds_read_b128 v[180:183], v16 offset:4096
	ds_read_b128 v[184:187], v16 offset:6144
	s_waitcnt lgkmcnt(8)
	v_mfma_f32_16x16x32_f16 v[56:59], v[136:139], v[156:159], v[56:59]
	s_add_u32 m0, s28, 0x20000
	v_mfma_f32_16x16x32_f16 v[60:63], v[136:139], v[160:163], v[60:63]
	global_load_lds_dwordx4 v13, s[4:5]
	s_add_u32 s4, s4, s20
	s_addc_u32 s5, s5, 0
	v_mfma_f32_16x16x32_f16 v[64:67], v[136:139], v[164:167], v[64:67]
	v_mfma_f32_16x16x32_f16 v[68:71], v[136:139], v[168:171], v[68:71]
	v_mfma_f32_16x16x32_f16 v[72:75], v[140:143], v[156:159], v[72:75]
	v_mfma_f32_16x16x32_f16 v[76:79], v[140:143], v[160:163], v[76:79]
	s_add_u32 m0, s28, 0x23000
	v_mfma_f32_16x16x32_f16 v[80:83], v[140:143], v[164:167], v[80:83]
	global_load_lds_dwordx4 v10, s[6:7]
	v_mfma_f32_16x16x32_f16 v[84:87], v[140:143], v[168:171], v[84:87]
	v_mfma_f32_16x16x32_f16 v[88:91], v[144:147], v[156:159], v[88:91]
	v_mfma_f32_16x16x32_f16 v[92:95], v[144:147], v[160:163], v[92:95]
	v_mfma_f32_16x16x32_f16 v[96:99], v[144:147], v[164:167], v[96:99]
	s_add_u32 m0, s28, 0x25000
	v_mfma_f32_16x16x32_f16 v[100:103], v[144:147], v[168:171], v[100:103]
	global_load_lds_dwordx4 v11, s[6:7]
	s_add_u32 s6, s6, s20
	s_addc_u32 s7, s7, 0
	v_mfma_f32_16x16x32_f16 v[104:107], v[148:151], v[156:159], v[104:107]
	v_mfma_f32_16x16x32_f16 v[108:111], v[148:151], v[160:163], v[108:111]
	v_mfma_f32_16x16x32_f16 v[112:115], v[148:151], v[164:167], v[112:115]
	v_mfma_f32_16x16x32_f16 v[116:119], v[148:151], v[168:171], v[116:119]
	s_waitcnt vmcnt(6) lgkmcnt(0)
	s_barrier
	s_waitcnt lgkmcnt(7)
	ds_read_b128 v[136:139], v15 offset:53248
	ds_read_b128 v[156:159], v17 offset:53248
	ds_read_b128 v[160:163], v17 offset:55296
	ds_read_b128 v[164:167], v17 offset:57344
	ds_read_b128 v[168:171], v17 offset:59392
	ds_read_b128 v[140:143], v15 offset:55296
	ds_read_b128 v[144:147], v15 offset:57344
	ds_read_b128 v[148:151], v15 offset:59392
	s_waitcnt lgkmcnt(8)
	v_mfma_f32_16x16x32_f16 v[56:59], v[172:175], v[192:195], v[56:59]
	s_add_u32 m0, s28, 0x0
	v_mfma_f32_16x16x32_f16 v[60:63], v[172:175], v[196:199], v[60:63]
	global_load_lds_dwordx4 v10, s[4:5]
	v_mfma_f32_16x16x32_f16 v[64:67], v[172:175], v[200:203], v[64:67]
	v_mfma_f32_16x16x32_f16 v[68:71], v[172:175], v[204:207], v[68:71]
	v_mfma_f32_16x16x32_f16 v[72:75], v[176:179], v[192:195], v[72:75]
	v_mfma_f32_16x16x32_f16 v[76:79], v[176:179], v[196:199], v[76:79]
	s_add_u32 m0, s28, 0x2000
	v_mfma_f32_16x16x32_f16 v[80:83], v[176:179], v[200:203], v[80:83]
	global_load_lds_dwordx4 v11, s[4:5]
	v_mfma_f32_16x16x32_f16 v[84:87], v[176:179], v[204:207], v[84:87]
	v_mfma_f32_16x16x32_f16 v[88:91], v[180:183], v[192:195], v[88:91]
	v_mfma_f32_16x16x32_f16 v[92:95], v[180:183], v[196:199], v[92:95]
	v_mfma_f32_16x16x32_f16 v[96:99], v[180:183], v[200:203], v[96:99]
	s_add_u32 m0, s28, 0x4000
	v_mfma_f32_16x16x32_f16 v[100:103], v[180:183], v[204:207], v[100:103]
	global_load_lds_dwordx4 v12, s[4:5]
	v_mfma_f32_16x16x32_f16 v[104:107], v[184:187], v[192:195], v[104:107]
	v_mfma_f32_16x16x32_f16 v[108:111], v[184:187], v[196:199], v[108:111]
	v_mfma_f32_16x16x32_f16 v[112:115], v[184:187], v[200:203], v[112:115]
	v_mfma_f32_16x16x32_f16 v[116:119], v[184:187], v[204:207], v[116:119]
	s_waitcnt lgkmcnt(7)
	ds_read_b128 v[172:175], v16 offset:53248
	ds_read_b128 v[192:195], v18 offset:53248
	ds_read_b128 v[196:199], v18 offset:55296
	ds_read_b128 v[200:203], v18 offset:57344
	ds_read_b128 v[204:207], v18 offset:59392
	ds_read_b128 v[176:179], v16 offset:55296
	ds_read_b128 v[180:183], v16 offset:57344
	ds_read_b128 v[184:187], v16 offset:59392
	s_waitcnt lgkmcnt(8)
	v_mfma_f32_16x16x32_f16 v[56:59], v[136:139], v[156:159], v[56:59]
	s_add_u32 m0, s28, 0x6000
	v_mfma_f32_16x16x32_f16 v[60:63], v[136:139], v[160:163], v[60:63]
	global_load_lds_dwordx4 v13, s[4:5]
	s_add_u32 s4, s4, s20
	s_addc_u32 s5, s5, 0
	v_mfma_f32_16x16x32_f16 v[64:67], v[136:139], v[164:167], v[64:67]
	v_mfma_f32_16x16x32_f16 v[68:71], v[136:139], v[168:171], v[68:71]
	v_mfma_f32_16x16x32_f16 v[72:75], v[140:143], v[156:159], v[72:75]
	v_mfma_f32_16x16x32_f16 v[76:79], v[140:143], v[160:163], v[76:79]
	s_add_u32 m0, s28, 0x9000
	v_mfma_f32_16x16x32_f16 v[80:83], v[140:143], v[164:167], v[80:83]
	global_load_lds_dwordx4 v10, s[6:7]
	v_mfma_f32_16x16x32_f16 v[84:87], v[140:143], v[168:171], v[84:87]
	v_mfma_f32_16x16x32_f16 v[88:91], v[144:147], v[156:159], v[88:91]
	v_mfma_f32_16x16x32_f16 v[92:95], v[144:147], v[160:163], v[92:95]
	v_mfma_f32_16x16x32_f16 v[96:99], v[144:147], v[164:167], v[96:99]
	s_add_u32 m0, s28, 0xb000
	v_mfma_f32_16x16x32_f16 v[100:103], v[144:147], v[168:171], v[100:103]
	global_load_lds_dwordx4 v11, s[6:7]
	s_add_u32 s6, s6, s20
	s_addc_u32 s7, s7, 0
	v_mfma_f32_16x16x32_f16 v[104:107], v[148:151], v[156:159], v[104:107]
	v_mfma_f32_16x16x32_f16 v[108:111], v[148:151], v[160:163], v[108:111]
	v_mfma_f32_16x16x32_f16 v[112:115], v[148:151], v[164:167], v[112:115]
	v_mfma_f32_16x16x32_f16 v[116:119], v[148:151], v[168:171], v[116:119]
	s_waitcnt vmcnt(6) lgkmcnt(0)
	s_barrier
	s_waitcnt lgkmcnt(7)
	ds_read_b128 v[136:139], v19
	ds_read_b128 v[156:159], v21
	ds_read_b128 v[160:163], v21 offset:2048
	ds_read_b128 v[164:167], v21 offset:4096
	ds_read_b128 v[168:171], v21 offset:6144
	ds_read_b128 v[140:143], v19 offset:2048
	ds_read_b128 v[144:147], v19 offset:4096
	ds_read_b128 v[148:151], v19 offset:6144
	s_waitcnt lgkmcnt(8)
	v_mfma_f32_16x16x32_f16 v[56:59], v[172:175], v[192:195], v[56:59]
	v_mfma_f32_16x16x32_f16 v[60:63], v[172:175], v[196:199], v[60:63]
	v_mfma_f32_16x16x32_f16 v[64:67], v[172:175], v[200:203], v[64:67]
	v_mfma_f32_16x16x32_f16 v[68:71], v[172:175], v[204:207], v[68:71]
	v_mfma_f32_16x16x32_f16 v[72:75], v[176:179], v[192:195], v[72:75]
	v_mfma_f32_16x16x32_f16 v[76:79], v[176:179], v[196:199], v[76:79]
	v_mfma_f32_16x16x32_f16 v[80:83], v[176:179], v[200:203], v[80:83]
	v_mfma_f32_16x16x32_f16 v[84:87], v[176:179], v[204:207], v[84:87]
	v_mfma_f32_16x16x32_f16 v[88:91], v[180:183], v[192:195], v[88:91]
	v_mfma_f32_16x16x32_f16 v[92:95], v[180:183], v[196:199], v[92:95]
	v_mfma_f32_16x16x32_f16 v[96:99], v[180:183], v[200:203], v[96:99]
	v_mfma_f32_16x16x32_f16 v[100:103], v[180:183], v[204:207], v[100:103]
	v_mfma_f32_16x16x32_f16 v[104:107], v[184:187], v[192:195], v[104:107]
	v_mfma_f32_16x16x32_f16 v[108:111], v[184:187], v[196:199], v[108:111]
	v_mfma_f32_16x16x32_f16 v[112:115], v[184:187], v[200:203], v[112:115]
	v_mfma_f32_16x16x32_f16 v[116:119], v[184:187], v[204:207], v[116:119]
	s_waitcnt lgkmcnt(7)
	ds_read_b128 v[172:175], v20
	ds_read_b128 v[192:195], v22
	ds_read_b128 v[196:199], v22 offset:2048
	ds_read_b128 v[200:203], v22 offset:4096
	ds_read_b128 v[204:207], v22 offset:6144
	ds_read_b128 v[176:179], v20 offset:2048
	ds_read_b128 v[180:183], v20 offset:4096
	ds_read_b128 v[184:187], v20 offset:6144
	s_waitcnt lgkmcnt(8)
	v_mfma_f32_16x16x32_f16 v[56:59], v[136:139], v[156:159], v[56:59]
	v_mfma_f32_16x16x32_f16 v[60:63], v[136:139], v[160:163], v[60:63]
	v_mfma_f32_16x16x32_f16 v[64:67], v[136:139], v[164:167], v[64:67]
	v_mfma_f32_16x16x32_f16 v[68:71], v[136:139], v[168:171], v[68:71]
	v_mfma_f32_16x16x32_f16 v[72:75], v[140:143], v[156:159], v[72:75]
	v_mfma_f32_16x16x32_f16 v[76:79], v[140:143], v[160:163], v[76:79]
	v_mfma_f32_16x16x32_f16 v[80:83], v[140:143], v[164:167], v[80:83]
	v_mfma_f32_16x16x32_f16 v[84:87], v[140:143], v[168:171], v[84:87]
	v_mfma_f32_16x16x32_f16 v[88:91], v[144:147], v[156:159], v[88:91]
	v_mfma_f32_16x16x32_f16 v[92:95], v[144:147], v[160:163], v[92:95]
	v_mfma_f32_16x16x32_f16 v[96:99], v[144:147], v[164:167], v[96:99]
	v_mfma_f32_16x16x32_f16 v[100:103], v[144:147], v[168:171], v[100:103]
	v_mfma_f32_16x16x32_f16 v[104:107], v[148:151], v[156:159], v[104:107]
	v_mfma_f32_16x16x32_f16 v[108:111], v[148:151], v[160:163], v[108:111]
	v_mfma_f32_16x16x32_f16 v[112:115], v[148:151], v[164:167], v[112:115]
	v_mfma_f32_16x16x32_f16 v[116:119], v[148:151], v[168:171], v[116:119]
	s_waitcnt vmcnt(0) lgkmcnt(0)
	s_barrier
	s_waitcnt lgkmcnt(7)
	ds_read_b128 v[136:139], v15
	ds_read_b128 v[156:159], v17
	ds_read_b128 v[160:163], v17 offset:2048
	ds_read_b128 v[164:167], v17 offset:4096
	ds_read_b128 v[168:171], v17 offset:6144
	ds_read_b128 v[140:143], v15 offset:2048
	ds_read_b128 v[144:147], v15 offset:4096
	ds_read_b128 v[148:151], v15 offset:6144
	s_waitcnt lgkmcnt(8)
	v_mfma_f32_16x16x32_f16 v[56:59], v[172:175], v[192:195], v[56:59]
	v_mfma_f32_16x16x32_f16 v[60:63], v[172:175], v[196:199], v[60:63]
	v_mfma_f32_16x16x32_f16 v[64:67], v[172:175], v[200:203], v[64:67]
	v_mfma_f32_16x16x32_f16 v[68:71], v[172:175], v[204:207], v[68:71]
	v_mfma_f32_16x16x32_f16 v[72:75], v[176:179], v[192:195], v[72:75]
	v_mfma_f32_16x16x32_f16 v[76:79], v[176:179], v[196:199], v[76:79]
	v_mfma_f32_16x16x32_f16 v[80:83], v[176:179], v[200:203], v[80:83]
	v_mfma_f32_16x16x32_f16 v[84:87], v[176:179], v[204:207], v[84:87]
	v_mfma_f32_16x16x32_f16 v[88:91], v[180:183], v[192:195], v[88:91]
	v_mfma_f32_16x16x32_f16 v[92:95], v[180:183], v[196:199], v[92:95]
	v_mfma_f32_16x16x32_f16 v[96:99], v[180:183], v[200:203], v[96:99]
	v_mfma_f32_16x16x32_f16 v[100:103], v[180:183], v[204:207], v[100:103]
	v_mfma_f32_16x16x32_f16 v[104:107], v[184:187], v[192:195], v[104:107]
	v_mfma_f32_16x16x32_f16 v[108:111], v[184:187], v[196:199], v[108:111]
	v_mfma_f32_16x16x32_f16 v[112:115], v[184:187], v[200:203], v[112:115]
	v_mfma_f32_16x16x32_f16 v[116:119], v[184:187], v[204:207], v[116:119]
	s_waitcnt lgkmcnt(7)
	ds_read_b128 v[172:175], v16
	ds_read_b128 v[192:195], v18
	ds_read_b128 v[196:199], v18 offset:2048
	ds_read_b128 v[200:203], v18 offset:4096
	ds_read_b128 v[204:207], v18 offset:6144
	ds_read_b128 v[176:179], v16 offset:2048
	ds_read_b128 v[180:183], v16 offset:4096
	ds_read_b128 v[184:187], v16 offset:6144
	s_waitcnt lgkmcnt(8)
	v_mfma_f32_16x16x32_f16 v[56:59], v[136:139], v[156:159], v[56:59]
	v_mfma_f32_16x16x32_f16 v[60:63], v[136:139], v[160:163], v[60:63]
	v_mfma_f32_16x16x32_f16 v[64:67], v[136:139], v[164:167], v[64:67]
	v_mfma_f32_16x16x32_f16 v[68:71], v[136:139], v[168:171], v[68:71]
	v_mfma_f32_16x16x32_f16 v[72:75], v[140:143], v[156:159], v[72:75]
	v_mfma_f32_16x16x32_f16 v[76:79], v[140:143], v[160:163], v[76:79]
	v_mfma_f32_16x16x32_f16 v[80:83], v[140:143], v[164:167], v[80:83]
	v_mfma_f32_16x16x32_f16 v[84:87], v[140:143], v[168:171], v[84:87]
	v_mfma_f32_16x16x32_f16 v[88:91], v[144:147], v[156:159], v[88:91]
	v_mfma_f32_16x16x32_f16 v[92:95], v[144:147], v[160:163], v[92:95]
	v_mfma_f32_16x16x32_f16 v[96:99], v[144:147], v[164:167], v[96:99]
	v_mfma_f32_16x16x32_f16 v[100:103], v[144:147], v[168:171], v[100:103]
	v_mfma_f32_16x16x32_f16 v[104:107], v[148:151], v[156:159], v[104:107]
	v_mfma_f32_16x16x32_f16 v[108:111], v[148:151], v[160:163], v[108:111]
	v_mfma_f32_16x16x32_f16 v[112:115], v[148:151], v[164:167], v[112:115]
	v_mfma_f32_16x16x32_f16 v[116:119], v[148:151], v[168:171], v[116:119]
	s_waitcnt lgkmcnt(0)
	v_mfma_f32_16x16x32_f16 v[56:59], v[172:175], v[192:195], v[56:59]
	v_mfma_f32_16x16x32_f16 v[60:63], v[172:175], v[196:199], v[60:63]
	v_mfma_f32_16x16x32_f16 v[64:67], v[172:175], v[200:203], v[64:67]
	v_mfma_f32_16x16x32_f16 v[68:71], v[172:175], v[204:207], v[68:71]
	v_mfma_f32_16x16x32_f16 v[72:75], v[176:179], v[192:195], v[72:75]
	v_mfma_f32_16x16x32_f16 v[76:79], v[176:179], v[196:199], v[76:79]
	v_mfma_f32_16x16x32_f16 v[80:83], v[176:179], v[200:203], v[80:83]
	v_mfma_f32_16x16x32_f16 v[84:87], v[176:179], v[204:207], v[84:87]
	v_mfma_f32_16x16x32_f16 v[88:91], v[180:183], v[192:195], v[88:91]
	v_mfma_f32_16x16x32_f16 v[92:95], v[180:183], v[196:199], v[92:95]
	v_mfma_f32_16x16x32_f16 v[96:99], v[180:183], v[200:203], v[96:99]
	v_mfma_f32_16x16x32_f16 v[100:103], v[180:183], v[204:207], v[100:103]
	v_mfma_f32_16x16x32_f16 v[104:107], v[184:187], v[192:195], v[104:107]
	v_mfma_f32_16x16x32_f16 v[108:111], v[184:187], v[196:199], v[108:111]
	v_mfma_f32_16x16x32_f16 v[112:115], v[184:187], v[200:203], v[112:115]
	v_mfma_f32_16x16x32_f16 v[116:119], v[184:187], v[204:207], v[116:119]
	s_nop 7
	s_nop 1
	s_add_u32 s24, s29, 0
	s_lshl_b32 s8, s24, 11
	v_add_u32_e32 v212, s8, v23
	v_pk_add_f32 v[56:57], v[56:57], v[24:25] op_sel_hi:[1,0]
	v_pk_add_f32 v[58:59], v[58:59], v[24:25] op_sel_hi:[1,0]
	v_cvt_pk_f16_f32 v56, v56, v57
	v_cvt_pk_f16_f32 v57, v58, v59
	global_store_dwordx2 v212, v[56:57], s[22:23] offset:0
	v_pk_add_f32 v[60:61], v[60:61], v[26:27] op_sel_hi:[1,0]
	v_pk_add_f32 v[62:63], v[62:63], v[26:27] op_sel_hi:[1,0]
	v_cvt_pk_f16_f32 v60, v60, v61
	v_cvt_pk_f16_f32 v61, v62, v63
	global_store_dwordx2 v212, v[60:61], s[22:23] offset:256
	v_pk_add_f32 v[64:65], v[64:65], v[28:29] op_sel_hi:[1,0]
	v_pk_add_f32 v[66:67], v[66:67], v[28:29] op_sel_hi:[1,0]
	v_cvt_pk_f16_f32 v64, v64, v65
	v_cvt_pk_f16_f32 v65, v66, v67
	global_store_dwordx2 v212, v[64:65], s[22:23] offset:1024
	v_pk_add_f32 v[68:69], v[68:69], v[30:31] op_sel_hi:[1,0]
	v_pk_add_f32 v[70:71], v[70:71], v[30:31] op_sel_hi:[1,0]
	v_cvt_pk_f16_f32 v68, v68, v69
	v_cvt_pk_f16_f32 v69, v70, v71
	global_store_dwordx2 v212, v[68:69], s[22:23] offset:1280
	s_add_u32 s24, s29, 1
	s_lshl_b32 s8, s24, 11
	v_add_u32_e32 v212, s8, v23
	v_pk_add_f32 v[72:73], v[72:73], v[24:25] op_sel_hi:[1,0]
	v_pk_add_f32 v[74:75], v[74:75], v[24:25] op_sel_hi:[1,0]
	v_cvt_pk_f16_f32 v72, v72, v73
	v_cvt_pk_f16_f32 v73, v74, v75
	global_store_dwordx2 v212, v[72:73], s[22:23] offset:0
	v_pk_add_f32 v[76:77], v[76:77], v[26:27] op_sel_hi:[1,0]
	v_pk_add_f32 v[78:79], v[78:79], v[26:27] op_sel_hi:[1,0]
	v_cvt_pk_f16_f32 v76, v76, v77
	v_cvt_pk_f16_f32 v77, v78, v79
	global_store_dwordx2 v212, v[76:77], s[22:23] offset:256
	v_pk_add_f32 v[80:81], v[80:81], v[28:29] op_sel_hi:[1,0]
	v_pk_add_f32 v[82:83], v[82:83], v[28:29] op_sel_hi:[1,0]
	v_cvt_pk_f16_f32 v80, v80, v81
	v_cvt_pk_f16_f32 v81, v82, v83
	global_store_dwordx2 v212, v[80:81], s[22:23] offset:1024
	v_pk_add_f32 v[84:85], v[84:85], v[30:31] op_sel_hi:[1,0]
	v_pk_add_f32 v[86:87], v[86:87], v[30:31] op_sel_hi:[1,0]
	v_cvt_pk_f16_f32 v84, v84, v85
	v_cvt_pk_f16_f32 v85, v86, v87
	global_store_dwordx2 v212, v[84:85], s[22:23] offset:1280
	s_add_u32 s24, s29, 2
	s_lshl_b32 s8, s24, 11
	v_add_u32_e32 v212, s8, v23
	v_pk_add_f32 v[88:89], v[88:89], v[24:25] op_sel_hi:[1,0]
	v_pk_add_f32 v[90:91], v[90:91], v[24:25] op_sel_hi:[1,0]
	v_cvt_pk_f16_f32 v88, v88, v89
	v_cvt_pk_f16_f32 v89, v90, v91
	global_store_dwordx2 v212, v[88:89], s[22:23] offset:0
	v_pk_add_f32 v[92:93], v[92:93], v[26:27] op_sel_hi:[1,0]
	v_pk_add_f32 v[94:95], v[94:95], v[26:27] op_sel_hi:[1,0]
	v_cvt_pk_f16_f32 v92, v92, v93
	v_cvt_pk_f16_f32 v93, v94, v95
	global_store_dwordx2 v212, v[92:93], s[22:23] offset:256
	v_pk_add_f32 v[96:97], v[96:97], v[28:29] op_sel_hi:[1,0]
	v_pk_add_f32 v[98:99], v[98:99], v[28:29] op_sel_hi:[1,0]
	v_cvt_pk_f16_f32 v96, v96, v97
	v_cvt_pk_f16_f32 v97, v98, v99
	global_store_dwordx2 v212, v[96:97], s[22:23] offset:1024
	v_pk_add_f32 v[100:101], v[100:101], v[30:31] op_sel_hi:[1,0]
	v_pk_add_f32 v[102:103], v[102:103], v[30:31] op_sel_hi:[1,0]
	v_cvt_pk_f16_f32 v100, v100, v101
	v_cvt_pk_f16_f32 v101, v102, v103
	global_store_dwordx2 v212, v[100:101], s[22:23] offset:1280
	s_add_u32 s24, s29, 3
	s_lshl_b32 s8, s24, 11
	v_add_u32_e32 v212, s8, v23
	v_pk_add_f32 v[104:105], v[104:105], v[24:25] op_sel_hi:[1,0]
	v_pk_add_f32 v[106:107], v[106:107], v[24:25] op_sel_hi:[1,0]
	v_cvt_pk_f16_f32 v104, v104, v105
	v_cvt_pk_f16_f32 v105, v106, v107
	global_store_dwordx2 v212, v[104:105], s[22:23] offset:0
	v_pk_add_f32 v[108:109], v[108:109], v[26:27] op_sel_hi:[1,0]
	v_pk_add_f32 v[110:111], v[110:111], v[26:27] op_sel_hi:[1,0]
	v_cvt_pk_f16_f32 v108, v108, v109
	v_cvt_pk_f16_f32 v109, v110, v111
	global_store_dwordx2 v212, v[108:109], s[22:23] offset:256
	v_pk_add_f32 v[112:113], v[112:113], v[28:29] op_sel_hi:[1,0]
	v_pk_add_f32 v[114:115], v[114:115], v[28:29] op_sel_hi:[1,0]
	v_cvt_pk_f16_f32 v112, v112, v113
	v_cvt_pk_f16_f32 v113, v114, v115
	global_store_dwordx2 v212, v[112:113], s[22:23] offset:1024
	v_pk_add_f32 v[116:117], v[116:117], v[30:31] op_sel_hi:[1,0]
	v_pk_add_f32 v[118:119], v[118:119], v[30:31] op_sel_hi:[1,0]
	v_cvt_pk_f16_f32 v116, v116, v117
	v_cvt_pk_f16_f32 v117, v118, v119
	global_store_dwordx2 v212, v[116:117], s[22:23] offset:1280
	s_branch .Lpf_done
